# speedup vs baseline: 1.0049x; 1.0049x over previous
_Z16closed_form_mainPKfS0_PKiPf:
	s_load_dwordx8 s[16:23], s[0:1], 0x0
	s_lshr_b32 s6, s2, 3
	v_readfirstlane_b32 s0, v0
	s_mul_hi_u32 s7, s6, 0x24924925
	s_lshr_b32 s4, s0, 6
	s_and_b32 s0, s2, 7
	s_mul_i32 s1, s7, 7
	s_bfe_u32 s5, s2, 0x10003
	s_sub_i32 s1, s6, s1
	s_mul_i32 s36, s0, 7
	s_xor_b32 s3, s4, s5
	s_add_i32 s36, s36, s1
	s_waitcnt lgkmcnt(0)
	s_mov_b64 s[28:29], s[22:23]
	v_and_b32_e32 v19, 63, v0
	s_cmp_lt_u32 s36, 52
	s_mov_b64 s[0:1], -1
	s_cbranch_scc0 .LBB0_32
	s_mul_hi_u32 s0, s6, 0x20820821
	s_lshr_b32 s38, s0, 3
	s_mul_hi_u32 s0, s7, 0x1c71c71d
	s_mul_i32 s0, s0, 9
	s_sub_i32 s0, s7, s0
	v_add_u32_e32 v2, -3, v19
	v_mad_u64_u32 v[0:1], s[0:1], s0, 57, v[2:3]
	s_mov_b64 s[24:25], s[18:19]
	v_mov_b32_e32 v1, 0x200
	v_med3_i32 v1, v0, 0, v1
	s_mul_i32 s34, s36, 10
	s_and_b32 s17, s17, 0xffff
	s_and_b32 s25, s25, 0xffff
	v_cmp_gt_u32_e64 s[0:1], 57, v2
	s_mov_b32 s19, 0x20000
	s_mov_b32 s18, 0xe0e038
	s_mov_b32 s26, 0x606018
	s_mul_i32 s35, s38, 0x70701c
	s_mul_i32 s33, s38, 0x30300c
	v_lshlrev_b32_e32 v28, 2, v1
	v_mul_u32_u24_e32 v27, 12, v1
	v_lshlrev_b32_e32 v23, 4, v19
	s_cmp_lg_u32 s4, s5
	v_sub_u32_e64 v29, s34, 2 clamp
	s_cbranch_scc0 .LBB0_15
	s_setprio 2
	s_mov_b32 s27, s19
	s_and_b32 s21, s21, 0xffff
	s_mov_b32 s22, 0x202008
	s_mov_b32 s23, s19
	s_mul_i32 s38, s38, 0x101004
	s_movk_i32 s37, 0x80
	v_add_u32_e32 v18, -1, v0
	s_movk_i32 s4, 0x201
	s_movk_i32 s5, 0x1ff
	v_cmp_gt_u32_e64 s[40:41], s4, v0
	v_cmp_gt_u32_e64 s[42:43], s5, v18
	v_mov_b32_e32 v18, 0x42c80000
	v_mov_b32_e32 v22, 0x3de38e39
	v_mov_b32_e32 v26, 0x3a3d6628
	v_mov_b32_e32 v1, 0
	s_add_i32 s4, s34, -3
	s_max_i32 s4, s4, 0
	s_mul_i32 s4, s4, 0x804
	s_add_i32 s4, s4, s38
	buffer_load_dword v29, v28, s[20:23], s4 offen nt
	s_add_i32 s4, s34, -2
	s_max_i32 s4, s4, 0
	s_mul_i32 s4, s4, 0x804
	s_add_i32 s4, s4, s38
	buffer_load_dword v2, v28, s[20:23], s4 offen nt
	s_add_i32 s5, s34, -2
	s_max_i32 s5, s5, 0
	s_mul_i32 s6, s5, 0x804
	s_add_i32 s6, s6, s35
	s_add_i32 s7, s6, 0x505014
	s_add_i32 s8, s6, 0x606018
	s_mul_i32 s9, s5, 0x180c
	s_add_i32 s9, s9, s33
	s_add_i32 s4, s34, -1
	s_max_i32 s4, s4, 0
	s_mul_i32 s4, s4, 0x804
	s_add_i32 s4, s4, s38
	buffer_load_dword v3, v28, s[20:23], s4 offen nt
	buffer_load_dwordx3 v[8:10], v27, s[24:27], s9 offen nt
	buffer_load_dword v4, v28, s[16:19], s7 offen nt
	buffer_load_dword v5, v28, s[16:19], s8 offen nt
	s_add_i32 s5, s34, -1
	s_max_i32 s5, s5, 0
	s_mul_i32 s6, s5, 0x804
	s_add_i32 s6, s6, s35
	s_add_i32 s7, s6, 0x505014
	s_add_i32 s8, s6, 0x606018
	s_mul_i32 s9, s5, 0x180c
	s_add_i32 s9, s9, s33
	s_add_i32 s4, s34, 0
	s_min_i32 s4, s4, 0x200
	s_mul_i32 s4, s4, 0x804
	s_add_i32 s4, s4, s38
	buffer_load_dword v16, v28, s[20:23], s4 offen nt
	buffer_load_dwordx3 v[12:14], v27, s[24:27], s9 offen nt
	buffer_load_dword v6, v28, s[16:19], s7 offen nt
	buffer_load_dword v7, v28, s[16:19], s8 offen nt
	s_waitcnt vmcnt(8)
	s_add_i32 s4, s34, -3
	s_cmpk_lt_u32 s4, 0x201
	s_cselect_b64 s[12:13], s[40:41], 0
	v_cmp_eq_u32_e64 s[14:15], s37, v29
	s_and_b64 s[14:15], s[14:15], s[12:13]
	v_cndmask_b32_e64 v17, 0, 1, s[14:15]
	s_add_i32 s4, s34, -2
	s_cmpk_lt_u32 s4, 0x201
	s_cselect_b64 s[12:13], s[40:41], 0
	v_cmp_eq_u32_e64 s[14:15], s37, v2
	s_and_b64 s[14:15], s[14:15], s[12:13]
	v_cndmask_b32_e64 v20, 0, 1, s[14:15]
	s_nop 0
	v_or_b32_dpp v21, v17, v17 wave_shr:1 row_mask:0xf bank_mask:0xf bound_ctrl:1
	v_or_b32_dpp v24, v20, v20 wave_shr:1 row_mask:0xf bank_mask:0xf bound_ctrl:1
	s_nop 1
	v_or_b32_dpp v21, v17, v21 wave_shl:1 row_mask:0xf bank_mask:0xf bound_ctrl:1
	v_or_b32_dpp v24, v20, v24 wave_shl:1 row_mask:0xf bank_mask:0xf bound_ctrl:1
	s_nop 1
	v_or_b32_dpp v25, v21, v21 wave_shr:1 row_mask:0xf bank_mask:0xf bound_ctrl:1
	v_or_b32_dpp v30, v24, v24 wave_shr:1 row_mask:0xf bank_mask:0xf bound_ctrl:1
	s_nop 1
	v_or_b32_dpp v25, v21, v25 wave_shl:1 row_mask:0xf bank_mask:0xf bound_ctrl:1
	v_or_b32_dpp v30, v24, v30 wave_shl:1 row_mask:0xf bank_mask:0xf bound_ctrl:1
	v_mov_b32_e32 v17, 0
	v_mov_b32_e32 v24, 0
	s_add_i32 s5, s34, 0
	s_min_i32 s5, s5, 0x200
	s_mul_i32 s6, s5, 0x804
	s_add_i32 s6, s6, s35
	s_add_i32 s7, s6, 0x505014
	s_add_i32 s8, s6, 0x606018
	s_mul_i32 s9, s5, 0x180c
	s_add_i32 s9, s9, s33
	s_add_i32 s4, s34, 1
	s_min_i32 s4, s4, 0x200
	s_mul_i32 s4, s4, 0x804
	s_add_i32 s4, s4, s38
	buffer_load_dword v31, v28, s[20:23], s4 offen nt
	buffer_load_dwordx3 v[32:34], v27, s[24:27], s9 offen nt
	buffer_load_dword v20, v28, s[16:19], s7 offen nt
	buffer_load_dword v21, v28, s[16:19], s8 offen nt
	s_waitcnt vmcnt(8)
	v_mov_b32_dpp v36, v8 wave_shr:1 row_mask:0xf bank_mask:0xf bound_ctrl:1
	v_mov_b32_dpp v37, v9 wave_shr:1 row_mask:0xf bank_mask:0xf bound_ctrl:1
	v_mov_b32_dpp v38, v10 wave_shr:1 row_mask:0xf bank_mask:0xf bound_ctrl:1
	v_mov_b32_dpp v40, v8 wave_shl:1 row_mask:0xf bank_mask:0xf bound_ctrl:1
	v_mov_b32_dpp v41, v9 wave_shl:1 row_mask:0xf bank_mask:0xf bound_ctrl:1
	v_mov_b32_dpp v42, v10 wave_shl:1 row_mask:0xf bank_mask:0xf bound_ctrl:1
	s_add_i32 s4, s34, -1
	s_cmpk_lt_u32 s4, 0x201
	s_cselect_b64 s[12:13], s[40:41], 0
	v_cmp_eq_u32_e64 s[14:15], s37, v3
	s_and_b64 s[14:15], s[14:15], s[12:13]
	v_cndmask_b32_e64 v44, 0, 1, s[14:15]
	v_mul_f32_e64 v46, v8, v8
	v_mul_f32_e64 v47, v8, v9
	v_or_b32_dpp v45, v44, v44 wave_shr:1 row_mask:0xf bank_mask:0xf bound_ctrl:1
	v_mul_f32_e64 v48, v8, v10
	v_or_b32_dpp v45, v44, v45 wave_shl:1 row_mask:0xf bank_mask:0xf bound_ctrl:1
	v_mul_f32_e64 v49, v9, v9
	v_mul_f32_e64 v50, v9, v10
	v_or_b32_dpp v52, v45, v45 wave_shr:1 row_mask:0xf bank_mask:0xf bound_ctrl:1
	v_mul_f32_e64 v51, v10, v10
	s_nop 0
	v_or_b32_dpp v52, v45, v52 wave_shl:1 row_mask:0xf bank_mask:0xf bound_ctrl:1
	v_or3_b32 v53, v52, v30, v25
	v_or3_b32 v53, v53, v17, v24
	s_add_i32 s4, s34, -4
	s_cmpk_lt_u32 s4, 0x1ff
	s_cselect_b64 s[12:13], s[42:43], 0
	v_cmp_ne_u32_e64 s[30:31], 0, v53
	s_and_b64 s[30:31], s[30:31], s[12:13]
	v_cndmask_b32_e64 v53, 0, 1.0, s[30:31]
	v_add_f32_e64 v44, v8, v36
	v_add_f32_e64 v45, v9, v37
	v_add_f32_e64 v54, v10, v38
	v_fma_f32 v46, v36, v36, v46
	v_fma_f32 v47, v36, v37, v47
	v_fma_f32 v48, v36, v38, v48
	v_fma_f32 v49, v37, v37, v49
	v_fma_f32 v50, v37, v38, v50
	v_fma_f32 v51, v38, v38, v51
	v_add_f32_dpp v61, v53, v53 wave_shr:1 row_mask:0xf bank_mask:0xf bound_ctrl:1
	v_add_f32_e64 v44, v44, v40
	v_add_f32_e64 v45, v45, v41
	v_add_f32_e64 v54, v54, v42
	v_fma_f32 v55, v40, v40, v46
	v_fma_f32 v56, v40, v41, v47
	v_fma_f32 v57, v40, v42, v48
	v_fma_f32 v58, v41, v41, v49
	v_fma_f32 v59, v41, v42, v50
	v_fma_f32 v60, v42, v42, v51
	v_add_f32_dpp v61, v53, v61 wave_shl:1 row_mask:0xf bank_mask:0xf bound_ctrl:1
	v_mov_b32_dpp v46, v4 wave_shr:1 row_mask:0xf bank_mask:0xf bound_ctrl:1
	v_mov_b32_dpp v47, v5 wave_shr:1 row_mask:0xf bank_mask:0xf bound_ctrl:1
	v_mov_b32_dpp v50, v4 wave_shl:1 row_mask:0xf bank_mask:0xf bound_ctrl:1
	v_mov_b32_dpp v51, v5 wave_shl:1 row_mask:0xf bank_mask:0xf bound_ctrl:1
	v_pk_mul_f32 v[48:49], v[4:5], v[8:9] op_sel_hi:[1,0]
	v_pk_mul_f32 v[64:65], v[4:5], v[8:9] op_sel:[0,1]
	v_pk_mul_f32 v[68:69], v[4:5], v[10:11] op_sel_hi:[1,0]
	v_pk_add_f32 v[72:73], v[4:5], v[46:47]
	v_pk_fma_f32 v[48:49], v[46:47], v[36:37], v[48:49] op_sel_hi:[1,0,1]
	v_pk_fma_f32 v[64:65], v[46:47], v[36:37], v[64:65] op_sel:[0,1,0]
	v_pk_fma_f32 v[68:69], v[46:47], v[38:39], v[68:69] op_sel_hi:[1,0,1]
	v_pk_add_f32 v[72:73], v[72:73], v[50:51]
	v_pk_fma_f32 v[48:49], v[50:51], v[40:41], v[48:49] op_sel_hi:[1,0,1]
	v_pk_fma_f32 v[64:65], v[50:51], v[40:41], v[64:65] op_sel:[0,1,0]
	v_pk_fma_f32 v[68:69], v[50:51], v[42:43], v[68:69] op_sel_hi:[1,0,1]
	s_barrier
	s_add_i32 s5, s34, 1
	s_min_i32 s5, s5, 0x200
	s_mul_i32 s6, s5, 0x804
	s_add_i32 s6, s6, s35
	s_add_i32 s7, s6, 0x505014
	s_add_i32 s8, s6, 0x606018
	s_mul_i32 s9, s5, 0x180c
	s_add_i32 s9, s9, s33
	s_add_i32 s4, s34, 2
	s_min_i32 s4, s4, 0x200
	s_mul_i32 s4, s4, 0x804
	s_add_i32 s4, s4, s38
	buffer_load_dword v24, v28, s[20:23], s4 offen nt
	buffer_load_dwordx3 v[76:78], v27, s[24:27], s9 offen nt
	buffer_load_dword v46, v28, s[16:19], s7 offen nt
	buffer_load_dword v47, v28, s[16:19], s8 offen nt
	s_waitcnt vmcnt(8)
	v_mov_b32_dpp v80, v12 wave_shr:1 row_mask:0xf bank_mask:0xf bound_ctrl:1
	v_mov_b32_dpp v81, v13 wave_shr:1 row_mask:0xf bank_mask:0xf bound_ctrl:1
	v_mov_b32_dpp v82, v14 wave_shr:1 row_mask:0xf bank_mask:0xf bound_ctrl:1
	v_mov_b32_dpp v84, v12 wave_shl:1 row_mask:0xf bank_mask:0xf bound_ctrl:1
	v_mov_b32_dpp v85, v13 wave_shl:1 row_mask:0xf bank_mask:0xf bound_ctrl:1
	v_mov_b32_dpp v86, v14 wave_shl:1 row_mask:0xf bank_mask:0xf bound_ctrl:1
	s_add_i32 s4, s34, 0
	s_cmpk_lt_u32 s4, 0x201
	s_cselect_b64 s[12:13], s[40:41], 0
	v_cmp_eq_u32_e64 s[14:15], s37, v16
	s_and_b64 s[14:15], s[14:15], s[12:13]
	v_cndmask_b32_e64 v53, 0, 1, s[14:15]
	v_mul_f32_e64 v50, v12, v12
	v_mul_f32_e64 v51, v12, v13
	v_or_b32_dpp v70, v53, v53 wave_shr:1 row_mask:0xf bank_mask:0xf bound_ctrl:1
	v_mul_f32_e64 v62, v12, v14
	v_or_b32_dpp v70, v53, v70 wave_shl:1 row_mask:0xf bank_mask:0xf bound_ctrl:1
	v_mul_f32_e64 v63, v13, v13
	v_mul_f32_e64 v66, v13, v14
	v_or_b32_dpp v71, v70, v70 wave_shr:1 row_mask:0xf bank_mask:0xf bound_ctrl:1
	v_mul_f32_e64 v67, v14, v14
	s_nop 0
	v_or_b32_dpp v71, v70, v71 wave_shl:1 row_mask:0xf bank_mask:0xf bound_ctrl:1
	v_or3_b32 v53, v71, v52, v30
	v_or3_b32 v53, v53, v25, v17
	s_add_i32 s4, s34, -3
	s_cmpk_lt_u32 s4, 0x1ff
	s_cselect_b64 s[12:13], s[42:43], 0
	v_cmp_ne_u32_e64 s[30:31], 0, v53
	s_and_b64 s[30:31], s[30:31], s[12:13]
	v_cndmask_b32_e64 v53, 0, 1.0, s[30:31]
	v_add_f32_e64 v74, v12, v80
	v_add_f32_e64 v75, v13, v81
	v_add_f32_e64 v88, v14, v82
	v_fma_f32 v50, v80, v80, v50
	v_fma_f32 v51, v80, v81, v51
	v_fma_f32 v62, v80, v82, v62
	v_fma_f32 v63, v81, v81, v63
	v_fma_f32 v66, v81, v82, v66
	v_fma_f32 v67, v82, v82, v67
	v_add_f32_dpp v95, v53, v53 wave_shr:1 row_mask:0xf bank_mask:0xf bound_ctrl:1
	v_add_f32_e64 v74, v74, v84
	v_add_f32_e64 v75, v75, v85
	v_add_f32_e64 v88, v88, v86
	v_fma_f32 v89, v84, v84, v50
	v_fma_f32 v90, v84, v85, v51
	v_fma_f32 v91, v84, v86, v62
	v_fma_f32 v92, v85, v85, v63
	v_fma_f32 v93, v85, v86, v66
	v_fma_f32 v94, v86, v86, v67
	v_add_f32_dpp v95, v53, v95 wave_shl:1 row_mask:0xf bank_mask:0xf bound_ctrl:1
	v_mov_b32_dpp v96, v6 wave_shr:1 row_mask:0xf bank_mask:0xf bound_ctrl:1
	v_mov_b32_dpp v97, v7 wave_shr:1 row_mask:0xf bank_mask:0xf bound_ctrl:1
	v_mov_b32_dpp v100, v6 wave_shl:1 row_mask:0xf bank_mask:0xf bound_ctrl:1
	v_mov_b32_dpp v101, v7 wave_shl:1 row_mask:0xf bank_mask:0xf bound_ctrl:1
	v_pk_mul_f32 v[50:51], v[6:7], v[12:13] op_sel_hi:[1,0]
	v_pk_mul_f32 v[62:63], v[6:7], v[12:13] op_sel:[0,1]
	v_pk_mul_f32 v[66:67], v[6:7], v[14:15] op_sel_hi:[1,0]
	v_pk_add_f32 v[98:99], v[6:7], v[96:97]
	v_pk_fma_f32 v[50:51], v[96:97], v[80:81], v[50:51] op_sel_hi:[1,0,1]
	v_pk_fma_f32 v[62:63], v[96:97], v[80:81], v[62:63] op_sel:[0,1,0]
	v_pk_fma_f32 v[66:67], v[96:97], v[82:83], v[66:67] op_sel_hi:[1,0,1]
	v_pk_add_f32 v[98:99], v[98:99], v[100:101]
	v_pk_fma_f32 v[50:51], v[100:101], v[84:85], v[50:51] op_sel_hi:[1,0,1]
	v_pk_fma_f32 v[62:63], v[100:101], v[84:85], v[62:63] op_sel:[0,1,0]
	v_pk_fma_f32 v[66:67], v[100:101], v[86:87], v[66:67] op_sel_hi:[1,0,1]
	s_barrier
	s_add_i32 s5, s34, 2
	s_min_i32 s5, s5, 0x200
	s_mul_i32 s6, s5, 0x804
	s_add_i32 s6, s6, s35
	s_add_i32 s7, s6, 0x505014
	s_add_i32 s8, s6, 0x606018
	s_mul_i32 s9, s5, 0x180c
	s_add_i32 s9, s9, s33
	s_add_i32 s4, s34, 3
	s_min_i32 s4, s4, 0x200
	s_mul_i32 s4, s4, 0x804
	s_add_i32 s4, s4, s38
	buffer_load_dword v17, v28, s[20:23], s4 offen nt
	buffer_load_dwordx3 v[100:102], v27, s[24:27], s9 offen nt
	buffer_load_dword v96, v28, s[16:19], s7 offen nt
	buffer_load_dword v97, v28, s[16:19], s8 offen nt
	s_waitcnt vmcnt(8)
	v_mov_b32_dpp v104, v32 wave_shr:1 row_mask:0xf bank_mask:0xf bound_ctrl:1
	v_mov_b32_dpp v105, v33 wave_shr:1 row_mask:0xf bank_mask:0xf bound_ctrl:1
	v_mov_b32_dpp v106, v34 wave_shr:1 row_mask:0xf bank_mask:0xf bound_ctrl:1
	v_mov_b32_dpp v108, v32 wave_shl:1 row_mask:0xf bank_mask:0xf bound_ctrl:1
	v_mov_b32_dpp v109, v33 wave_shl:1 row_mask:0xf bank_mask:0xf bound_ctrl:1
	v_mov_b32_dpp v110, v34 wave_shl:1 row_mask:0xf bank_mask:0xf bound_ctrl:1
	s_add_i32 s4, s34, 1
	s_cmpk_lt_u32 s4, 0x201
	s_cselect_b64 s[12:13], s[40:41], 0
	v_cmp_eq_u32_e64 s[14:15], s37, v31
	s_and_b64 s[14:15], s[14:15], s[12:13]
	v_cndmask_b32_e64 v29, 0, 1, s[14:15]
	v_mul_f32_e64 v112, v32, v32
	v_mul_f32_e64 v113, v32, v33
	v_or_b32_dpp v53, v29, v29 wave_shr:1 row_mask:0xf bank_mask:0xf bound_ctrl:1
	v_mul_f32_e64 v114, v32, v34
	v_or_b32_dpp v53, v29, v53 wave_shl:1 row_mask:0xf bank_mask:0xf bound_ctrl:1
	v_mul_f32_e64 v115, v33, v33
	v_mul_f32_e64 v116, v33, v34
	v_or_b32_dpp v70, v53, v53 wave_shr:1 row_mask:0xf bank_mask:0xf bound_ctrl:1
	v_mul_f32_e64 v117, v34, v34
	s_nop 0
	v_or_b32_dpp v70, v53, v70 wave_shl:1 row_mask:0xf bank_mask:0xf bound_ctrl:1
	v_or3_b32 v29, v70, v71, v52
	v_or3_b32 v29, v29, v30, v25
	s_add_i32 s4, s34, -2
	s_cmpk_lt_u32 s4, 0x1ff
	s_cselect_b64 s[12:13], s[42:43], 0
	v_cmp_ne_u32_e64 s[30:31], 0, v29
	s_and_b64 s[30:31], s[30:31], s[12:13]
	v_cndmask_b32_e64 v29, 0, 1.0, s[30:31]
	v_add_f32_e64 v118, v32, v104
	v_add_f32_e64 v119, v33, v105
	v_add_f32_e64 v120, v34, v106
	v_fma_f32 v112, v104, v104, v112
	v_fma_f32 v113, v104, v105, v113
	v_fma_f32 v114, v104, v106, v114
	v_fma_f32 v115, v105, v105, v115
	v_fma_f32 v116, v105, v106, v116
	v_fma_f32 v117, v106, v106, v117
	v_add_f32_dpp v127, v29, v29 wave_shr:1 row_mask:0xf bank_mask:0xf bound_ctrl:1
	v_add_f32_e64 v118, v118, v108
	v_add_f32_e64 v119, v119, v109
	v_add_f32_e64 v120, v120, v110
	v_fma_f32 v121, v108, v108, v112
	v_fma_f32 v122, v108, v109, v113
	v_fma_f32 v123, v108, v110, v114
	v_fma_f32 v124, v109, v109, v115
	v_fma_f32 v125, v109, v110, v116
	v_fma_f32 v126, v110, v110, v117
	v_add_f32_dpp v127, v29, v127 wave_shl:1 row_mask:0xf bank_mask:0xf bound_ctrl:1
	v_pk_add_f32 v[114:115], v[74:75], v[118:119]
	v_pk_add_f32 v[112:113], v[44:45], v[114:115]
	v_pk_add_f32 v[44:45], v[88:89], v[120:121]
	v_pk_add_f32 v[74:75], v[54:55], v[44:45]
	v_pk_add_f32 v[54:55], v[90:91], v[122:123]
	v_pk_add_f32 v[88:89], v[56:57], v[54:55]
	v_pk_add_f32 v[56:57], v[92:93], v[124:125]
	v_pk_add_f32 v[90:91], v[58:59], v[56:57]
	v_pk_add_f32 v[58:59], v[94:95], v[126:127]
	v_pk_add_f32 v[92:93], v[60:61], v[58:59]
	v_mul_f32_e64 v128, v112, v22
	v_mul_f32_e64 v129, v113, v22
	v_mul_f32_e64 v130, v74, v22
	v_fma_f32 v29, v75, v22, v26
	v_mul_f32_e64 v53, v88, v22
	v_mul_f32_e64 v60, v89, v22
	v_fma_f32 v61, v90, v22, v26
	v_mul_f32_e64 v94, v91, v22
	v_fma_f32 v95, v92, v22, v26
	v_fma_f32 v29, -v128, v128, v29
	v_fma_f32 v53, -v128, v129, v53
	v_fma_f32 v60, -v128, v130, v60
	v_fma_f32 v61, -v129, v129, v61
	v_fma_f32 v94, -v129, v130, v94
	v_fma_f32 v95, -v130, v130, v95
	v_mul_f32_e64 v116, v94, v94
	v_mul_f32_e64 v117, v53, v95
	v_mul_f32_e64 v140, v60, v61
	v_mul_f32_e64 v141, v60, v60
	v_mul_f32_e64 v142, v29, v94
	v_mul_f32_e64 v143, v53, v53
	v_fma_f32 v116, v61, v95, -v116
	v_fma_f32 v117, v60, v94, -v117
	v_fma_f32 v140, v53, v94, -v140
	v_fma_f32 v141, v29, v95, -v141
	v_fma_f32 v142, v53, v60, -v142
	v_fma_f32 v143, v29, v61, -v143
	v_mul_f32_e64 v144, v29, v116
	v_fma_f32 v144, v53, v117, v144
	v_fma_f32 v144, v60, v140, v144
	v_rcp_f32_e32 v144, v144
	v_cmp_ne_u32_e64 vcc, s37, v2
	v_mul_f32_e64 v144, v144, v22
	v_cndmask_b32_e64 v144, 0, v144, s[30:31]
	v_cndmask_b32_e64 v29, 0, v18, vcc
	v_cndmask_b32_e64 v137, 0, v22, s[30:31]
	v_mul_f32_e64 v131, v116, v144
	v_mul_f32_e64 v132, v117, v144
	v_mul_f32_e64 v133, v140, v144
	v_mul_f32_e64 v134, v141, v144
	v_mul_f32_e64 v135, v142, v144
	v_mul_f32_e64 v136, v143, v144
	v_add_f32_e64 v138, v93, v29
	v_mov_b32_e32 v139, v2
	ds_write_b128 v23, v[128:131]
	ds_write_b128 v23, v[132:135] offset:1024
	ds_write_b128 v23, v[136:139] offset:2048
	v_mov_b32_dpp v74, v20 wave_shr:1 row_mask:0xf bank_mask:0xf bound_ctrl:1
	v_mov_b32_dpp v75, v21 wave_shr:1 row_mask:0xf bank_mask:0xf bound_ctrl:1
	v_mov_b32_dpp v90, v20 wave_shl:1 row_mask:0xf bank_mask:0xf bound_ctrl:1
	v_mov_b32_dpp v91, v21 wave_shl:1 row_mask:0xf bank_mask:0xf bound_ctrl:1
	v_pk_mul_f32 v[60:61], v[20:21], v[32:33] op_sel_hi:[1,0]
	v_pk_mul_f32 v[88:89], v[20:21], v[32:33] op_sel:[0,1]
	v_pk_mul_f32 v[92:93], v[20:21], v[34:35] op_sel_hi:[1,0]
	v_pk_add_f32 v[112:113], v[20:21], v[74:75]
	v_pk_fma_f32 v[60:61], v[74:75], v[104:105], v[60:61] op_sel_hi:[1,0,1]
	v_pk_fma_f32 v[88:89], v[74:75], v[104:105], v[88:89] op_sel:[0,1,0]
	v_pk_fma_f32 v[92:93], v[74:75], v[106:107], v[92:93] op_sel_hi:[1,0,1]
	v_pk_add_f32 v[112:113], v[112:113], v[90:91]
	v_pk_fma_f32 v[60:61], v[90:91], v[108:109], v[60:61] op_sel_hi:[1,0,1]
	v_pk_fma_f32 v[88:89], v[90:91], v[108:109], v[88:89] op_sel:[0,1,0]
	v_pk_fma_f32 v[92:93], v[90:91], v[110:111], v[92:93] op_sel_hi:[1,0,1]
	s_waitcnt lgkmcnt(0)
	s_barrier
	v_pk_add_f32 v[74:75], v[98:99], v[112:113]
	v_pk_add_f32 v[90:91], v[72:73], v[74:75]
	v_pk_add_f32 v[94:95], v[50:51], v[60:61]
	v_pk_add_f32 v[72:73], v[48:49], v[94:95]
	v_pk_add_f32 v[50:51], v[62:63], v[88:89]
	v_pk_add_f32 v[48:49], v[64:65], v[50:51]
	v_pk_add_f32 v[62:63], v[66:67], v[92:93]
	v_pk_add_f32 v[64:65], v[68:69], v[62:63]
	v_pk_fma_f32 v[72:73], v[128:129], v[90:91], v[72:73] op_sel_hi:[0,1,1] neg_lo:[1,0,0] neg_hi:[1,0,0]
	v_pk_fma_f32 v[48:49], v[128:129], v[90:91], v[48:49] op_sel:[1,0,0] neg_lo:[1,0,0] neg_hi:[1,0,0]
	v_pk_fma_f32 v[64:65], v[130:131], v[90:91], v[64:65] op_sel_hi:[0,1,1] neg_lo:[1,0,0] neg_hi:[1,0,0]
	v_pk_mul_f32 v[66:67], v[130:131], v[72:73] op_sel:[1,0]
	v_pk_mul_f32 v[98:99], v[132:133], v[72:73] op_sel_hi:[0,1]
	v_pk_mul_f32 v[142:143], v[132:133], v[72:73] op_sel:[1,0]
	v_pk_fma_f32 v[66:67], v[132:133], v[48:49], v[66:67] op_sel_hi:[0,1,1]
	v_pk_fma_f32 v[98:99], v[134:135], v[48:49], v[98:99] op_sel_hi:[0,1,1]
	v_pk_fma_f32 v[142:143], v[134:135], v[48:49], v[142:143] op_sel:[1,0,0]
	v_pk_fma_f32 v[66:67], v[132:133], v[64:65], v[66:67] op_sel:[1,0,0]
	v_pk_fma_f32 v[98:99], v[134:135], v[64:65], v[98:99] op_sel:[1,0,0]
	v_pk_fma_f32 v[142:143], v[136:137], v[64:65], v[142:143] op_sel_hi:[0,1,1]
	v_pk_mul_f32 v[68:69], v[128:129], v[66:67] op_sel_hi:[0,1]
	v_pk_fma_f32 v[68:69], v[128:129], v[98:99], v[68:69] op_sel:[1,0,0]
	v_pk_fma_f32 v[68:69], v[130:131], v[142:143], v[68:69] op_sel_hi:[0,1,1]
	v_pk_fma_f32 v[68:69], v[136:137], v[90:91], v[68:69] op_sel:[1,0,0] neg_lo:[0,0,1] neg_hi:[0,0,1]
	s_add_i32 s5, s34, 3
	s_min_i32 s5, s5, 0x200
	s_mul_i32 s6, s5, 0x804
	s_add_i32 s6, s6, s35
	s_add_i32 s7, s6, 0x505014
	s_add_i32 s8, s6, 0x606018
	s_mul_i32 s9, s5, 0x180c
	s_add_i32 s9, s9, s33
	s_add_i32 s4, s34, 4
	s_min_i32 s4, s4, 0x200
	s_mul_i32 s4, s4, 0x804
	s_add_i32 s4, s4, s38
	buffer_load_dword v2, v28, s[20:23], s4 offen nt
	buffer_load_dwordx3 v[8:10], v27, s[24:27], s9 offen nt
	buffer_load_dword v4, v28, s[16:19], s7 offen nt
	buffer_load_dword v5, v28, s[16:19], s8 offen nt
	s_waitcnt vmcnt(8)
	v_mov_b32_dpp v36, v76 wave_shr:1 row_mask:0xf bank_mask:0xf bound_ctrl:1
	v_mov_b32_dpp v37, v77 wave_shr:1 row_mask:0xf bank_mask:0xf bound_ctrl:1
	v_mov_b32_dpp v38, v78 wave_shr:1 row_mask:0xf bank_mask:0xf bound_ctrl:1
	v_mov_b32_dpp v40, v76 wave_shl:1 row_mask:0xf bank_mask:0xf bound_ctrl:1
	v_mov_b32_dpp v41, v77 wave_shl:1 row_mask:0xf bank_mask:0xf bound_ctrl:1
	v_mov_b32_dpp v42, v78 wave_shl:1 row_mask:0xf bank_mask:0xf bound_ctrl:1
	s_add_i32 s4, s34, 2
	s_cmpk_lt_u32 s4, 0x201
	s_cselect_b64 s[12:13], s[40:41], 0
	v_cmp_eq_u32_e64 s[14:15], s37, v24
	s_and_b64 s[14:15], s[14:15], s[12:13]
	v_cndmask_b32_e64 v25, 0, 1, s[14:15]
	v_mul_f32_e64 v48, v76, v76
	v_mul_f32_e64 v49, v76, v77
	v_or_b32_dpp v29, v25, v25 wave_shr:1 row_mask:0xf bank_mask:0xf bound_ctrl:1
	v_mul_f32_e64 v64, v76, v78
	v_or_b32_dpp v29, v25, v29 wave_shl:1 row_mask:0xf bank_mask:0xf bound_ctrl:1
	v_mul_f32_e64 v65, v77, v77
	v_mul_f32_e64 v72, v77, v78
	v_or_b32_dpp v53, v29, v29 wave_shr:1 row_mask:0xf bank_mask:0xf bound_ctrl:1
	v_mul_f32_e64 v73, v78, v78
	s_nop 0
	v_or_b32_dpp v53, v29, v53 wave_shl:1 row_mask:0xf bank_mask:0xf bound_ctrl:1
	v_or3_b32 v25, v53, v70, v71
	v_or3_b32 v25, v25, v52, v30
	s_add_i32 s4, s34, -1
	s_cmpk_lt_u32 s4, 0x1ff
	s_cselect_b64 s[12:13], s[42:43], 0
	v_cmp_ne_u32_e64 s[30:31], 0, v25
	s_and_b64 s[30:31], s[30:31], s[12:13]
	v_cndmask_b32_e64 v25, 0, 1.0, s[30:31]
	v_add_f32_e64 v90, v76, v36
	v_add_f32_e64 v91, v77, v37
	v_add_f32_e64 v116, v78, v38
	v_fma_f32 v48, v36, v36, v48
	v_fma_f32 v49, v36, v37, v49
	v_fma_f32 v64, v36, v38, v64
	v_fma_f32 v65, v37, v37, v65
	v_fma_f32 v72, v37, v38, v72
	v_fma_f32 v73, v38, v38, v73
	v_add_f32_dpp v133, v25, v25 wave_shr:1 row_mask:0xf bank_mask:0xf bound_ctrl:1
	v_add_f32_e64 v90, v90, v40
	v_add_f32_e64 v91, v91, v41
	v_add_f32_e64 v116, v116, v42
	v_fma_f32 v117, v40, v40, v48
	v_fma_f32 v128, v40, v41, v49
	v_fma_f32 v129, v40, v42, v64
	v_fma_f32 v130, v41, v41, v65
	v_fma_f32 v131, v41, v42, v72
	v_fma_f32 v132, v42, v42, v73
	v_add_f32_dpp v133, v25, v133 wave_shl:1 row_mask:0xf bank_mask:0xf bound_ctrl:1
	v_pk_add_f32 v[48:49], v[114:115], v[90:91]
	v_pk_add_f32 v[64:65], v[44:45], v[116:117]
	v_pk_add_f32 v[44:45], v[54:55], v[128:129]
	v_pk_add_f32 v[54:55], v[56:57], v[130:131]
	v_pk_add_f32 v[56:57], v[58:59], v[132:133]
	v_mul_f32_e64 v136, v48, v22
	v_mul_f32_e64 v137, v49, v22
	v_mul_f32_e64 v138, v64, v22
	v_fma_f32 v25, v65, v22, v26
	v_mul_f32_e64 v29, v44, v22
	v_mul_f32_e64 v58, v45, v22
	v_fma_f32 v59, v54, v22, v26
	v_mul_f32_e64 v72, v55, v22
	v_fma_f32 v73, v56, v22, v26
	v_fma_f32 v25, -v136, v136, v25
	v_fma_f32 v29, -v136, v137, v29
	v_fma_f32 v58, -v136, v138, v58
	v_fma_f32 v59, -v137, v137, v59
	v_fma_f32 v72, -v137, v138, v72
	v_fma_f32 v73, -v138, v138, v73
	v_mul_f32_e64 v114, v72, v72
	v_mul_f32_e64 v115, v29, v73
	v_mul_f32_e64 v134, v58, v59
	v_mul_f32_e64 v135, v58, v58
	v_mul_f32_e64 v140, v25, v72
	v_mul_f32_e64 v141, v29, v29
	v_fma_f32 v114, v59, v73, -v114
	v_fma_f32 v115, v58, v72, -v115
	v_fma_f32 v134, v29, v72, -v134
	v_fma_f32 v135, v25, v73, -v135
	v_fma_f32 v140, v29, v58, -v140
	v_fma_f32 v141, v25, v59, -v141
	v_mul_f32_e64 v152, v25, v114
	v_fma_f32 v152, v29, v115, v152
	v_fma_f32 v152, v58, v134, v152
	v_rcp_f32_e32 v152, v152
	v_cmp_ne_u32_e64 vcc, s37, v3
	v_mul_f32_e64 v152, v152, v22
	v_cndmask_b32_e64 v152, 0, v152, s[30:31]
	v_cndmask_b32_e64 v25, 0, v18, vcc
	v_cndmask_b32_e64 v149, 0, v22, s[30:31]
	v_mul_f32_e64 v139, v114, v152
	v_mul_f32_e64 v144, v115, v152
	v_mul_f32_e64 v145, v134, v152
	v_mul_f32_e64 v146, v135, v152
	v_mul_f32_e64 v147, v140, v152
	v_mul_f32_e64 v148, v141, v152
	v_add_f32_e64 v150, v57, v25
	v_mov_b32_e32 v151, v3
	ds_write_b128 v23, v[136:139] offset:3072
	ds_write_b128 v23, v[144:147] offset:4096
	ds_write_b128 v23, v[148:151] offset:5120
	v_mov_b32_dpp v44, v46 wave_shr:1 row_mask:0xf bank_mask:0xf bound_ctrl:1
	v_mov_b32_dpp v45, v47 wave_shr:1 row_mask:0xf bank_mask:0xf bound_ctrl:1
	v_mov_b32_dpp v48, v46 wave_shl:1 row_mask:0xf bank_mask:0xf bound_ctrl:1
	v_mov_b32_dpp v49, v47 wave_shl:1 row_mask:0xf bank_mask:0xf bound_ctrl:1
	v_pk_mul_f32 v[54:55], v[46:47], v[76:77] op_sel_hi:[1,0]
	v_pk_mul_f32 v[58:59], v[46:47], v[76:77] op_sel:[0,1]
	v_pk_mul_f32 v[114:115], v[46:47], v[78:79] op_sel_hi:[1,0]
	v_pk_add_f32 v[134:135], v[46:47], v[44:45]
	v_pk_fma_f32 v[54:55], v[44:45], v[36:37], v[54:55] op_sel_hi:[1,0,1]
	v_pk_fma_f32 v[58:59], v[44:45], v[36:37], v[58:59] op_sel:[0,1,0]
	v_pk_fma_f32 v[114:115], v[44:45], v[38:39], v[114:115] op_sel_hi:[1,0,1]
	v_pk_add_f32 v[134:135], v[134:135], v[48:49]
	v_pk_fma_f32 v[54:55], v[48:49], v[40:41], v[54:55] op_sel_hi:[1,0,1]
	v_pk_fma_f32 v[58:59], v[48:49], v[40:41], v[58:59] op_sel:[0,1,0]
	v_pk_fma_f32 v[114:115], v[48:49], v[42:43], v[114:115] op_sel_hi:[1,0,1]
	s_waitcnt lgkmcnt(0)
	s_barrier
	v_pk_add_f32 v[44:45], v[74:75], v[134:135]
	v_pk_add_f32 v[74:75], v[94:95], v[54:55]
	v_pk_add_f32 v[94:95], v[50:51], v[58:59]
	v_pk_add_f32 v[50:51], v[62:63], v[114:115]
	v_pk_fma_f32 v[74:75], v[136:137], v[44:45], v[74:75] op_sel_hi:[0,1,1] neg_lo:[1,0,0] neg_hi:[1,0,0]
	v_pk_fma_f32 v[94:95], v[136:137], v[44:45], v[94:95] op_sel:[1,0,0] neg_lo:[1,0,0] neg_hi:[1,0,0]
	v_pk_fma_f32 v[50:51], v[138:139], v[44:45], v[50:51] op_sel_hi:[0,1,1] neg_lo:[1,0,0] neg_hi:[1,0,0]
	v_pk_mul_f32 v[48:49], v[138:139], v[74:75] op_sel:[1,0]
	v_pk_mul_f32 v[56:57], v[144:145], v[74:75] op_sel_hi:[0,1]
	v_pk_mul_f32 v[64:65], v[144:145], v[74:75] op_sel:[1,0]
	v_pk_fma_f32 v[48:49], v[144:145], v[94:95], v[48:49] op_sel_hi:[0,1,1]
	v_pk_fma_f32 v[56:57], v[146:147], v[94:95], v[56:57] op_sel_hi:[0,1,1]
	v_pk_fma_f32 v[64:65], v[146:147], v[94:95], v[64:65] op_sel:[1,0,0]
	v_pk_fma_f32 v[48:49], v[144:145], v[50:51], v[48:49] op_sel:[1,0,0]
	v_pk_fma_f32 v[56:57], v[146:147], v[50:51], v[56:57] op_sel:[1,0,0]
	v_pk_fma_f32 v[64:65], v[148:149], v[50:51], v[64:65] op_sel_hi:[0,1,1]
	v_pk_mul_f32 v[62:63], v[136:137], v[48:49] op_sel_hi:[0,1]
	v_pk_fma_f32 v[62:63], v[136:137], v[56:57], v[62:63] op_sel:[1,0,0]
	v_pk_fma_f32 v[62:63], v[138:139], v[64:65], v[62:63] op_sel_hi:[0,1,1]
	v_pk_fma_f32 v[62:63], v[148:149], v[44:45], v[62:63] op_sel:[1,0,0] neg_lo:[0,0,1] neg_hi:[0,0,1]
	s_add_i32 s5, s34, 4
	s_min_i32 s5, s5, 0x200
	s_mul_i32 s6, s5, 0x804
	s_add_i32 s6, s6, s35
	s_add_i32 s7, s6, 0x505014
	s_add_i32 s8, s6, 0x606018
	s_mul_i32 s9, s5, 0x180c
	s_add_i32 s9, s9, s33
	s_add_i32 s4, s34, 5
	s_min_i32 s4, s4, 0x200
	s_mul_i32 s4, s4, 0x804
	s_add_i32 s4, s4, s38
	buffer_load_dword v3, v28, s[20:23], s4 offen nt
	buffer_load_dwordx3 v[12:14], v27, s[24:27], s9 offen nt
	buffer_load_dword v6, v28, s[16:19], s7 offen nt
	buffer_load_dword v7, v28, s[16:19], s8 offen nt
	s_waitcnt vmcnt(8)
	v_mov_b32_dpp v72, v100 wave_shr:1 row_mask:0xf bank_mask:0xf bound_ctrl:1
	v_mov_b32_dpp v73, v101 wave_shr:1 row_mask:0xf bank_mask:0xf bound_ctrl:1
	v_mov_b32_dpp v74, v102 wave_shr:1 row_mask:0xf bank_mask:0xf bound_ctrl:1
	v_mov_b32_dpp v80, v100 wave_shl:1 row_mask:0xf bank_mask:0xf bound_ctrl:1
	v_mov_b32_dpp v81, v101 wave_shl:1 row_mask:0xf bank_mask:0xf bound_ctrl:1
	v_mov_b32_dpp v82, v102 wave_shl:1 row_mask:0xf bank_mask:0xf bound_ctrl:1
	s_add_i32 s4, s34, 3
	s_cmpk_lt_u32 s4, 0x201
	s_cselect_b64 s[12:13], s[40:41], 0
	v_cmp_eq_u32_e64 s[14:15], s37, v17
	s_and_b64 s[14:15], s[14:15], s[12:13]
	v_cndmask_b32_e64 v25, 0, 1, s[14:15]
	v_mul_f32_e64 v44, v100, v100
	v_mul_f32_e64 v45, v100, v101
	v_or_b32_dpp v29, v25, v25 wave_shr:1 row_mask:0xf bank_mask:0xf bound_ctrl:1
	v_mul_f32_e64 v50, v100, v102
	v_or_b32_dpp v29, v25, v29 wave_shl:1 row_mask:0xf bank_mask:0xf bound_ctrl:1
	v_mul_f32_e64 v51, v101, v101
	v_mul_f32_e64 v84, v101, v102
	v_or_b32_dpp v30, v29, v29 wave_shr:1 row_mask:0xf bank_mask:0xf bound_ctrl:1
	v_mul_f32_e64 v85, v102, v102
	s_nop 0
	v_or_b32_dpp v30, v29, v30 wave_shl:1 row_mask:0xf bank_mask:0xf bound_ctrl:1
	v_or3_b32 v25, v30, v53, v70
	v_or3_b32 v25, v25, v71, v52
	s_add_i32 s4, s34, 0
	s_cmpk_lt_u32 s4, 0x1ff
	s_cselect_b64 s[12:13], s[42:43], 0
	v_cmp_ne_u32_e64 s[30:31], 0, v25
	s_and_b64 s[30:31], s[30:31], s[12:13]
	v_cndmask_b32_e64 v25, 0, 1.0, s[30:31]
	v_add_f32_e64 v86, v100, v72
	v_add_f32_e64 v87, v101, v73
	v_add_f32_e64 v94, v102, v74
	v_fma_f32 v44, v72, v72, v44
	v_fma_f32 v45, v72, v73, v45
	v_fma_f32 v50, v72, v74, v50
	v_fma_f32 v51, v73, v73, v51
	v_fma_f32 v84, v73, v74, v84
	v_fma_f32 v85, v74, v74, v85
	v_add_f32_dpp v141, v25, v25 wave_shr:1 row_mask:0xf bank_mask:0xf bound_ctrl:1
	v_add_f32_e64 v86, v86, v80
	v_add_f32_e64 v87, v87, v81
	v_add_f32_e64 v94, v94, v82
	v_fma_f32 v95, v80, v80, v44
	v_fma_f32 v136, v80, v81, v45
	v_fma_f32 v137, v80, v82, v50
	v_fma_f32 v138, v81, v81, v51
	v_fma_f32 v139, v81, v82, v84
	v_fma_f32 v140, v82, v82, v85
	v_add_f32_dpp v141, v25, v141 wave_shl:1 row_mask:0xf bank_mask:0xf bound_ctrl:1
	v_pk_add_f32 v[44:45], v[90:91], v[86:87]
	v_pk_add_f32 v[50:51], v[118:119], v[44:45]
	v_pk_add_f32 v[90:91], v[116:117], v[94:95]
	v_pk_add_f32 v[84:85], v[120:121], v[90:91]
	v_pk_add_f32 v[116:117], v[128:129], v[136:137]
	v_pk_add_f32 v[118:119], v[122:123], v[116:117]
	v_pk_add_f32 v[122:123], v[130:131], v[138:139]
	v_pk_add_f32 v[120:121], v[124:125], v[122:123]
	v_pk_add_f32 v[124:125], v[132:133], v[140:141]
	v_pk_add_f32 v[128:129], v[126:127], v[124:125]
	v_mul_f32_e64 v144, v50, v22
	v_mul_f32_e64 v145, v51, v22
	v_mul_f32_e64 v146, v84, v22
	v_fma_f32 v25, v85, v22, v26
	v_mul_f32_e64 v29, v118, v22
	v_mul_f32_e64 v126, v119, v22
	v_fma_f32 v127, v120, v22, v26
	v_mul_f32_e64 v130, v121, v22
	v_fma_f32 v131, v128, v22, v26
	v_fma_f32 v25, -v144, v144, v25
	v_fma_f32 v29, -v144, v145, v29
	v_fma_f32 v126, -v144, v146, v126
	v_fma_f32 v127, -v145, v145, v127
	v_fma_f32 v130, -v145, v146, v130
	v_fma_f32 v131, -v146, v146, v131
	v_mul_f32_e64 v132, v130, v130
	v_mul_f32_e64 v133, v29, v131
	v_mul_f32_e64 v156, v126, v127
	v_mul_f32_e64 v157, v126, v126
	v_mul_f32_e64 v158, v25, v130
	v_mul_f32_e64 v159, v29, v29
	v_fma_f32 v132, v127, v131, -v132
	v_fma_f32 v133, v126, v130, -v133
	v_fma_f32 v156, v29, v130, -v156
	v_fma_f32 v157, v25, v131, -v157
	v_fma_f32 v158, v29, v126, -v158
	v_fma_f32 v159, v25, v127, -v159
	v_mul_f32_e64 v160, v25, v132
	v_fma_f32 v160, v29, v133, v160
	v_fma_f32 v160, v126, v156, v160
	v_rcp_f32_e32 v160, v160
	v_cmp_ne_u32_e64 vcc, s37, v16
	v_mul_f32_e64 v160, v160, v22
	v_cndmask_b32_e64 v160, 0, v160, s[30:31]
	v_cndmask_b32_e64 v25, 0, v18, vcc
	v_cndmask_b32_e64 v153, 0, v22, s[30:31]
	v_mul_f32_e64 v147, v132, v160
	v_mul_f32_e64 v148, v133, v160
	v_mul_f32_e64 v149, v156, v160
	v_mul_f32_e64 v150, v157, v160
	v_mul_f32_e64 v151, v158, v160
	v_mul_f32_e64 v152, v159, v160
	v_add_f32_e64 v154, v129, v25
	v_mov_b32_e32 v155, v16
	ds_write_b128 v23, v[144:147]
	ds_write_b128 v23, v[148:151] offset:1024
	ds_write_b128 v23, v[152:155] offset:2048
	v_mov_b32_dpp v50, v96 wave_shr:1 row_mask:0xf bank_mask:0xf bound_ctrl:1
	v_mov_b32_dpp v51, v97 wave_shr:1 row_mask:0xf bank_mask:0xf bound_ctrl:1
	v_mov_b32_dpp v118, v96 wave_shl:1 row_mask:0xf bank_mask:0xf bound_ctrl:1
	v_mov_b32_dpp v119, v97 wave_shl:1 row_mask:0xf bank_mask:0xf bound_ctrl:1
	v_pk_mul_f32 v[84:85], v[96:97], v[100:101] op_sel_hi:[1,0]
	v_pk_mul_f32 v[120:121], v[96:97], v[100:101] op_sel:[0,1]
	v_pk_mul_f32 v[128:129], v[96:97], v[102:103] op_sel_hi:[1,0]
	v_pk_add_f32 v[132:133], v[96:97], v[50:51]
	v_pk_fma_f32 v[84:85], v[50:51], v[72:73], v[84:85] op_sel_hi:[1,0,1]
	v_pk_fma_f32 v[120:121], v[50:51], v[72:73], v[120:121] op_sel:[0,1,0]
	v_pk_fma_f32 v[128:129], v[50:51], v[74:75], v[128:129] op_sel_hi:[1,0,1]
	v_pk_add_f32 v[132:133], v[132:133], v[118:119]
	v_pk_fma_f32 v[84:85], v[118:119], v[80:81], v[84:85] op_sel_hi:[1,0,1]
	v_pk_fma_f32 v[120:121], v[118:119], v[80:81], v[120:121] op_sel:[0,1,0]
	v_pk_fma_f32 v[128:129], v[118:119], v[82:83], v[128:129] op_sel_hi:[1,0,1]
	s_waitcnt lgkmcnt(0)
	s_barrier
	v_pk_add_f32 v[50:51], v[134:135], v[132:133]
	v_pk_add_f32 v[118:119], v[112:113], v[50:51]
	v_pk_add_f32 v[126:127], v[54:55], v[84:85]
	v_pk_add_f32 v[112:113], v[60:61], v[126:127]
	v_pk_add_f32 v[54:55], v[58:59], v[120:121]
	v_pk_add_f32 v[60:61], v[88:89], v[54:55]
	v_pk_add_f32 v[58:59], v[114:115], v[128:129]
	v_pk_add_f32 v[88:89], v[92:93], v[58:59]
	v_pk_fma_f32 v[112:113], v[144:145], v[118:119], v[112:113] op_sel_hi:[0,1,1] neg_lo:[1,0,0] neg_hi:[1,0,0]
	v_pk_fma_f32 v[60:61], v[144:145], v[118:119], v[60:61] op_sel:[1,0,0] neg_lo:[1,0,0] neg_hi:[1,0,0]
	v_pk_fma_f32 v[88:89], v[146:147], v[118:119], v[88:89] op_sel_hi:[0,1,1] neg_lo:[1,0,0] neg_hi:[1,0,0]
	v_pk_mul_f32 v[114:115], v[146:147], v[112:113] op_sel:[1,0]
	v_pk_mul_f32 v[130:131], v[148:149], v[112:113] op_sel_hi:[0,1]
	v_pk_mul_f32 v[134:135], v[148:149], v[112:113] op_sel:[1,0]
	v_pk_fma_f32 v[114:115], v[148:149], v[60:61], v[114:115] op_sel_hi:[0,1,1]
	v_pk_fma_f32 v[130:131], v[150:151], v[60:61], v[130:131] op_sel_hi:[0,1,1]
	v_pk_fma_f32 v[134:135], v[150:151], v[60:61], v[134:135] op_sel:[1,0,0]
	v_pk_fma_f32 v[114:115], v[148:149], v[88:89], v[114:115] op_sel:[1,0,0]
	v_pk_fma_f32 v[130:131], v[150:151], v[88:89], v[130:131] op_sel:[1,0,0]
	v_pk_fma_f32 v[134:135], v[152:153], v[88:89], v[134:135] op_sel_hi:[0,1,1]
	v_pk_mul_f32 v[92:93], v[144:145], v[114:115] op_sel_hi:[0,1]
	v_pk_fma_f32 v[92:93], v[144:145], v[130:131], v[92:93] op_sel:[1,0,0]
	v_pk_fma_f32 v[92:93], v[146:147], v[134:135], v[92:93] op_sel_hi:[0,1,1]
	v_pk_fma_f32 v[92:93], v[152:153], v[118:119], v[92:93] op_sel:[1,0,0] neg_lo:[0,0,1] neg_hi:[0,0,1]
	v_cmp_eq_u32_e64 s[10:11], 6, v155
	v_cmp_eq_u32_e64 s[14:15], 7, v155
	v_pk_add_f32 v[60:61], v[48:49], v[114:115]
	v_pk_add_f32 v[88:89], v[66:67], v[60:61]
	v_pk_add_f32 v[48:49], v[56:57], v[130:131]
	v_pk_add_f32 v[66:67], v[98:99], v[48:49]
	v_pk_add_f32 v[56:57], v[64:65], v[134:135]
	v_pk_add_f32 v[98:99], v[142:143], v[56:57]
	v_pk_add_f32 v[118:119], v[62:63], v[92:93]
	v_pk_add_f32 v[64:65], v[68:69], v[118:119]
	v_pk_fma_f32 v[68:69], v[104:105], v[88:89], v[64:65] op_sel_hi:[0,1,1]
	v_pk_fma_f32 v[112:113], v[108:109], v[88:89], v[64:65] op_sel_hi:[0,1,1]
	v_pk_fma_f32 v[68:69], v[104:105], v[66:67], v[68:69] op_sel:[1,0,0]
	v_pk_fma_f32 v[112:113], v[108:109], v[66:67], v[112:113] op_sel:[1,0,0]
	v_pk_fma_f32 v[68:69], v[106:107], v[98:99], v[68:69] op_sel_hi:[0,1,1]
	v_pk_fma_f32 v[112:113], v[110:111], v[98:99], v[112:113] op_sel_hi:[0,1,1]
	v_pk_fma_f32 v[64:65], v[32:33], v[88:89], v[64:65] op_sel_hi:[0,1,1]
	v_pk_fma_f32 v[64:65], v[32:33], v[66:67], v[64:65] op_sel:[1,0,0]
	v_pk_fma_f32 v[64:65], v[34:35], v[98:99], v[64:65] op_sel_hi:[0,1,1]
	v_cndmask_b32_e64 v62, 0, v18, s[10:11]
	v_cndmask_b32_e64 v63, 0, v18, s[14:15]
	v_add_f32_dpp v64, v68, v64 wave_shl:1 row_mask:0xf bank_mask:0xf bound_ctrl:1
	v_add_f32_dpp v65, v69, v65 wave_shl:1 row_mask:0xf bank_mask:0xf bound_ctrl:1
	s_add_i32 s4, s34, 0
	s_cmpk_lt_i32 s4, 0x201
	s_cselect_b64 s[12:13], s[0:1], 0
	v_add_f32_dpp v64, v112, v64 wave_shr:1 row_mask:0xf bank_mask:0xf bound_ctrl:1
	v_add_f32_dpp v65, v113, v65 wave_shr:1 row_mask:0xf bank_mask:0xf bound_ctrl:1
	v_pk_fma_f32 v[64:65], v[20:21], v[154:155], v[64:65] op_sel_hi:[1,0,1] neg_lo:[0,0,1] neg_hi:[0,0,1]
	v_pk_add_f32 v[64:65], v[64:65], v[62:63] neg_lo:[0,1] neg_hi:[0,1]
	v_pk_mul_f32 v[142:143], v[64:65], v[64:65]
	v_add_f32_e32 v142, v142, v143
	v_cndmask_b32_e64 v143, 0, v142, s[12:13]
	v_add_f32_e32 v1, v1, v143
	s_add_i32 s5, s34, 5
	s_min_i32 s5, s5, 0x200
	s_mul_i32 s6, s5, 0x804
	s_add_i32 s6, s6, s35
	s_add_i32 s7, s6, 0x505014
	s_add_i32 s8, s6, 0x606018
	s_mul_i32 s9, s5, 0x180c
	s_add_i32 s9, s9, s33
	s_add_i32 s4, s34, 6
	s_min_i32 s4, s4, 0x200
	s_mul_i32 s4, s4, 0x804
	s_add_i32 s4, s4, s38
	buffer_load_dword v16, v28, s[20:23], s4 offen nt
	buffer_load_dwordx3 v[32:34], v27, s[24:27], s9 offen nt
	buffer_load_dword v20, v28, s[16:19], s7 offen nt
	buffer_load_dword v21, v28, s[16:19], s8 offen nt
	s_waitcnt vmcnt(8)
	v_mov_b32_dpp v64, v8 wave_shr:1 row_mask:0xf bank_mask:0xf bound_ctrl:1
	v_mov_b32_dpp v65, v9 wave_shr:1 row_mask:0xf bank_mask:0xf bound_ctrl:1
	v_mov_b32_dpp v66, v10 wave_shr:1 row_mask:0xf bank_mask:0xf bound_ctrl:1
	v_mov_b32_dpp v104, v8 wave_shl:1 row_mask:0xf bank_mask:0xf bound_ctrl:1
	v_mov_b32_dpp v105, v9 wave_shl:1 row_mask:0xf bank_mask:0xf bound_ctrl:1
	v_mov_b32_dpp v106, v10 wave_shl:1 row_mask:0xf bank_mask:0xf bound_ctrl:1
	s_add_i32 s4, s34, 4
	s_cmpk_lt_u32 s4, 0x201
	s_cselect_b64 s[12:13], s[40:41], 0
	v_cmp_eq_u32_e64 s[14:15], s37, v2
	s_and_b64 s[14:15], s[14:15], s[12:13]
	v_cndmask_b32_e64 v25, 0, 1, s[14:15]
	v_mul_f32_e64 v62, v8, v8
	v_mul_f32_e64 v63, v8, v9
	v_or_b32_dpp v29, v25, v25 wave_shr:1 row_mask:0xf bank_mask:0xf bound_ctrl:1
	v_mul_f32_e64 v68, v8, v10
	v_or_b32_dpp v29, v25, v29 wave_shl:1 row_mask:0xf bank_mask:0xf bound_ctrl:1
	v_mul_f32_e64 v69, v9, v9
	v_mul_f32_e64 v88, v9, v10
	v_or_b32_dpp v52, v29, v29 wave_shr:1 row_mask:0xf bank_mask:0xf bound_ctrl:1
	v_mul_f32_e64 v89, v10, v10
	s_nop 0
	v_or_b32_dpp v52, v29, v52 wave_shl:1 row_mask:0xf bank_mask:0xf bound_ctrl:1
	v_or3_b32 v25, v52, v30, v53
	v_or3_b32 v25, v25, v70, v71
	s_add_i32 s4, s34, 1
	s_cmpk_lt_u32 s4, 0x1ff
	s_cselect_b64 s[12:13], s[42:43], 0
	v_cmp_ne_u32_e64 s[30:31], 0, v25
	s_and_b64 s[30:31], s[30:31], s[12:13]
	v_cndmask_b32_e64 v25, 0, 1.0, s[30:31]
	v_add_f32_e64 v98, v8, v64
	v_add_f32_e64 v99, v9, v65
	v_add_f32_e64 v108, v10, v66
	v_fma_f32 v62, v64, v64, v62
	v_fma_f32 v63, v64, v65, v63
	v_fma_f32 v68, v64, v66, v68
	v_fma_f32 v69, v65, v65, v69
	v_fma_f32 v88, v65, v66, v88
	v_fma_f32 v89, v66, v66, v89
	v_add_f32_dpp v143, v25, v25 wave_shr:1 row_mask:0xf bank_mask:0xf bound_ctrl:1
	v_add_f32_e64 v98, v98, v104
	v_add_f32_e64 v99, v99, v105
	v_add_f32_e64 v108, v108, v106
	v_fma_f32 v109, v104, v104, v62
	v_fma_f32 v110, v104, v105, v63
	v_fma_f32 v111, v104, v106, v68
	v_fma_f32 v112, v105, v105, v69
	v_fma_f32 v113, v105, v106, v88
	v_fma_f32 v142, v106, v106, v89
	v_add_f32_dpp v143, v25, v143 wave_shl:1 row_mask:0xf bank_mask:0xf bound_ctrl:1
	v_pk_add_f32 v[62:63], v[44:45], v[98:99]
	v_pk_add_f32 v[44:45], v[90:91], v[108:109]
	v_pk_add_f32 v[68:69], v[116:117], v[110:111]
	v_pk_add_f32 v[88:89], v[122:123], v[112:113]
	v_pk_add_f32 v[90:91], v[124:125], v[142:143]
	v_mul_f32_e64 v144, v62, v22
	v_mul_f32_e64 v145, v63, v22
	v_mul_f32_e64 v146, v44, v22
	v_fma_f32 v25, v45, v22, v26
	v_mul_f32_e64 v29, v68, v22
	v_mul_f32_e64 v116, v69, v22
	v_fma_f32 v117, v88, v22, v26
	v_mul_f32_e64 v122, v89, v22
	v_fma_f32 v123, v90, v22, v26
	v_fma_f32 v25, -v144, v144, v25
	v_fma_f32 v29, -v144, v145, v29
	v_fma_f32 v116, -v144, v146, v116
	v_fma_f32 v117, -v145, v145, v117
	v_fma_f32 v122, -v145, v146, v122
	v_fma_f32 v123, -v146, v146, v123
	v_mul_f32_e64 v124, v122, v122
	v_mul_f32_e64 v125, v29, v123
	v_mul_f32_e64 v156, v116, v117
	v_mul_f32_e64 v157, v116, v116
	v_mul_f32_e64 v158, v25, v122
	v_mul_f32_e64 v159, v29, v29
	v_fma_f32 v124, v117, v123, -v124
	v_fma_f32 v125, v116, v122, -v125
	v_fma_f32 v156, v29, v122, -v156
	v_fma_f32 v157, v25, v123, -v157
	v_fma_f32 v158, v29, v116, -v158
	v_fma_f32 v159, v25, v117, -v159
	v_mul_f32_e64 v160, v25, v124
	v_fma_f32 v160, v29, v125, v160
	v_fma_f32 v160, v116, v156, v160
	v_rcp_f32_e32 v160, v160
	v_cmp_ne_u32_e64 vcc, s37, v31
	v_mul_f32_e64 v160, v160, v22
	v_cndmask_b32_e64 v160, 0, v160, s[30:31]
	v_cndmask_b32_e64 v25, 0, v18, vcc
	v_cndmask_b32_e64 v153, 0, v22, s[30:31]
	v_mul_f32_e64 v147, v124, v160
	v_mul_f32_e64 v148, v125, v160
	v_mul_f32_e64 v149, v156, v160
	v_mul_f32_e64 v150, v157, v160
	v_mul_f32_e64 v151, v158, v160
	v_mul_f32_e64 v152, v159, v160
	v_add_f32_e64 v154, v91, v25
	v_mov_b32_e32 v155, v31
	ds_write_b128 v23, v[144:147] offset:3072
	ds_write_b128 v23, v[148:151] offset:4096
	ds_write_b128 v23, v[152:155] offset:5120
	v_mov_b32_dpp v62, v4 wave_shr:1 row_mask:0xf bank_mask:0xf bound_ctrl:1
	v_mov_b32_dpp v63, v5 wave_shr:1 row_mask:0xf bank_mask:0xf bound_ctrl:1
	v_mov_b32_dpp v90, v4 wave_shl:1 row_mask:0xf bank_mask:0xf bound_ctrl:1
	v_mov_b32_dpp v91, v5 wave_shl:1 row_mask:0xf bank_mask:0xf bound_ctrl:1
	v_pk_mul_f32 v[44:45], v[4:5], v[8:9] op_sel_hi:[1,0]
	v_pk_mul_f32 v[68:69], v[4:5], v[8:9] op_sel:[0,1]
	v_pk_mul_f32 v[88:89], v[4:5], v[10:11] op_sel_hi:[1,0]
	v_pk_add_f32 v[116:117], v[4:5], v[62:63]
	v_pk_fma_f32 v[44:45], v[62:63], v[64:65], v[44:45] op_sel_hi:[1,0,1]
	v_pk_fma_f32 v[68:69], v[62:63], v[64:65], v[68:69] op_sel:[0,1,0]
	v_pk_fma_f32 v[88:89], v[62:63], v[66:67], v[88:89] op_sel_hi:[1,0,1]
	v_pk_add_f32 v[116:117], v[116:117], v[90:91]
	v_pk_fma_f32 v[44:45], v[90:91], v[104:105], v[44:45] op_sel_hi:[1,0,1]
	v_pk_fma_f32 v[68:69], v[90:91], v[104:105], v[68:69] op_sel:[0,1,0]
	v_pk_fma_f32 v[88:89], v[90:91], v[106:107], v[88:89] op_sel_hi:[1,0,1]
	s_waitcnt lgkmcnt(0)
	s_barrier
	v_pk_add_f32 v[62:63], v[50:51], v[116:117]
	v_pk_add_f32 v[124:125], v[126:127], v[44:45]
	v_pk_add_f32 v[156:157], v[54:55], v[68:69]
	v_pk_add_f32 v[160:161], v[58:59], v[88:89]
	v_pk_fma_f32 v[124:125], v[144:145], v[62:63], v[124:125] op_sel_hi:[0,1,1] neg_lo:[1,0,0] neg_hi:[1,0,0]
	v_pk_fma_f32 v[156:157], v[144:145], v[62:63], v[156:157] op_sel:[1,0,0] neg_lo:[1,0,0] neg_hi:[1,0,0]
	v_pk_fma_f32 v[160:161], v[146:147], v[62:63], v[160:161] op_sel_hi:[0,1,1] neg_lo:[1,0,0] neg_hi:[1,0,0]
	v_pk_mul_f32 v[50:51], v[146:147], v[124:125] op_sel:[1,0]
	v_pk_mul_f32 v[54:55], v[148:149], v[124:125] op_sel_hi:[0,1]
	v_pk_mul_f32 v[58:59], v[148:149], v[124:125] op_sel:[1,0]
	v_pk_fma_f32 v[50:51], v[148:149], v[156:157], v[50:51] op_sel_hi:[0,1,1]
	v_pk_fma_f32 v[54:55], v[150:151], v[156:157], v[54:55] op_sel_hi:[0,1,1]
	v_pk_fma_f32 v[58:59], v[150:151], v[156:157], v[58:59] op_sel:[1,0,0]
	v_pk_fma_f32 v[50:51], v[148:149], v[160:161], v[50:51] op_sel:[1,0,0]
	v_pk_fma_f32 v[54:55], v[150:151], v[160:161], v[54:55] op_sel:[1,0,0]
	v_pk_fma_f32 v[58:59], v[152:153], v[160:161], v[58:59] op_sel_hi:[0,1,1]
	v_pk_mul_f32 v[164:165], v[144:145], v[50:51] op_sel_hi:[0,1]
	v_pk_fma_f32 v[164:165], v[144:145], v[54:55], v[164:165] op_sel:[1,0,0]
	v_pk_fma_f32 v[164:165], v[146:147], v[58:59], v[164:165] op_sel_hi:[0,1,1]
	v_pk_fma_f32 v[164:165], v[152:153], v[62:63], v[164:165] op_sel:[1,0,0] neg_lo:[0,0,1] neg_hi:[0,0,1]
	v_cmp_eq_u32_e64 s[10:11], 6, v155
	v_cmp_eq_u32_e64 s[14:15], 7, v155
	v_pk_add_f32 v[62:63], v[60:61], v[50:51]
	v_pk_add_f32 v[60:61], v[48:49], v[54:55]
	v_pk_add_f32 v[48:49], v[56:57], v[58:59]
	v_pk_add_f32 v[90:91], v[118:119], v[164:165]
	v_pk_fma_f32 v[118:119], v[36:37], v[62:63], v[90:91] op_sel_hi:[0,1,1]
	v_pk_fma_f32 v[122:123], v[40:41], v[62:63], v[90:91] op_sel_hi:[0,1,1]
	v_pk_fma_f32 v[118:119], v[36:37], v[60:61], v[118:119] op_sel:[1,0,0]
	v_pk_fma_f32 v[122:123], v[40:41], v[60:61], v[122:123] op_sel:[1,0,0]
	v_pk_fma_f32 v[118:119], v[38:39], v[48:49], v[118:119] op_sel_hi:[0,1,1]
	v_pk_fma_f32 v[122:123], v[42:43], v[48:49], v[122:123] op_sel_hi:[0,1,1]
	v_pk_fma_f32 v[90:91], v[76:77], v[62:63], v[90:91] op_sel_hi:[0,1,1]
	v_pk_fma_f32 v[90:91], v[76:77], v[60:61], v[90:91] op_sel:[1,0,0]
	v_pk_fma_f32 v[90:91], v[78:79], v[48:49], v[90:91] op_sel_hi:[0,1,1]
	v_cndmask_b32_e64 v56, 0, v18, s[10:11]
	v_cndmask_b32_e64 v57, 0, v18, s[14:15]
	v_add_f32_dpp v90, v118, v90 wave_shl:1 row_mask:0xf bank_mask:0xf bound_ctrl:1
	v_add_f32_dpp v91, v119, v91 wave_shl:1 row_mask:0xf bank_mask:0xf bound_ctrl:1
	s_add_i32 s4, s34, 1
	s_cmpk_lt_i32 s4, 0x201
	s_cselect_b64 s[12:13], s[0:1], 0
	v_add_f32_dpp v90, v122, v90 wave_shr:1 row_mask:0xf bank_mask:0xf bound_ctrl:1
	v_add_f32_dpp v91, v123, v91 wave_shr:1 row_mask:0xf bank_mask:0xf bound_ctrl:1
	v_pk_fma_f32 v[90:91], v[46:47], v[154:155], v[90:91] op_sel_hi:[1,0,1] neg_lo:[0,0,1] neg_hi:[0,0,1]
	v_pk_add_f32 v[90:91], v[90:91], v[56:57] neg_lo:[0,1] neg_hi:[0,1]
	v_pk_mul_f32 v[124:125], v[90:91], v[90:91]
	v_add_f32_e32 v124, v124, v125
	v_cndmask_b32_e64 v125, 0, v124, s[12:13]
	v_add_f32_e32 v1, v1, v125
	s_add_i32 s5, s34, 6
	s_min_i32 s5, s5, 0x200
	s_mul_i32 s6, s5, 0x804
	s_add_i32 s6, s6, s35
	s_add_i32 s7, s6, 0x505014
	s_add_i32 s8, s6, 0x606018
	s_mul_i32 s9, s5, 0x180c
	s_add_i32 s9, s9, s33
	s_add_i32 s4, s34, 7
	s_min_i32 s4, s4, 0x200
	s_mul_i32 s4, s4, 0x804
	s_add_i32 s4, s4, s38
	buffer_load_dword v25, v28, s[20:23], s4 offen nt
	buffer_load_dwordx3 v[40:42], v27, s[24:27], s9 offen nt
	buffer_load_dword v36, v28, s[16:19], s7 offen nt
	buffer_load_dword v37, v28, s[16:19], s8 offen nt
	s_waitcnt vmcnt(8)
	v_mov_b32_dpp v60, v12 wave_shr:1 row_mask:0xf bank_mask:0xf bound_ctrl:1
	v_mov_b32_dpp v61, v13 wave_shr:1 row_mask:0xf bank_mask:0xf bound_ctrl:1
	v_mov_b32_dpp v62, v14 wave_shr:1 row_mask:0xf bank_mask:0xf bound_ctrl:1
	v_mov_b32_dpp v76, v12 wave_shl:1 row_mask:0xf bank_mask:0xf bound_ctrl:1
	v_mov_b32_dpp v77, v13 wave_shl:1 row_mask:0xf bank_mask:0xf bound_ctrl:1
	v_mov_b32_dpp v78, v14 wave_shl:1 row_mask:0xf bank_mask:0xf bound_ctrl:1
	s_add_i32 s4, s34, 5
	s_cmpk_lt_u32 s4, 0x201
	s_cselect_b64 s[12:13], s[40:41], 0
	v_cmp_eq_u32_e64 s[14:15], s37, v3
	s_and_b64 s[14:15], s[14:15], s[12:13]
	v_cndmask_b32_e64 v29, 0, 1, s[14:15]
	v_mul_f32_e64 v38, v12, v12
	v_mul_f32_e64 v39, v12, v13
	v_or_b32_dpp v31, v29, v29 wave_shr:1 row_mask:0xf bank_mask:0xf bound_ctrl:1
	v_mul_f32_e64 v46, v12, v14
	v_or_b32_dpp v31, v29, v31 wave_shl:1 row_mask:0xf bank_mask:0xf bound_ctrl:1
	v_mul_f32_e64 v47, v13, v13
	v_mul_f32_e64 v48, v13, v14
	v_or_b32_dpp v71, v31, v31 wave_shr:1 row_mask:0xf bank_mask:0xf bound_ctrl:1
	v_mul_f32_e64 v49, v14, v14
	s_nop 0
	v_or_b32_dpp v71, v31, v71 wave_shl:1 row_mask:0xf bank_mask:0xf bound_ctrl:1
	v_or3_b32 v29, v71, v52, v30
	v_or3_b32 v29, v29, v53, v70
	s_add_i32 s4, s34, 2
	s_cmpk_lt_u32 s4, 0x1ff
	s_cselect_b64 s[12:13], s[42:43], 0
	v_cmp_ne_u32_e64 s[30:31], 0, v29
	s_and_b64 s[30:31], s[30:31], s[12:13]
	v_cndmask_b32_e64 v29, 0, 1.0, s[30:31]
	v_add_f32_e64 v56, v12, v60
	v_add_f32_e64 v57, v13, v61
	v_add_f32_e64 v90, v14, v62
	v_fma_f32 v38, v60, v60, v38
	v_fma_f32 v39, v60, v61, v39
	v_fma_f32 v46, v60, v62, v46
	v_fma_f32 v47, v61, v61, v47
	v_fma_f32 v48, v61, v62, v48
	v_fma_f32 v49, v62, v62, v49
	v_add_f32_dpp v125, v29, v29 wave_shr:1 row_mask:0xf bank_mask:0xf bound_ctrl:1
	v_add_f32_e64 v56, v56, v76
	v_add_f32_e64 v57, v57, v77
	v_add_f32_e64 v90, v90, v78
	v_fma_f32 v91, v76, v76, v38
	v_fma_f32 v118, v76, v77, v39
	v_fma_f32 v119, v76, v78, v46
	v_fma_f32 v122, v77, v77, v47
	v_fma_f32 v123, v77, v78, v48
	v_fma_f32 v124, v78, v78, v49
	v_add_f32_dpp v125, v29, v125 wave_shl:1 row_mask:0xf bank_mask:0xf bound_ctrl:1
	v_pk_add_f32 v[48:49], v[98:99], v[56:57]
	v_pk_add_f32 v[38:39], v[86:87], v[48:49]
	v_pk_add_f32 v[144:145], v[108:109], v[90:91]
	v_pk_add_f32 v[46:47], v[94:95], v[144:145]
	v_pk_add_f32 v[86:87], v[110:111], v[118:119]
	v_pk_add_f32 v[94:95], v[136:137], v[86:87]
	v_pk_add_f32 v[108:109], v[112:113], v[122:123]
	v_pk_add_f32 v[98:99], v[138:139], v[108:109]
	v_pk_add_f32 v[110:111], v[142:143], v[124:125]
	v_pk_add_f32 v[112:113], v[140:141], v[110:111]
	v_mul_f32_e64 v136, v38, v22
	v_mul_f32_e64 v137, v39, v22
	v_mul_f32_e64 v138, v46, v22
	v_fma_f32 v29, v47, v22, v26
	v_mul_f32_e64 v31, v94, v22
	v_mul_f32_e64 v126, v95, v22
	v_fma_f32 v127, v98, v22, v26
	v_mul_f32_e64 v146, v99, v22
	v_fma_f32 v147, v112, v22, v26
	v_fma_f32 v29, -v136, v136, v29
	v_fma_f32 v31, -v136, v137, v31
	v_fma_f32 v126, -v136, v138, v126
	v_fma_f32 v127, -v137, v137, v127
	v_fma_f32 v146, -v137, v138, v146
	v_fma_f32 v147, -v138, v138, v147
	v_mul_f32_e64 v152, v146, v146
	v_mul_f32_e64 v153, v31, v147
	v_mul_f32_e64 v154, v126, v127
	v_mul_f32_e64 v155, v126, v126
	v_mul_f32_e64 v156, v29, v146
	v_mul_f32_e64 v157, v31, v31
	v_fma_f32 v152, v127, v147, -v152
	v_fma_f32 v153, v126, v146, -v153
	v_fma_f32 v154, v31, v146, -v154
	v_fma_f32 v155, v29, v147, -v155
	v_fma_f32 v156, v31, v126, -v156
	v_fma_f32 v157, v29, v127, -v157
	v_mul_f32_e64 v158, v29, v152
	v_fma_f32 v158, v31, v153, v158
	v_fma_f32 v158, v126, v154, v158
	v_rcp_f32_e32 v158, v158
	v_cmp_ne_u32_e64 vcc, s37, v24
	v_mul_f32_e64 v158, v158, v22
	v_cndmask_b32_e64 v158, 0, v158, s[30:31]
	v_cndmask_b32_e64 v29, 0, v18, vcc
	v_cndmask_b32_e64 v149, 0, v22, s[30:31]
	v_mul_f32_e64 v139, v152, v158
	v_mul_f32_e64 v140, v153, v158
	v_mul_f32_e64 v141, v154, v158
	v_mul_f32_e64 v142, v155, v158
	v_mul_f32_e64 v143, v156, v158
	v_mul_f32_e64 v148, v157, v158
	v_add_f32_e64 v150, v113, v29
	v_mov_b32_e32 v151, v24
	ds_write_b128 v23, v[136:139]
	ds_write_b128 v23, v[140:143] offset:1024
	ds_write_b128 v23, v[148:151] offset:2048
	v_mov_b32_dpp v112, v6 wave_shr:1 row_mask:0xf bank_mask:0xf bound_ctrl:1
	v_mov_b32_dpp v113, v7 wave_shr:1 row_mask:0xf bank_mask:0xf bound_ctrl:1
	v_mov_b32_dpp v152, v6 wave_shl:1 row_mask:0xf bank_mask:0xf bound_ctrl:1
	v_mov_b32_dpp v153, v7 wave_shl:1 row_mask:0xf bank_mask:0xf bound_ctrl:1
	v_pk_mul_f32 v[38:39], v[6:7], v[12:13] op_sel_hi:[1,0]
	v_pk_mul_f32 v[46:47], v[6:7], v[12:13] op_sel:[0,1]
	v_pk_mul_f32 v[94:95], v[6:7], v[14:15] op_sel_hi:[1,0]
	v_pk_add_f32 v[98:99], v[6:7], v[112:113]
	v_pk_fma_f32 v[38:39], v[112:113], v[60:61], v[38:39] op_sel_hi:[1,0,1]
	v_pk_fma_f32 v[46:47], v[112:113], v[60:61], v[46:47] op_sel:[0,1,0]
	v_pk_fma_f32 v[94:95], v[112:113], v[62:63], v[94:95] op_sel_hi:[1,0,1]
	v_pk_add_f32 v[98:99], v[98:99], v[152:153]
	v_pk_fma_f32 v[38:39], v[152:153], v[76:77], v[38:39] op_sel_hi:[1,0,1]
	v_pk_fma_f32 v[46:47], v[152:153], v[76:77], v[46:47] op_sel:[0,1,0]
	v_pk_fma_f32 v[94:95], v[152:153], v[78:79], v[94:95] op_sel_hi:[1,0,1]
	s_waitcnt lgkmcnt(0)
	s_barrier
	v_pk_add_f32 v[126:127], v[116:117], v[98:99]
	v_pk_add_f32 v[112:113], v[132:133], v[126:127]
	v_pk_add_f32 v[146:147], v[44:45], v[38:39]
	v_pk_add_f32 v[154:155], v[84:85], v[146:147]
	v_pk_add_f32 v[158:159], v[68:69], v[46:47]
	v_pk_add_f32 v[162:163], v[120:121], v[158:159]
	v_pk_add_f32 v[166:167], v[88:89], v[94:95]
	v_pk_add_f32 v[170:171], v[128:129], v[166:167]
	v_pk_fma_f32 v[154:155], v[136:137], v[112:113], v[154:155] op_sel_hi:[0,1,1] neg_lo:[1,0,0] neg_hi:[1,0,0]
	v_pk_fma_f32 v[162:163], v[136:137], v[112:113], v[162:163] op_sel:[1,0,0] neg_lo:[1,0,0] neg_hi:[1,0,0]
	v_pk_fma_f32 v[170:171], v[138:139], v[112:113], v[170:171] op_sel_hi:[0,1,1] neg_lo:[1,0,0] neg_hi:[1,0,0]
	v_pk_mul_f32 v[44:45], v[138:139], v[154:155] op_sel:[1,0]
	v_pk_mul_f32 v[68:69], v[140:141], v[154:155] op_sel_hi:[0,1]
	v_pk_mul_f32 v[84:85], v[140:141], v[154:155] op_sel:[1,0]
	v_pk_fma_f32 v[44:45], v[140:141], v[162:163], v[44:45] op_sel_hi:[0,1,1]
	v_pk_fma_f32 v[68:69], v[142:143], v[162:163], v[68:69] op_sel_hi:[0,1,1]
	v_pk_fma_f32 v[84:85], v[142:143], v[162:163], v[84:85] op_sel:[1,0,0]
	v_pk_fma_f32 v[44:45], v[140:141], v[170:171], v[44:45] op_sel:[1,0,0]
	v_pk_fma_f32 v[68:69], v[142:143], v[170:171], v[68:69] op_sel:[1,0,0]
	v_pk_fma_f32 v[84:85], v[148:149], v[170:171], v[84:85] op_sel_hi:[0,1,1]
	v_pk_mul_f32 v[174:175], v[136:137], v[44:45] op_sel_hi:[0,1]
	v_pk_fma_f32 v[174:175], v[136:137], v[68:69], v[174:175] op_sel:[1,0,0]
	v_pk_fma_f32 v[174:175], v[138:139], v[84:85], v[174:175] op_sel_hi:[0,1,1]
	v_pk_fma_f32 v[174:175], v[148:149], v[112:113], v[174:175] op_sel:[1,0,0] neg_lo:[0,0,1] neg_hi:[0,0,1]
	v_cmp_eq_u32_e64 s[10:11], 6, v151
	v_cmp_eq_u32_e64 s[14:15], 7, v151
	v_pk_add_f32 v[88:89], v[50:51], v[44:45]
	v_pk_add_f32 v[112:113], v[114:115], v[88:89]
	v_pk_add_f32 v[116:117], v[54:55], v[68:69]
	v_pk_add_f32 v[50:51], v[130:131], v[116:117]
	v_pk_add_f32 v[120:121], v[58:59], v[84:85]
	v_pk_add_f32 v[54:55], v[134:135], v[120:121]
	v_pk_add_f32 v[58:59], v[164:165], v[174:175]
	v_pk_add_f32 v[128:129], v[92:93], v[58:59]
	v_pk_fma_f32 v[92:93], v[72:73], v[112:113], v[128:129] op_sel_hi:[0,1,1]
	v_pk_fma_f32 v[132:133], v[80:81], v[112:113], v[128:129] op_sel_hi:[0,1,1]
	v_pk_fma_f32 v[92:93], v[72:73], v[50:51], v[92:93] op_sel:[1,0,0]
	v_pk_fma_f32 v[132:133], v[80:81], v[50:51], v[132:133] op_sel:[1,0,0]
	v_pk_fma_f32 v[92:93], v[74:75], v[54:55], v[92:93] op_sel_hi:[0,1,1]
	v_pk_fma_f32 v[132:133], v[82:83], v[54:55], v[132:133] op_sel_hi:[0,1,1]
	v_pk_fma_f32 v[128:129], v[100:101], v[112:113], v[128:129] op_sel_hi:[0,1,1]
	v_pk_fma_f32 v[128:129], v[100:101], v[50:51], v[128:129] op_sel:[1,0,0]
	v_pk_fma_f32 v[128:129], v[102:103], v[54:55], v[128:129] op_sel_hi:[0,1,1]
	v_cndmask_b32_e64 v114, 0, v18, s[10:11]
	v_cndmask_b32_e64 v115, 0, v18, s[14:15]
	v_add_f32_dpp v128, v92, v128 wave_shl:1 row_mask:0xf bank_mask:0xf bound_ctrl:1
	v_add_f32_dpp v129, v93, v129 wave_shl:1 row_mask:0xf bank_mask:0xf bound_ctrl:1
	s_add_i32 s4, s34, 2
	s_cmpk_lt_i32 s4, 0x201
	s_cselect_b64 s[12:13], s[0:1], 0
	v_add_f32_dpp v128, v132, v128 wave_shr:1 row_mask:0xf bank_mask:0xf bound_ctrl:1
	v_add_f32_dpp v129, v133, v129 wave_shr:1 row_mask:0xf bank_mask:0xf bound_ctrl:1
	v_pk_fma_f32 v[128:129], v[96:97], v[150:151], v[128:129] op_sel_hi:[1,0,1] neg_lo:[0,0,1] neg_hi:[0,0,1]
	v_pk_add_f32 v[128:129], v[128:129], v[114:115] neg_lo:[0,1] neg_hi:[0,1]
	v_pk_mul_f32 v[130:131], v[128:129], v[128:129]
	v_add_f32_e32 v130, v130, v131
	v_cndmask_b32_e64 v131, 0, v130, s[12:13]
	v_add_f32_e32 v1, v1, v131
	s_add_i32 s5, s34, 7
	s_min_i32 s5, s5, 0x200
	s_mul_i32 s6, s5, 0x804
	s_add_i32 s6, s6, s35
	s_add_i32 s7, s6, 0x505014
	s_add_i32 s8, s6, 0x606018
	s_mul_i32 s9, s5, 0x180c
	s_add_i32 s9, s9, s33
	s_add_i32 s4, s34, 8
	s_min_i32 s4, s4, 0x200
	s_mul_i32 s4, s4, 0x804
	s_add_i32 s4, s4, s38
	buffer_load_dword v24, v28, s[20:23], s4 offen nt
	buffer_load_dwordx3 v[72:74], v27, s[24:27], s9 offen nt
	buffer_load_dword v50, v28, s[16:19], s7 offen nt
	buffer_load_dword v51, v28, s[16:19], s8 offen nt
	s_waitcnt vmcnt(8)
	v_mov_b32_dpp v80, v32 wave_shr:1 row_mask:0xf bank_mask:0xf bound_ctrl:1
	v_mov_b32_dpp v81, v33 wave_shr:1 row_mask:0xf bank_mask:0xf bound_ctrl:1
	v_mov_b32_dpp v82, v34 wave_shr:1 row_mask:0xf bank_mask:0xf bound_ctrl:1
	v_mov_b32_dpp v100, v32 wave_shl:1 row_mask:0xf bank_mask:0xf bound_ctrl:1
	v_mov_b32_dpp v101, v33 wave_shl:1 row_mask:0xf bank_mask:0xf bound_ctrl:1
	v_mov_b32_dpp v102, v34 wave_shl:1 row_mask:0xf bank_mask:0xf bound_ctrl:1
	s_add_i32 s4, s34, 6
	s_cmpk_lt_u32 s4, 0x201
	s_cselect_b64 s[12:13], s[40:41], 0
	v_cmp_eq_u32_e64 s[14:15], s37, v16
	s_and_b64 s[14:15], s[14:15], s[12:13]
	v_cndmask_b32_e64 v29, 0, 1, s[14:15]
	v_mul_f32_e64 v54, v32, v32
	v_mul_f32_e64 v55, v32, v33
	v_or_b32_dpp v31, v29, v29 wave_shr:1 row_mask:0xf bank_mask:0xf bound_ctrl:1
	v_mul_f32_e64 v92, v32, v34
	v_or_b32_dpp v31, v29, v31 wave_shl:1 row_mask:0xf bank_mask:0xf bound_ctrl:1
	v_mul_f32_e64 v93, v33, v33
	v_mul_f32_e64 v96, v33, v34
	v_or_b32_dpp v70, v31, v31 wave_shr:1 row_mask:0xf bank_mask:0xf bound_ctrl:1
	v_mul_f32_e64 v97, v34, v34
	s_nop 0
	v_or_b32_dpp v70, v31, v70 wave_shl:1 row_mask:0xf bank_mask:0xf bound_ctrl:1
	v_or3_b32 v29, v70, v71, v52
	v_or3_b32 v29, v29, v30, v53
	s_add_i32 s4, s34, 3
	s_cmpk_lt_u32 s4, 0x1ff
	s_cselect_b64 s[12:13], s[42:43], 0
	v_cmp_ne_u32_e64 s[30:31], 0, v29
	s_and_b64 s[30:31], s[30:31], s[12:13]
	v_cndmask_b32_e64 v29, 0, 1.0, s[30:31]
	v_add_f32_e64 v112, v32, v80
	v_add_f32_e64 v113, v33, v81
	v_add_f32_e64 v114, v34, v82
	v_fma_f32 v54, v80, v80, v54
	v_fma_f32 v55, v80, v81, v55
	v_fma_f32 v92, v80, v82, v92
	v_fma_f32 v93, v81, v81, v93
	v_fma_f32 v96, v81, v82, v96
	v_fma_f32 v97, v82, v82, v97
	v_add_f32_dpp v133, v29, v29 wave_shr:1 row_mask:0xf bank_mask:0xf bound_ctrl:1
	v_add_f32_e64 v112, v112, v100
	v_add_f32_e64 v113, v113, v101
	v_add_f32_e64 v114, v114, v102
	v_fma_f32 v115, v100, v100, v54
	v_fma_f32 v128, v100, v101, v55
	v_fma_f32 v129, v100, v102, v92
	v_fma_f32 v130, v101, v101, v93
	v_fma_f32 v131, v101, v102, v96
	v_fma_f32 v132, v102, v102, v97
	v_add_f32_dpp v133, v29, v133 wave_shl:1 row_mask:0xf bank_mask:0xf bound_ctrl:1
	v_pk_add_f32 v[54:55], v[48:49], v[112:113]
	v_pk_add_f32 v[48:49], v[144:145], v[114:115]
	v_pk_add_f32 v[92:93], v[86:87], v[128:129]
	v_pk_add_f32 v[86:87], v[108:109], v[130:131]
	v_pk_add_f32 v[96:97], v[110:111], v[132:133]
	v_mul_f32_e64 v108, v54, v22
	v_mul_f32_e64 v109, v55, v22
	v_mul_f32_e64 v110, v48, v22
	v_fma_f32 v29, v49, v22, v26
	v_mul_f32_e64 v31, v92, v22
	v_mul_f32_e64 v134, v93, v22
	v_fma_f32 v135, v86, v22, v26
	v_mul_f32_e64 v144, v87, v22
	v_fma_f32 v145, v96, v22, v26
	v_fma_f32 v29, -v108, v108, v29
	v_fma_f32 v31, -v108, v109, v31
	v_fma_f32 v134, -v108, v110, v134
	v_fma_f32 v135, -v109, v109, v135
	v_fma_f32 v144, -v109, v110, v144
	v_fma_f32 v145, -v110, v110, v145
	v_mul_f32_e64 v148, v144, v144
	v_mul_f32_e64 v149, v31, v145
	v_mul_f32_e64 v150, v134, v135
	v_mul_f32_e64 v151, v134, v134
	v_mul_f32_e64 v152, v29, v144
	v_mul_f32_e64 v153, v31, v31
	v_fma_f32 v148, v135, v145, -v148
	v_fma_f32 v149, v134, v144, -v149
	v_fma_f32 v150, v31, v144, -v150
	v_fma_f32 v151, v29, v145, -v151
	v_fma_f32 v152, v31, v134, -v152
	v_fma_f32 v153, v29, v135, -v153
	v_mul_f32_e64 v154, v29, v148
	v_fma_f32 v154, v31, v149, v154
	v_fma_f32 v154, v134, v150, v154
	v_rcp_f32_e32 v154, v154
	v_cmp_ne_u32_e64 vcc, s37, v17
	v_mul_f32_e64 v154, v154, v22
	v_cndmask_b32_e64 v154, 0, v154, s[30:31]
	v_cndmask_b32_e64 v29, 0, v18, vcc
	v_cndmask_b32_e64 v141, 0, v22, s[30:31]
	v_mul_f32_e64 v111, v148, v154
	v_mul_f32_e64 v136, v149, v154
	v_mul_f32_e64 v137, v150, v154
	v_mul_f32_e64 v138, v151, v154
	v_mul_f32_e64 v139, v152, v154
	v_mul_f32_e64 v140, v153, v154
	v_add_f32_e64 v142, v97, v29
	v_mov_b32_e32 v143, v17
	ds_write_b128 v23, v[108:111] offset:3072
	ds_write_b128 v23, v[136:139] offset:4096
	ds_write_b128 v23, v[140:143] offset:5120
	v_mov_b32_dpp v54, v20 wave_shr:1 row_mask:0xf bank_mask:0xf bound_ctrl:1
	v_mov_b32_dpp v55, v21 wave_shr:1 row_mask:0xf bank_mask:0xf bound_ctrl:1
	v_mov_b32_dpp v86, v20 wave_shl:1 row_mask:0xf bank_mask:0xf bound_ctrl:1
	v_mov_b32_dpp v87, v21 wave_shl:1 row_mask:0xf bank_mask:0xf bound_ctrl:1
	v_pk_mul_f32 v[48:49], v[20:21], v[32:33] op_sel_hi:[1,0]
	v_pk_mul_f32 v[92:93], v[20:21], v[32:33] op_sel:[0,1]
	v_pk_mul_f32 v[96:97], v[20:21], v[34:35] op_sel_hi:[1,0]
	v_pk_add_f32 v[144:145], v[20:21], v[54:55]
	v_pk_fma_f32 v[48:49], v[54:55], v[80:81], v[48:49] op_sel_hi:[1,0,1]
	v_pk_fma_f32 v[92:93], v[54:55], v[80:81], v[92:93] op_sel:[0,1,0]
	v_pk_fma_f32 v[96:97], v[54:55], v[82:83], v[96:97] op_sel_hi:[1,0,1]
	v_pk_add_f32 v[144:145], v[144:145], v[86:87]
	v_pk_fma_f32 v[48:49], v[86:87], v[100:101], v[48:49] op_sel_hi:[1,0,1]
	v_pk_fma_f32 v[92:93], v[86:87], v[100:101], v[92:93] op_sel:[0,1,0]
	v_pk_fma_f32 v[96:97], v[86:87], v[102:103], v[96:97] op_sel_hi:[1,0,1]
	s_waitcnt lgkmcnt(0)
	s_barrier
	v_pk_add_f32 v[54:55], v[126:127], v[144:145]
	v_pk_add_f32 v[148:149], v[146:147], v[48:49]
	v_pk_add_f32 v[152:153], v[158:159], v[92:93]
	v_pk_add_f32 v[156:157], v[166:167], v[96:97]
	v_pk_fma_f32 v[148:149], v[108:109], v[54:55], v[148:149] op_sel_hi:[0,1,1] neg_lo:[1,0,0] neg_hi:[1,0,0]
	v_pk_fma_f32 v[152:153], v[108:109], v[54:55], v[152:153] op_sel:[1,0,0] neg_lo:[1,0,0] neg_hi:[1,0,0]
	v_pk_fma_f32 v[156:157], v[110:111], v[54:55], v[156:157] op_sel_hi:[0,1,1] neg_lo:[1,0,0] neg_hi:[1,0,0]
	v_pk_mul_f32 v[86:87], v[110:111], v[148:149] op_sel:[1,0]
	v_pk_mul_f32 v[126:127], v[136:137], v[148:149] op_sel_hi:[0,1]
	v_pk_mul_f32 v[134:135], v[136:137], v[148:149] op_sel:[1,0]
	v_pk_fma_f32 v[86:87], v[136:137], v[152:153], v[86:87] op_sel_hi:[0,1,1]
	v_pk_fma_f32 v[126:127], v[138:139], v[152:153], v[126:127] op_sel_hi:[0,1,1]
	v_pk_fma_f32 v[134:135], v[138:139], v[152:153], v[134:135] op_sel:[1,0,0]
	v_pk_fma_f32 v[86:87], v[136:137], v[156:157], v[86:87] op_sel:[1,0,0]
	v_pk_fma_f32 v[126:127], v[138:139], v[156:157], v[126:127] op_sel:[1,0,0]
	v_pk_fma_f32 v[134:135], v[140:141], v[156:157], v[134:135] op_sel_hi:[0,1,1]
	v_pk_mul_f32 v[160:161], v[108:109], v[86:87] op_sel_hi:[0,1]
	v_pk_fma_f32 v[160:161], v[108:109], v[126:127], v[160:161] op_sel:[1,0,0]
	v_pk_fma_f32 v[160:161], v[110:111], v[134:135], v[160:161] op_sel_hi:[0,1,1]
	v_pk_fma_f32 v[160:161], v[140:141], v[54:55], v[160:161] op_sel:[1,0,0] neg_lo:[0,0,1] neg_hi:[0,0,1]
	v_cmp_eq_u32_e64 s[10:11], 6, v143
	v_cmp_eq_u32_e64 s[14:15], 7, v143
	v_pk_add_f32 v[54:55], v[88:89], v[86:87]
	v_pk_add_f32 v[88:89], v[116:117], v[126:127]
	v_pk_add_f32 v[116:117], v[120:121], v[134:135]
	v_pk_add_f32 v[146:147], v[58:59], v[160:161]
	v_pk_fma_f32 v[58:59], v[64:65], v[54:55], v[146:147] op_sel_hi:[0,1,1]
	v_pk_fma_f32 v[150:151], v[104:105], v[54:55], v[146:147] op_sel_hi:[0,1,1]
	v_pk_fma_f32 v[58:59], v[64:65], v[88:89], v[58:59] op_sel:[1,0,0]
	v_pk_fma_f32 v[150:151], v[104:105], v[88:89], v[150:151] op_sel:[1,0,0]
	v_pk_fma_f32 v[58:59], v[66:67], v[116:117], v[58:59] op_sel_hi:[0,1,1]
	v_pk_fma_f32 v[150:151], v[106:107], v[116:117], v[150:151] op_sel_hi:[0,1,1]
	v_pk_fma_f32 v[146:147], v[8:9], v[54:55], v[146:147] op_sel_hi:[0,1,1]
	v_pk_fma_f32 v[146:147], v[8:9], v[88:89], v[146:147] op_sel:[1,0,0]
	v_pk_fma_f32 v[146:147], v[10:11], v[116:117], v[146:147] op_sel_hi:[0,1,1]
	v_cndmask_b32_e64 v120, 0, v18, s[10:11]
	v_cndmask_b32_e64 v121, 0, v18, s[14:15]
	v_add_f32_dpp v146, v58, v146 wave_shl:1 row_mask:0xf bank_mask:0xf bound_ctrl:1
	v_add_f32_dpp v147, v59, v147 wave_shl:1 row_mask:0xf bank_mask:0xf bound_ctrl:1
	s_add_i32 s4, s34, 3
	s_cmpk_lt_i32 s4, 0x201
	s_cselect_b64 s[12:13], s[0:1], 0
	v_add_f32_dpp v146, v150, v146 wave_shr:1 row_mask:0xf bank_mask:0xf bound_ctrl:1
	v_add_f32_dpp v147, v151, v147 wave_shr:1 row_mask:0xf bank_mask:0xf bound_ctrl:1
	v_pk_fma_f32 v[146:147], v[4:5], v[142:143], v[146:147] op_sel_hi:[1,0,1] neg_lo:[0,0,1] neg_hi:[0,0,1]
	v_pk_add_f32 v[146:147], v[146:147], v[120:121] neg_lo:[0,1] neg_hi:[0,1]
	v_pk_mul_f32 v[148:149], v[146:147], v[146:147]
	v_add_f32_e32 v148, v148, v149
	v_cndmask_b32_e64 v149, 0, v148, s[12:13]
	v_add_f32_e32 v1, v1, v149
	s_add_i32 s5, s34, 8
	s_min_i32 s5, s5, 0x200
	s_mul_i32 s6, s5, 0x804
	s_add_i32 s6, s6, s35
	s_add_i32 s7, s6, 0x505014
	s_add_i32 s8, s6, 0x606018
	s_mul_i32 s9, s5, 0x180c
	s_add_i32 s9, s9, s33
	s_add_i32 s4, s34, 9
	s_min_i32 s4, s4, 0x200
	s_mul_i32 s4, s4, 0x804
	s_add_i32 s4, s4, s38
	buffer_load_dword v17, v28, s[20:23], s4 offen nt
	buffer_load_dwordx3 v[8:10], v27, s[24:27], s9 offen nt
	buffer_load_dword v4, v28, s[16:19], s7 offen nt
	buffer_load_dword v5, v28, s[16:19], s8 offen nt
	s_waitcnt vmcnt(8)
	v_mov_b32_dpp v64, v40 wave_shr:1 row_mask:0xf bank_mask:0xf bound_ctrl:1
	v_mov_b32_dpp v65, v41 wave_shr:1 row_mask:0xf bank_mask:0xf bound_ctrl:1
	v_mov_b32_dpp v66, v42 wave_shr:1 row_mask:0xf bank_mask:0xf bound_ctrl:1
	v_mov_b32_dpp v104, v40 wave_shl:1 row_mask:0xf bank_mask:0xf bound_ctrl:1
	v_mov_b32_dpp v105, v41 wave_shl:1 row_mask:0xf bank_mask:0xf bound_ctrl:1
	v_mov_b32_dpp v106, v42 wave_shl:1 row_mask:0xf bank_mask:0xf bound_ctrl:1
	s_add_i32 s4, s34, 7
	s_cmpk_lt_u32 s4, 0x201
	s_cselect_b64 s[12:13], s[40:41], 0
	v_cmp_eq_u32_e64 s[14:15], s37, v25
	s_and_b64 s[14:15], s[14:15], s[12:13]
	v_cndmask_b32_e64 v29, 0, 1, s[14:15]
	v_mul_f32_e64 v54, v40, v40
	v_mul_f32_e64 v55, v40, v41
	v_or_b32_dpp v31, v29, v29 wave_shr:1 row_mask:0xf bank_mask:0xf bound_ctrl:1
	v_mul_f32_e64 v58, v40, v42
	v_or_b32_dpp v31, v29, v31 wave_shl:1 row_mask:0xf bank_mask:0xf bound_ctrl:1
	v_mul_f32_e64 v59, v41, v41
	v_mul_f32_e64 v88, v41, v42
	v_or_b32_dpp v53, v31, v31 wave_shr:1 row_mask:0xf bank_mask:0xf bound_ctrl:1
	v_mul_f32_e64 v89, v42, v42
	s_nop 0
	v_or_b32_dpp v53, v31, v53 wave_shl:1 row_mask:0xf bank_mask:0xf bound_ctrl:1
	v_or3_b32 v29, v53, v70, v71
	v_or3_b32 v29, v29, v52, v30
	s_add_i32 s4, s34, 4
	s_cmpk_lt_u32 s4, 0x1ff
	s_cselect_b64 s[12:13], s[42:43], 0
	v_cmp_ne_u32_e64 s[30:31], 0, v29
	s_and_b64 s[30:31], s[30:31], s[12:13]
	v_cndmask_b32_e64 v29, 0, 1.0, s[30:31]
	v_add_f32_e64 v108, v40, v64
	v_add_f32_e64 v109, v41, v65
	v_add_f32_e64 v110, v42, v66
	v_fma_f32 v54, v64, v64, v54
	v_fma_f32 v55, v64, v65, v55
	v_fma_f32 v58, v64, v66, v58
	v_fma_f32 v59, v65, v65, v59
	v_fma_f32 v88, v65, v66, v88
	v_fma_f32 v89, v66, v66, v89
	v_add_f32_dpp v137, v29, v29 wave_shr:1 row_mask:0xf bank_mask:0xf bound_ctrl:1
	v_add_f32_e64 v108, v108, v104
	v_add_f32_e64 v109, v109, v105
	v_add_f32_e64 v110, v110, v106
	v_fma_f32 v111, v104, v104, v54
	v_fma_f32 v116, v104, v105, v55
	v_fma_f32 v117, v104, v106, v58
	v_fma_f32 v120, v105, v105, v59
	v_fma_f32 v121, v105, v106, v88
	v_fma_f32 v136, v106, v106, v89
	v_add_f32_dpp v137, v29, v137 wave_shl:1 row_mask:0xf bank_mask:0xf bound_ctrl:1
	v_pk_add_f32 v[54:55], v[112:113], v[108:109]
	v_pk_add_f32 v[58:59], v[56:57], v[54:55]
	v_pk_add_f32 v[56:57], v[114:115], v[110:111]
	v_pk_add_f32 v[88:89], v[90:91], v[56:57]
	v_pk_add_f32 v[112:113], v[128:129], v[116:117]
	v_pk_add_f32 v[90:91], v[118:119], v[112:113]
	v_pk_add_f32 v[128:129], v[130:131], v[120:121]
	v_pk_add_f32 v[114:115], v[122:123], v[128:129]
	v_pk_add_f32 v[118:119], v[132:133], v[136:137]
	v_pk_add_f32 v[122:123], v[124:125], v[118:119]
	v_mul_f32_e64 v140, v58, v22
	v_mul_f32_e64 v141, v59, v22
	v_mul_f32_e64 v142, v88, v22
	v_fma_f32 v29, v89, v22, v26
	v_mul_f32_e64 v31, v90, v22
	v_mul_f32_e64 v124, v91, v22
	v_fma_f32 v125, v114, v22, v26
	v_mul_f32_e64 v130, v115, v22
	v_fma_f32 v131, v122, v22, v26
	v_fma_f32 v29, -v140, v140, v29
	v_fma_f32 v31, -v140, v141, v31
	v_fma_f32 v124, -v140, v142, v124
	v_fma_f32 v125, -v141, v141, v125
	v_fma_f32 v130, -v141, v142, v130
	v_fma_f32 v131, -v142, v142, v131
	v_mul_f32_e64 v132, v130, v130
	v_mul_f32_e64 v133, v31, v131
	v_mul_f32_e64 v138, v124, v125
	v_mul_f32_e64 v139, v124, v124
	v_mul_f32_e64 v146, v29, v130
	v_mul_f32_e64 v147, v31, v31
	v_fma_f32 v132, v125, v131, -v132
	v_fma_f32 v133, v124, v130, -v133
	v_fma_f32 v138, v31, v130, -v138
	v_fma_f32 v139, v29, v131, -v139
	v_fma_f32 v146, v31, v124, -v146
	v_fma_f32 v147, v29, v125, -v147
	v_mul_f32_e64 v156, v29, v132
	v_fma_f32 v156, v31, v133, v156
	v_fma_f32 v156, v124, v138, v156
	v_rcp_f32_e32 v156, v156
	v_cmp_ne_u32_e64 vcc, s37, v2
	v_mul_f32_e64 v156, v156, v22
	v_cndmask_b32_e64 v156, 0, v156, s[30:31]
	v_cndmask_b32_e64 v29, 0, v18, vcc
	v_cndmask_b32_e64 v153, 0, v22, s[30:31]
	v_mul_f32_e64 v143, v132, v156
	v_mul_f32_e64 v148, v133, v156
	v_mul_f32_e64 v149, v138, v156
	v_mul_f32_e64 v150, v139, v156
	v_mul_f32_e64 v151, v146, v156
	v_mul_f32_e64 v152, v147, v156
	v_add_f32_e64 v154, v123, v29
	v_mov_b32_e32 v155, v2
	ds_write_b128 v23, v[140:143]
	ds_write_b128 v23, v[148:151] offset:1024
	ds_write_b128 v23, v[152:155] offset:2048
	v_mov_b32_dpp v30, v36 wave_shr:1 row_mask:0xf bank_mask:0xf bound_ctrl:1
	v_mov_b32_dpp v31, v37 wave_shr:1 row_mask:0xf bank_mask:0xf bound_ctrl:1
	v_mov_b32_dpp v58, v36 wave_shl:1 row_mask:0xf bank_mask:0xf bound_ctrl:1
	v_mov_b32_dpp v59, v37 wave_shl:1 row_mask:0xf bank_mask:0xf bound_ctrl:1
	v_pk_mul_f32 v[88:89], v[36:37], v[40:41] op_sel_hi:[1,0]
	v_pk_mul_f32 v[124:125], v[36:37], v[40:41] op_sel:[0,1]
	v_pk_mul_f32 v[132:133], v[36:37], v[42:43] op_sel_hi:[1,0]
	v_pk_add_f32 v[156:157], v[36:37], v[30:31]
	v_pk_fma_f32 v[88:89], v[30:31], v[64:65], v[88:89] op_sel_hi:[1,0,1]
	v_pk_fma_f32 v[124:125], v[30:31], v[64:65], v[124:125] op_sel:[0,1,0]
	v_pk_fma_f32 v[132:133], v[30:31], v[66:67], v[132:133] op_sel_hi:[1,0,1]
	v_pk_add_f32 v[156:157], v[156:157], v[58:59]
	v_pk_fma_f32 v[88:89], v[58:59], v[104:105], v[88:89] op_sel_hi:[1,0,1]
	v_pk_fma_f32 v[124:125], v[58:59], v[104:105], v[124:125] op_sel:[0,1,0]
	v_pk_fma_f32 v[132:133], v[58:59], v[106:107], v[132:133] op_sel_hi:[1,0,1]
	s_waitcnt lgkmcnt(0)
	s_barrier
	v_pk_add_f32 v[164:165], v[144:145], v[156:157]
	v_pk_add_f32 v[30:31], v[98:99], v[164:165]
	v_pk_add_f32 v[144:145], v[48:49], v[88:89]
	v_pk_add_f32 v[168:169], v[38:39], v[144:145]
	v_pk_add_f32 v[48:49], v[92:93], v[124:125]
	v_pk_add_f32 v[172:173], v[46:47], v[48:49]
	v_pk_add_f32 v[92:93], v[96:97], v[132:133]
	v_pk_add_f32 v[176:177], v[94:95], v[92:93]
	v_pk_fma_f32 v[168:169], v[140:141], v[30:31], v[168:169] op_sel_hi:[0,1,1] neg_lo:[1,0,0] neg_hi:[1,0,0]
	v_pk_fma_f32 v[172:173], v[140:141], v[30:31], v[172:173] op_sel:[1,0,0] neg_lo:[1,0,0] neg_hi:[1,0,0]
	v_pk_fma_f32 v[176:177], v[142:143], v[30:31], v[176:177] op_sel_hi:[0,1,1] neg_lo:[1,0,0] neg_hi:[1,0,0]
	v_pk_mul_f32 v[38:39], v[142:143], v[168:169] op_sel:[1,0]
	v_pk_mul_f32 v[46:47], v[148:149], v[168:169] op_sel_hi:[0,1]
	v_pk_mul_f32 v[58:59], v[148:149], v[168:169] op_sel:[1,0]
	v_pk_fma_f32 v[38:39], v[148:149], v[172:173], v[38:39] op_sel_hi:[0,1,1]
	v_pk_fma_f32 v[46:47], v[150:151], v[172:173], v[46:47] op_sel_hi:[0,1,1]
	v_pk_fma_f32 v[58:59], v[150:151], v[172:173], v[58:59] op_sel:[1,0,0]
	v_pk_fma_f32 v[38:39], v[148:149], v[176:177], v[38:39] op_sel:[1,0,0]
	v_pk_fma_f32 v[46:47], v[150:151], v[176:177], v[46:47] op_sel:[1,0,0]
	v_pk_fma_f32 v[58:59], v[152:153], v[176:177], v[58:59] op_sel_hi:[0,1,1]
	v_pk_mul_f32 v[96:97], v[140:141], v[38:39] op_sel_hi:[0,1]
	v_pk_fma_f32 v[96:97], v[140:141], v[46:47], v[96:97] op_sel:[1,0,0]
	v_pk_fma_f32 v[96:97], v[142:143], v[58:59], v[96:97] op_sel_hi:[0,1,1]
	v_pk_fma_f32 v[96:97], v[152:153], v[30:31], v[96:97] op_sel:[1,0,0] neg_lo:[0,0,1] neg_hi:[0,0,1]
	v_cmp_eq_u32_e64 s[10:11], 6, v155
	v_cmp_eq_u32_e64 s[14:15], 7, v155
	v_pk_add_f32 v[30:31], v[86:87], v[38:39]
	v_pk_add_f32 v[90:91], v[44:45], v[30:31]
	v_pk_add_f32 v[86:87], v[126:127], v[46:47]
	v_pk_add_f32 v[44:45], v[68:69], v[86:87]
	v_pk_add_f32 v[94:95], v[134:135], v[58:59]
	v_pk_add_f32 v[68:69], v[84:85], v[94:95]
	v_pk_add_f32 v[84:85], v[160:161], v[96:97]
	v_pk_add_f32 v[98:99], v[174:175], v[84:85]
	v_pk_fma_f32 v[114:115], v[60:61], v[90:91], v[98:99] op_sel_hi:[0,1,1]
	v_pk_fma_f32 v[122:123], v[76:77], v[90:91], v[98:99] op_sel_hi:[0,1,1]
	v_pk_fma_f32 v[114:115], v[60:61], v[44:45], v[114:115] op_sel:[1,0,0]
	v_pk_fma_f32 v[122:123], v[76:77], v[44:45], v[122:123] op_sel:[1,0,0]
	v_pk_fma_f32 v[114:115], v[62:63], v[68:69], v[114:115] op_sel_hi:[0,1,1]
	v_pk_fma_f32 v[122:123], v[78:79], v[68:69], v[122:123] op_sel_hi:[0,1,1]
	v_pk_fma_f32 v[98:99], v[12:13], v[90:91], v[98:99] op_sel_hi:[0,1,1]
	v_pk_fma_f32 v[98:99], v[12:13], v[44:45], v[98:99] op_sel:[1,0,0]
	v_pk_fma_f32 v[98:99], v[14:15], v[68:69], v[98:99] op_sel_hi:[0,1,1]
	v_cndmask_b32_e64 v160, 0, v18, s[10:11]
	v_cndmask_b32_e64 v161, 0, v18, s[14:15]
	v_add_f32_dpp v98, v114, v98 wave_shl:1 row_mask:0xf bank_mask:0xf bound_ctrl:1
	v_add_f32_dpp v99, v115, v99 wave_shl:1 row_mask:0xf bank_mask:0xf bound_ctrl:1
	s_add_i32 s4, s34, 4
	s_cmpk_lt_i32 s4, 0x201
	s_cselect_b64 s[12:13], s[0:1], 0
	v_add_f32_dpp v98, v122, v98 wave_shr:1 row_mask:0xf bank_mask:0xf bound_ctrl:1
	v_add_f32_dpp v99, v123, v99 wave_shr:1 row_mask:0xf bank_mask:0xf bound_ctrl:1
	v_pk_fma_f32 v[98:99], v[6:7], v[154:155], v[98:99] op_sel_hi:[1,0,1] neg_lo:[0,0,1] neg_hi:[0,0,1]
	v_pk_add_f32 v[98:99], v[98:99], v[160:161] neg_lo:[0,1] neg_hi:[0,1]
	v_pk_mul_f32 v[126:127], v[98:99], v[98:99]
	v_add_f32_e32 v126, v126, v127
	v_cndmask_b32_e64 v127, 0, v126, s[12:13]
	v_add_f32_e32 v1, v1, v127
	s_add_i32 s5, s34, 9
	s_min_i32 s5, s5, 0x200
	s_mul_i32 s6, s5, 0x804
	s_add_i32 s6, s6, s35
	s_add_i32 s7, s6, 0x505014
	s_add_i32 s8, s6, 0x606018
	s_mul_i32 s9, s5, 0x180c
	s_add_i32 s9, s9, s33
	s_add_i32 s4, s34, 10
	s_min_i32 s4, s4, 0x200
	s_mul_i32 s4, s4, 0x804
	s_add_i32 s4, s4, s38
	buffer_load_dword v2, v28, s[20:23], s4 offen nt
	buffer_load_dwordx3 v[12:14], v27, s[24:27], s9 offen nt
	buffer_load_dword v6, v28, s[16:19], s7 offen nt
	buffer_load_dword v7, v28, s[16:19], s8 offen nt
	s_waitcnt vmcnt(8)
	v_mov_b32_dpp v60, v72 wave_shr:1 row_mask:0xf bank_mask:0xf bound_ctrl:1
	v_mov_b32_dpp v61, v73 wave_shr:1 row_mask:0xf bank_mask:0xf bound_ctrl:1
	v_mov_b32_dpp v62, v74 wave_shr:1 row_mask:0xf bank_mask:0xf bound_ctrl:1
	v_mov_b32_dpp v76, v72 wave_shl:1 row_mask:0xf bank_mask:0xf bound_ctrl:1
	v_mov_b32_dpp v77, v73 wave_shl:1 row_mask:0xf bank_mask:0xf bound_ctrl:1
	v_mov_b32_dpp v78, v74 wave_shl:1 row_mask:0xf bank_mask:0xf bound_ctrl:1
	s_add_i32 s4, s34, 8
	s_cmpk_lt_u32 s4, 0x201
	s_cselect_b64 s[12:13], s[40:41], 0
	v_cmp_eq_u32_e64 s[14:15], s37, v24
	s_and_b64 s[14:15], s[14:15], s[12:13]
	v_cndmask_b32_e64 v29, 0, 1, s[14:15]
	v_mul_f32_e64 v44, v72, v72
	v_mul_f32_e64 v45, v72, v73
	v_or_b32_dpp v98, v29, v29 wave_shr:1 row_mask:0xf bank_mask:0xf bound_ctrl:1
	v_mul_f32_e64 v68, v72, v74
	v_or_b32_dpp v98, v29, v98 wave_shl:1 row_mask:0xf bank_mask:0xf bound_ctrl:1
	v_mul_f32_e64 v69, v73, v73
	v_mul_f32_e64 v90, v73, v74
	v_or_b32_dpp v99, v98, v98 wave_shr:1 row_mask:0xf bank_mask:0xf bound_ctrl:1
	v_mul_f32_e64 v91, v74, v74
	s_nop 0
	v_or_b32_dpp v99, v98, v99 wave_shl:1 row_mask:0xf bank_mask:0xf bound_ctrl:1
	v_or3_b32 v29, v99, v53, v70
	v_or3_b32 v29, v29, v71, v52
	s_add_i32 s4, s34, 5
	s_cmpk_lt_u32 s4, 0x1ff
	s_cselect_b64 s[12:13], s[42:43], 0
	v_cmp_ne_u32_e64 s[30:31], 0, v29
	s_and_b64 s[30:31], s[30:31], s[12:13]
	v_cndmask_b32_e64 v29, 0, 1.0, s[30:31]
	v_add_f32_e64 v114, v72, v60
	v_add_f32_e64 v115, v73, v61
	v_add_f32_e64 v122, v74, v62
	v_fma_f32 v44, v60, v60, v44
	v_fma_f32 v45, v60, v61, v45
	v_fma_f32 v68, v60, v62, v68
	v_fma_f32 v69, v61, v61, v69
	v_fma_f32 v90, v61, v62, v90
	v_fma_f32 v91, v62, v62, v91
	v_add_f32_dpp v135, v29, v29 wave_shr:1 row_mask:0xf bank_mask:0xf bound_ctrl:1
	v_add_f32_e64 v114, v114, v76
	v_add_f32_e64 v115, v115, v77
	v_add_f32_e64 v122, v122, v78
	v_fma_f32 v123, v76, v76, v44
	v_fma_f32 v126, v76, v77, v45
	v_fma_f32 v127, v76, v78, v68
	v_fma_f32 v130, v77, v77, v69
	v_fma_f32 v131, v77, v78, v90
	v_fma_f32 v134, v78, v78, v91
	v_add_f32_dpp v135, v29, v135 wave_shl:1 row_mask:0xf bank_mask:0xf bound_ctrl:1
	v_pk_add_f32 v[44:45], v[54:55], v[114:115]
	v_pk_add_f32 v[54:55], v[56:57], v[122:123]
	v_pk_add_f32 v[56:57], v[112:113], v[126:127]
	v_pk_add_f32 v[68:69], v[128:129], v[130:131]
	v_pk_add_f32 v[90:91], v[118:119], v[134:135]
	v_mul_f32_e64 v140, v44, v22
	v_mul_f32_e64 v141, v45, v22
	v_mul_f32_e64 v142, v54, v22
	v_fma_f32 v29, v55, v22, v26
	v_mul_f32_e64 v98, v56, v22
	v_mul_f32_e64 v112, v57, v22
	v_fma_f32 v113, v68, v22, v26
	v_mul_f32_e64 v118, v69, v22
	v_fma_f32 v119, v90, v22, v26
	v_fma_f32 v29, -v140, v140, v29
	v_fma_f32 v98, -v140, v141, v98
	v_fma_f32 v112, -v140, v142, v112
	v_fma_f32 v113, -v141, v141, v113
	v_fma_f32 v118, -v141, v142, v118
	v_fma_f32 v119, -v142, v142, v119
	v_mul_f32_e64 v128, v118, v118
	v_mul_f32_e64 v129, v98, v119
	v_mul_f32_e64 v138, v112, v113
	v_mul_f32_e64 v139, v112, v112
	v_mul_f32_e64 v146, v29, v118
	v_mul_f32_e64 v147, v98, v98
	v_fma_f32 v128, v113, v119, -v128
	v_fma_f32 v129, v112, v118, -v129
	v_fma_f32 v138, v98, v118, -v138
	v_fma_f32 v139, v29, v119, -v139
	v_fma_f32 v146, v98, v112, -v146
	v_fma_f32 v147, v29, v113, -v147
	v_mul_f32_e64 v158, v29, v128
	v_fma_f32 v158, v98, v129, v158
	v_fma_f32 v158, v112, v138, v158
	v_rcp_f32_e32 v158, v158
	v_cmp_ne_u32_e64 vcc, s37, v3
	v_mul_f32_e64 v158, v158, v22
	v_cndmask_b32_e64 v158, 0, v158, s[30:31]
	v_cndmask_b32_e64 v29, 0, v18, vcc
	v_cndmask_b32_e64 v153, 0, v22, s[30:31]
	v_mul_f32_e64 v143, v128, v158
	v_mul_f32_e64 v148, v129, v158
	v_mul_f32_e64 v149, v138, v158
	v_mul_f32_e64 v150, v139, v158
	v_mul_f32_e64 v151, v146, v158
	v_mul_f32_e64 v152, v147, v158
	v_add_f32_e64 v154, v91, v29
	v_mov_b32_e32 v155, v3
	ds_write_b128 v23, v[140:143] offset:3072
	ds_write_b128 v23, v[148:151] offset:4096
	ds_write_b128 v23, v[152:155] offset:5120
	v_mov_b32_dpp v44, v50 wave_shr:1 row_mask:0xf bank_mask:0xf bound_ctrl:1
	v_mov_b32_dpp v45, v51 wave_shr:1 row_mask:0xf bank_mask:0xf bound_ctrl:1
	v_mov_b32_dpp v56, v50 wave_shl:1 row_mask:0xf bank_mask:0xf bound_ctrl:1
	v_mov_b32_dpp v57, v51 wave_shl:1 row_mask:0xf bank_mask:0xf bound_ctrl:1
	v_pk_mul_f32 v[54:55], v[50:51], v[72:73] op_sel_hi:[1,0]
	v_pk_mul_f32 v[90:91], v[50:51], v[72:73] op_sel:[0,1]
	v_pk_mul_f32 v[118:119], v[50:51], v[74:75] op_sel_hi:[1,0]
	v_pk_add_f32 v[138:139], v[50:51], v[44:45]
	v_pk_fma_f32 v[54:55], v[44:45], v[60:61], v[54:55] op_sel_hi:[1,0,1]
	v_pk_fma_f32 v[90:91], v[44:45], v[60:61], v[90:91] op_sel:[0,1,0]
	v_pk_fma_f32 v[118:119], v[44:45], v[62:63], v[118:119] op_sel_hi:[1,0,1]
	v_pk_add_f32 v[138:139], v[138:139], v[56:57]
	v_pk_fma_f32 v[54:55], v[56:57], v[76:77], v[54:55] op_sel_hi:[1,0,1]
	v_pk_fma_f32 v[90:91], v[56:57], v[76:77], v[90:91] op_sel:[0,1,0]
	v_pk_fma_f32 v[118:119], v[56:57], v[78:79], v[118:119] op_sel_hi:[1,0,1]
	s_waitcnt lgkmcnt(0)
	s_barrier
	v_pk_add_f32 v[44:45], v[164:165], v[138:139]
	v_pk_add_f32 v[146:147], v[144:145], v[54:55]
	v_pk_add_f32 v[158:159], v[48:49], v[90:91]
	v_pk_add_f32 v[162:163], v[92:93], v[118:119]
	v_pk_fma_f32 v[146:147], v[140:141], v[44:45], v[146:147] op_sel_hi:[0,1,1] neg_lo:[1,0,0] neg_hi:[1,0,0]
	v_pk_fma_f32 v[158:159], v[140:141], v[44:45], v[158:159] op_sel:[1,0,0] neg_lo:[1,0,0] neg_hi:[1,0,0]
	v_pk_fma_f32 v[162:163], v[142:143], v[44:45], v[162:163] op_sel_hi:[0,1,1] neg_lo:[1,0,0] neg_hi:[1,0,0]
	v_pk_mul_f32 v[48:49], v[142:143], v[146:147] op_sel:[1,0]
	v_pk_mul_f32 v[56:57], v[148:149], v[146:147] op_sel_hi:[0,1]
	v_pk_mul_f32 v[68:69], v[148:149], v[146:147] op_sel:[1,0]
	v_pk_fma_f32 v[48:49], v[148:149], v[158:159], v[48:49] op_sel_hi:[0,1,1]
	v_pk_fma_f32 v[56:57], v[150:151], v[158:159], v[56:57] op_sel_hi:[0,1,1]
	v_pk_fma_f32 v[68:69], v[150:151], v[158:159], v[68:69] op_sel:[1,0,0]
	v_pk_fma_f32 v[48:49], v[148:149], v[162:163], v[48:49] op_sel:[1,0,0]
	v_pk_fma_f32 v[56:57], v[150:151], v[162:163], v[56:57] op_sel:[1,0,0]
	v_pk_fma_f32 v[68:69], v[152:153], v[162:163], v[68:69] op_sel_hi:[0,1,1]
	v_pk_mul_f32 v[166:167], v[140:141], v[48:49] op_sel_hi:[0,1]
	v_pk_fma_f32 v[166:167], v[140:141], v[56:57], v[166:167] op_sel:[1,0,0]
	v_pk_fma_f32 v[166:167], v[142:143], v[68:69], v[166:167] op_sel_hi:[0,1,1]
	v_pk_fma_f32 v[166:167], v[152:153], v[44:45], v[166:167] op_sel:[1,0,0] neg_lo:[0,0,1] neg_hi:[0,0,1]
	v_cmp_eq_u32_e64 s[10:11], 6, v155
	v_cmp_eq_u32_e64 s[14:15], 7, v155
	v_pk_add_f32 v[44:45], v[30:31], v[48:49]
	v_pk_add_f32 v[30:31], v[86:87], v[56:57]
	v_pk_add_f32 v[86:87], v[94:95], v[68:69]
	v_pk_add_f32 v[92:93], v[84:85], v[166:167]
	v_pk_fma_f32 v[84:85], v[80:81], v[44:45], v[92:93] op_sel_hi:[0,1,1]
	v_pk_fma_f32 v[112:113], v[100:101], v[44:45], v[92:93] op_sel_hi:[0,1,1]
	v_pk_fma_f32 v[84:85], v[80:81], v[30:31], v[84:85] op_sel:[1,0,0]
	v_pk_fma_f32 v[112:113], v[100:101], v[30:31], v[112:113] op_sel:[1,0,0]
	v_pk_fma_f32 v[84:85], v[82:83], v[86:87], v[84:85] op_sel_hi:[0,1,1]
	v_pk_fma_f32 v[112:113], v[102:103], v[86:87], v[112:113] op_sel_hi:[0,1,1]
	v_pk_fma_f32 v[92:93], v[32:33], v[44:45], v[92:93] op_sel_hi:[0,1,1]
	v_pk_fma_f32 v[92:93], v[32:33], v[30:31], v[92:93] op_sel:[1,0,0]
	v_pk_fma_f32 v[92:93], v[34:35], v[86:87], v[92:93] op_sel_hi:[0,1,1]
	v_cndmask_b32_e64 v94, 0, v18, s[10:11]
	v_cndmask_b32_e64 v95, 0, v18, s[14:15]
	v_add_f32_dpp v92, v84, v92 wave_shl:1 row_mask:0xf bank_mask:0xf bound_ctrl:1
	v_add_f32_dpp v93, v85, v93 wave_shl:1 row_mask:0xf bank_mask:0xf bound_ctrl:1
	s_add_i32 s4, s34, 5
	s_cmpk_lt_i32 s4, 0x201
	s_cselect_b64 s[12:13], s[0:1], 0
	v_add_f32_dpp v92, v112, v92 wave_shr:1 row_mask:0xf bank_mask:0xf bound_ctrl:1
	v_add_f32_dpp v93, v113, v93 wave_shr:1 row_mask:0xf bank_mask:0xf bound_ctrl:1
	v_pk_fma_f32 v[92:93], v[20:21], v[154:155], v[92:93] op_sel_hi:[1,0,1] neg_lo:[0,0,1] neg_hi:[0,0,1]
	v_pk_add_f32 v[92:93], v[92:93], v[94:95] neg_lo:[0,1] neg_hi:[0,1]
	v_pk_mul_f32 v[128:129], v[92:93], v[92:93]
	v_add_f32_e32 v128, v128, v129
	v_cndmask_b32_e64 v129, 0, v128, s[12:13]
	v_add_f32_e32 v1, v1, v129
	s_add_i32 s5, s34, 10
	s_min_i32 s5, s5, 0x200
	s_mul_i32 s6, s5, 0x804
	s_add_i32 s6, s6, s35
	s_add_i32 s7, s6, 0x505014
	s_add_i32 s8, s6, 0x606018
	s_mul_i32 s9, s5, 0x180c
	s_add_i32 s9, s9, s33
	s_add_i32 s4, s34, 11
	s_min_i32 s4, s4, 0x200
	s_mul_i32 s4, s4, 0x804
	s_add_i32 s4, s4, s38
	buffer_load_dword v3, v28, s[20:23], s4 offen nt
	buffer_load_dwordx3 v[32:34], v27, s[24:27], s9 offen nt
	buffer_load_dword v20, v28, s[16:19], s7 offen nt
	buffer_load_dword v21, v28, s[16:19], s8 offen nt
	s_waitcnt vmcnt(8)
	v_mov_b32_dpp v80, v8 wave_shr:1 row_mask:0xf bank_mask:0xf bound_ctrl:1
	v_mov_b32_dpp v81, v9 wave_shr:1 row_mask:0xf bank_mask:0xf bound_ctrl:1
	v_mov_b32_dpp v82, v10 wave_shr:1 row_mask:0xf bank_mask:0xf bound_ctrl:1
	v_mov_b32_dpp v84, v8 wave_shl:1 row_mask:0xf bank_mask:0xf bound_ctrl:1
	v_mov_b32_dpp v85, v9 wave_shl:1 row_mask:0xf bank_mask:0xf bound_ctrl:1
	v_mov_b32_dpp v86, v10 wave_shl:1 row_mask:0xf bank_mask:0xf bound_ctrl:1
	s_add_i32 s4, s34, 9
	s_cmpk_lt_u32 s4, 0x201
	s_cselect_b64 s[12:13], s[40:41], 0
	v_cmp_eq_u32_e64 s[14:15], s37, v17
	s_and_b64 s[14:15], s[14:15], s[12:13]
	v_cndmask_b32_e64 v29, 0, 1, s[14:15]
	v_mul_f32_e64 v30, v8, v8
	v_mul_f32_e64 v31, v8, v9
	v_or_b32_dpp v52, v29, v29 wave_shr:1 row_mask:0xf bank_mask:0xf bound_ctrl:1
	v_mul_f32_e64 v44, v8, v10
	v_or_b32_dpp v52, v29, v52 wave_shl:1 row_mask:0xf bank_mask:0xf bound_ctrl:1
	v_mul_f32_e64 v45, v9, v9
	v_mul_f32_e64 v92, v9, v10
	v_or_b32_dpp v98, v52, v52 wave_shr:1 row_mask:0xf bank_mask:0xf bound_ctrl:1
	v_mul_f32_e64 v93, v10, v10
	s_nop 0
	v_or_b32_dpp v98, v52, v98 wave_shl:1 row_mask:0xf bank_mask:0xf bound_ctrl:1
	v_or3_b32 v29, v98, v99, v53
	v_or3_b32 v29, v29, v70, v71
	s_add_i32 s4, s34, 6
	s_cmpk_lt_u32 s4, 0x1ff
	s_cselect_b64 s[12:13], s[42:43], 0
	v_cmp_ne_u32_e64 s[30:31], 0, v29
	s_and_b64 s[30:31], s[30:31], s[12:13]
	v_cndmask_b32_e64 v29, 0, 1.0, s[30:31]
	v_add_f32_e64 v94, v8, v80
	v_add_f32_e64 v95, v9, v81
	v_add_f32_e64 v100, v10, v82
	v_fma_f32 v30, v80, v80, v30
	v_fma_f32 v31, v80, v81, v31
	v_fma_f32 v44, v80, v82, v44
	v_fma_f32 v45, v81, v81, v45
	v_fma_f32 v92, v81, v82, v92
	v_fma_f32 v93, v82, v82, v93
	v_add_f32_dpp v129, v29, v29 wave_shr:1 row_mask:0xf bank_mask:0xf bound_ctrl:1
	v_add_f32_e64 v94, v94, v84
	v_add_f32_e64 v95, v95, v85
	v_add_f32_e64 v100, v100, v86
	v_fma_f32 v101, v84, v84, v30
	v_fma_f32 v102, v84, v85, v31
	v_fma_f32 v103, v84, v86, v44
	v_fma_f32 v112, v85, v85, v45
	v_fma_f32 v113, v85, v86, v92
	v_fma_f32 v128, v86, v86, v93
	v_add_f32_dpp v129, v29, v129 wave_shl:1 row_mask:0xf bank_mask:0xf bound_ctrl:1
	v_pk_add_f32 v[30:31], v[114:115], v[94:95]
	v_pk_add_f32 v[44:45], v[108:109], v[30:31]
	v_pk_add_f32 v[92:93], v[122:123], v[100:101]
	v_pk_add_f32 v[108:109], v[110:111], v[92:93]
	v_pk_add_f32 v[110:111], v[126:127], v[102:103]
	v_pk_add_f32 v[114:115], v[116:117], v[110:111]
	v_pk_add_f32 v[122:123], v[130:131], v[112:113]
	v_pk_add_f32 v[116:117], v[120:121], v[122:123]
	v_pk_add_f32 v[126:127], v[134:135], v[128:129]
	v_pk_add_f32 v[120:121], v[136:137], v[126:127]
	v_mul_f32_e64 v140, v44, v22
	v_mul_f32_e64 v141, v45, v22
	v_mul_f32_e64 v142, v108, v22
	v_fma_f32 v29, v109, v22, v26
	v_mul_f32_e64 v52, v114, v22
	v_mul_f32_e64 v130, v115, v22
	v_fma_f32 v131, v116, v22, v26
	v_mul_f32_e64 v134, v117, v22
	v_fma_f32 v135, v120, v22, v26
	v_fma_f32 v29, -v140, v140, v29
	v_fma_f32 v52, -v140, v141, v52
	v_fma_f32 v130, -v140, v142, v130
	v_fma_f32 v131, -v141, v141, v131
	v_fma_f32 v134, -v141, v142, v134
	v_fma_f32 v135, -v142, v142, v135
	v_mul_f32_e64 v136, v134, v134
	v_mul_f32_e64 v137, v52, v135
	v_mul_f32_e64 v152, v130, v131
	v_mul_f32_e64 v153, v130, v130
	v_mul_f32_e64 v154, v29, v134
	v_mul_f32_e64 v155, v52, v52
	v_fma_f32 v136, v131, v135, -v136
	v_fma_f32 v137, v130, v134, -v137
	v_fma_f32 v152, v52, v134, -v152
	v_fma_f32 v153, v29, v135, -v153
	v_fma_f32 v154, v52, v130, -v154
	v_fma_f32 v155, v29, v131, -v155
	v_mul_f32_e64 v158, v29, v136
	v_fma_f32 v158, v52, v137, v158
	v_fma_f32 v158, v130, v152, v158
	v_rcp_f32_e32 v158, v158
	v_cmp_ne_u32_e64 vcc, s37, v16
	v_mul_f32_e64 v158, v158, v22
	v_cndmask_b32_e64 v158, 0, v158, s[30:31]
	v_cndmask_b32_e64 v29, 0, v18, vcc
	v_cndmask_b32_e64 v149, 0, v22, s[30:31]
	v_mul_f32_e64 v143, v136, v158
	v_mul_f32_e64 v144, v137, v158
	v_mul_f32_e64 v145, v152, v158
	v_mul_f32_e64 v146, v153, v158
	v_mul_f32_e64 v147, v154, v158
	v_mul_f32_e64 v148, v155, v158
	v_add_f32_e64 v150, v121, v29
	v_mov_b32_e32 v151, v16
	ds_write_b128 v23, v[140:143]
	ds_write_b128 v23, v[144:147] offset:1024
	ds_write_b128 v23, v[148:151] offset:2048
	v_mov_b32_dpp v114, v4 wave_shr:1 row_mask:0xf bank_mask:0xf bound_ctrl:1
	v_mov_b32_dpp v115, v5 wave_shr:1 row_mask:0xf bank_mask:0xf bound_ctrl:1
	v_mov_b32_dpp v130, v4 wave_shl:1 row_mask:0xf bank_mask:0xf bound_ctrl:1
	v_mov_b32_dpp v131, v5 wave_shl:1 row_mask:0xf bank_mask:0xf bound_ctrl:1
	v_pk_mul_f32 v[44:45], v[4:5], v[8:9] op_sel_hi:[1,0]
	v_pk_mul_f32 v[108:109], v[4:5], v[8:9] op_sel:[0,1]
	v_pk_mul_f32 v[116:117], v[4:5], v[10:11] op_sel_hi:[1,0]
	v_pk_add_f32 v[120:121], v[4:5], v[114:115]
	v_pk_fma_f32 v[44:45], v[114:115], v[80:81], v[44:45] op_sel_hi:[1,0,1]
	v_pk_fma_f32 v[108:109], v[114:115], v[80:81], v[108:109] op_sel:[0,1,0]
	v_pk_fma_f32 v[116:117], v[114:115], v[82:83], v[116:117] op_sel_hi:[1,0,1]
	v_pk_add_f32 v[120:121], v[120:121], v[130:131]
	v_pk_fma_f32 v[44:45], v[130:131], v[84:85], v[44:45] op_sel_hi:[1,0,1]
	v_pk_fma_f32 v[108:109], v[130:131], v[84:85], v[108:109] op_sel:[0,1,0]
	v_pk_fma_f32 v[116:117], v[130:131], v[86:87], v[116:117] op_sel_hi:[1,0,1]
	s_waitcnt lgkmcnt(0)
	s_barrier
	v_pk_add_f32 v[114:115], v[138:139], v[120:121]
	v_pk_add_f32 v[130:131], v[156:157], v[114:115]
	v_pk_add_f32 v[134:135], v[54:55], v[44:45]
	v_pk_add_f32 v[136:137], v[88:89], v[134:135]
	v_pk_add_f32 v[54:55], v[90:91], v[108:109]
	v_pk_add_f32 v[88:89], v[124:125], v[54:55]
	v_pk_add_f32 v[90:91], v[118:119], v[116:117]
	v_pk_add_f32 v[124:125], v[132:133], v[90:91]
	v_pk_fma_f32 v[136:137], v[140:141], v[130:131], v[136:137] op_sel_hi:[0,1,1] neg_lo:[1,0,0] neg_hi:[1,0,0]
	v_pk_fma_f32 v[88:89], v[140:141], v[130:131], v[88:89] op_sel:[1,0,0] neg_lo:[1,0,0] neg_hi:[1,0,0]
	v_pk_fma_f32 v[124:125], v[142:143], v[130:131], v[124:125] op_sel_hi:[0,1,1] neg_lo:[1,0,0] neg_hi:[1,0,0]
	v_pk_mul_f32 v[118:119], v[142:143], v[136:137] op_sel:[1,0]
	v_pk_mul_f32 v[138:139], v[144:145], v[136:137] op_sel_hi:[0,1]
	v_pk_mul_f32 v[154:155], v[144:145], v[136:137] op_sel:[1,0]
	v_pk_fma_f32 v[118:119], v[144:145], v[88:89], v[118:119] op_sel_hi:[0,1,1]
	v_pk_fma_f32 v[138:139], v[146:147], v[88:89], v[138:139] op_sel_hi:[0,1,1]
	v_pk_fma_f32 v[154:155], v[146:147], v[88:89], v[154:155] op_sel:[1,0,0]
	v_pk_fma_f32 v[118:119], v[144:145], v[124:125], v[118:119] op_sel:[1,0,0]
	v_pk_fma_f32 v[138:139], v[146:147], v[124:125], v[138:139] op_sel:[1,0,0]
	v_pk_fma_f32 v[154:155], v[148:149], v[124:125], v[154:155] op_sel_hi:[0,1,1]
	v_pk_mul_f32 v[132:133], v[140:141], v[118:119] op_sel_hi:[0,1]
	v_pk_fma_f32 v[132:133], v[140:141], v[138:139], v[132:133] op_sel:[1,0,0]
	v_pk_fma_f32 v[132:133], v[142:143], v[154:155], v[132:133] op_sel_hi:[0,1,1]
	v_pk_fma_f32 v[132:133], v[148:149], v[130:131], v[132:133] op_sel:[1,0,0] neg_lo:[0,0,1] neg_hi:[0,0,1]
	v_cmp_eq_u32_e64 s[10:11], 6, v151
	v_cmp_eq_u32_e64 s[14:15], 7, v151
	v_pk_add_f32 v[88:89], v[48:49], v[118:119]
	v_pk_add_f32 v[124:125], v[38:39], v[88:89]
	v_pk_add_f32 v[48:49], v[56:57], v[138:139]
	v_pk_add_f32 v[38:39], v[46:47], v[48:49]
	v_pk_add_f32 v[56:57], v[68:69], v[154:155]
	v_pk_add_f32 v[46:47], v[58:59], v[56:57]
	v_pk_add_f32 v[58:59], v[166:167], v[132:133]
	v_pk_add_f32 v[68:69], v[96:97], v[58:59]
	v_pk_fma_f32 v[96:97], v[64:65], v[124:125], v[68:69] op_sel_hi:[0,1,1]
	v_pk_fma_f32 v[136:137], v[104:105], v[124:125], v[68:69] op_sel_hi:[0,1,1]
	v_pk_fma_f32 v[96:97], v[64:65], v[38:39], v[96:97] op_sel:[1,0,0]
	v_pk_fma_f32 v[136:137], v[104:105], v[38:39], v[136:137] op_sel:[1,0,0]
	v_pk_fma_f32 v[96:97], v[66:67], v[46:47], v[96:97] op_sel_hi:[0,1,1]
	v_pk_fma_f32 v[136:137], v[106:107], v[46:47], v[136:137] op_sel_hi:[0,1,1]
	v_pk_fma_f32 v[68:69], v[40:41], v[124:125], v[68:69] op_sel_hi:[0,1,1]
	v_pk_fma_f32 v[68:69], v[40:41], v[38:39], v[68:69] op_sel:[1,0,0]
	v_pk_fma_f32 v[68:69], v[42:43], v[46:47], v[68:69] op_sel_hi:[0,1,1]
	v_cndmask_b32_e64 v130, 0, v18, s[10:11]
	v_cndmask_b32_e64 v131, 0, v18, s[14:15]
	v_add_f32_dpp v68, v96, v68 wave_shl:1 row_mask:0xf bank_mask:0xf bound_ctrl:1
	v_add_f32_dpp v69, v97, v69 wave_shl:1 row_mask:0xf bank_mask:0xf bound_ctrl:1
	s_add_i32 s4, s34, 6
	s_cmpk_lt_i32 s4, 0x201
	s_cselect_b64 s[12:13], s[0:1], 0
	v_add_f32_dpp v68, v136, v68 wave_shr:1 row_mask:0xf bank_mask:0xf bound_ctrl:1
	v_add_f32_dpp v69, v137, v69 wave_shr:1 row_mask:0xf bank_mask:0xf bound_ctrl:1
	v_pk_fma_f32 v[68:69], v[36:37], v[150:151], v[68:69] op_sel_hi:[1,0,1] neg_lo:[0,0,1] neg_hi:[0,0,1]
	v_pk_add_f32 v[68:69], v[68:69], v[130:131] neg_lo:[0,1] neg_hi:[0,1]
	v_pk_mul_f32 v[152:153], v[68:69], v[68:69]
	v_add_f32_e32 v152, v152, v153
	v_cndmask_b32_e64 v153, 0, v152, s[12:13]
	v_add_f32_e32 v1, v1, v153
	s_add_i32 s5, s34, 11
	s_min_i32 s5, s5, 0x200
	s_mul_i32 s6, s5, 0x804
	s_add_i32 s6, s6, s35
	s_add_i32 s7, s6, 0x505014
	s_add_i32 s8, s6, 0x606018
	s_mul_i32 s9, s5, 0x180c
	s_add_i32 s9, s9, s33
	s_add_i32 s4, s34, 12
	s_min_i32 s4, s4, 0x200
	s_mul_i32 s4, s4, 0x804
	s_add_i32 s4, s4, s38
	buffer_load_dword v16, v28, s[20:23], s4 offen nt
	buffer_load_dwordx3 v[40:42], v27, s[24:27], s9 offen nt
	buffer_load_dword v36, v28, s[16:19], s7 offen nt
	buffer_load_dword v37, v28, s[16:19], s8 offen nt
	s_waitcnt vmcnt(8)
	v_mov_b32_dpp v64, v12 wave_shr:1 row_mask:0xf bank_mask:0xf bound_ctrl:1
	v_mov_b32_dpp v65, v13 wave_shr:1 row_mask:0xf bank_mask:0xf bound_ctrl:1
	v_mov_b32_dpp v66, v14 wave_shr:1 row_mask:0xf bank_mask:0xf bound_ctrl:1
	v_mov_b32_dpp v104, v12 wave_shl:1 row_mask:0xf bank_mask:0xf bound_ctrl:1
	v_mov_b32_dpp v105, v13 wave_shl:1 row_mask:0xf bank_mask:0xf bound_ctrl:1
	v_mov_b32_dpp v106, v14 wave_shl:1 row_mask:0xf bank_mask:0xf bound_ctrl:1
	s_add_i32 s4, s34, 10
	s_cmpk_lt_u32 s4, 0x201
	s_cselect_b64 s[12:13], s[40:41], 0
	v_cmp_eq_u32_e64 s[14:15], s37, v2
	s_and_b64 s[14:15], s[14:15], s[12:13]
	v_cndmask_b32_e64 v29, 0, 1, s[14:15]
	v_mul_f32_e64 v38, v12, v12
	v_mul_f32_e64 v39, v12, v13
	v_or_b32_dpp v52, v29, v29 wave_shr:1 row_mask:0xf bank_mask:0xf bound_ctrl:1
	v_mul_f32_e64 v46, v12, v14
	v_or_b32_dpp v52, v29, v52 wave_shl:1 row_mask:0xf bank_mask:0xf bound_ctrl:1
	v_mul_f32_e64 v47, v13, v13
	v_mul_f32_e64 v68, v13, v14
	v_or_b32_dpp v71, v52, v52 wave_shr:1 row_mask:0xf bank_mask:0xf bound_ctrl:1
	v_mul_f32_e64 v69, v14, v14
	s_nop 0
	v_or_b32_dpp v71, v52, v71 wave_shl:1 row_mask:0xf bank_mask:0xf bound_ctrl:1
	v_or3_b32 v29, v71, v98, v99
	v_or3_b32 v29, v29, v53, v70
	s_add_i32 s4, s34, 7
	s_cmpk_lt_u32 s4, 0x1ff
	s_cselect_b64 s[12:13], s[42:43], 0
	v_cmp_ne_u32_e64 s[30:31], 0, v29
	s_and_b64 s[30:31], s[30:31], s[12:13]
	v_cndmask_b32_e64 v29, 0, 1.0, s[30:31]
	v_add_f32_e64 v96, v12, v64
	v_add_f32_e64 v97, v13, v65
	v_add_f32_e64 v124, v14, v66
	v_fma_f32 v38, v64, v64, v38
	v_fma_f32 v39, v64, v65, v39
	v_fma_f32 v46, v64, v66, v46
	v_fma_f32 v47, v65, v65, v47
	v_fma_f32 v68, v65, v66, v68
	v_fma_f32 v69, v66, v66, v69
	v_add_f32_dpp v141, v29, v29 wave_shr:1 row_mask:0xf bank_mask:0xf bound_ctrl:1
	v_add_f32_e64 v96, v96, v104
	v_add_f32_e64 v97, v97, v105
	v_add_f32_e64 v124, v124, v106
	v_fma_f32 v125, v104, v104, v38
	v_fma_f32 v130, v104, v105, v39
	v_fma_f32 v131, v104, v106, v46
	v_fma_f32 v136, v105, v105, v47
	v_fma_f32 v137, v105, v106, v68
	v_fma_f32 v140, v106, v106, v69
	v_add_f32_dpp v141, v29, v141 wave_shl:1 row_mask:0xf bank_mask:0xf bound_ctrl:1
	v_pk_add_f32 v[38:39], v[30:31], v[96:97]
	v_pk_add_f32 v[30:31], v[92:93], v[124:125]
	v_pk_add_f32 v[46:47], v[110:111], v[130:131]
	v_pk_add_f32 v[68:69], v[122:123], v[136:137]
	v_pk_add_f32 v[92:93], v[126:127], v[140:141]
	v_mul_f32_e64 v144, v38, v22
	v_mul_f32_e64 v145, v39, v22
	v_mul_f32_e64 v146, v30, v22
	v_fma_f32 v29, v31, v22, v26
	v_mul_f32_e64 v52, v46, v22
	v_mul_f32_e64 v110, v47, v22
	v_fma_f32 v111, v68, v22, v26
	v_mul_f32_e64 v122, v69, v22
	v_fma_f32 v123, v92, v22, v26
	v_fma_f32 v29, -v144, v144, v29
	v_fma_f32 v52, -v144, v145, v52
	v_fma_f32 v110, -v144, v146, v110
	v_fma_f32 v111, -v145, v145, v111
	v_fma_f32 v122, -v145, v146, v122
	v_fma_f32 v123, -v146, v146, v123
	v_mul_f32_e64 v126, v122, v122
	v_mul_f32_e64 v127, v52, v123
	v_mul_f32_e64 v142, v110, v111
	v_mul_f32_e64 v143, v110, v110
	v_mul_f32_e64 v152, v29, v122
	v_mul_f32_e64 v153, v52, v52
	v_fma_f32 v126, v111, v123, -v126
	v_fma_f32 v127, v110, v122, -v127
	v_fma_f32 v142, v52, v122, -v142
	v_fma_f32 v143, v29, v123, -v143
	v_fma_f32 v152, v52, v110, -v152
	v_fma_f32 v153, v29, v111, -v153
	v_mul_f32_e64 v160, v29, v126
	v_fma_f32 v160, v52, v127, v160
	v_fma_f32 v160, v110, v142, v160
	v_rcp_f32_e32 v160, v160
	v_cmp_ne_u32_e64 vcc, s37, v25
	v_mul_f32_e64 v160, v160, v22
	v_cndmask_b32_e64 v160, 0, v160, s[30:31]
	v_cndmask_b32_e64 v29, 0, v18, vcc
	v_cndmask_b32_e64 v157, 0, v22, s[30:31]
	v_mul_f32_e64 v147, v126, v160
	v_mul_f32_e64 v148, v127, v160
	v_mul_f32_e64 v149, v142, v160
	v_mul_f32_e64 v150, v143, v160
	v_mul_f32_e64 v151, v152, v160
	v_mul_f32_e64 v156, v153, v160
	v_add_f32_e64 v158, v93, v29
	v_mov_b32_e32 v159, v25
	ds_write_b128 v23, v[144:147] offset:3072
	ds_write_b128 v23, v[148:151] offset:4096
	ds_write_b128 v23, v[156:159] offset:5120
	v_mov_b32_dpp v68, v6 wave_shr:1 row_mask:0xf bank_mask:0xf bound_ctrl:1
	v_mov_b32_dpp v69, v7 wave_shr:1 row_mask:0xf bank_mask:0xf bound_ctrl:1
	v_mov_b32_dpp v92, v6 wave_shl:1 row_mask:0xf bank_mask:0xf bound_ctrl:1
	v_mov_b32_dpp v93, v7 wave_shl:1 row_mask:0xf bank_mask:0xf bound_ctrl:1
	v_pk_mul_f32 v[30:31], v[6:7], v[12:13] op_sel_hi:[1,0]
	v_pk_mul_f32 v[38:39], v[6:7], v[12:13] op_sel:[0,1]
	v_pk_mul_f32 v[46:47], v[6:7], v[14:15] op_sel_hi:[1,0]
	v_pk_add_f32 v[110:111], v[6:7], v[68:69]
	v_pk_fma_f32 v[30:31], v[68:69], v[64:65], v[30:31] op_sel_hi:[1,0,1]
	v_pk_fma_f32 v[38:39], v[68:69], v[64:65], v[38:39] op_sel:[0,1,0]
	v_pk_fma_f32 v[46:47], v[68:69], v[66:67], v[46:47] op_sel_hi:[1,0,1]
	v_pk_add_f32 v[110:111], v[110:111], v[92:93]
	v_pk_fma_f32 v[30:31], v[92:93], v[104:105], v[30:31] op_sel_hi:[1,0,1]
	v_pk_fma_f32 v[38:39], v[92:93], v[104:105], v[38:39] op_sel:[0,1,0]
	v_pk_fma_f32 v[46:47], v[92:93], v[106:107], v[46:47] op_sel_hi:[1,0,1]
	s_waitcnt lgkmcnt(0)
	s_barrier
	v_pk_add_f32 v[68:69], v[114:115], v[110:111]
	v_pk_add_f32 v[114:115], v[134:135], v[30:31]
	v_pk_add_f32 v[122:123], v[54:55], v[38:39]
	v_pk_add_f32 v[54:55], v[90:91], v[46:47]
	v_pk_fma_f32 v[114:115], v[144:145], v[68:69], v[114:115] op_sel_hi:[0,1,1] neg_lo:[1,0,0] neg_hi:[1,0,0]
	v_pk_fma_f32 v[122:123], v[144:145], v[68:69], v[122:123] op_sel:[1,0,0] neg_lo:[1,0,0] neg_hi:[1,0,0]
	v_pk_fma_f32 v[54:55], v[146:147], v[68:69], v[54:55] op_sel_hi:[0,1,1] neg_lo:[1,0,0] neg_hi:[1,0,0]
	v_pk_mul_f32 v[92:93], v[146:147], v[114:115] op_sel:[1,0]
	v_pk_mul_f32 v[152:153], v[148:149], v[114:115] op_sel_hi:[0,1]
	v_pk_mul_f32 v[160:161], v[148:149], v[114:115] op_sel:[1,0]
	v_pk_fma_f32 v[92:93], v[148:149], v[122:123], v[92:93] op_sel_hi:[0,1,1]
	v_pk_fma_f32 v[152:153], v[150:151], v[122:123], v[152:153] op_sel_hi:[0,1,1]
	v_pk_fma_f32 v[160:161], v[150:151], v[122:123], v[160:161] op_sel:[1,0,0]
	v_pk_fma_f32 v[92:93], v[148:149], v[54:55], v[92:93] op_sel:[1,0,0]
	v_pk_fma_f32 v[152:153], v[150:151], v[54:55], v[152:153] op_sel:[1,0,0]
	v_pk_fma_f32 v[160:161], v[156:157], v[54:55], v[160:161] op_sel_hi:[0,1,1]
	v_pk_mul_f32 v[90:91], v[144:145], v[92:93] op_sel_hi:[0,1]
	v_pk_fma_f32 v[90:91], v[144:145], v[152:153], v[90:91] op_sel:[1,0,0]
	v_pk_fma_f32 v[90:91], v[146:147], v[160:161], v[90:91] op_sel_hi:[0,1,1]
	v_pk_fma_f32 v[90:91], v[156:157], v[68:69], v[90:91] op_sel:[1,0,0] neg_lo:[0,0,1] neg_hi:[0,0,1]
	v_cmp_eq_u32_e64 s[10:11], 6, v159
	v_cmp_eq_u32_e64 s[14:15], 7, v159
	v_pk_add_f32 v[54:55], v[88:89], v[92:93]
	v_pk_add_f32 v[68:69], v[48:49], v[152:153]
	v_pk_add_f32 v[48:49], v[56:57], v[160:161]
	v_pk_add_f32 v[114:115], v[58:59], v[90:91]
	v_pk_fma_f32 v[58:59], v[60:61], v[54:55], v[114:115] op_sel_hi:[0,1,1]
	v_pk_fma_f32 v[122:123], v[76:77], v[54:55], v[114:115] op_sel_hi:[0,1,1]
	v_pk_fma_f32 v[58:59], v[60:61], v[68:69], v[58:59] op_sel:[1,0,0]
	v_pk_fma_f32 v[122:123], v[76:77], v[68:69], v[122:123] op_sel:[1,0,0]
	v_pk_fma_f32 v[58:59], v[62:63], v[48:49], v[58:59] op_sel_hi:[0,1,1]
	v_pk_fma_f32 v[122:123], v[78:79], v[48:49], v[122:123] op_sel_hi:[0,1,1]
	v_pk_fma_f32 v[114:115], v[72:73], v[54:55], v[114:115] op_sel_hi:[0,1,1]
	v_pk_fma_f32 v[114:115], v[72:73], v[68:69], v[114:115] op_sel:[1,0,0]
	v_pk_fma_f32 v[114:115], v[74:75], v[48:49], v[114:115] op_sel_hi:[0,1,1]
	v_cndmask_b32_e64 v56, 0, v18, s[10:11]
	v_cndmask_b32_e64 v57, 0, v18, s[14:15]
	v_add_f32_dpp v114, v58, v114 wave_shl:1 row_mask:0xf bank_mask:0xf bound_ctrl:1
	v_add_f32_dpp v115, v59, v115 wave_shl:1 row_mask:0xf bank_mask:0xf bound_ctrl:1
	s_add_i32 s4, s34, 7
	s_cmpk_lt_i32 s4, 0x201
	s_cselect_b64 s[12:13], s[0:1], 0
	v_add_f32_dpp v114, v122, v114 wave_shr:1 row_mask:0xf bank_mask:0xf bound_ctrl:1
	v_add_f32_dpp v115, v123, v115 wave_shr:1 row_mask:0xf bank_mask:0xf bound_ctrl:1
	v_pk_fma_f32 v[114:115], v[50:51], v[158:159], v[114:115] op_sel_hi:[1,0,1] neg_lo:[0,0,1] neg_hi:[0,0,1]
	v_pk_add_f32 v[114:115], v[114:115], v[56:57] neg_lo:[0,1] neg_hi:[0,1]
	v_pk_mul_f32 v[88:89], v[114:115], v[114:115]
	v_add_f32_e32 v88, v88, v89
	v_cndmask_b32_e64 v89, 0, v88, s[12:13]
	v_add_f32_e32 v1, v1, v89
	s_waitcnt vmcnt(4)
	v_mov_b32_dpp v48, v32 wave_shr:1 row_mask:0xf bank_mask:0xf bound_ctrl:1
	v_mov_b32_dpp v49, v33 wave_shr:1 row_mask:0xf bank_mask:0xf bound_ctrl:1
	v_mov_b32_dpp v50, v34 wave_shr:1 row_mask:0xf bank_mask:0xf bound_ctrl:1
	v_mov_b32_dpp v56, v32 wave_shl:1 row_mask:0xf bank_mask:0xf bound_ctrl:1
	v_mov_b32_dpp v57, v33 wave_shl:1 row_mask:0xf bank_mask:0xf bound_ctrl:1
	v_mov_b32_dpp v58, v34 wave_shl:1 row_mask:0xf bank_mask:0xf bound_ctrl:1
	s_add_i32 s4, s34, 11
	s_cmpk_lt_u32 s4, 0x201
	s_cselect_b64 s[12:13], s[40:41], 0
	v_cmp_eq_u32_e64 s[14:15], s37, v3
	s_and_b64 s[14:15], s[14:15], s[12:13]
	v_cndmask_b32_e64 v25, 0, 1, s[14:15]
	v_mul_f32_e64 v54, v32, v32
	v_mul_f32_e64 v55, v32, v33
	v_or_b32_dpp v29, v25, v25 wave_shr:1 row_mask:0xf bank_mask:0xf bound_ctrl:1
	v_mul_f32_e64 v60, v32, v34
	v_or_b32_dpp v29, v25, v29 wave_shl:1 row_mask:0xf bank_mask:0xf bound_ctrl:1
	v_mul_f32_e64 v61, v33, v33
	v_mul_f32_e64 v62, v33, v34
	v_or_b32_dpp v52, v29, v29 wave_shr:1 row_mask:0xf bank_mask:0xf bound_ctrl:1
	v_mul_f32_e64 v63, v34, v34
	s_nop 0
	v_or_b32_dpp v52, v29, v52 wave_shl:1 row_mask:0xf bank_mask:0xf bound_ctrl:1
	v_or3_b32 v25, v52, v71, v98
	v_or3_b32 v25, v25, v99, v53
	s_add_i32 s4, s34, 8
	s_cmpk_lt_u32 s4, 0x1ff
	s_cselect_b64 s[12:13], s[42:43], 0
	v_cmp_ne_u32_e64 s[30:31], 0, v25
	s_and_b64 s[30:31], s[30:31], s[12:13]
	v_cndmask_b32_e64 v25, 0, 1.0, s[30:31]
	v_add_f32_e64 v68, v32, v48
	v_add_f32_e64 v69, v33, v49
	v_add_f32_e64 v72, v34, v50
	v_fma_f32 v54, v48, v48, v54
	v_fma_f32 v55, v48, v49, v55
	v_fma_f32 v60, v48, v50, v60
	v_fma_f32 v61, v49, v49, v61
	v_fma_f32 v62, v49, v50, v62
	v_fma_f32 v63, v50, v50, v63
	v_add_f32_dpp v79, v25, v25 wave_shr:1 row_mask:0xf bank_mask:0xf bound_ctrl:1
	v_add_f32_e64 v68, v68, v56
	v_add_f32_e64 v69, v69, v57
	v_add_f32_e64 v72, v72, v58
	v_fma_f32 v73, v56, v56, v54
	v_fma_f32 v74, v56, v57, v55
	v_fma_f32 v75, v56, v58, v60
	v_fma_f32 v76, v57, v57, v61
	v_fma_f32 v77, v57, v58, v62
	v_fma_f32 v78, v58, v58, v63
	v_add_f32_dpp v79, v25, v79 wave_shl:1 row_mask:0xf bank_mask:0xf bound_ctrl:1
	v_pk_add_f32 v[60:61], v[96:97], v[68:69]
	v_pk_add_f32 v[54:55], v[94:95], v[60:61]
	v_pk_add_f32 v[62:63], v[124:125], v[72:73]
	v_pk_add_f32 v[88:89], v[100:101], v[62:63]
	v_pk_add_f32 v[96:97], v[130:131], v[74:75]
	v_pk_add_f32 v[94:95], v[102:103], v[96:97]
	v_pk_add_f32 v[102:103], v[136:137], v[76:77]
	v_pk_add_f32 v[100:101], v[112:113], v[102:103]
	v_pk_add_f32 v[114:115], v[140:141], v[78:79]
	v_pk_add_f32 v[112:113], v[128:129], v[114:115]
	v_mul_f32_e64 v124, v54, v22
	v_mul_f32_e64 v125, v55, v22
	v_mul_f32_e64 v126, v88, v22
	v_fma_f32 v25, v89, v22, v26
	v_mul_f32_e64 v29, v94, v22
	v_mul_f32_e64 v70, v95, v22
	v_fma_f32 v122, v100, v22, v26
	v_mul_f32_e64 v123, v101, v22
	v_fma_f32 v134, v112, v22, v26
	v_fma_f32 v25, -v124, v124, v25
	v_fma_f32 v29, -v124, v125, v29
	v_fma_f32 v70, -v124, v126, v70
	v_fma_f32 v122, -v125, v125, v122
	v_fma_f32 v123, -v125, v126, v123
	v_fma_f32 v134, -v126, v126, v134
	v_mul_f32_e64 v135, v123, v123
	v_mul_f32_e64 v136, v29, v134
	v_mul_f32_e64 v137, v70, v122
	v_mul_f32_e64 v144, v70, v70
	v_mul_f32_e64 v145, v25, v123
	v_mul_f32_e64 v146, v29, v29
	v_fma_f32 v135, v122, v134, -v135
	v_fma_f32 v136, v70, v123, -v136
	v_fma_f32 v137, v29, v123, -v137
	v_fma_f32 v144, v25, v134, -v144
	v_fma_f32 v145, v29, v70, -v145
	v_fma_f32 v146, v25, v122, -v146
	v_mul_f32_e64 v147, v25, v135
	v_fma_f32 v147, v29, v136, v147
	v_fma_f32 v147, v70, v137, v147
	v_rcp_f32_e32 v147, v147
	v_cmp_ne_u32_e64 vcc, s37, v24
	v_mul_f32_e64 v147, v147, v22
	v_cndmask_b32_e64 v147, 0, v147, s[30:31]
	v_cndmask_b32_e64 v25, 0, v18, vcc
	v_cndmask_b32_e64 v141, 0, v22, s[30:31]
	v_mul_f32_e64 v127, v135, v147
	v_mul_f32_e64 v128, v136, v147
	v_mul_f32_e64 v129, v137, v147
	v_mul_f32_e64 v130, v144, v147
	v_mul_f32_e64 v131, v145, v147
	v_mul_f32_e64 v140, v146, v147
	v_add_f32_e64 v142, v113, v25
	v_mov_b32_e32 v143, v24
	ds_write_b128 v23, v[124:127]
	ds_write_b128 v23, v[128:131] offset:1024
	ds_write_b128 v23, v[140:143] offset:2048
	v_mov_b32_dpp v54, v20 wave_shr:1 row_mask:0xf bank_mask:0xf bound_ctrl:1
	v_mov_b32_dpp v55, v21 wave_shr:1 row_mask:0xf bank_mask:0xf bound_ctrl:1
	v_mov_b32_dpp v94, v20 wave_shl:1 row_mask:0xf bank_mask:0xf bound_ctrl:1
	v_mov_b32_dpp v95, v21 wave_shl:1 row_mask:0xf bank_mask:0xf bound_ctrl:1
	v_pk_mul_f32 v[24:25], v[20:21], v[32:33] op_sel_hi:[1,0]
	v_pk_mul_f32 v[88:89], v[20:21], v[32:33] op_sel:[0,1]
	v_pk_mul_f32 v[100:101], v[20:21], v[34:35] op_sel_hi:[1,0]
	v_pk_add_f32 v[112:113], v[20:21], v[54:55]
	v_pk_fma_f32 v[24:25], v[54:55], v[48:49], v[24:25] op_sel_hi:[1,0,1]
	v_pk_fma_f32 v[88:89], v[54:55], v[48:49], v[88:89] op_sel:[0,1,0]
	v_pk_fma_f32 v[100:101], v[54:55], v[50:51], v[100:101] op_sel_hi:[1,0,1]
	v_pk_add_f32 v[112:113], v[112:113], v[94:95]
	v_pk_fma_f32 v[24:25], v[94:95], v[56:57], v[24:25] op_sel_hi:[1,0,1]
	v_pk_fma_f32 v[88:89], v[94:95], v[56:57], v[88:89] op_sel:[0,1,0]
	v_pk_fma_f32 v[100:101], v[94:95], v[58:59], v[100:101] op_sel_hi:[1,0,1]
	s_waitcnt lgkmcnt(0)
	s_barrier
	v_pk_add_f32 v[54:55], v[110:111], v[112:113]
	v_pk_add_f32 v[94:95], v[120:121], v[54:55]
	v_pk_add_f32 v[110:111], v[30:31], v[24:25]
	v_pk_add_f32 v[120:121], v[44:45], v[110:111]
	v_pk_add_f32 v[30:31], v[38:39], v[88:89]
	v_pk_add_f32 v[44:45], v[108:109], v[30:31]
	v_pk_add_f32 v[38:39], v[46:47], v[100:101]
	v_pk_add_f32 v[108:109], v[116:117], v[38:39]
	v_pk_fma_f32 v[120:121], v[124:125], v[94:95], v[120:121] op_sel_hi:[0,1,1] neg_lo:[1,0,0] neg_hi:[1,0,0]
	v_pk_fma_f32 v[44:45], v[124:125], v[94:95], v[44:45] op_sel:[1,0,0] neg_lo:[1,0,0] neg_hi:[1,0,0]
	v_pk_fma_f32 v[108:109], v[126:127], v[94:95], v[108:109] op_sel_hi:[0,1,1] neg_lo:[1,0,0] neg_hi:[1,0,0]
	v_pk_mul_f32 v[46:47], v[126:127], v[120:121] op_sel:[1,0]
	v_pk_mul_f32 v[122:123], v[128:129], v[120:121] op_sel_hi:[0,1]
	v_pk_mul_f32 v[134:135], v[128:129], v[120:121] op_sel:[1,0]
	v_pk_fma_f32 v[46:47], v[128:129], v[44:45], v[46:47] op_sel_hi:[0,1,1]
	v_pk_fma_f32 v[122:123], v[130:131], v[44:45], v[122:123] op_sel_hi:[0,1,1]
	v_pk_fma_f32 v[134:135], v[130:131], v[44:45], v[134:135] op_sel:[1,0,0]
	v_pk_fma_f32 v[46:47], v[128:129], v[108:109], v[46:47] op_sel:[1,0,0]
	v_pk_fma_f32 v[122:123], v[130:131], v[108:109], v[122:123] op_sel:[1,0,0]
	v_pk_fma_f32 v[134:135], v[140:141], v[108:109], v[134:135] op_sel_hi:[0,1,1]
	v_pk_mul_f32 v[116:117], v[124:125], v[46:47] op_sel_hi:[0,1]
	v_pk_fma_f32 v[116:117], v[124:125], v[122:123], v[116:117] op_sel:[1,0,0]
	v_pk_fma_f32 v[116:117], v[126:127], v[134:135], v[116:117] op_sel_hi:[0,1,1]
	v_pk_fma_f32 v[116:117], v[140:141], v[94:95], v[116:117] op_sel:[1,0,0] neg_lo:[0,0,1] neg_hi:[0,0,1]
	v_cmp_eq_u32_e64 s[10:11], 6, v143
	v_cmp_eq_u32_e64 s[14:15], 7, v143
	v_pk_add_f32 v[44:45], v[92:93], v[46:47]
	v_pk_add_f32 v[94:95], v[118:119], v[44:45]
	v_pk_add_f32 v[92:93], v[152:153], v[122:123]
	v_pk_add_f32 v[108:109], v[138:139], v[92:93]
	v_pk_add_f32 v[120:121], v[160:161], v[134:135]
	v_pk_add_f32 v[118:119], v[154:155], v[120:121]
	v_pk_add_f32 v[138:139], v[90:91], v[116:117]
	v_pk_add_f32 v[136:137], v[132:133], v[138:139]
	v_pk_fma_f32 v[132:133], v[80:81], v[94:95], v[136:137] op_sel_hi:[0,1,1]
	v_pk_fma_f32 v[144:145], v[84:85], v[94:95], v[136:137] op_sel_hi:[0,1,1]
	v_pk_fma_f32 v[132:133], v[80:81], v[108:109], v[132:133] op_sel:[1,0,0]
	v_pk_fma_f32 v[144:145], v[84:85], v[108:109], v[144:145] op_sel:[1,0,0]
	v_pk_fma_f32 v[132:133], v[82:83], v[118:119], v[132:133] op_sel_hi:[0,1,1]
	v_pk_fma_f32 v[144:145], v[86:87], v[118:119], v[144:145] op_sel_hi:[0,1,1]
	v_pk_fma_f32 v[136:137], v[8:9], v[94:95], v[136:137] op_sel_hi:[0,1,1]
	v_pk_fma_f32 v[136:137], v[8:9], v[108:109], v[136:137] op_sel:[1,0,0]
	v_pk_fma_f32 v[136:137], v[10:11], v[118:119], v[136:137] op_sel_hi:[0,1,1]
	v_cndmask_b32_e64 v90, 0, v18, s[10:11]
	v_cndmask_b32_e64 v91, 0, v18, s[14:15]
	v_add_f32_dpp v136, v132, v136 wave_shl:1 row_mask:0xf bank_mask:0xf bound_ctrl:1
	v_add_f32_dpp v137, v133, v137 wave_shl:1 row_mask:0xf bank_mask:0xf bound_ctrl:1
	s_add_i32 s4, s34, 8
	s_cmpk_lt_i32 s4, 0x201
	s_cselect_b64 s[12:13], s[0:1], 0
	v_add_f32_dpp v136, v144, v136 wave_shr:1 row_mask:0xf bank_mask:0xf bound_ctrl:1
	v_add_f32_dpp v137, v145, v137 wave_shr:1 row_mask:0xf bank_mask:0xf bound_ctrl:1
	v_pk_fma_f32 v[136:137], v[4:5], v[142:143], v[136:137] op_sel_hi:[1,0,1] neg_lo:[0,0,1] neg_hi:[0,0,1]
	v_pk_add_f32 v[136:137], v[136:137], v[90:91] neg_lo:[0,1] neg_hi:[0,1]
	v_pk_mul_f32 v[146:147], v[136:137], v[136:137]
	v_add_f32_e32 v146, v146, v147
	v_cndmask_b32_e64 v147, 0, v146, s[12:13]
	v_add_f32_e32 v1, v1, v147
	s_waitcnt vmcnt(0)
	v_mov_b32_dpp v8, v40 wave_shr:1 row_mask:0xf bank_mask:0xf bound_ctrl:1
	v_mov_b32_dpp v9, v41 wave_shr:1 row_mask:0xf bank_mask:0xf bound_ctrl:1
	v_mov_b32_dpp v10, v42 wave_shr:1 row_mask:0xf bank_mask:0xf bound_ctrl:1
	v_mov_b32_dpp v80, v40 wave_shl:1 row_mask:0xf bank_mask:0xf bound_ctrl:1
	v_mov_b32_dpp v81, v41 wave_shl:1 row_mask:0xf bank_mask:0xf bound_ctrl:1
	v_mov_b32_dpp v82, v42 wave_shl:1 row_mask:0xf bank_mask:0xf bound_ctrl:1
	s_add_i32 s4, s34, 12
	s_cmpk_lt_u32 s4, 0x201
	s_cselect_b64 s[12:13], s[40:41], 0
	v_cmp_eq_u32_e64 s[14:15], s37, v16
	s_and_b64 s[14:15], s[14:15], s[12:13]
	v_cndmask_b32_e64 v29, 0, 1, s[14:15]
	v_mul_f32_e64 v4, v40, v40
	v_mul_f32_e64 v5, v40, v41
	v_or_b32_dpp v53, v29, v29 wave_shr:1 row_mask:0xf bank_mask:0xf bound_ctrl:1
	v_mul_f32_e64 v84, v40, v42
	v_or_b32_dpp v53, v29, v53 wave_shl:1 row_mask:0xf bank_mask:0xf bound_ctrl:1
	v_mul_f32_e64 v85, v41, v41
	v_mul_f32_e64 v86, v41, v42
	v_or_b32_dpp v70, v53, v53 wave_shr:1 row_mask:0xf bank_mask:0xf bound_ctrl:1
	v_mul_f32_e64 v87, v42, v42
	s_nop 0
	v_or_b32_dpp v70, v53, v70 wave_shl:1 row_mask:0xf bank_mask:0xf bound_ctrl:1
	v_or3_b32 v29, v70, v52, v71
	v_or3_b32 v29, v29, v98, v99
	s_add_i32 s4, s34, 9
	s_cmpk_lt_u32 s4, 0x1ff
	s_cselect_b64 s[12:13], s[42:43], 0
	v_cmp_ne_u32_e64 s[30:31], 0, v29
	s_and_b64 s[30:31], s[30:31], s[12:13]
	v_cndmask_b32_e64 v29, 0, 1.0, s[30:31]
	v_add_f32_e64 v90, v40, v8
	v_add_f32_e64 v91, v41, v9
	v_add_f32_e64 v94, v42, v10
	v_fma_f32 v4, v8, v8, v4
	v_fma_f32 v5, v8, v9, v5
	v_fma_f32 v84, v8, v10, v84
	v_fma_f32 v85, v9, v9, v85
	v_fma_f32 v86, v9, v10, v86
	v_fma_f32 v87, v10, v10, v87
	v_add_f32_dpp v125, v29, v29 wave_shr:1 row_mask:0xf bank_mask:0xf bound_ctrl:1
	v_add_f32_e64 v90, v90, v80
	v_add_f32_e64 v91, v91, v81
	v_add_f32_e64 v94, v94, v82
	v_fma_f32 v95, v80, v80, v4
	v_fma_f32 v108, v80, v81, v5
	v_fma_f32 v109, v80, v82, v84
	v_fma_f32 v118, v81, v81, v85
	v_fma_f32 v119, v81, v82, v86
	v_fma_f32 v124, v82, v82, v87
	v_add_f32_dpp v125, v29, v125 wave_shl:1 row_mask:0xf bank_mask:0xf bound_ctrl:1
	v_pk_add_f32 v[4:5], v[60:61], v[90:91]
	v_pk_add_f32 v[60:61], v[62:63], v[94:95]
	v_pk_add_f32 v[62:63], v[96:97], v[108:109]
	v_pk_add_f32 v[84:85], v[102:103], v[118:119]
	v_pk_add_f32 v[86:87], v[114:115], v[124:125]
	v_mul_f32_e64 v128, v4, v22
	v_mul_f32_e64 v129, v5, v22
	v_mul_f32_e64 v130, v60, v22
	v_fma_f32 v29, v61, v22, v26
	v_mul_f32_e64 v53, v62, v22
	v_mul_f32_e64 v96, v63, v22
	v_fma_f32 v97, v84, v22, v26
	v_mul_f32_e64 v102, v85, v22
	v_fma_f32 v103, v86, v22, v26
	v_fma_f32 v29, -v128, v128, v29
	v_fma_f32 v53, -v128, v129, v53
	v_fma_f32 v96, -v128, v130, v96
	v_fma_f32 v97, -v129, v129, v97
	v_fma_f32 v102, -v129, v130, v102
	v_fma_f32 v103, -v130, v130, v103
	v_mul_f32_e64 v114, v102, v102
	v_mul_f32_e64 v115, v53, v103
	v_mul_f32_e64 v126, v96, v97
	v_mul_f32_e64 v127, v96, v96
	v_mul_f32_e64 v132, v29, v102
	v_mul_f32_e64 v133, v53, v53
	v_fma_f32 v114, v97, v103, -v114
	v_fma_f32 v115, v96, v102, -v115
	v_fma_f32 v126, v53, v102, -v126
	v_fma_f32 v127, v29, v103, -v127
	v_fma_f32 v132, v53, v96, -v132
	v_fma_f32 v133, v29, v97, -v133
	v_mul_f32_e64 v136, v29, v114
	v_fma_f32 v136, v53, v115, v136
	v_fma_f32 v136, v96, v126, v136
	v_rcp_f32_e32 v136, v136
	v_cmp_ne_u32_e64 vcc, s37, v17
	v_mul_f32_e64 v136, v136, v22
	v_cndmask_b32_e64 v136, 0, v136, s[30:31]
	v_cndmask_b32_e64 v29, 0, v18, vcc
	v_cndmask_b32_e64 v145, 0, v22, s[30:31]
	v_mul_f32_e64 v131, v114, v136
	v_mul_f32_e64 v140, v115, v136
	v_mul_f32_e64 v141, v126, v136
	v_mul_f32_e64 v142, v127, v136
	v_mul_f32_e64 v143, v132, v136
	v_mul_f32_e64 v144, v133, v136
	v_add_f32_e64 v146, v87, v29
	v_mov_b32_e32 v147, v17
	ds_write_b128 v23, v[128:131] offset:3072
	ds_write_b128 v23, v[140:143] offset:4096
	ds_write_b128 v23, v[144:147] offset:5120
	v_mov_b32_dpp v62, v36 wave_shr:1 row_mask:0xf bank_mask:0xf bound_ctrl:1
	v_mov_b32_dpp v63, v37 wave_shr:1 row_mask:0xf bank_mask:0xf bound_ctrl:1
	v_mov_b32_dpp v86, v36 wave_shl:1 row_mask:0xf bank_mask:0xf bound_ctrl:1
	v_mov_b32_dpp v87, v37 wave_shl:1 row_mask:0xf bank_mask:0xf bound_ctrl:1
	v_pk_mul_f32 v[4:5], v[36:37], v[40:41] op_sel_hi:[1,0]
	v_pk_mul_f32 v[60:61], v[36:37], v[40:41] op_sel:[0,1]
	v_pk_mul_f32 v[84:85], v[36:37], v[42:43] op_sel_hi:[1,0]
	v_pk_add_f32 v[96:97], v[36:37], v[62:63]
	v_pk_fma_f32 v[4:5], v[62:63], v[8:9], v[4:5] op_sel_hi:[1,0,1]
	v_pk_fma_f32 v[60:61], v[62:63], v[8:9], v[60:61] op_sel:[0,1,0]
	v_pk_fma_f32 v[84:85], v[62:63], v[10:11], v[84:85] op_sel_hi:[1,0,1]
	v_pk_add_f32 v[96:97], v[96:97], v[86:87]
	v_pk_fma_f32 v[4:5], v[86:87], v[80:81], v[4:5] op_sel_hi:[1,0,1]
	v_pk_fma_f32 v[60:61], v[86:87], v[80:81], v[60:61] op_sel:[0,1,0]
	v_pk_fma_f32 v[84:85], v[86:87], v[82:83], v[84:85] op_sel_hi:[1,0,1]
	s_waitcnt lgkmcnt(0)
	s_barrier
	v_pk_add_f32 v[62:63], v[54:55], v[96:97]
	v_pk_add_f32 v[132:133], v[110:111], v[4:5]
	v_pk_add_f32 v[136:137], v[30:31], v[60:61]
	v_pk_add_f32 v[148:149], v[38:39], v[84:85]
	v_pk_fma_f32 v[132:133], v[128:129], v[62:63], v[132:133] op_sel_hi:[0,1,1] neg_lo:[1,0,0] neg_hi:[1,0,0]
	v_pk_fma_f32 v[136:137], v[128:129], v[62:63], v[136:137] op_sel:[1,0,0] neg_lo:[1,0,0] neg_hi:[1,0,0]
	v_pk_fma_f32 v[148:149], v[130:131], v[62:63], v[148:149] op_sel_hi:[0,1,1] neg_lo:[1,0,0] neg_hi:[1,0,0]
	v_pk_mul_f32 v[30:31], v[130:131], v[132:133] op_sel:[1,0]
	v_pk_mul_f32 v[38:39], v[140:141], v[132:133] op_sel_hi:[0,1]
	v_pk_mul_f32 v[54:55], v[140:141], v[132:133] op_sel:[1,0]
	v_pk_fma_f32 v[30:31], v[140:141], v[136:137], v[30:31] op_sel_hi:[0,1,1]
	v_pk_fma_f32 v[38:39], v[142:143], v[136:137], v[38:39] op_sel_hi:[0,1,1]
	v_pk_fma_f32 v[54:55], v[142:143], v[136:137], v[54:55] op_sel:[1,0,0]
	v_pk_fma_f32 v[30:31], v[140:141], v[148:149], v[30:31] op_sel:[1,0,0]
	v_pk_fma_f32 v[38:39], v[142:143], v[148:149], v[38:39] op_sel:[1,0,0]
	v_pk_fma_f32 v[54:55], v[144:145], v[148:149], v[54:55] op_sel_hi:[0,1,1]
	v_pk_mul_f32 v[152:153], v[128:129], v[30:31] op_sel_hi:[0,1]
	v_pk_fma_f32 v[152:153], v[128:129], v[38:39], v[152:153] op_sel:[1,0,0]
	v_pk_fma_f32 v[152:153], v[130:131], v[54:55], v[152:153] op_sel_hi:[0,1,1]
	v_pk_fma_f32 v[152:153], v[144:145], v[62:63], v[152:153] op_sel:[1,0,0] neg_lo:[0,0,1] neg_hi:[0,0,1]
	v_cmp_eq_u32_e64 s[10:11], 6, v147
	v_cmp_eq_u32_e64 s[14:15], 7, v147
	v_pk_add_f32 v[62:63], v[44:45], v[30:31]
	v_pk_add_f32 v[44:45], v[92:93], v[38:39]
	v_pk_add_f32 v[86:87], v[120:121], v[54:55]
	v_pk_add_f32 v[92:93], v[138:139], v[152:153]
	v_pk_fma_f32 v[120:121], v[64:65], v[62:63], v[92:93] op_sel_hi:[0,1,1]
	v_pk_fma_f32 v[132:133], v[104:105], v[62:63], v[92:93] op_sel_hi:[0,1,1]
	v_pk_fma_f32 v[120:121], v[64:65], v[44:45], v[120:121] op_sel:[1,0,0]
	v_pk_fma_f32 v[132:133], v[104:105], v[44:45], v[132:133] op_sel:[1,0,0]
	v_pk_fma_f32 v[120:121], v[66:67], v[86:87], v[120:121] op_sel_hi:[0,1,1]
	v_pk_fma_f32 v[132:133], v[106:107], v[86:87], v[132:133] op_sel_hi:[0,1,1]
	v_pk_fma_f32 v[92:93], v[12:13], v[62:63], v[92:93] op_sel_hi:[0,1,1]
	v_pk_fma_f32 v[92:93], v[12:13], v[44:45], v[92:93] op_sel:[1,0,0]
	v_pk_fma_f32 v[92:93], v[14:15], v[86:87], v[92:93] op_sel_hi:[0,1,1]
	v_cndmask_b32_e64 v102, 0, v18, s[10:11]
	v_cndmask_b32_e64 v103, 0, v18, s[14:15]
	v_add_f32_dpp v92, v120, v92 wave_shl:1 row_mask:0xf bank_mask:0xf bound_ctrl:1
	v_add_f32_dpp v93, v121, v93 wave_shl:1 row_mask:0xf bank_mask:0xf bound_ctrl:1
	s_add_i32 s4, s34, 9
	s_cmpk_lt_i32 s4, 0x201
	s_cselect_b64 s[12:13], s[0:1], 0
	v_add_f32_dpp v92, v132, v92 wave_shr:1 row_mask:0xf bank_mask:0xf bound_ctrl:1
	v_add_f32_dpp v93, v133, v93 wave_shr:1 row_mask:0xf bank_mask:0xf bound_ctrl:1
	v_pk_fma_f32 v[92:93], v[6:7], v[146:147], v[92:93] op_sel_hi:[1,0,1] neg_lo:[0,0,1] neg_hi:[0,0,1]
	v_pk_add_f32 v[92:93], v[92:93], v[102:103] neg_lo:[0,1] neg_hi:[0,1]
	v_pk_mul_f32 v[110:111], v[92:93], v[92:93]
	v_add_f32_e32 v110, v110, v111
	v_cndmask_b32_e64 v111, 0, v110, s[12:13]
	v_add_f32_e32 v1, v1, v111
	v_mov_b32_e32 v0, v1
	s_branch .LBB0_29
.LBB0_15:
.LBB0_16:
	s_mov_b32 s27, s19
	v_mov_b32_e32 v1, 0x42c80000
	v_mov_b32_e32 v0, 0
	s_add_i32 s4, s34, -2
	s_max_i32 s4, s4, 0
	s_mul_i32 s5, s4, 0x804
	s_add_i32 s5, s5, s35
	s_add_i32 s6, s5, 0x0
	s_add_i32 s7, s5, 0x101004
	s_add_i32 s8, s5, 0x202008
	s_add_i32 s11, s5, 0x30300c
	s_add_i32 s15, s5, 0x404010
	s_mul_i32 s9, s4, 0x180c
	s_add_i32 s9, s9, s33
	buffer_load_dword v2, v28, s[16:19], s6 offen nt
	buffer_load_dword v3, v28, s[16:19], s7 offen nt
	buffer_load_dword v4, v28, s[16:19], s8 offen nt
	buffer_load_dword v5, v28, s[16:19], s11 offen nt
	buffer_load_dword v6, v28, s[16:19], s15 offen nt
	buffer_load_dwordx3 v[8:10], v27, s[24:27], s9 offen nt
	s_add_i32 s4, s34, -1
	s_max_i32 s4, s4, 0
	s_mul_i32 s5, s4, 0x804
	s_add_i32 s5, s5, s35
	s_add_i32 s6, s5, 0x0
	s_add_i32 s7, s5, 0x101004
	s_add_i32 s8, s5, 0x202008
	s_add_i32 s11, s5, 0x30300c
	s_add_i32 s15, s5, 0x404010
	s_mul_i32 s9, s4, 0x180c
	s_add_i32 s9, s9, s33
	buffer_load_dword v12, v28, s[16:19], s6 offen nt
	buffer_load_dword v13, v28, s[16:19], s7 offen nt
	buffer_load_dword v14, v28, s[16:19], s8 offen nt
	buffer_load_dword v15, v28, s[16:19], s11 offen nt
	buffer_load_dword v16, v28, s[16:19], s15 offen nt
	buffer_load_dwordx3 v[32:34], v27, s[24:27], s9 offen nt
	s_add_i32 s4, s34, 0
	s_min_i32 s4, s4, 0x200
	s_mul_i32 s5, s4, 0x804
	s_add_i32 s5, s5, s35
	s_add_i32 s6, s5, 0x0
	s_add_i32 s7, s5, 0x101004
	s_add_i32 s8, s5, 0x202008
	s_add_i32 s11, s5, 0x30300c
	s_add_i32 s15, s5, 0x404010
	s_mul_i32 s9, s4, 0x180c
	s_add_i32 s9, s9, s33
	buffer_load_dword v20, v28, s[16:19], s6 offen nt
	buffer_load_dword v21, v28, s[16:19], s7 offen nt
	buffer_load_dword v24, v28, s[16:19], s8 offen nt
	buffer_load_dword v25, v28, s[16:19], s11 offen nt
	buffer_load_dword v30, v28, s[16:19], s15 offen nt
	buffer_load_dwordx3 v[36:38], v27, s[24:27], s9 offen nt
	s_waitcnt vmcnt(12)
	v_mov_b32_dpp v40, v8 wave_shr:1 row_mask:0xf bank_mask:0xf bound_ctrl:1
	v_mov_b32_dpp v41, v9 wave_shr:1 row_mask:0xf bank_mask:0xf bound_ctrl:1
	v_mov_b32_dpp v42, v10 wave_shr:1 row_mask:0xf bank_mask:0xf bound_ctrl:1
	v_mov_b32_dpp v44, v8 wave_shl:1 row_mask:0xf bank_mask:0xf bound_ctrl:1
	v_mov_b32_dpp v45, v9 wave_shl:1 row_mask:0xf bank_mask:0xf bound_ctrl:1
	v_mov_b32_dpp v46, v10 wave_shl:1 row_mask:0xf bank_mask:0xf bound_ctrl:1
	v_mov_b32_dpp v48, v2 wave_shr:1 row_mask:0xf bank_mask:0xf bound_ctrl:1
	v_mov_b32_dpp v49, v3 wave_shr:1 row_mask:0xf bank_mask:0xf bound_ctrl:1
	v_mov_b32_dpp v50, v4 wave_shr:1 row_mask:0xf bank_mask:0xf bound_ctrl:1
	v_mov_b32_dpp v51, v5 wave_shr:1 row_mask:0xf bank_mask:0xf bound_ctrl:1
	v_mov_b32_dpp v52, v6 wave_shr:1 row_mask:0xf bank_mask:0xf bound_ctrl:1
	v_mov_b32_dpp v56, v2 wave_shl:1 row_mask:0xf bank_mask:0xf bound_ctrl:1
	v_mov_b32_dpp v57, v3 wave_shl:1 row_mask:0xf bank_mask:0xf bound_ctrl:1
	v_mov_b32_dpp v54, v4 wave_shl:1 row_mask:0xf bank_mask:0xf bound_ctrl:1
	v_mov_b32_dpp v55, v5 wave_shl:1 row_mask:0xf bank_mask:0xf bound_ctrl:1
	v_mov_b32_dpp v60, v6 wave_shl:1 row_mask:0xf bank_mask:0xf bound_ctrl:1
	v_pk_mul_f32 v[58:59], v[2:3], v[8:9] op_sel_hi:[1,0]
	v_pk_mul_f32 v[64:65], v[4:5], v[8:9] op_sel_hi:[1,0]
	v_mul_f32_e64 v62, v6, v8
	v_pk_mul_f32 v[66:67], v[2:3], v[8:9] op_sel:[0,1]
	v_pk_mul_f32 v[68:69], v[4:5], v[8:9] op_sel:[0,1]
	v_mul_f32_e64 v70, v6, v9
	v_pk_mul_f32 v[74:75], v[2:3], v[10:11] op_sel_hi:[1,0]
	v_pk_mul_f32 v[72:73], v[4:5], v[10:11] op_sel_hi:[1,0]
	v_mul_f32_e64 v78, v6, v10
	v_pk_add_f32 v[82:83], v[2:3], v[48:49]
	v_pk_add_f32 v[76:77], v[4:5], v[50:51]
	v_add_f32_e64 v86, v6, v52
	v_pk_fma_f32 v[58:59], v[48:49], v[40:41], v[58:59] op_sel_hi:[1,0,1]
	v_pk_fma_f32 v[64:65], v[50:51], v[40:41], v[64:65] op_sel_hi:[1,0,1]
	v_fma_f32 v62, v52, v40, v62
	v_pk_fma_f32 v[66:67], v[48:49], v[40:41], v[66:67] op_sel:[0,1,0]
	v_pk_fma_f32 v[68:69], v[50:51], v[40:41], v[68:69] op_sel:[0,1,0]
	v_fma_f32 v70, v52, v41, v70
	v_pk_fma_f32 v[74:75], v[48:49], v[42:43], v[74:75] op_sel_hi:[1,0,1]
	v_pk_fma_f32 v[72:73], v[50:51], v[42:43], v[72:73] op_sel_hi:[1,0,1]
	v_fma_f32 v78, v52, v42, v78
	v_pk_add_f32 v[82:83], v[82:83], v[56:57]
	v_pk_add_f32 v[76:77], v[76:77], v[54:55]
	v_add_f32_e64 v86, v86, v60
	v_pk_fma_f32 v[58:59], v[56:57], v[44:45], v[58:59] op_sel_hi:[1,0,1]
	v_pk_fma_f32 v[64:65], v[54:55], v[44:45], v[64:65] op_sel_hi:[1,0,1]
	v_fma_f32 v62, v60, v44, v62
	v_pk_fma_f32 v[66:67], v[56:57], v[44:45], v[66:67] op_sel:[0,1,0]
	v_pk_fma_f32 v[68:69], v[54:55], v[44:45], v[68:69] op_sel:[0,1,0]
	v_fma_f32 v70, v60, v45, v70
	v_pk_fma_f32 v[74:75], v[56:57], v[46:47], v[74:75] op_sel_hi:[1,0,1]
	v_pk_fma_f32 v[72:73], v[54:55], v[46:47], v[72:73] op_sel_hi:[1,0,1]
	v_fma_f32 v78, v60, v46, v78
	s_barrier
	s_add_i32 s4, s34, 1
	s_min_i32 s4, s4, 0x200
	s_mul_i32 s5, s4, 0x804
	s_add_i32 s5, s5, s35
	s_add_i32 s6, s5, 0x0
	s_add_i32 s7, s5, 0x101004
	s_add_i32 s8, s5, 0x202008
	s_add_i32 s11, s5, 0x30300c
	s_add_i32 s15, s5, 0x404010
	s_mul_i32 s9, s4, 0x180c
	s_add_i32 s9, s9, s33
	buffer_load_dword v48, v28, s[16:19], s6 offen nt
	buffer_load_dword v49, v28, s[16:19], s7 offen nt
	buffer_load_dword v50, v28, s[16:19], s8 offen nt
	buffer_load_dword v51, v28, s[16:19], s11 offen nt
	buffer_load_dword v52, v28, s[16:19], s15 offen nt
	buffer_load_dwordx3 v[88:90], v27, s[24:27], s9 offen nt
	s_waitcnt vmcnt(12)
	v_mov_b32_dpp v92, v32 wave_shr:1 row_mask:0xf bank_mask:0xf bound_ctrl:1
	v_mov_b32_dpp v93, v33 wave_shr:1 row_mask:0xf bank_mask:0xf bound_ctrl:1
	v_mov_b32_dpp v94, v34 wave_shr:1 row_mask:0xf bank_mask:0xf bound_ctrl:1
	v_mov_b32_dpp v96, v32 wave_shl:1 row_mask:0xf bank_mask:0xf bound_ctrl:1
	v_mov_b32_dpp v97, v33 wave_shl:1 row_mask:0xf bank_mask:0xf bound_ctrl:1
	v_mov_b32_dpp v98, v34 wave_shl:1 row_mask:0xf bank_mask:0xf bound_ctrl:1
	v_mov_b32_dpp v54, v12 wave_shr:1 row_mask:0xf bank_mask:0xf bound_ctrl:1
	v_mov_b32_dpp v55, v13 wave_shr:1 row_mask:0xf bank_mask:0xf bound_ctrl:1
	v_mov_b32_dpp v56, v14 wave_shr:1 row_mask:0xf bank_mask:0xf bound_ctrl:1
	v_mov_b32_dpp v57, v15 wave_shr:1 row_mask:0xf bank_mask:0xf bound_ctrl:1
	v_mov_b32_dpp v102, v16 wave_shr:1 row_mask:0xf bank_mask:0xf bound_ctrl:1
	v_mov_b32_dpp v106, v12 wave_shl:1 row_mask:0xf bank_mask:0xf bound_ctrl:1
	v_mov_b32_dpp v107, v13 wave_shl:1 row_mask:0xf bank_mask:0xf bound_ctrl:1
	v_mov_b32_dpp v60, v14 wave_shl:1 row_mask:0xf bank_mask:0xf bound_ctrl:1
	v_mov_b32_dpp v61, v15 wave_shl:1 row_mask:0xf bank_mask:0xf bound_ctrl:1
	v_mov_b32_dpp v110, v16 wave_shl:1 row_mask:0xf bank_mask:0xf bound_ctrl:1
	v_pk_mul_f32 v[80:81], v[12:13], v[32:33] op_sel_hi:[1,0]
	v_pk_mul_f32 v[114:115], v[14:15], v[32:33] op_sel_hi:[1,0]
	v_mul_f32_e64 v84, v16, v32
	v_pk_mul_f32 v[100:101], v[12:13], v[32:33] op_sel:[0,1]
	v_pk_mul_f32 v[118:119], v[14:15], v[32:33] op_sel:[0,1]
	v_mul_f32_e64 v104, v16, v33
	v_pk_mul_f32 v[108:109], v[12:13], v[34:35] op_sel_hi:[1,0]
	v_pk_mul_f32 v[122:123], v[14:15], v[34:35] op_sel_hi:[1,0]
	v_mul_f32_e64 v112, v16, v34
	v_pk_add_f32 v[116:117], v[12:13], v[54:55]
	v_pk_add_f32 v[126:127], v[14:15], v[56:57]
	v_add_f32_e64 v120, v16, v102
	v_pk_fma_f32 v[80:81], v[54:55], v[92:93], v[80:81] op_sel_hi:[1,0,1]
	v_pk_fma_f32 v[114:115], v[56:57], v[92:93], v[114:115] op_sel_hi:[1,0,1]
	v_fma_f32 v84, v102, v92, v84
	v_pk_fma_f32 v[100:101], v[54:55], v[92:93], v[100:101] op_sel:[0,1,0]
	v_pk_fma_f32 v[118:119], v[56:57], v[92:93], v[118:119] op_sel:[0,1,0]
	v_fma_f32 v104, v102, v93, v104
	v_pk_fma_f32 v[108:109], v[54:55], v[94:95], v[108:109] op_sel_hi:[1,0,1]
	v_pk_fma_f32 v[122:123], v[56:57], v[94:95], v[122:123] op_sel_hi:[1,0,1]
	v_fma_f32 v112, v102, v94, v112
	v_pk_add_f32 v[116:117], v[116:117], v[106:107]
	v_pk_add_f32 v[126:127], v[126:127], v[60:61]
	v_add_f32_e64 v120, v120, v110
	v_pk_fma_f32 v[80:81], v[106:107], v[96:97], v[80:81] op_sel_hi:[1,0,1]
	v_pk_fma_f32 v[114:115], v[60:61], v[96:97], v[114:115] op_sel_hi:[1,0,1]
	v_fma_f32 v84, v110, v96, v84
	v_pk_fma_f32 v[100:101], v[106:107], v[96:97], v[100:101] op_sel:[0,1,0]
	v_pk_fma_f32 v[118:119], v[60:61], v[96:97], v[118:119] op_sel:[0,1,0]
	v_fma_f32 v104, v110, v97, v104
	v_pk_fma_f32 v[108:109], v[106:107], v[98:99], v[108:109] op_sel_hi:[1,0,1]
	v_pk_fma_f32 v[122:123], v[60:61], v[98:99], v[122:123] op_sel_hi:[1,0,1]
	v_fma_f32 v112, v110, v98, v112
	s_barrier
	s_add_i32 s4, s34, 2
	s_min_i32 s4, s4, 0x200
	s_mul_i32 s5, s4, 0x804
	s_add_i32 s5, s5, s35
	s_add_i32 s6, s5, 0x0
	s_add_i32 s7, s5, 0x101004
	s_add_i32 s8, s5, 0x202008
	s_add_i32 s11, s5, 0x30300c
	s_add_i32 s15, s5, 0x404010
	s_mul_i32 s9, s4, 0x180c
	s_add_i32 s9, s9, s33
	buffer_load_dword v54, v28, s[16:19], s6 offen nt
	buffer_load_dword v55, v28, s[16:19], s7 offen nt
	buffer_load_dword v56, v28, s[16:19], s8 offen nt
	buffer_load_dword v57, v28, s[16:19], s11 offen nt
	buffer_load_dword v60, v28, s[16:19], s15 offen nt
	buffer_load_dwordx3 v[128:130], v27, s[24:27], s9 offen nt
	s_waitcnt vmcnt(12)
	v_mov_b32_dpp v132, v36 wave_shr:1 row_mask:0xf bank_mask:0xf bound_ctrl:1
	v_mov_b32_dpp v133, v37 wave_shr:1 row_mask:0xf bank_mask:0xf bound_ctrl:1
	v_mov_b32_dpp v134, v38 wave_shr:1 row_mask:0xf bank_mask:0xf bound_ctrl:1
	v_mov_b32_dpp v136, v36 wave_shl:1 row_mask:0xf bank_mask:0xf bound_ctrl:1
	v_mov_b32_dpp v137, v37 wave_shl:1 row_mask:0xf bank_mask:0xf bound_ctrl:1
	v_mov_b32_dpp v138, v38 wave_shl:1 row_mask:0xf bank_mask:0xf bound_ctrl:1
	v_mov_b32_dpp v102, v20 wave_shr:1 row_mask:0xf bank_mask:0xf bound_ctrl:1
	v_mov_b32_dpp v103, v21 wave_shr:1 row_mask:0xf bank_mask:0xf bound_ctrl:1
	v_mov_b32_dpp v106, v24 wave_shr:1 row_mask:0xf bank_mask:0xf bound_ctrl:1
	v_mov_b32_dpp v107, v25 wave_shr:1 row_mask:0xf bank_mask:0xf bound_ctrl:1
	v_mov_b32_dpp v124, v30 wave_shr:1 row_mask:0xf bank_mask:0xf bound_ctrl:1
	v_mov_b32_dpp v110, v20 wave_shl:1 row_mask:0xf bank_mask:0xf bound_ctrl:1
	v_mov_b32_dpp v111, v21 wave_shl:1 row_mask:0xf bank_mask:0xf bound_ctrl:1
	v_mov_b32_dpp v142, v24 wave_shl:1 row_mask:0xf bank_mask:0xf bound_ctrl:1
	v_mov_b32_dpp v143, v25 wave_shl:1 row_mask:0xf bank_mask:0xf bound_ctrl:1
	v_mov_b32_dpp v140, v30 wave_shl:1 row_mask:0xf bank_mask:0xf bound_ctrl:1
	v_pk_mul_f32 v[144:145], v[20:21], v[36:37] op_sel_hi:[1,0]
	v_pk_mul_f32 v[148:149], v[24:25], v[36:37] op_sel_hi:[1,0]
	v_mul_f32_e64 v146, v30, v36
	v_pk_mul_f32 v[152:153], v[20:21], v[36:37] op_sel:[0,1]
	v_pk_mul_f32 v[156:157], v[24:25], v[36:37] op_sel:[0,1]
	v_mul_f32_e64 v150, v30, v37
	v_pk_mul_f32 v[160:161], v[20:21], v[38:39] op_sel_hi:[1,0]
	v_pk_mul_f32 v[164:165], v[24:25], v[38:39] op_sel_hi:[1,0]
	v_mul_f32_e64 v154, v30, v38
	v_pk_add_f32 v[168:169], v[20:21], v[102:103]
	v_pk_add_f32 v[172:173], v[24:25], v[106:107]
	v_add_f32_e64 v158, v30, v124
	v_pk_fma_f32 v[144:145], v[102:103], v[132:133], v[144:145] op_sel_hi:[1,0,1]
	v_pk_fma_f32 v[148:149], v[106:107], v[132:133], v[148:149] op_sel_hi:[1,0,1]
	v_fma_f32 v146, v124, v132, v146
	v_pk_fma_f32 v[152:153], v[102:103], v[132:133], v[152:153] op_sel:[0,1,0]
	v_pk_fma_f32 v[156:157], v[106:107], v[132:133], v[156:157] op_sel:[0,1,0]
	v_fma_f32 v150, v124, v133, v150
	v_pk_fma_f32 v[160:161], v[102:103], v[134:135], v[160:161] op_sel_hi:[1,0,1]
	v_pk_fma_f32 v[164:165], v[106:107], v[134:135], v[164:165] op_sel_hi:[1,0,1]
	v_fma_f32 v154, v124, v134, v154
	v_pk_add_f32 v[168:169], v[168:169], v[110:111]
	v_pk_add_f32 v[172:173], v[172:173], v[142:143]
	v_add_f32_e64 v158, v158, v140
	v_pk_fma_f32 v[144:145], v[110:111], v[136:137], v[144:145] op_sel_hi:[1,0,1]
	v_pk_fma_f32 v[148:149], v[142:143], v[136:137], v[148:149] op_sel_hi:[1,0,1]
	v_fma_f32 v146, v140, v136, v146
	v_pk_fma_f32 v[152:153], v[110:111], v[136:137], v[152:153] op_sel:[0,1,0]
	v_pk_fma_f32 v[156:157], v[142:143], v[136:137], v[156:157] op_sel:[0,1,0]
	v_fma_f32 v150, v140, v137, v150
	v_pk_fma_f32 v[160:161], v[110:111], v[138:139], v[160:161] op_sel_hi:[1,0,1]
	v_pk_fma_f32 v[164:165], v[142:143], v[138:139], v[164:165] op_sel_hi:[1,0,1]
	v_fma_f32 v154, v140, v138, v154
	s_barrier
	ds_read_b128 v[140:143], v23 offset:0
	ds_read_b128 v[176:179], v23 offset:1024
	ds_read_b128 v[180:183], v23 offset:2048
	v_pk_add_f32 v[124:125], v[116:117], v[168:169]
	v_pk_add_f32 v[102:103], v[82:83], v[124:125]
	v_pk_add_f32 v[82:83], v[126:127], v[172:173]
	v_pk_add_f32 v[106:107], v[76:77], v[82:83]
	v_add_f32_e64 v76, v120, v158
	v_add_f32_e64 v110, v86, v76
	v_pk_add_f32 v[116:117], v[80:81], v[144:145]
	v_pk_add_f32 v[120:121], v[58:59], v[116:117]
	v_pk_add_f32 v[58:59], v[114:115], v[148:149]
	v_pk_add_f32 v[80:81], v[64:65], v[58:59]
	v_add_f32_e64 v64, v84, v146
	v_add_f32_e64 v184, v62, v64
	v_pk_add_f32 v[84:85], v[100:101], v[152:153]
	v_pk_add_f32 v[188:189], v[66:67], v[84:85]
	v_pk_add_f32 v[62:63], v[118:119], v[156:157]
	v_pk_add_f32 v[100:101], v[68:69], v[62:63]
	v_add_f32_e64 v68, v104, v150
	v_add_f32_e64 v192, v70, v68
	v_pk_add_f32 v[104:105], v[108:109], v[160:161]
	v_pk_add_f32 v[196:197], v[74:75], v[104:105]
	v_pk_add_f32 v[66:67], v[122:123], v[164:165]
	v_pk_add_f32 v[108:109], v[72:73], v[66:67]
	v_add_f32_e64 v72, v112, v154
	v_add_f32_e64 v200, v78, v72
	s_waitcnt lgkmcnt(2)
	v_pk_fma_f32 v[120:121], v[140:141], v[102:103], v[120:121] op_sel_hi:[0,1,1] neg_lo:[1,0,0] neg_hi:[1,0,0]
	v_pk_fma_f32 v[80:81], v[140:141], v[106:107], v[80:81] op_sel_hi:[0,1,1] neg_lo:[1,0,0] neg_hi:[1,0,0]
	v_fma_f32 v184, -v140, v110, v184
	v_pk_fma_f32 v[188:189], v[140:141], v[102:103], v[188:189] op_sel:[1,0,0] neg_lo:[1,0,0] neg_hi:[1,0,0]
	v_pk_fma_f32 v[100:101], v[140:141], v[106:107], v[100:101] op_sel:[1,0,0] neg_lo:[1,0,0] neg_hi:[1,0,0]
	v_fma_f32 v192, -v141, v110, v192
	v_pk_fma_f32 v[196:197], v[142:143], v[102:103], v[196:197] op_sel_hi:[0,1,1] neg_lo:[1,0,0] neg_hi:[1,0,0]
	v_pk_fma_f32 v[108:109], v[142:143], v[106:107], v[108:109] op_sel_hi:[0,1,1] neg_lo:[1,0,0] neg_hi:[1,0,0]
	v_fma_f32 v200, -v142, v110, v200
	v_pk_mul_f32 v[70:71], v[142:143], v[120:121] op_sel:[1,0]
	v_pk_mul_f32 v[86:87], v[142:143], v[80:81] op_sel:[1,0]
	v_mul_f32_e64 v122, v143, v184
	s_waitcnt lgkmcnt(1)
	v_pk_mul_f32 v[74:75], v[176:177], v[120:121] op_sel_hi:[0,1]
	v_pk_mul_f32 v[114:115], v[176:177], v[80:81] op_sel_hi:[0,1]
	v_mul_f32_e64 v126, v176, v184
	v_pk_mul_f32 v[78:79], v[176:177], v[120:121] op_sel:[1,0]
	v_pk_mul_f32 v[118:119], v[176:177], v[80:81] op_sel:[1,0]
	v_mul_f32_e64 v162, v177, v184
	v_pk_fma_f32 v[70:71], v[176:177], v[188:189], v[70:71] op_sel_hi:[0,1,1]
	v_pk_fma_f32 v[86:87], v[176:177], v[100:101], v[86:87] op_sel_hi:[0,1,1]
	v_fma_f32 v122, v176, v192, v122
	v_pk_fma_f32 v[74:75], v[178:179], v[188:189], v[74:75] op_sel_hi:[0,1,1]
	v_pk_fma_f32 v[114:115], v[178:179], v[100:101], v[114:115] op_sel_hi:[0,1,1]
	v_fma_f32 v126, v178, v192, v126
	v_pk_fma_f32 v[78:79], v[178:179], v[188:189], v[78:79] op_sel:[1,0,0]
	v_pk_fma_f32 v[118:119], v[178:179], v[100:101], v[118:119] op_sel:[1,0,0]
	v_fma_f32 v162, v179, v192, v162
	v_pk_fma_f32 v[70:71], v[176:177], v[196:197], v[70:71] op_sel:[1,0,0]
	v_pk_fma_f32 v[86:87], v[176:177], v[108:109], v[86:87] op_sel:[1,0,0]
	v_fma_f32 v122, v177, v200, v122
	v_pk_fma_f32 v[74:75], v[178:179], v[196:197], v[74:75] op_sel:[1,0,0]
	v_pk_fma_f32 v[114:115], v[178:179], v[108:109], v[114:115] op_sel:[1,0,0]
	v_fma_f32 v126, v179, v200, v126
	s_waitcnt lgkmcnt(0)
	v_pk_fma_f32 v[78:79], v[180:181], v[196:197], v[78:79] op_sel_hi:[0,1,1]
	v_pk_fma_f32 v[118:119], v[180:181], v[108:109], v[118:119] op_sel_hi:[0,1,1]
	v_fma_f32 v162, v180, v200, v162
	v_pk_mul_f32 v[112:113], v[140:141], v[70:71] op_sel_hi:[0,1]
	v_pk_mul_f32 v[204:205], v[140:141], v[86:87] op_sel_hi:[0,1]
	v_mul_f32_e64 v208, v140, v122
	v_pk_fma_f32 v[112:113], v[140:141], v[74:75], v[112:113] op_sel:[1,0,0]
	v_pk_fma_f32 v[204:205], v[140:141], v[114:115], v[204:205] op_sel:[1,0,0]
	v_fma_f32 v208, v141, v126, v208
	v_pk_fma_f32 v[112:113], v[142:143], v[78:79], v[112:113] op_sel_hi:[0,1,1]
	v_pk_fma_f32 v[204:205], v[142:143], v[118:119], v[204:205] op_sel_hi:[0,1,1]
	v_fma_f32 v208, v142, v162, v208
	v_pk_fma_f32 v[112:113], v[180:181], v[102:103], v[112:113] op_sel:[1,0,0] neg_lo:[0,0,1] neg_hi:[0,0,1]
	v_pk_fma_f32 v[204:205], v[180:181], v[106:107], v[204:205] op_sel:[1,0,0] neg_lo:[0,0,1] neg_hi:[0,0,1]
	v_fma_f32 v208, v181, v110, -v208
	s_add_i32 s4, s34, 3
	s_min_i32 s4, s4, 0x200
	s_mul_i32 s5, s4, 0x804
	s_add_i32 s5, s5, s35
	s_add_i32 s6, s5, 0x0
	s_add_i32 s7, s5, 0x101004
	s_add_i32 s8, s5, 0x202008
	s_add_i32 s11, s5, 0x30300c
	s_add_i32 s15, s5, 0x404010
	s_mul_i32 s9, s4, 0x180c
	s_add_i32 s9, s9, s33
	buffer_load_dword v2, v28, s[16:19], s6 offen nt
	buffer_load_dword v3, v28, s[16:19], s7 offen nt
	buffer_load_dword v4, v28, s[16:19], s8 offen nt
	buffer_load_dword v5, v28, s[16:19], s11 offen nt
	buffer_load_dword v6, v28, s[16:19], s15 offen nt
	buffer_load_dwordx3 v[8:10], v27, s[24:27], s9 offen nt
	s_waitcnt vmcnt(12)
	v_mov_b32_dpp v40, v88 wave_shr:1 row_mask:0xf bank_mask:0xf bound_ctrl:1
	v_mov_b32_dpp v41, v89 wave_shr:1 row_mask:0xf bank_mask:0xf bound_ctrl:1
	v_mov_b32_dpp v42, v90 wave_shr:1 row_mask:0xf bank_mask:0xf bound_ctrl:1
	v_mov_b32_dpp v44, v88 wave_shl:1 row_mask:0xf bank_mask:0xf bound_ctrl:1
	v_mov_b32_dpp v45, v89 wave_shl:1 row_mask:0xf bank_mask:0xf bound_ctrl:1
	v_mov_b32_dpp v46, v90 wave_shl:1 row_mask:0xf bank_mask:0xf bound_ctrl:1
	v_mov_b32_dpp v102, v48 wave_shr:1 row_mask:0xf bank_mask:0xf bound_ctrl:1
	v_mov_b32_dpp v103, v49 wave_shr:1 row_mask:0xf bank_mask:0xf bound_ctrl:1
	v_mov_b32_dpp v80, v50 wave_shr:1 row_mask:0xf bank_mask:0xf bound_ctrl:1
	v_mov_b32_dpp v81, v51 wave_shr:1 row_mask:0xf bank_mask:0xf bound_ctrl:1
	v_mov_b32_dpp v106, v52 wave_shr:1 row_mask:0xf bank_mask:0xf bound_ctrl:1
	v_mov_b32_dpp v110, v48 wave_shl:1 row_mask:0xf bank_mask:0xf bound_ctrl:1
	v_mov_b32_dpp v111, v49 wave_shl:1 row_mask:0xf bank_mask:0xf bound_ctrl:1
	v_mov_b32_dpp v100, v50 wave_shl:1 row_mask:0xf bank_mask:0xf bound_ctrl:1
	v_mov_b32_dpp v101, v51 wave_shl:1 row_mask:0xf bank_mask:0xf bound_ctrl:1
	v_mov_b32_dpp v142, v52 wave_shl:1 row_mask:0xf bank_mask:0xf bound_ctrl:1
	v_pk_mul_f32 v[108:109], v[48:49], v[88:89] op_sel_hi:[1,0]
	v_pk_mul_f32 v[166:167], v[50:51], v[88:89] op_sel_hi:[1,0]
	v_mul_f32_e64 v120, v52, v88
	v_pk_mul_f32 v[140:141], v[48:49], v[88:89] op_sel:[0,1]
	v_pk_mul_f32 v[170:171], v[50:51], v[88:89] op_sel:[0,1]
	v_mul_f32_e64 v176, v52, v89
	v_pk_mul_f32 v[180:181], v[48:49], v[90:91] op_sel_hi:[1,0]
	v_pk_mul_f32 v[174:175], v[50:51], v[90:91] op_sel_hi:[1,0]
	v_mul_f32_e64 v184, v52, v90
	v_pk_add_f32 v[188:189], v[48:49], v[102:103]
	v_pk_add_f32 v[178:179], v[50:51], v[80:81]
	v_add_f32_e64 v192, v52, v106
	v_pk_fma_f32 v[108:109], v[102:103], v[40:41], v[108:109] op_sel_hi:[1,0,1]
	v_pk_fma_f32 v[166:167], v[80:81], v[40:41], v[166:167] op_sel_hi:[1,0,1]
	v_fma_f32 v120, v106, v40, v120
	v_pk_fma_f32 v[140:141], v[102:103], v[40:41], v[140:141] op_sel:[0,1,0]
	v_pk_fma_f32 v[170:171], v[80:81], v[40:41], v[170:171] op_sel:[0,1,0]
	v_fma_f32 v176, v106, v41, v176
	v_pk_fma_f32 v[180:181], v[102:103], v[42:43], v[180:181] op_sel_hi:[1,0,1]
	v_pk_fma_f32 v[174:175], v[80:81], v[42:43], v[174:175] op_sel_hi:[1,0,1]
	v_fma_f32 v184, v106, v42, v184
	v_pk_add_f32 v[188:189], v[188:189], v[110:111]
	v_pk_add_f32 v[178:179], v[178:179], v[100:101]
	v_add_f32_e64 v192, v192, v142
	v_pk_fma_f32 v[108:109], v[110:111], v[44:45], v[108:109] op_sel_hi:[1,0,1]
	v_pk_fma_f32 v[166:167], v[100:101], v[44:45], v[166:167] op_sel_hi:[1,0,1]
	v_fma_f32 v120, v142, v44, v120
	v_pk_fma_f32 v[140:141], v[110:111], v[44:45], v[140:141] op_sel:[0,1,0]
	v_pk_fma_f32 v[170:171], v[100:101], v[44:45], v[170:171] op_sel:[0,1,0]
	v_fma_f32 v176, v142, v45, v176
	v_pk_fma_f32 v[180:181], v[110:111], v[46:47], v[180:181] op_sel_hi:[1,0,1]
	v_pk_fma_f32 v[174:175], v[100:101], v[46:47], v[174:175] op_sel_hi:[1,0,1]
	v_fma_f32 v184, v142, v46, v184
	s_barrier
	ds_read_b128 v[100:103], v23 offset:3072
	ds_read_b128 v[196:199], v23 offset:4096
	ds_read_b128 v[200:203], v23 offset:5120
	v_pk_add_f32 v[80:81], v[124:125], v[188:189]
	v_pk_add_f32 v[106:107], v[82:83], v[178:179]
	v_add_f32_e64 v82, v76, v192
	v_pk_add_f32 v[110:111], v[116:117], v[108:109]
	v_pk_add_f32 v[76:77], v[58:59], v[166:167]
	v_add_f32_e64 v116, v64, v120
	v_pk_add_f32 v[58:59], v[84:85], v[140:141]
	v_pk_add_f32 v[64:65], v[62:63], v[170:171]
	v_add_f32_e64 v84, v68, v176
	v_pk_add_f32 v[62:63], v[104:105], v[180:181]
	v_pk_add_f32 v[68:69], v[66:67], v[174:175]
	v_add_f32_e64 v104, v72, v184
	s_waitcnt lgkmcnt(2)
	v_pk_fma_f32 v[110:111], v[100:101], v[80:81], v[110:111] op_sel_hi:[0,1,1] neg_lo:[1,0,0] neg_hi:[1,0,0]
	v_pk_fma_f32 v[76:77], v[100:101], v[106:107], v[76:77] op_sel_hi:[0,1,1] neg_lo:[1,0,0] neg_hi:[1,0,0]
	v_fma_f32 v116, -v100, v82, v116
	v_pk_fma_f32 v[58:59], v[100:101], v[80:81], v[58:59] op_sel:[1,0,0] neg_lo:[1,0,0] neg_hi:[1,0,0]
	v_pk_fma_f32 v[64:65], v[100:101], v[106:107], v[64:65] op_sel:[1,0,0] neg_lo:[1,0,0] neg_hi:[1,0,0]
	v_fma_f32 v84, -v101, v82, v84
	v_pk_fma_f32 v[62:63], v[102:103], v[80:81], v[62:63] op_sel_hi:[0,1,1] neg_lo:[1,0,0] neg_hi:[1,0,0]
	v_pk_fma_f32 v[68:69], v[102:103], v[106:107], v[68:69] op_sel_hi:[0,1,1] neg_lo:[1,0,0] neg_hi:[1,0,0]
	v_fma_f32 v104, -v102, v82, v104
	v_pk_mul_f32 v[72:73], v[102:103], v[110:111] op_sel:[1,0]
	v_pk_mul_f32 v[66:67], v[102:103], v[76:77] op_sel:[1,0]
	v_mul_f32_e64 v186, v103, v116
	s_waitcnt lgkmcnt(1)
	v_pk_mul_f32 v[124:125], v[196:197], v[110:111] op_sel_hi:[0,1]
	v_pk_mul_f32 v[142:143], v[196:197], v[76:77] op_sel_hi:[0,1]
	v_mul_f32_e64 v190, v196, v116
	v_pk_mul_f32 v[212:213], v[196:197], v[110:111] op_sel:[1,0]
	v_pk_mul_f32 v[182:183], v[196:197], v[76:77] op_sel:[1,0]
	v_mul_f32_e64 v194, v197, v116
	v_pk_fma_f32 v[72:73], v[196:197], v[58:59], v[72:73] op_sel_hi:[0,1,1]
	v_pk_fma_f32 v[66:67], v[196:197], v[64:65], v[66:67] op_sel_hi:[0,1,1]
	v_fma_f32 v186, v196, v84, v186
	v_pk_fma_f32 v[124:125], v[198:199], v[58:59], v[124:125] op_sel_hi:[0,1,1]
	v_pk_fma_f32 v[142:143], v[198:199], v[64:65], v[142:143] op_sel_hi:[0,1,1]
	v_fma_f32 v190, v198, v84, v190
	v_pk_fma_f32 v[212:213], v[198:199], v[58:59], v[212:213] op_sel:[1,0,0]
	v_pk_fma_f32 v[182:183], v[198:199], v[64:65], v[182:183] op_sel:[1,0,0]
	v_fma_f32 v194, v199, v84, v194
	v_pk_fma_f32 v[72:73], v[196:197], v[62:63], v[72:73] op_sel:[1,0,0]
	v_pk_fma_f32 v[66:67], v[196:197], v[68:69], v[66:67] op_sel:[1,0,0]
	v_fma_f32 v186, v197, v104, v186
	v_pk_fma_f32 v[124:125], v[198:199], v[62:63], v[124:125] op_sel:[1,0,0]
	v_pk_fma_f32 v[142:143], v[198:199], v[68:69], v[142:143] op_sel:[1,0,0]
	v_fma_f32 v190, v199, v104, v190
	s_waitcnt lgkmcnt(0)
	v_pk_fma_f32 v[212:213], v[200:201], v[62:63], v[212:213] op_sel_hi:[0,1,1]
	v_pk_fma_f32 v[182:183], v[200:201], v[68:69], v[182:183] op_sel_hi:[0,1,1]
	v_fma_f32 v194, v200, v104, v194
	v_pk_mul_f32 v[206:207], v[100:101], v[72:73] op_sel_hi:[0,1]
	v_pk_mul_f32 v[216:217], v[100:101], v[66:67] op_sel_hi:[0,1]
	v_mul_f32_e64 v220, v100, v186
	v_pk_fma_f32 v[206:207], v[100:101], v[124:125], v[206:207] op_sel:[1,0,0]
	v_pk_fma_f32 v[216:217], v[100:101], v[142:143], v[216:217] op_sel:[1,0,0]
	v_fma_f32 v220, v101, v190, v220
	v_pk_fma_f32 v[206:207], v[102:103], v[212:213], v[206:207] op_sel_hi:[0,1,1]
	v_pk_fma_f32 v[216:217], v[102:103], v[182:183], v[216:217] op_sel_hi:[0,1,1]
	v_fma_f32 v220, v102, v194, v220
	v_pk_fma_f32 v[206:207], v[200:201], v[80:81], v[206:207] op_sel:[1,0,0] neg_lo:[0,0,1] neg_hi:[0,0,1]
	v_pk_fma_f32 v[216:217], v[200:201], v[106:107], v[216:217] op_sel:[1,0,0] neg_lo:[0,0,1] neg_hi:[0,0,1]
	v_fma_f32 v220, v201, v82, -v220
	s_add_i32 s4, s34, 4
	s_min_i32 s4, s4, 0x200
	s_mul_i32 s5, s4, 0x804
	s_add_i32 s5, s5, s35
	s_add_i32 s6, s5, 0x0
	s_add_i32 s7, s5, 0x101004
	s_add_i32 s8, s5, 0x202008
	s_add_i32 s11, s5, 0x30300c
	s_add_i32 s15, s5, 0x404010
	s_mul_i32 s9, s4, 0x180c
	s_add_i32 s9, s9, s33
	buffer_load_dword v12, v28, s[16:19], s6 offen nt
	buffer_load_dword v13, v28, s[16:19], s7 offen nt
	buffer_load_dword v14, v28, s[16:19], s8 offen nt
	buffer_load_dword v15, v28, s[16:19], s11 offen nt
	buffer_load_dword v16, v28, s[16:19], s15 offen nt
	buffer_load_dwordx3 v[32:34], v27, s[24:27], s9 offen nt
	s_waitcnt vmcnt(12)
	v_mov_b32_dpp v80, v128 wave_shr:1 row_mask:0xf bank_mask:0xf bound_ctrl:1
	v_mov_b32_dpp v81, v129 wave_shr:1 row_mask:0xf bank_mask:0xf bound_ctrl:1
	v_mov_b32_dpp v82, v130 wave_shr:1 row_mask:0xf bank_mask:0xf bound_ctrl:1
	v_mov_b32_dpp v92, v128 wave_shl:1 row_mask:0xf bank_mask:0xf bound_ctrl:1
	v_mov_b32_dpp v93, v129 wave_shl:1 row_mask:0xf bank_mask:0xf bound_ctrl:1
	v_mov_b32_dpp v94, v130 wave_shl:1 row_mask:0xf bank_mask:0xf bound_ctrl:1
	v_mov_b32_dpp v64, v54 wave_shr:1 row_mask:0xf bank_mask:0xf bound_ctrl:1
	v_mov_b32_dpp v65, v55 wave_shr:1 row_mask:0xf bank_mask:0xf bound_ctrl:1
	v_mov_b32_dpp v58, v56 wave_shr:1 row_mask:0xf bank_mask:0xf bound_ctrl:1
	v_mov_b32_dpp v59, v57 wave_shr:1 row_mask:0xf bank_mask:0xf bound_ctrl:1
	v_mov_b32_dpp v62, v60 wave_shr:1 row_mask:0xf bank_mask:0xf bound_ctrl:1
	v_mov_b32_dpp v68, v54 wave_shl:1 row_mask:0xf bank_mask:0xf bound_ctrl:1
	v_mov_b32_dpp v69, v55 wave_shl:1 row_mask:0xf bank_mask:0xf bound_ctrl:1
	v_mov_b32_dpp v98, v56 wave_shl:1 row_mask:0xf bank_mask:0xf bound_ctrl:1
	v_mov_b32_dpp v99, v57 wave_shl:1 row_mask:0xf bank_mask:0xf bound_ctrl:1
	v_mov_b32_dpp v102, v60 wave_shl:1 row_mask:0xf bank_mask:0xf bound_ctrl:1
	v_pk_mul_f32 v[106:107], v[54:55], v[128:129] op_sel_hi:[1,0]
	v_pk_mul_f32 v[76:77], v[56:57], v[128:129] op_sel_hi:[1,0]
	v_mul_f32_e64 v84, v60, v128
	v_pk_mul_f32 v[110:111], v[54:55], v[128:129] op_sel:[0,1]
	v_pk_mul_f32 v[96:97], v[56:57], v[128:129] op_sel:[0,1]
	v_mul_f32_e64 v100, v60, v129
	v_pk_mul_f32 v[198:199], v[54:55], v[130:131] op_sel_hi:[1,0]
	v_pk_mul_f32 v[104:105], v[56:57], v[130:131] op_sel_hi:[1,0]
	v_mul_f32_e64 v116, v60, v130
	v_pk_add_f32 v[202:203], v[54:55], v[64:65]
	v_pk_add_f32 v[196:197], v[56:57], v[58:59]
	v_add_f32_e64 v200, v60, v62
	v_pk_fma_f32 v[106:107], v[64:65], v[80:81], v[106:107] op_sel_hi:[1,0,1]
	v_pk_fma_f32 v[76:77], v[58:59], v[80:81], v[76:77] op_sel_hi:[1,0,1]
	v_fma_f32 v84, v62, v80, v84
	v_pk_fma_f32 v[110:111], v[64:65], v[80:81], v[110:111] op_sel:[0,1,0]
	v_pk_fma_f32 v[96:97], v[58:59], v[80:81], v[96:97] op_sel:[0,1,0]
	v_fma_f32 v100, v62, v81, v100
	v_pk_fma_f32 v[198:199], v[64:65], v[82:83], v[198:199] op_sel_hi:[1,0,1]
	v_pk_fma_f32 v[104:105], v[58:59], v[82:83], v[104:105] op_sel_hi:[1,0,1]
	v_fma_f32 v116, v62, v82, v116
	v_pk_add_f32 v[202:203], v[202:203], v[68:69]
	v_pk_add_f32 v[196:197], v[196:197], v[98:99]
	v_add_f32_e64 v200, v200, v102
	v_pk_fma_f32 v[106:107], v[68:69], v[92:93], v[106:107] op_sel_hi:[1,0,1]
	v_pk_fma_f32 v[76:77], v[98:99], v[92:93], v[76:77] op_sel_hi:[1,0,1]
	v_fma_f32 v84, v102, v92, v84
	v_pk_fma_f32 v[110:111], v[68:69], v[92:93], v[110:111] op_sel:[0,1,0]
	v_pk_fma_f32 v[96:97], v[98:99], v[92:93], v[96:97] op_sel:[0,1,0]
	v_fma_f32 v100, v102, v93, v100
	v_pk_fma_f32 v[198:199], v[68:69], v[94:95], v[198:199] op_sel_hi:[1,0,1]
	v_pk_fma_f32 v[104:105], v[98:99], v[94:95], v[104:105] op_sel_hi:[1,0,1]
	v_fma_f32 v116, v102, v94, v116
	s_barrier
	ds_read_b128 v[224:227], v23 offset:0
	ds_read_b128 v[228:231], v23 offset:1024
	ds_read_b128 v[232:235], v23 offset:2048
	v_pk_add_f32 v[58:59], v[188:189], v[202:203]
	v_pk_add_f32 v[62:63], v[168:169], v[58:59]
	v_pk_add_f32 v[98:99], v[178:179], v[196:197]
	v_pk_add_f32 v[64:65], v[172:173], v[98:99]
	v_add_f32_e64 v68, v192, v200
	v_add_f32_e64 v102, v158, v68
	v_pk_add_f32 v[158:159], v[108:109], v[106:107]
	v_pk_add_f32 v[168:169], v[144:145], v[158:159]
	v_pk_add_f32 v[178:179], v[166:167], v[76:77]
	v_pk_add_f32 v[210:211], v[148:149], v[178:179]
	v_add_f32_e64 v108, v120, v84
	v_add_f32_e64 v144, v146, v108
	v_pk_add_f32 v[146:147], v[140:141], v[110:111]
	v_pk_add_f32 v[120:121], v[152:153], v[146:147]
	v_pk_add_f32 v[166:167], v[170:171], v[96:97]
	v_pk_add_f32 v[214:215], v[156:157], v[166:167]
	v_add_f32_e64 v140, v176, v100
	v_add_f32_e64 v148, v150, v140
	v_pk_add_f32 v[150:151], v[180:181], v[198:199]
	v_pk_add_f32 v[152:153], v[160:161], v[150:151]
	v_pk_add_f32 v[170:171], v[174:175], v[104:105]
	v_pk_add_f32 v[218:219], v[164:165], v[170:171]
	v_add_f32_e64 v156, v184, v116
	v_add_f32_e64 v160, v154, v156
	s_waitcnt lgkmcnt(2)
	v_pk_fma_f32 v[168:169], v[224:225], v[62:63], v[168:169] op_sel_hi:[0,1,1] neg_lo:[1,0,0] neg_hi:[1,0,0]
	v_pk_fma_f32 v[210:211], v[224:225], v[64:65], v[210:211] op_sel_hi:[0,1,1] neg_lo:[1,0,0] neg_hi:[1,0,0]
	v_fma_f32 v144, -v224, v102, v144
	v_pk_fma_f32 v[120:121], v[224:225], v[62:63], v[120:121] op_sel:[1,0,0] neg_lo:[1,0,0] neg_hi:[1,0,0]
	v_pk_fma_f32 v[214:215], v[224:225], v[64:65], v[214:215] op_sel:[1,0,0] neg_lo:[1,0,0] neg_hi:[1,0,0]
	v_fma_f32 v148, -v225, v102, v148
	v_pk_fma_f32 v[152:153], v[226:227], v[62:63], v[152:153] op_sel_hi:[0,1,1] neg_lo:[1,0,0] neg_hi:[1,0,0]
	v_pk_fma_f32 v[218:219], v[226:227], v[64:65], v[218:219] op_sel_hi:[0,1,1] neg_lo:[1,0,0] neg_hi:[1,0,0]
	v_fma_f32 v160, -v226, v102, v160
	v_pk_mul_f32 v[154:155], v[226:227], v[168:169] op_sel:[1,0]
	v_pk_mul_f32 v[164:165], v[226:227], v[210:211] op_sel:[1,0]
	v_mul_f32_e64 v238, v227, v144
	s_waitcnt lgkmcnt(1)
	v_pk_mul_f32 v[174:175], v[228:229], v[168:169] op_sel_hi:[0,1]
	v_pk_mul_f32 v[172:173], v[228:229], v[210:211] op_sel_hi:[0,1]
	v_mul_f32_e64 v242, v228, v144
	v_pk_mul_f32 v[222:223], v[228:229], v[168:169] op_sel:[1,0]
	v_pk_mul_f32 v[176:177], v[228:229], v[210:211] op_sel:[1,0]
	v_mul_f32_e64 v246, v229, v144
	v_pk_fma_f32 v[154:155], v[228:229], v[120:121], v[154:155] op_sel_hi:[0,1,1]
	v_pk_fma_f32 v[164:165], v[228:229], v[214:215], v[164:165] op_sel_hi:[0,1,1]
	v_fma_f32 v238, v228, v148, v238
	v_pk_fma_f32 v[174:175], v[230:231], v[120:121], v[174:175] op_sel_hi:[0,1,1]
	v_pk_fma_f32 v[172:173], v[230:231], v[214:215], v[172:173] op_sel_hi:[0,1,1]
	v_fma_f32 v242, v230, v148, v242
	v_pk_fma_f32 v[222:223], v[230:231], v[120:121], v[222:223] op_sel:[1,0,0]
	v_pk_fma_f32 v[176:177], v[230:231], v[214:215], v[176:177] op_sel:[1,0,0]
	v_fma_f32 v246, v231, v148, v246
	v_pk_fma_f32 v[154:155], v[228:229], v[152:153], v[154:155] op_sel:[1,0,0]
	v_pk_fma_f32 v[164:165], v[228:229], v[218:219], v[164:165] op_sel:[1,0,0]
	v_fma_f32 v238, v229, v160, v238
	v_pk_fma_f32 v[174:175], v[230:231], v[152:153], v[174:175] op_sel:[1,0,0]
	v_pk_fma_f32 v[172:173], v[230:231], v[218:219], v[172:173] op_sel:[1,0,0]
	v_fma_f32 v242, v231, v160, v242
	s_waitcnt lgkmcnt(0)
	v_pk_fma_f32 v[222:223], v[232:233], v[152:153], v[222:223] op_sel_hi:[0,1,1]
	v_pk_fma_f32 v[176:177], v[232:233], v[218:219], v[176:177] op_sel_hi:[0,1,1]
	v_fma_f32 v246, v232, v160, v246
	v_pk_mul_f32 v[180:181], v[224:225], v[154:155] op_sel_hi:[0,1]
	v_pk_mul_f32 v[184:185], v[224:225], v[164:165] op_sel_hi:[0,1]
	v_mul_f32_e64 v188, v224, v238
	v_pk_fma_f32 v[180:181], v[224:225], v[174:175], v[180:181] op_sel:[1,0,0]
	v_pk_fma_f32 v[184:185], v[224:225], v[172:173], v[184:185] op_sel:[1,0,0]
	v_fma_f32 v188, v225, v242, v188
	v_pk_fma_f32 v[180:181], v[226:227], v[222:223], v[180:181] op_sel_hi:[0,1,1]
	v_pk_fma_f32 v[184:185], v[226:227], v[176:177], v[184:185] op_sel_hi:[0,1,1]
	v_fma_f32 v188, v226, v246, v188
	v_pk_fma_f32 v[180:181], v[232:233], v[62:63], v[180:181] op_sel:[1,0,0] neg_lo:[0,0,1] neg_hi:[0,0,1]
	v_pk_fma_f32 v[184:185], v[232:233], v[64:65], v[184:185] op_sel:[1,0,0] neg_lo:[0,0,1] neg_hi:[0,0,1]
	v_fma_f32 v188, v233, v102, -v188
	v_cmp_eq_u32_e64 s[10:11], 1, v235
	v_cmp_eq_u32_e64 s[14:15], 2, v235
	v_cmp_eq_u32_e64 s[20:21], 3, v235
	v_cmp_eq_u32_e64 s[22:23], 4, v235
	v_cmp_eq_u32_e64 s[30:31], 5, v235
	v_pk_add_f32 v[64:65], v[72:73], v[154:155]
	v_pk_add_f32 v[62:63], v[70:71], v[64:65]
	v_pk_add_f32 v[72:73], v[66:67], v[164:165]
	v_pk_add_f32 v[70:71], v[86:87], v[72:73]
	v_add_f32_e64 v120, v186, v238
	v_add_f32_e64 v66, v122, v120
	v_pk_add_f32 v[144:145], v[124:125], v[174:175]
	v_pk_add_f32 v[86:87], v[74:75], v[144:145]
	v_pk_add_f32 v[124:125], v[142:143], v[172:173]
	v_pk_add_f32 v[74:75], v[114:115], v[124:125]
	v_add_f32_e64 v148, v190, v242
	v_add_f32_e64 v102, v126, v148
	v_pk_add_f32 v[152:153], v[212:213], v[222:223]
	v_pk_add_f32 v[114:115], v[78:79], v[152:153]
	v_pk_add_f32 v[160:161], v[182:183], v[176:177]
	v_pk_add_f32 v[78:79], v[118:119], v[160:161]
	v_add_f32_e64 v168, v194, v246
	v_add_f32_e64 v118, v162, v168
	v_pk_add_f32 v[122:123], v[206:207], v[180:181]
	v_pk_add_f32 v[192:193], v[112:113], v[122:123]
	v_pk_add_f32 v[126:127], v[216:217], v[184:185]
	v_pk_add_f32 v[112:113], v[204:205], v[126:127]
	v_add_f32_e64 v142, v220, v188
	v_add_f32_e64 v204, v208, v142
	v_pk_fma_f32 v[208:209], v[132:133], v[62:63], v[192:193] op_sel_hi:[0,1,1]
	v_pk_fma_f32 v[212:213], v[132:133], v[70:71], v[112:113] op_sel_hi:[0,1,1]
	v_fma_f32 v216, v132, v66, v204
	v_pk_fma_f32 v[220:221], v[136:137], v[62:63], v[192:193] op_sel_hi:[0,1,1]
	v_pk_fma_f32 v[236:237], v[136:137], v[70:71], v[112:113] op_sel_hi:[0,1,1]
	v_fma_f32 v240, v136, v66, v204
	v_pk_fma_f32 v[208:209], v[132:133], v[86:87], v[208:209] op_sel:[1,0,0]
	v_pk_fma_f32 v[212:213], v[132:133], v[74:75], v[212:213] op_sel:[1,0,0]
	v_fma_f32 v216, v133, v102, v216
	v_pk_fma_f32 v[220:221], v[136:137], v[86:87], v[220:221] op_sel:[1,0,0]
	v_pk_fma_f32 v[236:237], v[136:137], v[74:75], v[236:237] op_sel:[1,0,0]
	v_fma_f32 v240, v137, v102, v240
	v_pk_fma_f32 v[208:209], v[134:135], v[114:115], v[208:209] op_sel_hi:[0,1,1]
	v_pk_fma_f32 v[212:213], v[134:135], v[78:79], v[212:213] op_sel_hi:[0,1,1]
	v_fma_f32 v216, v134, v118, v216
	v_pk_fma_f32 v[220:221], v[138:139], v[114:115], v[220:221] op_sel_hi:[0,1,1]
	v_pk_fma_f32 v[236:237], v[138:139], v[78:79], v[236:237] op_sel_hi:[0,1,1]
	v_fma_f32 v240, v138, v118, v240
	v_pk_fma_f32 v[192:193], v[36:37], v[62:63], v[192:193] op_sel_hi:[0,1,1]
	v_pk_fma_f32 v[112:113], v[36:37], v[70:71], v[112:113] op_sel_hi:[0,1,1]
	v_fma_f32 v204, v36, v66, v204
	v_pk_fma_f32 v[192:193], v[36:37], v[86:87], v[192:193] op_sel:[1,0,0]
	v_pk_fma_f32 v[112:113], v[36:37], v[74:75], v[112:113] op_sel:[1,0,0]
	v_fma_f32 v204, v37, v102, v204
	v_pk_fma_f32 v[192:193], v[38:39], v[114:115], v[192:193] op_sel_hi:[0,1,1]
	v_pk_fma_f32 v[112:113], v[38:39], v[78:79], v[112:113] op_sel_hi:[0,1,1]
	v_fma_f32 v204, v38, v118, v204
	v_cndmask_b32_e64 v162, 0, v1, s[10:11]
	v_cndmask_b32_e64 v163, 0, v1, s[14:15]
	v_cndmask_b32_e64 v182, 0, v1, s[20:21]
	v_cndmask_b32_e64 v183, 0, v1, s[22:23]
	v_cndmask_b32_e64 v186, 0, v1, s[30:31]
	v_add_f32_dpp v192, v208, v192 wave_shl:1 row_mask:0xf bank_mask:0xf bound_ctrl:1
	v_add_f32_dpp v193, v209, v193 wave_shl:1 row_mask:0xf bank_mask:0xf bound_ctrl:1
	v_add_f32_dpp v112, v212, v112 wave_shl:1 row_mask:0xf bank_mask:0xf bound_ctrl:1
	v_add_f32_dpp v113, v213, v113 wave_shl:1 row_mask:0xf bank_mask:0xf bound_ctrl:1
	v_add_f32_dpp v204, v216, v204 wave_shl:1 row_mask:0xf bank_mask:0xf bound_ctrl:1
	s_add_i32 s4, s34, 0
	s_cmpk_lt_i32 s4, 0x201
	s_cselect_b64 s[12:13], s[0:1], 0
	v_add_f32_dpp v192, v220, v192 wave_shr:1 row_mask:0xf bank_mask:0xf bound_ctrl:1
	v_add_f32_dpp v193, v221, v193 wave_shr:1 row_mask:0xf bank_mask:0xf bound_ctrl:1
	v_add_f32_dpp v112, v236, v112 wave_shr:1 row_mask:0xf bank_mask:0xf bound_ctrl:1
	v_add_f32_dpp v113, v237, v113 wave_shr:1 row_mask:0xf bank_mask:0xf bound_ctrl:1
	v_add_f32_dpp v204, v240, v204 wave_shr:1 row_mask:0xf bank_mask:0xf bound_ctrl:1
	v_pk_fma_f32 v[192:193], v[20:21], v[234:235], v[192:193] op_sel_hi:[1,0,1] neg_lo:[0,0,1] neg_hi:[0,0,1]
	v_pk_fma_f32 v[112:113], v[24:25], v[234:235], v[112:113] op_sel_hi:[1,0,1] neg_lo:[0,0,1] neg_hi:[0,0,1]
	v_fma_f32 v204, v30, v234, -v204
	v_pk_add_f32 v[192:193], v[192:193], v[162:163] neg_lo:[0,1] neg_hi:[0,1]
	v_pk_add_f32 v[112:113], v[112:113], v[182:183] neg_lo:[0,1] neg_hi:[0,1]
	v_add_f32_e64 v204, v204, -v186
	v_pk_mul_f32 v[190:191], v[192:193], v[192:193]
	v_pk_fma_f32 v[190:191], v[112:113], v[112:113], v[190:191]
	v_add_f32_e32 v190, v190, v191
	v_fma_f32 v190, v204, v204, v190
	v_cndmask_b32_e64 v191, 0, v190, s[12:13]
	v_add_f32_e32 v0, v0, v191
	s_add_i32 s4, s34, 5
	s_min_i32 s4, s4, 0x200
	s_mul_i32 s5, s4, 0x804
	s_add_i32 s5, s5, s35
	s_add_i32 s6, s5, 0x0
	s_add_i32 s7, s5, 0x101004
	s_add_i32 s8, s5, 0x202008
	s_add_i32 s11, s5, 0x30300c
	s_add_i32 s15, s5, 0x404010
	s_mul_i32 s9, s4, 0x180c
	s_add_i32 s9, s9, s33
	buffer_load_dword v20, v28, s[16:19], s6 offen nt
	buffer_load_dword v21, v28, s[16:19], s7 offen nt
	buffer_load_dword v24, v28, s[16:19], s8 offen nt
	buffer_load_dword v25, v28, s[16:19], s11 offen nt
	buffer_load_dword v30, v28, s[16:19], s15 offen nt
	buffer_load_dwordx3 v[36:38], v27, s[24:27], s9 offen nt
	s_waitcnt vmcnt(12)
	v_mov_b32_dpp v112, v8 wave_shr:1 row_mask:0xf bank_mask:0xf bound_ctrl:1
	v_mov_b32_dpp v113, v9 wave_shr:1 row_mask:0xf bank_mask:0xf bound_ctrl:1
	v_mov_b32_dpp v114, v10 wave_shr:1 row_mask:0xf bank_mask:0xf bound_ctrl:1
	v_mov_b32_dpp v132, v8 wave_shl:1 row_mask:0xf bank_mask:0xf bound_ctrl:1
	v_mov_b32_dpp v133, v9 wave_shl:1 row_mask:0xf bank_mask:0xf bound_ctrl:1
	v_mov_b32_dpp v134, v10 wave_shl:1 row_mask:0xf bank_mask:0xf bound_ctrl:1
	v_mov_b32_dpp v136, v2 wave_shr:1 row_mask:0xf bank_mask:0xf bound_ctrl:1
	v_mov_b32_dpp v137, v3 wave_shr:1 row_mask:0xf bank_mask:0xf bound_ctrl:1
	v_mov_b32_dpp v62, v4 wave_shr:1 row_mask:0xf bank_mask:0xf bound_ctrl:1
	v_mov_b32_dpp v63, v5 wave_shr:1 row_mask:0xf bank_mask:0xf bound_ctrl:1
	v_mov_b32_dpp v192, v6 wave_shr:1 row_mask:0xf bank_mask:0xf bound_ctrl:1
	v_mov_b32_dpp v204, v2 wave_shl:1 row_mask:0xf bank_mask:0xf bound_ctrl:1
	v_mov_b32_dpp v205, v3 wave_shl:1 row_mask:0xf bank_mask:0xf bound_ctrl:1
	v_mov_b32_dpp v66, v4 wave_shl:1 row_mask:0xf bank_mask:0xf bound_ctrl:1
	v_mov_b32_dpp v67, v5 wave_shl:1 row_mask:0xf bank_mask:0xf bound_ctrl:1
	v_mov_b32_dpp v208, v6 wave_shl:1 row_mask:0xf bank_mask:0xf bound_ctrl:1
	v_pk_mul_f32 v[70:71], v[2:3], v[8:9] op_sel_hi:[1,0]
	v_pk_mul_f32 v[212:213], v[4:5], v[8:9] op_sel_hi:[1,0]
	v_mul_f32_e64 v74, v6, v8
	v_pk_mul_f32 v[78:79], v[2:3], v[8:9] op_sel:[0,1]
	v_pk_mul_f32 v[216:217], v[4:5], v[8:9] op_sel:[0,1]
	v_mul_f32_e64 v86, v6, v9
	v_pk_mul_f32 v[102:103], v[2:3], v[10:11] op_sel_hi:[1,0]
	v_pk_mul_f32 v[220:221], v[4:5], v[10:11] op_sel_hi:[1,0]
	v_mul_f32_e64 v118, v6, v10
	v_pk_add_f32 v[138:139], v[2:3], v[136:137]
	v_pk_add_f32 v[224:225], v[4:5], v[62:63]
	v_add_f32_e64 v162, v6, v192
	v_pk_fma_f32 v[70:71], v[136:137], v[112:113], v[70:71] op_sel_hi:[1,0,1]
	v_pk_fma_f32 v[212:213], v[62:63], v[112:113], v[212:213] op_sel_hi:[1,0,1]
	v_fma_f32 v74, v192, v112, v74
	v_pk_fma_f32 v[78:79], v[136:137], v[112:113], v[78:79] op_sel:[0,1,0]
	v_pk_fma_f32 v[216:217], v[62:63], v[112:113], v[216:217] op_sel:[0,1,0]
	v_fma_f32 v86, v192, v113, v86
	v_pk_fma_f32 v[102:103], v[136:137], v[114:115], v[102:103] op_sel_hi:[1,0,1]
	v_pk_fma_f32 v[220:221], v[62:63], v[114:115], v[220:221] op_sel_hi:[1,0,1]
	v_fma_f32 v118, v192, v114, v118
	v_pk_add_f32 v[138:139], v[138:139], v[204:205]
	v_pk_add_f32 v[224:225], v[224:225], v[66:67]
	v_add_f32_e64 v162, v162, v208
	v_pk_fma_f32 v[70:71], v[204:205], v[132:133], v[70:71] op_sel_hi:[1,0,1]
	v_pk_fma_f32 v[212:213], v[66:67], v[132:133], v[212:213] op_sel_hi:[1,0,1]
	v_fma_f32 v74, v208, v132, v74
	v_pk_fma_f32 v[78:79], v[204:205], v[132:133], v[78:79] op_sel:[0,1,0]
	v_pk_fma_f32 v[216:217], v[66:67], v[132:133], v[216:217] op_sel:[0,1,0]
	v_fma_f32 v86, v208, v133, v86
	v_pk_fma_f32 v[102:103], v[204:205], v[134:135], v[102:103] op_sel_hi:[1,0,1]
	v_pk_fma_f32 v[220:221], v[66:67], v[134:135], v[220:221] op_sel_hi:[1,0,1]
	v_fma_f32 v118, v208, v134, v118
	s_barrier
	ds_read_b128 v[192:195], v23 offset:3072
	ds_read_b128 v[204:207], v23 offset:4096
	ds_read_b128 v[208:211], v23 offset:5120
	v_pk_add_f32 v[62:63], v[58:59], v[138:139]
	v_pk_add_f32 v[58:59], v[98:99], v[224:225]
	v_add_f32_e64 v66, v68, v162
	v_pk_add_f32 v[68:69], v[158:159], v[70:71]
	v_pk_add_f32 v[136:137], v[178:179], v[212:213]
	v_add_f32_e64 v228, v108, v74
	v_pk_add_f32 v[108:109], v[146:147], v[78:79]
	v_pk_add_f32 v[232:233], v[166:167], v[216:217]
	v_add_f32_e64 v236, v140, v86
	v_pk_add_f32 v[140:141], v[150:151], v[102:103]
	v_pk_add_f32 v[240:241], v[170:171], v[220:221]
	v_add_f32_e64 v244, v156, v118
	s_waitcnt lgkmcnt(2)
	v_pk_fma_f32 v[68:69], v[192:193], v[62:63], v[68:69] op_sel_hi:[0,1,1] neg_lo:[1,0,0] neg_hi:[1,0,0]
	v_pk_fma_f32 v[136:137], v[192:193], v[58:59], v[136:137] op_sel_hi:[0,1,1] neg_lo:[1,0,0] neg_hi:[1,0,0]
	v_fma_f32 v228, -v192, v66, v228
	v_pk_fma_f32 v[108:109], v[192:193], v[62:63], v[108:109] op_sel:[1,0,0] neg_lo:[1,0,0] neg_hi:[1,0,0]
	v_pk_fma_f32 v[232:233], v[192:193], v[58:59], v[232:233] op_sel:[1,0,0] neg_lo:[1,0,0] neg_hi:[1,0,0]
	v_fma_f32 v236, -v193, v66, v236
	v_pk_fma_f32 v[140:141], v[194:195], v[62:63], v[140:141] op_sel_hi:[0,1,1] neg_lo:[1,0,0] neg_hi:[1,0,0]
	v_pk_fma_f32 v[240:241], v[194:195], v[58:59], v[240:241] op_sel_hi:[0,1,1] neg_lo:[1,0,0] neg_hi:[1,0,0]
	v_fma_f32 v244, -v194, v66, v244
	v_pk_mul_f32 v[98:99], v[194:195], v[68:69] op_sel:[1,0]
	v_pk_mul_f32 v[158:159], v[194:195], v[136:137] op_sel:[1,0]
	v_mul_f32_e64 v178, v195, v228
	s_waitcnt lgkmcnt(1)
	v_pk_mul_f32 v[146:147], v[204:205], v[68:69] op_sel_hi:[0,1]
	v_pk_mul_f32 v[166:167], v[204:205], v[136:137] op_sel_hi:[0,1]
	v_mul_f32_e64 v182, v204, v228
	v_pk_mul_f32 v[150:151], v[204:205], v[68:69] op_sel:[1,0]
	v_pk_mul_f32 v[170:171], v[204:205], v[136:137] op_sel:[1,0]
	v_mul_f32_e64 v186, v205, v228
	v_pk_fma_f32 v[98:99], v[204:205], v[108:109], v[98:99] op_sel_hi:[0,1,1]
	v_pk_fma_f32 v[158:159], v[204:205], v[232:233], v[158:159] op_sel_hi:[0,1,1]
	v_fma_f32 v178, v204, v236, v178
	v_pk_fma_f32 v[146:147], v[206:207], v[108:109], v[146:147] op_sel_hi:[0,1,1]
	v_pk_fma_f32 v[166:167], v[206:207], v[232:233], v[166:167] op_sel_hi:[0,1,1]
	v_fma_f32 v182, v206, v236, v182
	v_pk_fma_f32 v[150:151], v[206:207], v[108:109], v[150:151] op_sel:[1,0,0]
	v_pk_fma_f32 v[170:171], v[206:207], v[232:233], v[170:171] op_sel:[1,0,0]
	v_fma_f32 v186, v207, v236, v186
	v_pk_fma_f32 v[98:99], v[204:205], v[140:141], v[98:99] op_sel:[1,0,0]
	v_pk_fma_f32 v[158:159], v[204:205], v[240:241], v[158:159] op_sel:[1,0,0]
	v_fma_f32 v178, v205, v244, v178
	v_pk_fma_f32 v[146:147], v[206:207], v[140:141], v[146:147] op_sel:[1,0,0]
	v_pk_fma_f32 v[166:167], v[206:207], v[240:241], v[166:167] op_sel:[1,0,0]
	v_fma_f32 v182, v207, v244, v182
	s_waitcnt lgkmcnt(0)
	v_pk_fma_f32 v[150:151], v[208:209], v[140:141], v[150:151] op_sel_hi:[0,1,1]
	v_pk_fma_f32 v[170:171], v[208:209], v[240:241], v[170:171] op_sel_hi:[0,1,1]
	v_fma_f32 v186, v208, v244, v186
	v_pk_mul_f32 v[156:157], v[192:193], v[98:99] op_sel_hi:[0,1]
	v_pk_mul_f32 v[248:249], v[192:193], v[158:159] op_sel_hi:[0,1]
	v_mul_f32_e64 v190, v192, v178
	v_pk_fma_f32 v[156:157], v[192:193], v[146:147], v[156:157] op_sel:[1,0,0]
	v_pk_fma_f32 v[248:249], v[192:193], v[166:167], v[248:249] op_sel:[1,0,0]
	v_fma_f32 v190, v193, v182, v190
	v_pk_fma_f32 v[156:157], v[194:195], v[150:151], v[156:157] op_sel_hi:[0,1,1]
	v_pk_fma_f32 v[248:249], v[194:195], v[170:171], v[248:249] op_sel_hi:[0,1,1]
	v_fma_f32 v190, v194, v186, v190
	v_pk_fma_f32 v[156:157], v[208:209], v[62:63], v[156:157] op_sel:[1,0,0] neg_lo:[0,0,1] neg_hi:[0,0,1]
	v_pk_fma_f32 v[248:249], v[208:209], v[58:59], v[248:249] op_sel:[1,0,0] neg_lo:[0,0,1] neg_hi:[0,0,1]
	v_fma_f32 v190, v209, v66, -v190
	v_cmp_eq_u32_e64 s[10:11], 1, v211
	v_cmp_eq_u32_e64 s[14:15], 2, v211
	v_cmp_eq_u32_e64 s[20:21], 3, v211
	v_cmp_eq_u32_e64 s[22:23], 4, v211
	v_cmp_eq_u32_e64 s[30:31], 5, v211
	v_pk_add_f32 v[58:59], v[64:65], v[98:99]
	v_pk_add_f32 v[62:63], v[72:73], v[158:159]
	v_add_f32_e64 v64, v120, v178
	v_pk_add_f32 v[66:67], v[144:145], v[146:147]
	v_pk_add_f32 v[68:69], v[124:125], v[166:167]
	v_add_f32_e64 v72, v148, v182
	v_pk_add_f32 v[108:109], v[152:153], v[150:151]
	v_pk_add_f32 v[120:121], v[160:161], v[170:171]
	v_add_f32_e64 v124, v168, v186
	v_pk_add_f32 v[136:137], v[122:123], v[156:157]
	v_pk_add_f32 v[122:123], v[126:127], v[248:249]
	v_add_f32_e64 v126, v142, v190
	v_pk_fma_f32 v[140:141], v[40:41], v[58:59], v[136:137] op_sel_hi:[0,1,1]
	v_pk_fma_f32 v[142:143], v[40:41], v[62:63], v[122:123] op_sel_hi:[0,1,1]
	v_fma_f32 v214, v40, v64, v126
	v_pk_fma_f32 v[144:145], v[44:45], v[58:59], v[136:137] op_sel_hi:[0,1,1]
	v_pk_fma_f32 v[218:219], v[44:45], v[62:63], v[122:123] op_sel_hi:[0,1,1]
	v_fma_f32 v226, v44, v64, v126
	v_pk_fma_f32 v[140:141], v[40:41], v[66:67], v[140:141] op_sel:[1,0,0]
	v_pk_fma_f32 v[142:143], v[40:41], v[68:69], v[142:143] op_sel:[1,0,0]
	v_fma_f32 v214, v41, v72, v214
	v_pk_fma_f32 v[144:145], v[44:45], v[66:67], v[144:145] op_sel:[1,0,0]
	v_pk_fma_f32 v[218:219], v[44:45], v[68:69], v[218:219] op_sel:[1,0,0]
	v_fma_f32 v226, v45, v72, v226
	v_pk_fma_f32 v[140:141], v[42:43], v[108:109], v[140:141] op_sel_hi:[0,1,1]
	v_pk_fma_f32 v[142:143], v[42:43], v[120:121], v[142:143] op_sel_hi:[0,1,1]
	v_fma_f32 v214, v42, v124, v214
	v_pk_fma_f32 v[144:145], v[46:47], v[108:109], v[144:145] op_sel_hi:[0,1,1]
	v_pk_fma_f32 v[218:219], v[46:47], v[120:121], v[218:219] op_sel_hi:[0,1,1]
	v_fma_f32 v226, v46, v124, v226
	v_pk_fma_f32 v[136:137], v[88:89], v[58:59], v[136:137] op_sel_hi:[0,1,1]
	v_pk_fma_f32 v[122:123], v[88:89], v[62:63], v[122:123] op_sel_hi:[0,1,1]
	v_fma_f32 v126, v88, v64, v126
	v_pk_fma_f32 v[136:137], v[88:89], v[66:67], v[136:137] op_sel:[1,0,0]
	v_pk_fma_f32 v[122:123], v[88:89], v[68:69], v[122:123] op_sel:[1,0,0]
	v_fma_f32 v126, v89, v72, v126
	v_pk_fma_f32 v[136:137], v[90:91], v[108:109], v[136:137] op_sel_hi:[0,1,1]
	v_pk_fma_f32 v[122:123], v[90:91], v[120:121], v[122:123] op_sel_hi:[0,1,1]
	v_fma_f32 v126, v90, v124, v126
	v_cndmask_b32_e64 v230, 0, v1, s[10:11]
	v_cndmask_b32_e64 v231, 0, v1, s[14:15]
	v_cndmask_b32_e64 v148, 0, v1, s[20:21]
	v_cndmask_b32_e64 v149, 0, v1, s[22:23]
	v_cndmask_b32_e64 v152, 0, v1, s[30:31]
	v_add_f32_dpp v136, v140, v136 wave_shl:1 row_mask:0xf bank_mask:0xf bound_ctrl:1
	v_add_f32_dpp v137, v141, v137 wave_shl:1 row_mask:0xf bank_mask:0xf bound_ctrl:1
	v_add_f32_dpp v122, v142, v122 wave_shl:1 row_mask:0xf bank_mask:0xf bound_ctrl:1
	v_add_f32_dpp v123, v143, v123 wave_shl:1 row_mask:0xf bank_mask:0xf bound_ctrl:1
	v_add_f32_dpp v126, v214, v126 wave_shl:1 row_mask:0xf bank_mask:0xf bound_ctrl:1
	s_add_i32 s4, s34, 1
	s_cmpk_lt_i32 s4, 0x201
	s_cselect_b64 s[12:13], s[0:1], 0
	v_add_f32_dpp v136, v144, v136 wave_shr:1 row_mask:0xf bank_mask:0xf bound_ctrl:1
	v_add_f32_dpp v137, v145, v137 wave_shr:1 row_mask:0xf bank_mask:0xf bound_ctrl:1
	v_add_f32_dpp v122, v218, v122 wave_shr:1 row_mask:0xf bank_mask:0xf bound_ctrl:1
	v_add_f32_dpp v123, v219, v123 wave_shr:1 row_mask:0xf bank_mask:0xf bound_ctrl:1
	v_add_f32_dpp v126, v226, v126 wave_shr:1 row_mask:0xf bank_mask:0xf bound_ctrl:1
	v_pk_fma_f32 v[136:137], v[48:49], v[210:211], v[136:137] op_sel_hi:[1,0,1] neg_lo:[0,0,1] neg_hi:[0,0,1]
	v_pk_fma_f32 v[122:123], v[50:51], v[210:211], v[122:123] op_sel_hi:[1,0,1] neg_lo:[0,0,1] neg_hi:[0,0,1]
	v_fma_f32 v126, v52, v210, -v126
	v_pk_add_f32 v[136:137], v[136:137], v[230:231] neg_lo:[0,1] neg_hi:[0,1]
	v_pk_add_f32 v[122:123], v[122:123], v[148:149] neg_lo:[0,1] neg_hi:[0,1]
	v_add_f32_e64 v126, v126, -v152
	v_pk_mul_f32 v[160:161], v[136:137], v[136:137]
	v_pk_fma_f32 v[160:161], v[122:123], v[122:123], v[160:161]
	v_add_f32_e32 v160, v160, v161
	v_fma_f32 v160, v126, v126, v160
	v_cndmask_b32_e64 v161, 0, v160, s[12:13]
	v_add_f32_e32 v0, v0, v161
	s_add_i32 s4, s34, 6
	s_min_i32 s4, s4, 0x200
	s_mul_i32 s5, s4, 0x804
	s_add_i32 s5, s5, s35
	s_add_i32 s6, s5, 0x0
	s_add_i32 s7, s5, 0x101004
	s_add_i32 s8, s5, 0x202008
	s_add_i32 s11, s5, 0x30300c
	s_add_i32 s15, s5, 0x404010
	s_mul_i32 s9, s4, 0x180c
	s_add_i32 s9, s9, s33
	buffer_load_dword v40, v28, s[16:19], s6 offen nt
	buffer_load_dword v41, v28, s[16:19], s7 offen nt
	buffer_load_dword v42, v28, s[16:19], s8 offen nt
	buffer_load_dword v43, v28, s[16:19], s11 offen nt
	buffer_load_dword v44, v28, s[16:19], s15 offen nt
	buffer_load_dwordx3 v[48:50], v27, s[24:27], s9 offen nt
	s_waitcnt vmcnt(12)
	v_mov_b32_dpp v64, v32 wave_shr:1 row_mask:0xf bank_mask:0xf bound_ctrl:1
	v_mov_b32_dpp v65, v33 wave_shr:1 row_mask:0xf bank_mask:0xf bound_ctrl:1
	v_mov_b32_dpp v66, v34 wave_shr:1 row_mask:0xf bank_mask:0xf bound_ctrl:1
	v_mov_b32_dpp v88, v32 wave_shl:1 row_mask:0xf bank_mask:0xf bound_ctrl:1
	v_mov_b32_dpp v89, v33 wave_shl:1 row_mask:0xf bank_mask:0xf bound_ctrl:1
	v_mov_b32_dpp v90, v34 wave_shl:1 row_mask:0xf bank_mask:0xf bound_ctrl:1
	v_mov_b32_dpp v46, v12 wave_shr:1 row_mask:0xf bank_mask:0xf bound_ctrl:1
	v_mov_b32_dpp v47, v13 wave_shr:1 row_mask:0xf bank_mask:0xf bound_ctrl:1
	v_mov_b32_dpp v52, v14 wave_shr:1 row_mask:0xf bank_mask:0xf bound_ctrl:1
	v_mov_b32_dpp v53, v15 wave_shr:1 row_mask:0xf bank_mask:0xf bound_ctrl:1
	v_mov_b32_dpp v58, v16 wave_shr:1 row_mask:0xf bank_mask:0xf bound_ctrl:1
	v_mov_b32_dpp v62, v12 wave_shl:1 row_mask:0xf bank_mask:0xf bound_ctrl:1
	v_mov_b32_dpp v63, v13 wave_shl:1 row_mask:0xf bank_mask:0xf bound_ctrl:1
	v_mov_b32_dpp v68, v14 wave_shl:1 row_mask:0xf bank_mask:0xf bound_ctrl:1
	v_mov_b32_dpp v69, v15 wave_shl:1 row_mask:0xf bank_mask:0xf bound_ctrl:1
	v_mov_b32_dpp v122, v16 wave_shl:1 row_mask:0xf bank_mask:0xf bound_ctrl:1
	v_pk_mul_f32 v[72:73], v[12:13], v[32:33] op_sel_hi:[1,0]
	v_pk_mul_f32 v[126:127], v[14:15], v[32:33] op_sel_hi:[1,0]
	v_mul_f32_e64 v108, v16, v32
	v_pk_mul_f32 v[120:121], v[12:13], v[32:33] op_sel:[0,1]
	v_pk_mul_f32 v[142:143], v[14:15], v[32:33] op_sel:[0,1]
	v_mul_f32_e64 v124, v16, v33
	v_pk_mul_f32 v[136:137], v[12:13], v[34:35] op_sel_hi:[1,0]
	v_pk_mul_f32 v[194:195], v[14:15], v[34:35] op_sel_hi:[1,0]
	v_mul_f32_e64 v140, v16, v34
	v_pk_add_f32 v[144:145], v[12:13], v[46:47]
	v_pk_add_f32 v[206:207], v[14:15], v[52:53]
	v_add_f32_e64 v148, v16, v58
	v_pk_fma_f32 v[72:73], v[46:47], v[64:65], v[72:73] op_sel_hi:[1,0,1]
	v_pk_fma_f32 v[126:127], v[52:53], v[64:65], v[126:127] op_sel_hi:[1,0,1]
	v_fma_f32 v108, v58, v64, v108
	v_pk_fma_f32 v[120:121], v[46:47], v[64:65], v[120:121] op_sel:[0,1,0]
	v_pk_fma_f32 v[142:143], v[52:53], v[64:65], v[142:143] op_sel:[0,1,0]
	v_fma_f32 v124, v58, v65, v124
	v_pk_fma_f32 v[136:137], v[46:47], v[66:67], v[136:137] op_sel_hi:[1,0,1]
	v_pk_fma_f32 v[194:195], v[52:53], v[66:67], v[194:195] op_sel_hi:[1,0,1]
	v_fma_f32 v140, v58, v66, v140
	v_pk_add_f32 v[144:145], v[144:145], v[62:63]
	v_pk_add_f32 v[206:207], v[206:207], v[68:69]
	v_add_f32_e64 v148, v148, v122
	v_pk_fma_f32 v[72:73], v[62:63], v[88:89], v[72:73] op_sel_hi:[1,0,1]
	v_pk_fma_f32 v[126:127], v[68:69], v[88:89], v[126:127] op_sel_hi:[1,0,1]
	v_fma_f32 v108, v122, v88, v108
	v_pk_fma_f32 v[120:121], v[62:63], v[88:89], v[120:121] op_sel:[0,1,0]
	v_pk_fma_f32 v[142:143], v[68:69], v[88:89], v[142:143] op_sel:[0,1,0]
	v_fma_f32 v124, v122, v89, v124
	v_pk_fma_f32 v[136:137], v[62:63], v[90:91], v[136:137] op_sel_hi:[1,0,1]
	v_pk_fma_f32 v[194:195], v[68:69], v[90:91], v[194:195] op_sel_hi:[1,0,1]
	v_fma_f32 v140, v122, v90, v140
	s_barrier
	ds_read_b128 v[208:211], v23 offset:0
	ds_read_b128 v[228:231], v23 offset:1024
	ds_read_b128 v[232:235], v23 offset:2048
	v_pk_add_f32 v[52:53], v[138:139], v[144:145]
	v_pk_add_f32 v[46:47], v[202:203], v[52:53]
	v_pk_add_f32 v[58:59], v[224:225], v[206:207]
	v_pk_add_f32 v[62:63], v[196:197], v[58:59]
	v_add_f32_e64 v122, v162, v148
	v_add_f32_e64 v68, v200, v122
	v_pk_add_f32 v[152:153], v[70:71], v[72:73]
	v_pk_add_f32 v[160:161], v[106:107], v[152:153]
	v_pk_add_f32 v[70:71], v[212:213], v[126:127]
	v_pk_add_f32 v[168:169], v[76:77], v[70:71]
	v_add_f32_e64 v106, v74, v108
	v_add_f32_e64 v138, v84, v106
	v_pk_add_f32 v[76:77], v[78:79], v[120:121]
	v_pk_add_f32 v[84:85], v[110:111], v[76:77]
	v_pk_add_f32 v[74:75], v[216:217], v[142:143]
	v_pk_add_f32 v[192:193], v[96:97], v[74:75]
	v_add_f32_e64 v78, v86, v124
	v_add_f32_e64 v110, v100, v78
	v_pk_add_f32 v[96:97], v[102:103], v[136:137]
	v_pk_add_f32 v[100:101], v[198:199], v[96:97]
	v_pk_add_f32 v[86:87], v[220:221], v[194:195]
	v_pk_add_f32 v[196:197], v[104:105], v[86:87]
	v_add_f32_e64 v102, v118, v140
	v_add_f32_e64 v162, v116, v102
	s_waitcnt lgkmcnt(2)
	v_pk_fma_f32 v[160:161], v[208:209], v[46:47], v[160:161] op_sel_hi:[0,1,1] neg_lo:[1,0,0] neg_hi:[1,0,0]
	v_pk_fma_f32 v[168:169], v[208:209], v[62:63], v[168:169] op_sel_hi:[0,1,1] neg_lo:[1,0,0] neg_hi:[1,0,0]
	v_fma_f32 v138, -v208, v68, v138
	v_pk_fma_f32 v[84:85], v[208:209], v[46:47], v[84:85] op_sel:[1,0,0] neg_lo:[1,0,0] neg_hi:[1,0,0]
	v_pk_fma_f32 v[192:193], v[208:209], v[62:63], v[192:193] op_sel:[1,0,0] neg_lo:[1,0,0] neg_hi:[1,0,0]
	v_fma_f32 v110, -v209, v68, v110
	v_pk_fma_f32 v[100:101], v[210:211], v[46:47], v[100:101] op_sel_hi:[0,1,1] neg_lo:[1,0,0] neg_hi:[1,0,0]
	v_pk_fma_f32 v[196:197], v[210:211], v[62:63], v[196:197] op_sel_hi:[0,1,1] neg_lo:[1,0,0] neg_hi:[1,0,0]
	v_fma_f32 v162, -v210, v68, v162
	v_pk_mul_f32 v[118:119], v[210:211], v[160:161] op_sel:[1,0]
	v_pk_mul_f32 v[214:215], v[210:211], v[168:169] op_sel:[1,0]
	v_mul_f32_e64 v104, v211, v138
	s_waitcnt lgkmcnt(1)
	v_pk_mul_f32 v[198:199], v[228:229], v[160:161] op_sel_hi:[0,1]
	v_pk_mul_f32 v[218:219], v[228:229], v[168:169] op_sel_hi:[0,1]
	v_mul_f32_e64 v116, v228, v138
	v_pk_mul_f32 v[202:203], v[228:229], v[160:161] op_sel:[1,0]
	v_pk_mul_f32 v[226:227], v[228:229], v[168:169] op_sel:[1,0]
	v_mul_f32_e64 v200, v229, v138
	v_pk_fma_f32 v[118:119], v[228:229], v[84:85], v[118:119] op_sel_hi:[0,1,1]
	v_pk_fma_f32 v[214:215], v[228:229], v[192:193], v[214:215] op_sel_hi:[0,1,1]
	v_fma_f32 v104, v228, v110, v104
	v_pk_fma_f32 v[198:199], v[230:231], v[84:85], v[198:199] op_sel_hi:[0,1,1]
	v_pk_fma_f32 v[218:219], v[230:231], v[192:193], v[218:219] op_sel_hi:[0,1,1]
	v_fma_f32 v116, v230, v110, v116
	v_pk_fma_f32 v[202:203], v[230:231], v[84:85], v[202:203] op_sel:[1,0,0]
	v_pk_fma_f32 v[226:227], v[230:231], v[192:193], v[226:227] op_sel:[1,0,0]
	v_fma_f32 v200, v231, v110, v200
	v_pk_fma_f32 v[118:119], v[228:229], v[100:101], v[118:119] op_sel:[1,0,0]
	v_pk_fma_f32 v[214:215], v[228:229], v[196:197], v[214:215] op_sel:[1,0,0]
	v_fma_f32 v104, v229, v162, v104
	v_pk_fma_f32 v[198:199], v[230:231], v[100:101], v[198:199] op_sel:[1,0,0]
	v_pk_fma_f32 v[218:219], v[230:231], v[196:197], v[218:219] op_sel:[1,0,0]
	v_fma_f32 v116, v231, v162, v116
	s_waitcnt lgkmcnt(0)
	v_pk_fma_f32 v[202:203], v[232:233], v[100:101], v[202:203] op_sel_hi:[0,1,1]
	v_pk_fma_f32 v[226:227], v[232:233], v[196:197], v[226:227] op_sel_hi:[0,1,1]
	v_fma_f32 v200, v232, v162, v200
	v_pk_mul_f32 v[204:205], v[208:209], v[118:119] op_sel_hi:[0,1]
	v_pk_mul_f32 v[212:213], v[208:209], v[214:215] op_sel_hi:[0,1]
	v_mul_f32_e64 v216, v208, v104
	v_pk_fma_f32 v[204:205], v[208:209], v[198:199], v[204:205] op_sel:[1,0,0]
	v_pk_fma_f32 v[212:213], v[208:209], v[218:219], v[212:213] op_sel:[1,0,0]
	v_fma_f32 v216, v209, v116, v216
	v_pk_fma_f32 v[204:205], v[210:211], v[202:203], v[204:205] op_sel_hi:[0,1,1]
	v_pk_fma_f32 v[212:213], v[210:211], v[226:227], v[212:213] op_sel_hi:[0,1,1]
	v_fma_f32 v216, v210, v200, v216
	v_pk_fma_f32 v[204:205], v[232:233], v[46:47], v[204:205] op_sel:[1,0,0] neg_lo:[0,0,1] neg_hi:[0,0,1]
	v_pk_fma_f32 v[212:213], v[232:233], v[62:63], v[212:213] op_sel:[1,0,0] neg_lo:[0,0,1] neg_hi:[0,0,1]
	v_fma_f32 v216, v233, v68, -v216
	v_cmp_eq_u32_e64 s[10:11], 1, v235
	v_cmp_eq_u32_e64 s[14:15], 2, v235
	v_cmp_eq_u32_e64 s[20:21], 3, v235
	v_cmp_eq_u32_e64 s[22:23], 4, v235
	v_cmp_eq_u32_e64 s[30:31], 5, v235
	v_pk_add_f32 v[68:69], v[98:99], v[118:119]
	v_pk_add_f32 v[46:47], v[154:155], v[68:69]
	v_pk_add_f32 v[62:63], v[158:159], v[214:215]
	v_pk_add_f32 v[84:85], v[164:165], v[62:63]
	v_add_f32_e64 v100, v178, v104
	v_add_f32_e64 v98, v238, v100
	v_pk_add_f32 v[160:161], v[146:147], v[198:199]
	v_pk_add_f32 v[110:111], v[174:175], v[160:161]
	v_pk_add_f32 v[138:139], v[166:167], v[218:219]
	v_pk_add_f32 v[146:147], v[172:173], v[138:139]
	v_add_f32_e64 v164, v182, v116
	v_add_f32_e64 v154, v242, v164
	v_pk_add_f32 v[168:169], v[150:151], v[202:203]
	v_pk_add_f32 v[158:159], v[222:223], v[168:169]
	v_pk_add_f32 v[150:151], v[170:171], v[226:227]
	v_pk_add_f32 v[162:163], v[176:177], v[150:151]
	v_add_f32_e64 v172, v186, v200
	v_add_f32_e64 v166, v246, v172
	v_pk_add_f32 v[170:171], v[156:157], v[204:205]
	v_pk_add_f32 v[176:177], v[180:181], v[170:171]
	v_pk_add_f32 v[174:175], v[248:249], v[212:213]
	v_pk_add_f32 v[156:157], v[184:185], v[174:175]
	v_add_f32_e64 v178, v190, v216
	v_add_f32_e64 v180, v188, v178
	v_pk_fma_f32 v[184:185], v[80:81], v[46:47], v[176:177] op_sel_hi:[0,1,1]
	v_pk_fma_f32 v[188:189], v[80:81], v[84:85], v[156:157] op_sel_hi:[0,1,1]
	v_fma_f32 v192, v80, v98, v180
	v_pk_fma_f32 v[196:197], v[92:93], v[46:47], v[176:177] op_sel_hi:[0,1,1]
	v_pk_fma_f32 v[220:221], v[92:93], v[84:85], v[156:157] op_sel_hi:[0,1,1]
	v_fma_f32 v224, v92, v98, v180
	v_pk_fma_f32 v[184:185], v[80:81], v[110:111], v[184:185] op_sel:[1,0,0]
	v_pk_fma_f32 v[188:189], v[80:81], v[146:147], v[188:189] op_sel:[1,0,0]
	v_fma_f32 v192, v81, v154, v192
	v_pk_fma_f32 v[196:197], v[92:93], v[110:111], v[196:197] op_sel:[1,0,0]
	v_pk_fma_f32 v[220:221], v[92:93], v[146:147], v[220:221] op_sel:[1,0,0]
	v_fma_f32 v224, v93, v154, v224
	v_pk_fma_f32 v[184:185], v[82:83], v[158:159], v[184:185] op_sel_hi:[0,1,1]
	v_pk_fma_f32 v[188:189], v[82:83], v[162:163], v[188:189] op_sel_hi:[0,1,1]
	v_fma_f32 v192, v82, v166, v192
	v_pk_fma_f32 v[196:197], v[94:95], v[158:159], v[196:197] op_sel_hi:[0,1,1]
	v_pk_fma_f32 v[220:221], v[94:95], v[162:163], v[220:221] op_sel_hi:[0,1,1]
	v_fma_f32 v224, v94, v166, v224
	v_pk_fma_f32 v[176:177], v[128:129], v[46:47], v[176:177] op_sel_hi:[0,1,1]
	v_pk_fma_f32 v[156:157], v[128:129], v[84:85], v[156:157] op_sel_hi:[0,1,1]
	v_fma_f32 v180, v128, v98, v180
	v_pk_fma_f32 v[176:177], v[128:129], v[110:111], v[176:177] op_sel:[1,0,0]
	v_pk_fma_f32 v[156:157], v[128:129], v[146:147], v[156:157] op_sel:[1,0,0]
	v_fma_f32 v180, v129, v154, v180
	v_pk_fma_f32 v[176:177], v[130:131], v[158:159], v[176:177] op_sel_hi:[0,1,1]
	v_pk_fma_f32 v[156:157], v[130:131], v[162:163], v[156:157] op_sel_hi:[0,1,1]
	v_fma_f32 v180, v130, v166, v180
	v_cndmask_b32_e64 v182, 0, v1, s[10:11]
	v_cndmask_b32_e64 v183, 0, v1, s[14:15]
	v_cndmask_b32_e64 v186, 0, v1, s[20:21]
	v_cndmask_b32_e64 v187, 0, v1, s[22:23]
	v_cndmask_b32_e64 v190, 0, v1, s[30:31]
	v_add_f32_dpp v176, v184, v176 wave_shl:1 row_mask:0xf bank_mask:0xf bound_ctrl:1
	v_add_f32_dpp v177, v185, v177 wave_shl:1 row_mask:0xf bank_mask:0xf bound_ctrl:1
	v_add_f32_dpp v156, v188, v156 wave_shl:1 row_mask:0xf bank_mask:0xf bound_ctrl:1
	v_add_f32_dpp v157, v189, v157 wave_shl:1 row_mask:0xf bank_mask:0xf bound_ctrl:1
	v_add_f32_dpp v180, v192, v180 wave_shl:1 row_mask:0xf bank_mask:0xf bound_ctrl:1
	s_add_i32 s4, s34, 2
	s_cmpk_lt_i32 s4, 0x201
	s_cselect_b64 s[12:13], s[0:1], 0
	v_add_f32_dpp v176, v196, v176 wave_shr:1 row_mask:0xf bank_mask:0xf bound_ctrl:1
	v_add_f32_dpp v177, v197, v177 wave_shr:1 row_mask:0xf bank_mask:0xf bound_ctrl:1
	v_add_f32_dpp v156, v220, v156 wave_shr:1 row_mask:0xf bank_mask:0xf bound_ctrl:1
	v_add_f32_dpp v157, v221, v157 wave_shr:1 row_mask:0xf bank_mask:0xf bound_ctrl:1
	v_add_f32_dpp v180, v224, v180 wave_shr:1 row_mask:0xf bank_mask:0xf bound_ctrl:1
	v_pk_fma_f32 v[176:177], v[54:55], v[234:235], v[176:177] op_sel_hi:[1,0,1] neg_lo:[0,0,1] neg_hi:[0,0,1]
	v_pk_fma_f32 v[156:157], v[56:57], v[234:235], v[156:157] op_sel_hi:[1,0,1] neg_lo:[0,0,1] neg_hi:[0,0,1]
	v_fma_f32 v180, v60, v234, -v180
	v_pk_add_f32 v[176:177], v[176:177], v[182:183] neg_lo:[0,1] neg_hi:[0,1]
	v_pk_add_f32 v[156:157], v[156:157], v[186:187] neg_lo:[0,1] neg_hi:[0,1]
	v_add_f32_e64 v180, v180, -v190
	v_pk_mul_f32 v[222:223], v[176:177], v[176:177]
	v_pk_fma_f32 v[222:223], v[156:157], v[156:157], v[222:223]
	v_add_f32_e32 v222, v222, v223
	v_fma_f32 v222, v180, v180, v222
	v_cndmask_b32_e64 v223, 0, v222, s[12:13]
	v_add_f32_e32 v0, v0, v223
	s_add_i32 s4, s34, 7
	s_min_i32 s4, s4, 0x200
	s_mul_i32 s5, s4, 0x804
	s_add_i32 s5, s5, s35
	s_add_i32 s6, s5, 0x0
	s_add_i32 s7, s5, 0x101004
	s_add_i32 s8, s5, 0x202008
	s_add_i32 s11, s5, 0x30300c
	s_add_i32 s15, s5, 0x404010
	s_mul_i32 s9, s4, 0x180c
	s_add_i32 s9, s9, s33
	buffer_load_dword v46, v28, s[16:19], s6 offen nt
	buffer_load_dword v47, v28, s[16:19], s7 offen nt
	buffer_load_dword v54, v28, s[16:19], s8 offen nt
	buffer_load_dword v55, v28, s[16:19], s11 offen nt
	buffer_load_dword v56, v28, s[16:19], s15 offen nt
	buffer_load_dwordx3 v[80:82], v27, s[24:27], s9 offen nt
	s_waitcnt vmcnt(12)
	v_mov_b32_dpp v92, v36 wave_shr:1 row_mask:0xf bank_mask:0xf bound_ctrl:1
	v_mov_b32_dpp v93, v37 wave_shr:1 row_mask:0xf bank_mask:0xf bound_ctrl:1
	v_mov_b32_dpp v94, v38 wave_shr:1 row_mask:0xf bank_mask:0xf bound_ctrl:1
	v_mov_b32_dpp v128, v36 wave_shl:1 row_mask:0xf bank_mask:0xf bound_ctrl:1
	v_mov_b32_dpp v129, v37 wave_shl:1 row_mask:0xf bank_mask:0xf bound_ctrl:1
	v_mov_b32_dpp v130, v38 wave_shl:1 row_mask:0xf bank_mask:0xf bound_ctrl:1
	v_mov_b32_dpp v98, v20 wave_shr:1 row_mask:0xf bank_mask:0xf bound_ctrl:1
	v_mov_b32_dpp v99, v21 wave_shr:1 row_mask:0xf bank_mask:0xf bound_ctrl:1
	v_mov_b32_dpp v110, v24 wave_shr:1 row_mask:0xf bank_mask:0xf bound_ctrl:1
	v_mov_b32_dpp v111, v25 wave_shr:1 row_mask:0xf bank_mask:0xf bound_ctrl:1
	v_mov_b32_dpp v60, v30 wave_shr:1 row_mask:0xf bank_mask:0xf bound_ctrl:1
	v_mov_b32_dpp v146, v20 wave_shl:1 row_mask:0xf bank_mask:0xf bound_ctrl:1
	v_mov_b32_dpp v147, v21 wave_shl:1 row_mask:0xf bank_mask:0xf bound_ctrl:1
	v_mov_b32_dpp v154, v24 wave_shl:1 row_mask:0xf bank_mask:0xf bound_ctrl:1
	v_mov_b32_dpp v155, v25 wave_shl:1 row_mask:0xf bank_mask:0xf bound_ctrl:1
	v_mov_b32_dpp v84, v30 wave_shl:1 row_mask:0xf bank_mask:0xf bound_ctrl:1
	v_pk_mul_f32 v[156:157], v[20:21], v[36:37] op_sel_hi:[1,0]
	v_pk_mul_f32 v[176:177], v[24:25], v[36:37] op_sel_hi:[1,0]
	v_mul_f32_e64 v158, v30, v36
	v_pk_mul_f32 v[180:181], v[20:21], v[36:37] op_sel:[0,1]
	v_pk_mul_f32 v[184:185], v[24:25], v[36:37] op_sel:[0,1]
	v_mul_f32_e64 v162, v30, v37
	v_pk_mul_f32 v[188:189], v[20:21], v[38:39] op_sel_hi:[1,0]
	v_pk_mul_f32 v[192:193], v[24:25], v[38:39] op_sel_hi:[1,0]
	v_mul_f32_e64 v166, v30, v38
	v_pk_add_f32 v[196:197], v[20:21], v[98:99]
	v_pk_add_f32 v[208:209], v[24:25], v[110:111]
	v_add_f32_e64 v182, v30, v60
	v_pk_fma_f32 v[156:157], v[98:99], v[92:93], v[156:157] op_sel_hi:[1,0,1]
	v_pk_fma_f32 v[176:177], v[110:111], v[92:93], v[176:177] op_sel_hi:[1,0,1]
	v_fma_f32 v158, v60, v92, v158
	v_pk_fma_f32 v[180:181], v[98:99], v[92:93], v[180:181] op_sel:[0,1,0]
	v_pk_fma_f32 v[184:185], v[110:111], v[92:93], v[184:185] op_sel:[0,1,0]
	v_fma_f32 v162, v60, v93, v162
	v_pk_fma_f32 v[188:189], v[98:99], v[94:95], v[188:189] op_sel_hi:[1,0,1]
	v_pk_fma_f32 v[192:193], v[110:111], v[94:95], v[192:193] op_sel_hi:[1,0,1]
	v_fma_f32 v166, v60, v94, v166
	v_pk_add_f32 v[196:197], v[196:197], v[146:147]
	v_pk_add_f32 v[208:209], v[208:209], v[154:155]
	v_add_f32_e64 v182, v182, v84
	v_pk_fma_f32 v[156:157], v[146:147], v[128:129], v[156:157] op_sel_hi:[1,0,1]
	v_pk_fma_f32 v[176:177], v[154:155], v[128:129], v[176:177] op_sel_hi:[1,0,1]
	v_fma_f32 v158, v84, v128, v158
	v_pk_fma_f32 v[180:181], v[146:147], v[128:129], v[180:181] op_sel:[0,1,0]
	v_pk_fma_f32 v[184:185], v[154:155], v[128:129], v[184:185] op_sel:[0,1,0]
	v_fma_f32 v162, v84, v129, v162
	v_pk_fma_f32 v[188:189], v[146:147], v[130:131], v[188:189] op_sel_hi:[1,0,1]
	v_pk_fma_f32 v[192:193], v[154:155], v[130:131], v[192:193] op_sel_hi:[1,0,1]
	v_fma_f32 v166, v84, v130, v166
	s_barrier
	ds_read_b128 v[220:223], v23 offset:3072
	ds_read_b128 v[228:231], v23 offset:4096
	ds_read_b128 v[232:235], v23 offset:5120
	v_pk_add_f32 v[60:61], v[52:53], v[196:197]
	v_pk_add_f32 v[52:53], v[58:59], v[208:209]
	v_add_f32_e64 v58, v122, v182
	v_pk_add_f32 v[98:99], v[152:153], v[156:157]
	v_pk_add_f32 v[110:111], v[70:71], v[176:177]
	v_add_f32_e64 v84, v106, v158
	v_pk_add_f32 v[70:71], v[76:77], v[180:181]
	v_pk_add_f32 v[106:107], v[74:75], v[184:185]
	v_add_f32_e64 v76, v78, v162
	v_pk_add_f32 v[74:75], v[96:97], v[188:189]
	v_pk_add_f32 v[78:79], v[86:87], v[192:193]
	v_add_f32_e64 v96, v102, v166
	s_waitcnt lgkmcnt(2)
	v_pk_fma_f32 v[98:99], v[220:221], v[60:61], v[98:99] op_sel_hi:[0,1,1] neg_lo:[1,0,0] neg_hi:[1,0,0]
	v_pk_fma_f32 v[110:111], v[220:221], v[52:53], v[110:111] op_sel_hi:[0,1,1] neg_lo:[1,0,0] neg_hi:[1,0,0]
	v_fma_f32 v84, -v220, v58, v84
	v_pk_fma_f32 v[70:71], v[220:221], v[60:61], v[70:71] op_sel:[1,0,0] neg_lo:[1,0,0] neg_hi:[1,0,0]
	v_pk_fma_f32 v[106:107], v[220:221], v[52:53], v[106:107] op_sel:[1,0,0] neg_lo:[1,0,0] neg_hi:[1,0,0]
	v_fma_f32 v76, -v221, v58, v76
	v_pk_fma_f32 v[74:75], v[222:223], v[60:61], v[74:75] op_sel_hi:[0,1,1] neg_lo:[1,0,0] neg_hi:[1,0,0]
	v_pk_fma_f32 v[78:79], v[222:223], v[52:53], v[78:79] op_sel_hi:[0,1,1] neg_lo:[1,0,0] neg_hi:[1,0,0]
	v_fma_f32 v96, -v222, v58, v96
	v_pk_mul_f32 v[152:153], v[222:223], v[98:99] op_sel:[1,0]
	v_pk_mul_f32 v[240:241], v[222:223], v[110:111] op_sel:[1,0]
	v_mul_f32_e64 v86, v223, v84
	s_waitcnt lgkmcnt(1)
	v_pk_mul_f32 v[224:225], v[228:229], v[98:99] op_sel_hi:[0,1]
	v_pk_mul_f32 v[244:245], v[228:229], v[110:111] op_sel_hi:[0,1]
	v_mul_f32_e64 v102, v228, v84
	v_pk_mul_f32 v[236:237], v[228:229], v[98:99] op_sel:[1,0]
	v_pk_mul_f32 v[248:249], v[228:229], v[110:111] op_sel:[1,0]
	v_mul_f32_e64 v122, v229, v84
	v_pk_fma_f32 v[152:153], v[228:229], v[70:71], v[152:153] op_sel_hi:[0,1,1]
	v_pk_fma_f32 v[240:241], v[228:229], v[106:107], v[240:241] op_sel_hi:[0,1,1]
	v_fma_f32 v86, v228, v76, v86
	v_pk_fma_f32 v[224:225], v[230:231], v[70:71], v[224:225] op_sel_hi:[0,1,1]
	v_pk_fma_f32 v[244:245], v[230:231], v[106:107], v[244:245] op_sel_hi:[0,1,1]
	v_fma_f32 v102, v230, v76, v102
	v_pk_fma_f32 v[236:237], v[230:231], v[70:71], v[236:237] op_sel:[1,0,0]
	v_pk_fma_f32 v[248:249], v[230:231], v[106:107], v[248:249] op_sel:[1,0,0]
	v_fma_f32 v122, v231, v76, v122
	v_pk_fma_f32 v[152:153], v[228:229], v[74:75], v[152:153] op_sel:[1,0,0]
	v_pk_fma_f32 v[240:241], v[228:229], v[78:79], v[240:241] op_sel:[1,0,0]
	v_fma_f32 v86, v229, v96, v86
	v_pk_fma_f32 v[224:225], v[230:231], v[74:75], v[224:225] op_sel:[1,0,0]
	v_pk_fma_f32 v[244:245], v[230:231], v[78:79], v[244:245] op_sel:[1,0,0]
	v_fma_f32 v102, v231, v96, v102
	s_waitcnt lgkmcnt(0)
	v_pk_fma_f32 v[236:237], v[232:233], v[74:75], v[236:237] op_sel_hi:[0,1,1]
	v_pk_fma_f32 v[248:249], v[232:233], v[78:79], v[248:249] op_sel_hi:[0,1,1]
	v_fma_f32 v122, v232, v96, v122
	v_pk_mul_f32 v[146:147], v[220:221], v[152:153] op_sel_hi:[0,1]
	v_pk_mul_f32 v[154:155], v[220:221], v[240:241] op_sel_hi:[0,1]
	v_mul_f32_e64 v186, v220, v86
	v_pk_fma_f32 v[146:147], v[220:221], v[224:225], v[146:147] op_sel:[1,0,0]
	v_pk_fma_f32 v[154:155], v[220:221], v[244:245], v[154:155] op_sel:[1,0,0]
	v_fma_f32 v186, v221, v102, v186
	v_pk_fma_f32 v[146:147], v[222:223], v[236:237], v[146:147] op_sel_hi:[0,1,1]
	v_pk_fma_f32 v[154:155], v[222:223], v[248:249], v[154:155] op_sel_hi:[0,1,1]
	v_fma_f32 v186, v222, v122, v186
	v_pk_fma_f32 v[146:147], v[232:233], v[60:61], v[146:147] op_sel:[1,0,0] neg_lo:[0,0,1] neg_hi:[0,0,1]
	v_pk_fma_f32 v[154:155], v[232:233], v[52:53], v[154:155] op_sel:[1,0,0] neg_lo:[0,0,1] neg_hi:[0,0,1]
	v_fma_f32 v186, v233, v58, -v186
	v_cmp_eq_u32_e64 s[10:11], 1, v235
	v_cmp_eq_u32_e64 s[14:15], 2, v235
	v_cmp_eq_u32_e64 s[20:21], 3, v235
	v_cmp_eq_u32_e64 s[22:23], 4, v235
	v_cmp_eq_u32_e64 s[30:31], 5, v235
	v_pk_add_f32 v[52:53], v[68:69], v[152:153]
	v_pk_add_f32 v[58:59], v[62:63], v[240:241]
	v_add_f32_e64 v60, v100, v86
	v_pk_add_f32 v[62:63], v[160:161], v[224:225]
	v_pk_add_f32 v[68:69], v[138:139], v[244:245]
	v_add_f32_e64 v70, v164, v102
	v_pk_add_f32 v[74:75], v[168:169], v[236:237]
	v_pk_add_f32 v[76:77], v[150:151], v[248:249]
	v_add_f32_e64 v78, v172, v122
	v_pk_add_f32 v[84:85], v[170:171], v[146:147]
	v_pk_add_f32 v[98:99], v[174:175], v[154:155]
	v_add_f32_e64 v96, v178, v186
	v_pk_fma_f32 v[100:101], v[112:113], v[52:53], v[84:85] op_sel_hi:[0,1,1]
	v_pk_fma_f32 v[106:107], v[112:113], v[58:59], v[98:99] op_sel_hi:[0,1,1]
	v_fma_f32 v160, v112, v60, v96
	v_pk_fma_f32 v[164:165], v[132:133], v[52:53], v[84:85] op_sel_hi:[0,1,1]
	v_pk_fma_f32 v[110:111], v[132:133], v[58:59], v[98:99] op_sel_hi:[0,1,1]
	v_fma_f32 v168, v132, v60, v96
	v_pk_fma_f32 v[100:101], v[112:113], v[62:63], v[100:101] op_sel:[1,0,0]
	v_pk_fma_f32 v[106:107], v[112:113], v[68:69], v[106:107] op_sel:[1,0,0]
	v_fma_f32 v160, v113, v70, v160
	v_pk_fma_f32 v[164:165], v[132:133], v[62:63], v[164:165] op_sel:[1,0,0]
	v_pk_fma_f32 v[110:111], v[132:133], v[68:69], v[110:111] op_sel:[1,0,0]
	v_fma_f32 v168, v133, v70, v168
	v_pk_fma_f32 v[100:101], v[114:115], v[74:75], v[100:101] op_sel_hi:[0,1,1]
	v_pk_fma_f32 v[106:107], v[114:115], v[76:77], v[106:107] op_sel_hi:[0,1,1]
	v_fma_f32 v160, v114, v78, v160
	v_pk_fma_f32 v[164:165], v[134:135], v[74:75], v[164:165] op_sel_hi:[0,1,1]
	v_pk_fma_f32 v[110:111], v[134:135], v[76:77], v[110:111] op_sel_hi:[0,1,1]
	v_fma_f32 v168, v134, v78, v168
	v_pk_fma_f32 v[84:85], v[8:9], v[52:53], v[84:85] op_sel_hi:[0,1,1]
	v_pk_fma_f32 v[98:99], v[8:9], v[58:59], v[98:99] op_sel_hi:[0,1,1]
	v_fma_f32 v96, v8, v60, v96
	v_pk_fma_f32 v[84:85], v[8:9], v[62:63], v[84:85] op_sel:[1,0,0]
	v_pk_fma_f32 v[98:99], v[8:9], v[68:69], v[98:99] op_sel:[1,0,0]
	v_fma_f32 v96, v9, v70, v96
	v_pk_fma_f32 v[84:85], v[10:11], v[74:75], v[84:85] op_sel_hi:[0,1,1]
	v_pk_fma_f32 v[98:99], v[10:11], v[76:77], v[98:99] op_sel_hi:[0,1,1]
	v_fma_f32 v96, v10, v78, v96
	v_cndmask_b32_e64 v138, 0, v1, s[10:11]
	v_cndmask_b32_e64 v139, 0, v1, s[14:15]
	v_cndmask_b32_e64 v172, 0, v1, s[20:21]
	v_cndmask_b32_e64 v173, 0, v1, s[22:23]
	v_cndmask_b32_e64 v150, 0, v1, s[30:31]
	v_add_f32_dpp v84, v100, v84 wave_shl:1 row_mask:0xf bank_mask:0xf bound_ctrl:1
	v_add_f32_dpp v85, v101, v85 wave_shl:1 row_mask:0xf bank_mask:0xf bound_ctrl:1
	v_add_f32_dpp v98, v106, v98 wave_shl:1 row_mask:0xf bank_mask:0xf bound_ctrl:1
	v_add_f32_dpp v99, v107, v99 wave_shl:1 row_mask:0xf bank_mask:0xf bound_ctrl:1
	v_add_f32_dpp v96, v160, v96 wave_shl:1 row_mask:0xf bank_mask:0xf bound_ctrl:1
	s_add_i32 s4, s34, 3
	s_cmpk_lt_i32 s4, 0x201
	s_cselect_b64 s[12:13], s[0:1], 0
	v_add_f32_dpp v84, v164, v84 wave_shr:1 row_mask:0xf bank_mask:0xf bound_ctrl:1
	v_add_f32_dpp v85, v165, v85 wave_shr:1 row_mask:0xf bank_mask:0xf bound_ctrl:1
	v_add_f32_dpp v98, v110, v98 wave_shr:1 row_mask:0xf bank_mask:0xf bound_ctrl:1
	v_add_f32_dpp v99, v111, v99 wave_shr:1 row_mask:0xf bank_mask:0xf bound_ctrl:1
	v_add_f32_dpp v96, v168, v96 wave_shr:1 row_mask:0xf bank_mask:0xf bound_ctrl:1
	v_pk_fma_f32 v[84:85], v[2:3], v[234:235], v[84:85] op_sel_hi:[1,0,1] neg_lo:[0,0,1] neg_hi:[0,0,1]
	v_pk_fma_f32 v[98:99], v[4:5], v[234:235], v[98:99] op_sel_hi:[1,0,1] neg_lo:[0,0,1] neg_hi:[0,0,1]
	v_fma_f32 v96, v6, v234, -v96
	v_pk_add_f32 v[84:85], v[84:85], v[138:139] neg_lo:[0,1] neg_hi:[0,1]
	v_pk_add_f32 v[98:99], v[98:99], v[172:173] neg_lo:[0,1] neg_hi:[0,1]
	v_add_f32_e64 v96, v96, -v150
	v_pk_mul_f32 v[170:171], v[84:85], v[84:85]
	v_pk_fma_f32 v[170:171], v[98:99], v[98:99], v[170:171]
	v_add_f32_e32 v170, v170, v171
	v_fma_f32 v170, v96, v96, v170
	v_cndmask_b32_e64 v171, 0, v170, s[12:13]
	v_add_f32_e32 v0, v0, v171
	s_add_i32 s4, s34, 8
	s_min_i32 s4, s4, 0x200
	s_mul_i32 s5, s4, 0x804
	s_add_i32 s5, s5, s35
	s_add_i32 s6, s5, 0x0
	s_add_i32 s7, s5, 0x101004
	s_add_i32 s8, s5, 0x202008
	s_add_i32 s11, s5, 0x30300c
	s_add_i32 s15, s5, 0x404010
	s_mul_i32 s9, s4, 0x180c
	s_add_i32 s9, s9, s33
	buffer_load_dword v2, v28, s[16:19], s6 offen nt
	buffer_load_dword v3, v28, s[16:19], s7 offen nt
	buffer_load_dword v4, v28, s[16:19], s8 offen nt
	buffer_load_dword v5, v28, s[16:19], s11 offen nt
	buffer_load_dword v6, v28, s[16:19], s15 offen nt
	buffer_load_dwordx3 v[8:10], v27, s[24:27], s9 offen nt
	s_waitcnt vmcnt(12)
	v_mov_b32_dpp v60, v48 wave_shr:1 row_mask:0xf bank_mask:0xf bound_ctrl:1
	v_mov_b32_dpp v61, v49 wave_shr:1 row_mask:0xf bank_mask:0xf bound_ctrl:1
	v_mov_b32_dpp v62, v50 wave_shr:1 row_mask:0xf bank_mask:0xf bound_ctrl:1
	v_mov_b32_dpp v68, v48 wave_shl:1 row_mask:0xf bank_mask:0xf bound_ctrl:1
	v_mov_b32_dpp v69, v49 wave_shl:1 row_mask:0xf bank_mask:0xf bound_ctrl:1
	v_mov_b32_dpp v70, v50 wave_shl:1 row_mask:0xf bank_mask:0xf bound_ctrl:1
	v_mov_b32_dpp v58, v40 wave_shr:1 row_mask:0xf bank_mask:0xf bound_ctrl:1
	v_mov_b32_dpp v59, v41 wave_shr:1 row_mask:0xf bank_mask:0xf bound_ctrl:1
	v_mov_b32_dpp v52, v42 wave_shr:1 row_mask:0xf bank_mask:0xf bound_ctrl:1
	v_mov_b32_dpp v53, v43 wave_shr:1 row_mask:0xf bank_mask:0xf bound_ctrl:1
	v_mov_b32_dpp v74, v44 wave_shr:1 row_mask:0xf bank_mask:0xf bound_ctrl:1
	v_mov_b32_dpp v78, v40 wave_shl:1 row_mask:0xf bank_mask:0xf bound_ctrl:1
	v_mov_b32_dpp v79, v41 wave_shl:1 row_mask:0xf bank_mask:0xf bound_ctrl:1
	v_mov_b32_dpp v76, v42 wave_shl:1 row_mask:0xf bank_mask:0xf bound_ctrl:1
	v_mov_b32_dpp v77, v43 wave_shl:1 row_mask:0xf bank_mask:0xf bound_ctrl:1
	v_mov_b32_dpp v98, v44 wave_shl:1 row_mask:0xf bank_mask:0xf bound_ctrl:1
	v_pk_mul_f32 v[84:85], v[40:41], v[48:49] op_sel_hi:[1,0]
	v_pk_mul_f32 v[106:107], v[42:43], v[48:49] op_sel_hi:[1,0]
	v_mul_f32_e64 v96, v44, v48
	v_pk_mul_f32 v[100:101], v[40:41], v[48:49] op_sel:[0,1]
	v_pk_mul_f32 v[110:111], v[42:43], v[48:49] op_sel:[0,1]
	v_mul_f32_e64 v112, v44, v49
	v_pk_mul_f32 v[132:133], v[40:41], v[50:51] op_sel_hi:[1,0]
	v_pk_mul_f32 v[114:115], v[42:43], v[50:51] op_sel_hi:[1,0]
	v_mul_f32_e64 v160, v44, v50
	v_pk_add_f32 v[164:165], v[40:41], v[58:59]
	v_pk_add_f32 v[134:135], v[42:43], v[52:53]
	v_add_f32_e64 v168, v44, v74
	v_pk_fma_f32 v[84:85], v[58:59], v[60:61], v[84:85] op_sel_hi:[1,0,1]
	v_pk_fma_f32 v[106:107], v[52:53], v[60:61], v[106:107] op_sel_hi:[1,0,1]
	v_fma_f32 v96, v74, v60, v96
	v_pk_fma_f32 v[100:101], v[58:59], v[60:61], v[100:101] op_sel:[0,1,0]
	v_pk_fma_f32 v[110:111], v[52:53], v[60:61], v[110:111] op_sel:[0,1,0]
	v_fma_f32 v112, v74, v61, v112
	v_pk_fma_f32 v[132:133], v[58:59], v[62:63], v[132:133] op_sel_hi:[1,0,1]
	v_pk_fma_f32 v[114:115], v[52:53], v[62:63], v[114:115] op_sel_hi:[1,0,1]
	v_fma_f32 v160, v74, v62, v160
	v_pk_add_f32 v[164:165], v[164:165], v[78:79]
	v_pk_add_f32 v[134:135], v[134:135], v[76:77]
	v_add_f32_e64 v168, v168, v98
	v_pk_fma_f32 v[84:85], v[78:79], v[68:69], v[84:85] op_sel_hi:[1,0,1]
	v_pk_fma_f32 v[106:107], v[76:77], v[68:69], v[106:107] op_sel_hi:[1,0,1]
	v_fma_f32 v96, v98, v68, v96
	v_pk_fma_f32 v[100:101], v[78:79], v[68:69], v[100:101] op_sel:[0,1,0]
	v_pk_fma_f32 v[110:111], v[76:77], v[68:69], v[110:111] op_sel:[0,1,0]
	v_fma_f32 v112, v98, v69, v112
	v_pk_fma_f32 v[132:133], v[78:79], v[70:71], v[132:133] op_sel_hi:[1,0,1]
	v_pk_fma_f32 v[114:115], v[76:77], v[70:71], v[114:115] op_sel_hi:[1,0,1]
	v_fma_f32 v160, v98, v70, v160
	s_barrier
	ds_read_b128 v[76:79], v23 offset:0
	ds_read_b128 v[172:175], v23 offset:1024
	ds_read_b128 v[220:223], v23 offset:2048
	v_pk_add_f32 v[58:59], v[196:197], v[164:165]
	v_pk_add_f32 v[52:53], v[144:145], v[58:59]
	v_pk_add_f32 v[144:145], v[208:209], v[134:135]
	v_pk_add_f32 v[74:75], v[206:207], v[144:145]
	v_add_f32_e64 v98, v182, v168
	v_add_f32_e64 v138, v148, v98
	v_pk_add_f32 v[150:151], v[156:157], v[84:85]
	v_pk_add_f32 v[170:171], v[72:73], v[150:151]
	v_pk_add_f32 v[72:73], v[176:177], v[106:107]
	v_pk_add_f32 v[148:149], v[126:127], v[72:73]
	v_add_f32_e64 v126, v158, v96
	v_add_f32_e64 v156, v108, v126
	v_pk_add_f32 v[158:159], v[180:181], v[100:101]
	v_pk_add_f32 v[178:179], v[120:121], v[158:159]
	v_pk_add_f32 v[108:109], v[184:185], v[110:111]
	v_pk_add_f32 v[120:121], v[142:143], v[108:109]
	v_add_f32_e64 v142, v162, v112
	v_add_f32_e64 v176, v124, v142
	v_pk_add_f32 v[162:163], v[188:189], v[132:133]
	v_pk_add_f32 v[182:183], v[136:137], v[162:163]
	v_pk_add_f32 v[124:125], v[192:193], v[114:115]
	v_pk_add_f32 v[136:137], v[194:195], v[124:125]
	v_add_f32_e64 v190, v166, v160
	v_add_f32_e64 v180, v140, v190
	s_waitcnt lgkmcnt(2)
	v_pk_fma_f32 v[170:171], v[76:77], v[52:53], v[170:171] op_sel_hi:[0,1,1] neg_lo:[1,0,0] neg_hi:[1,0,0]
	v_pk_fma_f32 v[148:149], v[76:77], v[74:75], v[148:149] op_sel_hi:[0,1,1] neg_lo:[1,0,0] neg_hi:[1,0,0]
	v_fma_f32 v156, -v76, v138, v156
	v_pk_fma_f32 v[178:179], v[76:77], v[52:53], v[178:179] op_sel:[1,0,0] neg_lo:[1,0,0] neg_hi:[1,0,0]
	v_pk_fma_f32 v[120:121], v[76:77], v[74:75], v[120:121] op_sel:[1,0,0] neg_lo:[1,0,0] neg_hi:[1,0,0]
	v_fma_f32 v176, -v77, v138, v176
	v_pk_fma_f32 v[182:183], v[78:79], v[52:53], v[182:183] op_sel_hi:[0,1,1] neg_lo:[1,0,0] neg_hi:[1,0,0]
	v_pk_fma_f32 v[136:137], v[78:79], v[74:75], v[136:137] op_sel_hi:[0,1,1] neg_lo:[1,0,0] neg_hi:[1,0,0]
	v_fma_f32 v180, -v78, v138, v180
	v_pk_mul_f32 v[140:141], v[78:79], v[170:171] op_sel:[1,0]
	v_pk_mul_f32 v[166:167], v[78:79], v[148:149] op_sel:[1,0]
	v_mul_f32_e64 v210, v79, v156
	s_waitcnt lgkmcnt(1)
	v_pk_mul_f32 v[184:185], v[172:173], v[170:171] op_sel_hi:[0,1]
	v_pk_mul_f32 v[194:195], v[172:173], v[148:149] op_sel_hi:[0,1]
	v_mul_f32_e64 v230, v172, v156
	v_pk_mul_f32 v[188:189], v[172:173], v[170:171] op_sel:[1,0]
	v_pk_mul_f32 v[206:207], v[172:173], v[148:149] op_sel:[1,0]
	v_mul_f32_e64 v234, v173, v156
	v_pk_fma_f32 v[140:141], v[172:173], v[178:179], v[140:141] op_sel_hi:[0,1,1]
	v_pk_fma_f32 v[166:167], v[172:173], v[120:121], v[166:167] op_sel_hi:[0,1,1]
	v_fma_f32 v210, v172, v176, v210
	v_pk_fma_f32 v[184:185], v[174:175], v[178:179], v[184:185] op_sel_hi:[0,1,1]
	v_pk_fma_f32 v[194:195], v[174:175], v[120:121], v[194:195] op_sel_hi:[0,1,1]
	v_fma_f32 v230, v174, v176, v230
	v_pk_fma_f32 v[188:189], v[174:175], v[178:179], v[188:189] op_sel:[1,0,0]
	v_pk_fma_f32 v[206:207], v[174:175], v[120:121], v[206:207] op_sel:[1,0,0]
	v_fma_f32 v234, v175, v176, v234
	v_pk_fma_f32 v[140:141], v[172:173], v[182:183], v[140:141] op_sel:[1,0,0]
	v_pk_fma_f32 v[166:167], v[172:173], v[136:137], v[166:167] op_sel:[1,0,0]
	v_fma_f32 v210, v173, v180, v210
	v_pk_fma_f32 v[184:185], v[174:175], v[182:183], v[184:185] op_sel:[1,0,0]
	v_pk_fma_f32 v[194:195], v[174:175], v[136:137], v[194:195] op_sel:[1,0,0]
	v_fma_f32 v230, v175, v180, v230
	s_waitcnt lgkmcnt(0)
	v_pk_fma_f32 v[188:189], v[220:221], v[182:183], v[188:189] op_sel_hi:[0,1,1]
	v_pk_fma_f32 v[206:207], v[220:221], v[136:137], v[206:207] op_sel_hi:[0,1,1]
	v_fma_f32 v234, v220, v180, v234
	v_pk_mul_f32 v[238:239], v[76:77], v[140:141] op_sel_hi:[0,1]
	v_pk_mul_f32 v[192:193], v[76:77], v[166:167] op_sel_hi:[0,1]
	v_mul_f32_e64 v196, v76, v210
	v_pk_fma_f32 v[238:239], v[76:77], v[184:185], v[238:239] op_sel:[1,0,0]
	v_pk_fma_f32 v[192:193], v[76:77], v[194:195], v[192:193] op_sel:[1,0,0]
	v_fma_f32 v196, v77, v230, v196
	v_pk_fma_f32 v[238:239], v[78:79], v[188:189], v[238:239] op_sel_hi:[0,1,1]
	v_pk_fma_f32 v[192:193], v[78:79], v[206:207], v[192:193] op_sel_hi:[0,1,1]
	v_fma_f32 v196, v78, v234, v196
	v_pk_fma_f32 v[238:239], v[220:221], v[52:53], v[238:239] op_sel:[1,0,0] neg_lo:[0,0,1] neg_hi:[0,0,1]
	v_pk_fma_f32 v[192:193], v[220:221], v[74:75], v[192:193] op_sel:[1,0,0] neg_lo:[0,0,1] neg_hi:[0,0,1]
	v_fma_f32 v196, v221, v138, -v196
	v_cmp_eq_u32_e64 s[10:11], 1, v223
	v_cmp_eq_u32_e64 s[14:15], 2, v223
	v_cmp_eq_u32_e64 s[20:21], 3, v223
	v_cmp_eq_u32_e64 s[22:23], 4, v223
	v_cmp_eq_u32_e64 s[30:31], 5, v223
	v_pk_add_f32 v[52:53], v[152:153], v[140:141]
	v_pk_add_f32 v[74:75], v[118:119], v[52:53]
	v_pk_add_f32 v[120:121], v[240:241], v[166:167]
	v_pk_add_f32 v[118:119], v[214:215], v[120:121]
	v_add_f32_e64 v138, v86, v210
	v_add_f32_e64 v136, v104, v138
	v_pk_add_f32 v[104:105], v[224:225], v[184:185]
	v_pk_add_f32 v[86:87], v[198:199], v[104:105]
	v_pk_add_f32 v[148:149], v[244:245], v[194:195]
	v_pk_add_f32 v[152:153], v[218:219], v[148:149]
	v_add_f32_e64 v170, v102, v230
	v_add_f32_e64 v156, v116, v170
	v_pk_add_f32 v[116:117], v[236:237], v[188:189]
	v_pk_add_f32 v[102:103], v[202:203], v[116:117]
	v_pk_add_f32 v[176:177], v[248:249], v[206:207]
	v_pk_add_f32 v[178:179], v[226:227], v[176:177]
	v_add_f32_e64 v182, v122, v234
	v_add_f32_e64 v180, v200, v182
	v_pk_add_f32 v[122:123], v[146:147], v[238:239]
	v_pk_add_f32 v[200:201], v[204:205], v[122:123]
	v_pk_add_f32 v[146:147], v[154:155], v[192:193]
	v_pk_add_f32 v[204:205], v[212:213], v[146:147]
	v_add_f32_e64 v154, v186, v196
	v_add_f32_e64 v198, v216, v154
	v_pk_fma_f32 v[208:209], v[64:65], v[74:75], v[200:201] op_sel_hi:[0,1,1]
	v_pk_fma_f32 v[212:213], v[64:65], v[118:119], v[204:205] op_sel_hi:[0,1,1]
	v_fma_f32 v186, v64, v136, v198
	v_pk_fma_f32 v[216:217], v[88:89], v[74:75], v[200:201] op_sel_hi:[0,1,1]
	v_pk_fma_f32 v[224:225], v[88:89], v[118:119], v[204:205] op_sel_hi:[0,1,1]
	v_fma_f32 v202, v88, v136, v198
	v_pk_fma_f32 v[208:209], v[64:65], v[86:87], v[208:209] op_sel:[1,0,0]
	v_pk_fma_f32 v[212:213], v[64:65], v[152:153], v[212:213] op_sel:[1,0,0]
	v_fma_f32 v186, v65, v156, v186
	v_pk_fma_f32 v[216:217], v[88:89], v[86:87], v[216:217] op_sel:[1,0,0]
	v_pk_fma_f32 v[224:225], v[88:89], v[152:153], v[224:225] op_sel:[1,0,0]
	v_fma_f32 v202, v89, v156, v202
	v_pk_fma_f32 v[208:209], v[66:67], v[102:103], v[208:209] op_sel_hi:[0,1,1]
	v_pk_fma_f32 v[212:213], v[66:67], v[178:179], v[212:213] op_sel_hi:[0,1,1]
	v_fma_f32 v186, v66, v180, v186
	v_pk_fma_f32 v[216:217], v[90:91], v[102:103], v[216:217] op_sel_hi:[0,1,1]
	v_pk_fma_f32 v[224:225], v[90:91], v[178:179], v[224:225] op_sel_hi:[0,1,1]
	v_fma_f32 v202, v90, v180, v202
	v_pk_fma_f32 v[200:201], v[32:33], v[74:75], v[200:201] op_sel_hi:[0,1,1]
	v_pk_fma_f32 v[204:205], v[32:33], v[118:119], v[204:205] op_sel_hi:[0,1,1]
	v_fma_f32 v198, v32, v136, v198
	v_pk_fma_f32 v[200:201], v[32:33], v[86:87], v[200:201] op_sel:[1,0,0]
	v_pk_fma_f32 v[204:205], v[32:33], v[152:153], v[204:205] op_sel:[1,0,0]
	v_fma_f32 v198, v33, v156, v198
	v_pk_fma_f32 v[200:201], v[34:35], v[102:103], v[200:201] op_sel_hi:[0,1,1]
	v_pk_fma_f32 v[204:205], v[34:35], v[178:179], v[204:205] op_sel_hi:[0,1,1]
	v_fma_f32 v198, v34, v180, v198
	v_cndmask_b32_e64 v214, 0, v1, s[10:11]
	v_cndmask_b32_e64 v215, 0, v1, s[14:15]
	v_cndmask_b32_e64 v218, 0, v1, s[20:21]
	v_cndmask_b32_e64 v219, 0, v1, s[22:23]
	v_cndmask_b32_e64 v228, 0, v1, s[30:31]
	v_add_f32_dpp v200, v208, v200 wave_shl:1 row_mask:0xf bank_mask:0xf bound_ctrl:1
	v_add_f32_dpp v201, v209, v201 wave_shl:1 row_mask:0xf bank_mask:0xf bound_ctrl:1
	v_add_f32_dpp v204, v212, v204 wave_shl:1 row_mask:0xf bank_mask:0xf bound_ctrl:1
	v_add_f32_dpp v205, v213, v205 wave_shl:1 row_mask:0xf bank_mask:0xf bound_ctrl:1
	v_add_f32_dpp v198, v186, v198 wave_shl:1 row_mask:0xf bank_mask:0xf bound_ctrl:1
	s_add_i32 s4, s34, 4
	s_cmpk_lt_i32 s4, 0x201
	s_cselect_b64 s[12:13], s[0:1], 0
	v_add_f32_dpp v200, v216, v200 wave_shr:1 row_mask:0xf bank_mask:0xf bound_ctrl:1
	v_add_f32_dpp v201, v217, v201 wave_shr:1 row_mask:0xf bank_mask:0xf bound_ctrl:1
	v_add_f32_dpp v204, v224, v204 wave_shr:1 row_mask:0xf bank_mask:0xf bound_ctrl:1
	v_add_f32_dpp v205, v225, v205 wave_shr:1 row_mask:0xf bank_mask:0xf bound_ctrl:1
	v_add_f32_dpp v198, v202, v198 wave_shr:1 row_mask:0xf bank_mask:0xf bound_ctrl:1
	v_pk_fma_f32 v[200:201], v[12:13], v[222:223], v[200:201] op_sel_hi:[1,0,1] neg_lo:[0,0,1] neg_hi:[0,0,1]
	v_pk_fma_f32 v[204:205], v[14:15], v[222:223], v[204:205] op_sel_hi:[1,0,1] neg_lo:[0,0,1] neg_hi:[0,0,1]
	v_fma_f32 v198, v16, v222, -v198
	v_pk_add_f32 v[200:201], v[200:201], v[214:215] neg_lo:[0,1] neg_hi:[0,1]
	v_pk_add_f32 v[204:205], v[204:205], v[218:219] neg_lo:[0,1] neg_hi:[0,1]
	v_add_f32_e64 v198, v198, -v228
	v_pk_mul_f32 v[226:227], v[200:201], v[200:201]
	v_pk_fma_f32 v[226:227], v[204:205], v[204:205], v[226:227]
	v_add_f32_e32 v226, v226, v227
	v_fma_f32 v226, v198, v198, v226
	v_cndmask_b32_e64 v227, 0, v226, s[12:13]
	v_add_f32_e32 v0, v0, v227
	s_add_i32 s4, s34, 9
	s_min_i32 s4, s4, 0x200
	s_mul_i32 s5, s4, 0x804
	s_add_i32 s5, s5, s35
	s_add_i32 s6, s5, 0x0
	s_add_i32 s7, s5, 0x101004
	s_add_i32 s8, s5, 0x202008
	s_add_i32 s11, s5, 0x30300c
	s_add_i32 s15, s5, 0x404010
	s_mul_i32 s9, s4, 0x180c
	s_add_i32 s9, s9, s33
	buffer_load_dword v12, v28, s[16:19], s6 offen nt
	buffer_load_dword v13, v28, s[16:19], s7 offen nt
	buffer_load_dword v14, v28, s[16:19], s8 offen nt
	buffer_load_dword v15, v28, s[16:19], s11 offen nt
	buffer_load_dword v16, v28, s[16:19], s15 offen nt
	buffer_load_dwordx3 v[32:34], v27, s[24:27], s9 offen nt
	s_waitcnt vmcnt(12)
	v_mov_b32_dpp v64, v80 wave_shr:1 row_mask:0xf bank_mask:0xf bound_ctrl:1
	v_mov_b32_dpp v65, v81 wave_shr:1 row_mask:0xf bank_mask:0xf bound_ctrl:1
	v_mov_b32_dpp v66, v82 wave_shr:1 row_mask:0xf bank_mask:0xf bound_ctrl:1
	v_mov_b32_dpp v76, v80 wave_shl:1 row_mask:0xf bank_mask:0xf bound_ctrl:1
	v_mov_b32_dpp v77, v81 wave_shl:1 row_mask:0xf bank_mask:0xf bound_ctrl:1
	v_mov_b32_dpp v78, v82 wave_shl:1 row_mask:0xf bank_mask:0xf bound_ctrl:1
	v_mov_b32_dpp v88, v46 wave_shr:1 row_mask:0xf bank_mask:0xf bound_ctrl:1
	v_mov_b32_dpp v89, v47 wave_shr:1 row_mask:0xf bank_mask:0xf bound_ctrl:1
	v_mov_b32_dpp v136, v54 wave_shr:1 row_mask:0xf bank_mask:0xf bound_ctrl:1
	v_mov_b32_dpp v137, v55 wave_shr:1 row_mask:0xf bank_mask:0xf bound_ctrl:1
	v_mov_b32_dpp v74, v56 wave_shr:1 row_mask:0xf bank_mask:0xf bound_ctrl:1
	v_mov_b32_dpp v152, v46 wave_shl:1 row_mask:0xf bank_mask:0xf bound_ctrl:1
	v_mov_b32_dpp v153, v47 wave_shl:1 row_mask:0xf bank_mask:0xf bound_ctrl:1
	v_mov_b32_dpp v156, v54 wave_shl:1 row_mask:0xf bank_mask:0xf bound_ctrl:1
	v_mov_b32_dpp v157, v55 wave_shl:1 row_mask:0xf bank_mask:0xf bound_ctrl:1
	v_mov_b32_dpp v86, v56 wave_shl:1 row_mask:0xf bank_mask:0xf bound_ctrl:1
	v_pk_mul_f32 v[90:91], v[46:47], v[80:81] op_sel_hi:[1,0]
	v_pk_mul_f32 v[102:103], v[54:55], v[80:81] op_sel_hi:[1,0]
	v_mul_f32_e64 v172, v56, v80
	v_pk_mul_f32 v[118:119], v[46:47], v[80:81] op_sel:[0,1]
	v_pk_mul_f32 v[174:175], v[54:55], v[80:81] op_sel:[0,1]
	v_mul_f32_e64 v180, v56, v81
	v_pk_mul_f32 v[178:179], v[46:47], v[82:83] op_sel_hi:[1,0]
	v_pk_mul_f32 v[186:187], v[54:55], v[82:83] op_sel_hi:[1,0]
	v_mul_f32_e64 v200, v56, v82
	v_pk_add_f32 v[198:199], v[46:47], v[88:89]
	v_pk_add_f32 v[202:203], v[54:55], v[136:137]
	v_add_f32_e64 v204, v56, v74
	v_pk_fma_f32 v[90:91], v[88:89], v[64:65], v[90:91] op_sel_hi:[1,0,1]
	v_pk_fma_f32 v[102:103], v[136:137], v[64:65], v[102:103] op_sel_hi:[1,0,1]
	v_fma_f32 v172, v74, v64, v172
	v_pk_fma_f32 v[118:119], v[88:89], v[64:65], v[118:119] op_sel:[0,1,0]
	v_pk_fma_f32 v[174:175], v[136:137], v[64:65], v[174:175] op_sel:[0,1,0]
	v_fma_f32 v180, v74, v65, v180
	v_pk_fma_f32 v[178:179], v[88:89], v[66:67], v[178:179] op_sel_hi:[1,0,1]
	v_pk_fma_f32 v[186:187], v[136:137], v[66:67], v[186:187] op_sel_hi:[1,0,1]
	v_fma_f32 v200, v74, v66, v200
	v_pk_add_f32 v[198:199], v[198:199], v[152:153]
	v_pk_add_f32 v[202:203], v[202:203], v[156:157]
	v_add_f32_e64 v204, v204, v86
	v_pk_fma_f32 v[90:91], v[152:153], v[76:77], v[90:91] op_sel_hi:[1,0,1]
	v_pk_fma_f32 v[102:103], v[156:157], v[76:77], v[102:103] op_sel_hi:[1,0,1]
	v_fma_f32 v172, v86, v76, v172
	v_pk_fma_f32 v[118:119], v[152:153], v[76:77], v[118:119] op_sel:[0,1,0]
	v_pk_fma_f32 v[174:175], v[156:157], v[76:77], v[174:175] op_sel:[0,1,0]
	v_fma_f32 v180, v86, v77, v180
	v_pk_fma_f32 v[178:179], v[152:153], v[78:79], v[178:179] op_sel_hi:[1,0,1]
	v_pk_fma_f32 v[186:187], v[156:157], v[78:79], v[186:187] op_sel_hi:[1,0,1]
	v_fma_f32 v200, v86, v78, v200
	s_barrier
	ds_read_b128 v[212:215], v23 offset:3072
	ds_read_b128 v[216:219], v23 offset:4096
	ds_read_b128 v[220:223], v23 offset:5120
	v_pk_add_f32 v[74:75], v[58:59], v[198:199]
	v_pk_add_f32 v[58:59], v[144:145], v[202:203]
	v_add_f32_e64 v86, v98, v204
	v_pk_add_f32 v[88:89], v[150:151], v[90:91]
	v_pk_add_f32 v[136:137], v[72:73], v[102:103]
	v_add_f32_e64 v72, v126, v172
	v_pk_add_f32 v[144:145], v[158:159], v[118:119]
	v_pk_add_f32 v[152:153], v[108:109], v[174:175]
	v_add_f32_e64 v108, v142, v180
	v_pk_add_f32 v[156:157], v[162:163], v[178:179]
	v_pk_add_f32 v[208:209], v[124:125], v[186:187]
	v_add_f32_e64 v124, v190, v200
	s_waitcnt lgkmcnt(2)
	v_pk_fma_f32 v[88:89], v[212:213], v[74:75], v[88:89] op_sel_hi:[0,1,1] neg_lo:[1,0,0] neg_hi:[1,0,0]
	v_pk_fma_f32 v[136:137], v[212:213], v[58:59], v[136:137] op_sel_hi:[0,1,1] neg_lo:[1,0,0] neg_hi:[1,0,0]
	v_fma_f32 v72, -v212, v86, v72
	v_pk_fma_f32 v[144:145], v[212:213], v[74:75], v[144:145] op_sel:[1,0,0] neg_lo:[1,0,0] neg_hi:[1,0,0]
	v_pk_fma_f32 v[152:153], v[212:213], v[58:59], v[152:153] op_sel:[1,0,0] neg_lo:[1,0,0] neg_hi:[1,0,0]
	v_fma_f32 v108, -v213, v86, v108
	v_pk_fma_f32 v[156:157], v[214:215], v[74:75], v[156:157] op_sel_hi:[0,1,1] neg_lo:[1,0,0] neg_hi:[1,0,0]
	v_pk_fma_f32 v[208:209], v[214:215], v[58:59], v[208:209] op_sel_hi:[0,1,1] neg_lo:[1,0,0] neg_hi:[1,0,0]
	v_fma_f32 v124, -v214, v86, v124
	v_pk_mul_f32 v[98:99], v[214:215], v[88:89] op_sel:[1,0]
	v_pk_mul_f32 v[150:151], v[214:215], v[136:137] op_sel:[1,0]
	v_mul_f32_e64 v190, v215, v72
	s_waitcnt lgkmcnt(1)
	v_pk_mul_f32 v[126:127], v[216:217], v[88:89] op_sel_hi:[0,1]
	v_pk_mul_f32 v[158:159], v[216:217], v[136:137] op_sel_hi:[0,1]
	v_mul_f32_e64 v226, v216, v72
	v_pk_mul_f32 v[142:143], v[216:217], v[88:89] op_sel:[1,0]
	v_pk_mul_f32 v[162:163], v[216:217], v[136:137] op_sel:[1,0]
	v_mul_f32_e64 v242, v217, v72
	v_pk_fma_f32 v[98:99], v[216:217], v[144:145], v[98:99] op_sel_hi:[0,1,1]
	v_pk_fma_f32 v[150:151], v[216:217], v[152:153], v[150:151] op_sel_hi:[0,1,1]
	v_fma_f32 v190, v216, v108, v190
	v_pk_fma_f32 v[126:127], v[218:219], v[144:145], v[126:127] op_sel_hi:[0,1,1]
	v_pk_fma_f32 v[158:159], v[218:219], v[152:153], v[158:159] op_sel_hi:[0,1,1]
	v_fma_f32 v226, v218, v108, v226
	v_pk_fma_f32 v[142:143], v[218:219], v[144:145], v[142:143] op_sel:[1,0,0]
	v_pk_fma_f32 v[162:163], v[218:219], v[152:153], v[162:163] op_sel:[1,0,0]
	v_fma_f32 v242, v219, v108, v242
	v_pk_fma_f32 v[98:99], v[216:217], v[156:157], v[98:99] op_sel:[1,0,0]
	v_pk_fma_f32 v[150:151], v[216:217], v[208:209], v[150:151] op_sel:[1,0,0]
	v_fma_f32 v190, v217, v124, v190
	v_pk_fma_f32 v[126:127], v[218:219], v[156:157], v[126:127] op_sel:[1,0,0]
	v_pk_fma_f32 v[158:159], v[218:219], v[208:209], v[158:159] op_sel:[1,0,0]
	v_fma_f32 v226, v219, v124, v226
	s_waitcnt lgkmcnt(0)
	v_pk_fma_f32 v[142:143], v[220:221], v[156:157], v[142:143] op_sel_hi:[0,1,1]
	v_pk_fma_f32 v[162:163], v[220:221], v[208:209], v[162:163] op_sel_hi:[0,1,1]
	v_fma_f32 v242, v220, v124, v242
	v_pk_mul_f32 v[224:225], v[212:213], v[98:99] op_sel_hi:[0,1]
	v_pk_mul_f32 v[228:229], v[212:213], v[150:151] op_sel_hi:[0,1]
	v_mul_f32_e64 v232, v212, v190
	v_pk_fma_f32 v[224:225], v[212:213], v[126:127], v[224:225] op_sel:[1,0,0]
	v_pk_fma_f32 v[228:229], v[212:213], v[158:159], v[228:229] op_sel:[1,0,0]
	v_fma_f32 v232, v213, v226, v232
	v_pk_fma_f32 v[224:225], v[214:215], v[142:143], v[224:225] op_sel_hi:[0,1,1]
	v_pk_fma_f32 v[228:229], v[214:215], v[162:163], v[228:229] op_sel_hi:[0,1,1]
	v_fma_f32 v232, v214, v242, v232
	v_pk_fma_f32 v[224:225], v[220:221], v[74:75], v[224:225] op_sel:[1,0,0] neg_lo:[0,0,1] neg_hi:[0,0,1]
	v_pk_fma_f32 v[228:229], v[220:221], v[58:59], v[228:229] op_sel:[1,0,0] neg_lo:[0,0,1] neg_hi:[0,0,1]
	v_fma_f32 v232, v221, v86, -v232
	v_cmp_eq_u32_e64 s[10:11], 1, v223
	v_cmp_eq_u32_e64 s[14:15], 2, v223
	v_cmp_eq_u32_e64 s[20:21], 3, v223
	v_cmp_eq_u32_e64 s[22:23], 4, v223
	v_cmp_eq_u32_e64 s[30:31], 5, v223
	v_pk_add_f32 v[58:59], v[52:53], v[98:99]
	v_pk_add_f32 v[52:53], v[120:121], v[150:151]
	v_add_f32_e64 v72, v138, v190
	v_pk_add_f32 v[74:75], v[104:105], v[126:127]
	v_pk_add_f32 v[86:87], v[148:149], v[158:159]
	v_add_f32_e64 v88, v170, v226
	v_pk_add_f32 v[104:105], v[116:117], v[142:143]
	v_pk_add_f32 v[108:109], v[176:177], v[162:163]
	v_add_f32_e64 v116, v182, v242
	v_pk_add_f32 v[120:121], v[122:123], v[224:225]
	v_pk_add_f32 v[122:123], v[146:147], v[228:229]
	v_add_f32_e64 v138, v154, v232
	v_pk_fma_f32 v[124:125], v[92:93], v[58:59], v[120:121] op_sel_hi:[0,1,1]
	v_pk_fma_f32 v[146:147], v[92:93], v[52:53], v[122:123] op_sel_hi:[0,1,1]
	v_fma_f32 v154, v92, v72, v138
	v_pk_fma_f32 v[136:137], v[128:129], v[58:59], v[120:121] op_sel_hi:[0,1,1]
	v_pk_fma_f32 v[170:171], v[128:129], v[52:53], v[122:123] op_sel_hi:[0,1,1]
	v_fma_f32 v182, v128, v72, v138
	v_pk_fma_f32 v[124:125], v[92:93], v[74:75], v[124:125] op_sel:[1,0,0]
	v_pk_fma_f32 v[146:147], v[92:93], v[86:87], v[146:147] op_sel:[1,0,0]
	v_fma_f32 v154, v93, v88, v154
	v_pk_fma_f32 v[136:137], v[128:129], v[74:75], v[136:137] op_sel:[1,0,0]
	v_pk_fma_f32 v[170:171], v[128:129], v[86:87], v[170:171] op_sel:[1,0,0]
	v_fma_f32 v182, v129, v88, v182
	v_pk_fma_f32 v[124:125], v[94:95], v[104:105], v[124:125] op_sel_hi:[0,1,1]
	v_pk_fma_f32 v[146:147], v[94:95], v[108:109], v[146:147] op_sel_hi:[0,1,1]
	v_fma_f32 v154, v94, v116, v154
	v_pk_fma_f32 v[136:137], v[130:131], v[104:105], v[136:137] op_sel_hi:[0,1,1]
	v_pk_fma_f32 v[170:171], v[130:131], v[108:109], v[170:171] op_sel_hi:[0,1,1]
	v_fma_f32 v182, v130, v116, v182
	v_pk_fma_f32 v[120:121], v[36:37], v[58:59], v[120:121] op_sel_hi:[0,1,1]
	v_pk_fma_f32 v[122:123], v[36:37], v[52:53], v[122:123] op_sel_hi:[0,1,1]
	v_fma_f32 v138, v36, v72, v138
	v_pk_fma_f32 v[120:121], v[36:37], v[74:75], v[120:121] op_sel:[1,0,0]
	v_pk_fma_f32 v[122:123], v[36:37], v[86:87], v[122:123] op_sel:[1,0,0]
	v_fma_f32 v138, v37, v88, v138
	v_pk_fma_f32 v[120:121], v[38:39], v[104:105], v[120:121] op_sel_hi:[0,1,1]
	v_pk_fma_f32 v[122:123], v[38:39], v[108:109], v[122:123] op_sel_hi:[0,1,1]
	v_fma_f32 v138, v38, v116, v138
	v_cndmask_b32_e64 v246, 0, v1, s[10:11]
	v_cndmask_b32_e64 v247, 0, v1, s[14:15]
	v_cndmask_b32_e64 v144, 0, v1, s[20:21]
	v_cndmask_b32_e64 v145, 0, v1, s[22:23]
	v_cndmask_b32_e64 v148, 0, v1, s[30:31]
	v_add_f32_dpp v120, v124, v120 wave_shl:1 row_mask:0xf bank_mask:0xf bound_ctrl:1
	v_add_f32_dpp v121, v125, v121 wave_shl:1 row_mask:0xf bank_mask:0xf bound_ctrl:1
	v_add_f32_dpp v122, v146, v122 wave_shl:1 row_mask:0xf bank_mask:0xf bound_ctrl:1
	v_add_f32_dpp v123, v147, v123 wave_shl:1 row_mask:0xf bank_mask:0xf bound_ctrl:1
	v_add_f32_dpp v138, v154, v138 wave_shl:1 row_mask:0xf bank_mask:0xf bound_ctrl:1
	s_add_i32 s4, s34, 5
	s_cmpk_lt_i32 s4, 0x201
	s_cselect_b64 s[12:13], s[0:1], 0
	v_add_f32_dpp v120, v136, v120 wave_shr:1 row_mask:0xf bank_mask:0xf bound_ctrl:1
	v_add_f32_dpp v121, v137, v121 wave_shr:1 row_mask:0xf bank_mask:0xf bound_ctrl:1
	v_add_f32_dpp v122, v170, v122 wave_shr:1 row_mask:0xf bank_mask:0xf bound_ctrl:1
	v_add_f32_dpp v123, v171, v123 wave_shr:1 row_mask:0xf bank_mask:0xf bound_ctrl:1
	v_add_f32_dpp v138, v182, v138 wave_shr:1 row_mask:0xf bank_mask:0xf bound_ctrl:1
	v_pk_fma_f32 v[120:121], v[20:21], v[222:223], v[120:121] op_sel_hi:[1,0,1] neg_lo:[0,0,1] neg_hi:[0,0,1]
	v_pk_fma_f32 v[122:123], v[24:25], v[222:223], v[122:123] op_sel_hi:[1,0,1] neg_lo:[0,0,1] neg_hi:[0,0,1]
	v_fma_f32 v138, v30, v222, -v138
	v_pk_add_f32 v[120:121], v[120:121], v[246:247] neg_lo:[0,1] neg_hi:[0,1]
	v_pk_add_f32 v[122:123], v[122:123], v[144:145] neg_lo:[0,1] neg_hi:[0,1]
	v_add_f32_e64 v138, v138, -v148
	v_pk_mul_f32 v[152:153], v[120:121], v[120:121]
	v_pk_fma_f32 v[152:153], v[122:123], v[122:123], v[152:153]
	v_add_f32_e32 v152, v152, v153
	v_fma_f32 v152, v138, v138, v152
	v_cndmask_b32_e64 v153, 0, v152, s[12:13]
	v_add_f32_e32 v0, v0, v153
	s_add_i32 s4, s34, 10
	s_min_i32 s4, s4, 0x200
	s_mul_i32 s5, s4, 0x804
	s_add_i32 s5, s5, s35
	s_add_i32 s6, s5, 0x0
	s_add_i32 s7, s5, 0x101004
	s_add_i32 s8, s5, 0x202008
	s_add_i32 s11, s5, 0x30300c
	s_add_i32 s15, s5, 0x404010
	s_mul_i32 s9, s4, 0x180c
	s_add_i32 s9, s9, s33
	buffer_load_dword v20, v28, s[16:19], s6 offen nt
	buffer_load_dword v21, v28, s[16:19], s7 offen nt
	buffer_load_dword v24, v28, s[16:19], s8 offen nt
	buffer_load_dword v25, v28, s[16:19], s11 offen nt
	buffer_load_dword v30, v28, s[16:19], s15 offen nt
	buffer_load_dwordx3 v[36:38], v27, s[24:27], s9 offen nt
	s_waitcnt vmcnt(12)
	v_mov_b32_dpp v72, v8 wave_shr:1 row_mask:0xf bank_mask:0xf bound_ctrl:1
	v_mov_b32_dpp v73, v9 wave_shr:1 row_mask:0xf bank_mask:0xf bound_ctrl:1
	v_mov_b32_dpp v74, v10 wave_shr:1 row_mask:0xf bank_mask:0xf bound_ctrl:1
	v_mov_b32_dpp v92, v8 wave_shl:1 row_mask:0xf bank_mask:0xf bound_ctrl:1
	v_mov_b32_dpp v93, v9 wave_shl:1 row_mask:0xf bank_mask:0xf bound_ctrl:1
	v_mov_b32_dpp v94, v10 wave_shl:1 row_mask:0xf bank_mask:0xf bound_ctrl:1
	v_mov_b32_dpp v52, v2 wave_shr:1 row_mask:0xf bank_mask:0xf bound_ctrl:1
	v_mov_b32_dpp v53, v3 wave_shr:1 row_mask:0xf bank_mask:0xf bound_ctrl:1
	v_mov_b32_dpp v58, v4 wave_shr:1 row_mask:0xf bank_mask:0xf bound_ctrl:1
	v_mov_b32_dpp v59, v5 wave_shr:1 row_mask:0xf bank_mask:0xf bound_ctrl:1
	v_mov_b32_dpp v88, v6 wave_shr:1 row_mask:0xf bank_mask:0xf bound_ctrl:1
	v_mov_b32_dpp v104, v2 wave_shl:1 row_mask:0xf bank_mask:0xf bound_ctrl:1
	v_mov_b32_dpp v105, v3 wave_shl:1 row_mask:0xf bank_mask:0xf bound_ctrl:1
	v_mov_b32_dpp v86, v4 wave_shl:1 row_mask:0xf bank_mask:0xf bound_ctrl:1
	v_mov_b32_dpp v87, v5 wave_shl:1 row_mask:0xf bank_mask:0xf bound_ctrl:1
	v_mov_b32_dpp v108, v6 wave_shl:1 row_mask:0xf bank_mask:0xf bound_ctrl:1
	v_pk_mul_f32 v[122:123], v[2:3], v[8:9] op_sel_hi:[1,0]
	v_pk_mul_f32 v[116:117], v[4:5], v[8:9] op_sel_hi:[1,0]
	v_mul_f32_e64 v130, v6, v8
	v_pk_mul_f32 v[138:139], v[2:3], v[8:9] op_sel:[0,1]
	v_pk_mul_f32 v[120:121], v[4:5], v[8:9] op_sel:[0,1]
	v_mul_f32_e64 v146, v6, v9
	v_pk_mul_f32 v[154:155], v[2:3], v[10:11] op_sel_hi:[1,0]
	v_pk_mul_f32 v[124:125], v[4:5], v[10:11] op_sel_hi:[1,0]
	v_mul_f32_e64 v170, v6, v10
	v_pk_add_f32 v[182:183], v[2:3], v[52:53]
	v_pk_add_f32 v[128:129], v[4:5], v[58:59]
	v_add_f32_e64 v214, v6, v88
	v_pk_fma_f32 v[122:123], v[52:53], v[72:73], v[122:123] op_sel_hi:[1,0,1]
	v_pk_fma_f32 v[116:117], v[58:59], v[72:73], v[116:117] op_sel_hi:[1,0,1]
	v_fma_f32 v130, v88, v72, v130
	v_pk_fma_f32 v[138:139], v[52:53], v[72:73], v[138:139] op_sel:[0,1,0]
	v_pk_fma_f32 v[120:121], v[58:59], v[72:73], v[120:121] op_sel:[0,1,0]
	v_fma_f32 v146, v88, v73, v146
	v_pk_fma_f32 v[154:155], v[52:53], v[74:75], v[154:155] op_sel_hi:[1,0,1]
	v_pk_fma_f32 v[124:125], v[58:59], v[74:75], v[124:125] op_sel_hi:[1,0,1]
	v_fma_f32 v170, v88, v74, v170
	v_pk_add_f32 v[182:183], v[182:183], v[104:105]
	v_pk_add_f32 v[128:129], v[128:129], v[86:87]
	v_add_f32_e64 v214, v214, v108
	v_pk_fma_f32 v[122:123], v[104:105], v[92:93], v[122:123] op_sel_hi:[1,0,1]
	v_pk_fma_f32 v[116:117], v[86:87], v[92:93], v[116:117] op_sel_hi:[1,0,1]
	v_fma_f32 v130, v108, v92, v130
	v_pk_fma_f32 v[138:139], v[104:105], v[92:93], v[138:139] op_sel:[0,1,0]
	v_pk_fma_f32 v[120:121], v[86:87], v[92:93], v[120:121] op_sel:[0,1,0]
	v_fma_f32 v146, v108, v93, v146
	v_pk_fma_f32 v[154:155], v[104:105], v[94:95], v[154:155] op_sel_hi:[1,0,1]
	v_pk_fma_f32 v[124:125], v[86:87], v[94:95], v[124:125] op_sel_hi:[1,0,1]
	v_fma_f32 v170, v108, v94, v170
	s_barrier
	ds_read_b128 v[216:219], v23 offset:0
	ds_read_b128 v[220:223], v23 offset:1024
	ds_read_b128 v[244:247], v23 offset:2048
	v_pk_add_f32 v[58:59], v[198:199], v[182:183]
	v_pk_add_f32 v[52:53], v[164:165], v[58:59]
	v_pk_add_f32 v[88:89], v[202:203], v[128:129]
	v_pk_add_f32 v[86:87], v[134:135], v[88:89]
	v_add_f32_e64 v134, v204, v214
	v_add_f32_e64 v104, v168, v134
	v_pk_add_f32 v[198:199], v[90:91], v[122:123]
	v_pk_add_f32 v[202:203], v[84:85], v[198:199]
	v_pk_add_f32 v[84:85], v[102:103], v[116:117]
	v_pk_add_f32 v[108:109], v[106:107], v[84:85]
	v_add_f32_e64 v90, v172, v130
	v_add_f32_e64 v102, v96, v90
	v_pk_add_f32 v[106:107], v[118:119], v[138:139]
	v_pk_add_f32 v[96:97], v[100:101], v[106:107]
	v_pk_add_f32 v[100:101], v[174:175], v[120:121]
	v_pk_add_f32 v[136:137], v[110:111], v[100:101]
	v_add_f32_e64 v110, v180, v146
	v_add_f32_e64 v118, v112, v110
	v_pk_add_f32 v[174:175], v[178:179], v[154:155]
	v_pk_add_f32 v[112:113], v[132:133], v[174:175]
	v_pk_add_f32 v[132:133], v[186:187], v[124:125]
	v_pk_add_f32 v[144:145], v[114:115], v[132:133]
	v_add_f32_e64 v114, v200, v170
	v_add_f32_e64 v178, v160, v114
	s_waitcnt lgkmcnt(2)
	v_pk_fma_f32 v[202:203], v[216:217], v[52:53], v[202:203] op_sel_hi:[0,1,1] neg_lo:[1,0,0] neg_hi:[1,0,0]
	v_pk_fma_f32 v[108:109], v[216:217], v[86:87], v[108:109] op_sel_hi:[0,1,1] neg_lo:[1,0,0] neg_hi:[1,0,0]
	v_fma_f32 v102, -v216, v104, v102
	v_pk_fma_f32 v[96:97], v[216:217], v[52:53], v[96:97] op_sel:[1,0,0] neg_lo:[1,0,0] neg_hi:[1,0,0]
	v_pk_fma_f32 v[136:137], v[216:217], v[86:87], v[136:137] op_sel:[1,0,0] neg_lo:[1,0,0] neg_hi:[1,0,0]
	v_fma_f32 v118, -v217, v104, v118
	v_pk_fma_f32 v[112:113], v[218:219], v[52:53], v[112:113] op_sel_hi:[0,1,1] neg_lo:[1,0,0] neg_hi:[1,0,0]
	v_pk_fma_f32 v[144:145], v[218:219], v[86:87], v[144:145] op_sel_hi:[0,1,1] neg_lo:[1,0,0] neg_hi:[1,0,0]
	v_fma_f32 v178, -v218, v104, v178
	v_pk_mul_f32 v[186:187], v[218:219], v[202:203] op_sel:[1,0]
	v_pk_mul_f32 v[156:157], v[218:219], v[108:109] op_sel:[1,0]
	v_mul_f32_e64 v168, v219, v102
	s_waitcnt lgkmcnt(1)
	v_pk_mul_f32 v[148:149], v[220:221], v[202:203] op_sel_hi:[0,1]
	v_pk_mul_f32 v[160:161], v[220:221], v[108:109] op_sel_hi:[0,1]
	v_mul_f32_e64 v172, v220, v102
	v_pk_mul_f32 v[152:153], v[220:221], v[202:203] op_sel:[1,0]
	v_pk_mul_f32 v[164:165], v[220:221], v[108:109] op_sel:[1,0]
	v_mul_f32_e64 v176, v221, v102
	v_pk_fma_f32 v[186:187], v[220:221], v[96:97], v[186:187] op_sel_hi:[0,1,1]
	v_pk_fma_f32 v[156:157], v[220:221], v[136:137], v[156:157] op_sel_hi:[0,1,1]
	v_fma_f32 v168, v220, v118, v168
	v_pk_fma_f32 v[148:149], v[222:223], v[96:97], v[148:149] op_sel_hi:[0,1,1]
	v_pk_fma_f32 v[160:161], v[222:223], v[136:137], v[160:161] op_sel_hi:[0,1,1]
	v_fma_f32 v172, v222, v118, v172
	v_pk_fma_f32 v[152:153], v[222:223], v[96:97], v[152:153] op_sel:[1,0,0]
	v_pk_fma_f32 v[164:165], v[222:223], v[136:137], v[164:165] op_sel:[1,0,0]
	v_fma_f32 v176, v223, v118, v176
	v_pk_fma_f32 v[186:187], v[220:221], v[112:113], v[186:187] op_sel:[1,0,0]
	v_pk_fma_f32 v[156:157], v[220:221], v[144:145], v[156:157] op_sel:[1,0,0]
	v_fma_f32 v168, v221, v178, v168
	v_pk_fma_f32 v[148:149], v[222:223], v[112:113], v[148:149] op_sel:[1,0,0]
	v_pk_fma_f32 v[160:161], v[222:223], v[144:145], v[160:161] op_sel:[1,0,0]
	v_fma_f32 v172, v223, v178, v172
	s_waitcnt lgkmcnt(0)
	v_pk_fma_f32 v[152:153], v[244:245], v[112:113], v[152:153] op_sel_hi:[0,1,1]
	v_pk_fma_f32 v[164:165], v[244:245], v[144:145], v[164:165] op_sel_hi:[0,1,1]
	v_fma_f32 v176, v244, v178, v176
	v_pk_mul_f32 v[180:181], v[216:217], v[186:187] op_sel_hi:[0,1]
	v_pk_mul_f32 v[200:201], v[216:217], v[156:157] op_sel_hi:[0,1]
	v_mul_f32_e64 v204, v216, v168
	v_pk_fma_f32 v[180:181], v[216:217], v[148:149], v[180:181] op_sel:[1,0,0]
	v_pk_fma_f32 v[200:201], v[216:217], v[160:161], v[200:201] op_sel:[1,0,0]
	v_fma_f32 v204, v217, v172, v204
	v_pk_fma_f32 v[180:181], v[218:219], v[152:153], v[180:181] op_sel_hi:[0,1,1]
	v_pk_fma_f32 v[200:201], v[218:219], v[164:165], v[200:201] op_sel_hi:[0,1,1]
	v_fma_f32 v204, v218, v176, v204
	v_pk_fma_f32 v[180:181], v[244:245], v[52:53], v[180:181] op_sel:[1,0,0] neg_lo:[0,0,1] neg_hi:[0,0,1]
	v_pk_fma_f32 v[200:201], v[244:245], v[86:87], v[200:201] op_sel:[1,0,0] neg_lo:[0,0,1] neg_hi:[0,0,1]
	v_fma_f32 v204, v245, v104, -v204
	v_cmp_eq_u32_e64 s[10:11], 1, v247
	v_cmp_eq_u32_e64 s[14:15], 2, v247
	v_cmp_eq_u32_e64 s[20:21], 3, v247
	v_cmp_eq_u32_e64 s[22:23], 4, v247
	v_cmp_eq_u32_e64 s[30:31], 5, v247
	v_pk_add_f32 v[86:87], v[98:99], v[186:187]
	v_pk_add_f32 v[52:53], v[140:141], v[86:87]
	v_pk_add_f32 v[96:97], v[150:151], v[156:157]
	v_pk_add_f32 v[98:99], v[166:167], v[96:97]
	v_add_f32_e64 v104, v190, v168
	v_add_f32_e64 v102, v210, v104
	v_pk_add_f32 v[118:119], v[126:127], v[148:149]
	v_pk_add_f32 v[108:109], v[184:185], v[118:119]
	v_pk_add_f32 v[112:113], v[158:159], v[160:161]
	v_pk_add_f32 v[126:127], v[194:195], v[112:113]
	v_add_f32_e64 v136, v226, v172
	v_add_f32_e64 v140, v230, v136
	v_pk_add_f32 v[150:151], v[142:143], v[152:153]
	v_pk_add_f32 v[144:145], v[188:189], v[150:151]
	v_pk_add_f32 v[184:185], v[162:163], v[164:165]
	v_pk_add_f32 v[142:143], v[206:207], v[184:185]
	v_add_f32_e64 v188, v242, v176
	v_add_f32_e64 v158, v234, v188
	v_pk_add_f32 v[208:209], v[224:225], v[180:181]
	v_pk_add_f32 v[162:163], v[238:239], v[208:209]
	v_pk_add_f32 v[166:167], v[228:229], v[200:201]
	v_pk_add_f32 v[212:213], v[192:193], v[166:167]
	v_add_f32_e64 v178, v232, v204
	v_add_f32_e64 v192, v196, v178
	v_pk_fma_f32 v[190:191], v[60:61], v[52:53], v[162:163] op_sel_hi:[0,1,1]
	v_pk_fma_f32 v[196:197], v[60:61], v[98:99], v[212:213] op_sel_hi:[0,1,1]
	v_fma_f32 v224, v60, v102, v192
	v_pk_fma_f32 v[194:195], v[68:69], v[52:53], v[162:163] op_sel_hi:[0,1,1]
	v_pk_fma_f32 v[228:229], v[68:69], v[98:99], v[212:213] op_sel_hi:[0,1,1]
	v_fma_f32 v232, v68, v102, v192
	v_pk_fma_f32 v[190:191], v[60:61], v[108:109], v[190:191] op_sel:[1,0,0]
	v_pk_fma_f32 v[196:197], v[60:61], v[126:127], v[196:197] op_sel:[1,0,0]
	v_fma_f32 v224, v61, v140, v224
	v_pk_fma_f32 v[194:195], v[68:69], v[108:109], v[194:195] op_sel:[1,0,0]
	v_pk_fma_f32 v[228:229], v[68:69], v[126:127], v[228:229] op_sel:[1,0,0]
	v_fma_f32 v232, v69, v140, v232
	v_pk_fma_f32 v[190:191], v[62:63], v[144:145], v[190:191] op_sel_hi:[0,1,1]
	v_pk_fma_f32 v[196:197], v[62:63], v[142:143], v[196:197] op_sel_hi:[0,1,1]
	v_fma_f32 v224, v62, v158, v224
	v_pk_fma_f32 v[194:195], v[70:71], v[144:145], v[194:195] op_sel_hi:[0,1,1]
	v_pk_fma_f32 v[228:229], v[70:71], v[142:143], v[228:229] op_sel_hi:[0,1,1]
	v_fma_f32 v232, v70, v158, v232
	v_pk_fma_f32 v[162:163], v[48:49], v[52:53], v[162:163] op_sel_hi:[0,1,1]
	v_pk_fma_f32 v[212:213], v[48:49], v[98:99], v[212:213] op_sel_hi:[0,1,1]
	v_fma_f32 v192, v48, v102, v192
	v_pk_fma_f32 v[162:163], v[48:49], v[108:109], v[162:163] op_sel:[1,0,0]
	v_pk_fma_f32 v[212:213], v[48:49], v[126:127], v[212:213] op_sel:[1,0,0]
	v_fma_f32 v192, v49, v140, v192
	v_pk_fma_f32 v[162:163], v[50:51], v[144:145], v[162:163] op_sel_hi:[0,1,1]
	v_pk_fma_f32 v[212:213], v[50:51], v[142:143], v[212:213] op_sel_hi:[0,1,1]
	v_fma_f32 v192, v50, v158, v192
	v_cndmask_b32_e64 v236, 0, v1, s[10:11]
	v_cndmask_b32_e64 v237, 0, v1, s[14:15]
	v_cndmask_b32_e64 v202, 0, v1, s[20:21]
	v_cndmask_b32_e64 v203, 0, v1, s[22:23]
	v_cndmask_b32_e64 v206, 0, v1, s[30:31]
	v_add_f32_dpp v162, v190, v162 wave_shl:1 row_mask:0xf bank_mask:0xf bound_ctrl:1
	v_add_f32_dpp v163, v191, v163 wave_shl:1 row_mask:0xf bank_mask:0xf bound_ctrl:1
	v_add_f32_dpp v212, v196, v212 wave_shl:1 row_mask:0xf bank_mask:0xf bound_ctrl:1
	v_add_f32_dpp v213, v197, v213 wave_shl:1 row_mask:0xf bank_mask:0xf bound_ctrl:1
	v_add_f32_dpp v192, v224, v192 wave_shl:1 row_mask:0xf bank_mask:0xf bound_ctrl:1
	s_add_i32 s4, s34, 6
	s_cmpk_lt_i32 s4, 0x201
	s_cselect_b64 s[12:13], s[0:1], 0
	v_add_f32_dpp v162, v194, v162 wave_shr:1 row_mask:0xf bank_mask:0xf bound_ctrl:1
	v_add_f32_dpp v163, v195, v163 wave_shr:1 row_mask:0xf bank_mask:0xf bound_ctrl:1
	v_add_f32_dpp v212, v228, v212 wave_shr:1 row_mask:0xf bank_mask:0xf bound_ctrl:1
	v_add_f32_dpp v213, v229, v213 wave_shr:1 row_mask:0xf bank_mask:0xf bound_ctrl:1
	v_add_f32_dpp v192, v232, v192 wave_shr:1 row_mask:0xf bank_mask:0xf bound_ctrl:1
	v_pk_fma_f32 v[162:163], v[40:41], v[246:247], v[162:163] op_sel_hi:[1,0,1] neg_lo:[0,0,1] neg_hi:[0,0,1]
	v_pk_fma_f32 v[212:213], v[42:43], v[246:247], v[212:213] op_sel_hi:[1,0,1] neg_lo:[0,0,1] neg_hi:[0,0,1]
	v_fma_f32 v192, v44, v246, -v192
	v_pk_add_f32 v[162:163], v[162:163], v[236:237] neg_lo:[0,1] neg_hi:[0,1]
	v_pk_add_f32 v[212:213], v[212:213], v[202:203] neg_lo:[0,1] neg_hi:[0,1]
	v_add_f32_e64 v192, v192, -v206
	v_pk_mul_f32 v[210:211], v[162:163], v[162:163]
	v_pk_fma_f32 v[210:211], v[212:213], v[212:213], v[210:211]
	v_add_f32_e32 v210, v210, v211
	v_fma_f32 v210, v192, v192, v210
	v_cndmask_b32_e64 v211, 0, v210, s[12:13]
	v_add_f32_e32 v0, v0, v211
	s_add_i32 s4, s34, 11
	s_min_i32 s4, s4, 0x200
	s_mul_i32 s5, s4, 0x804
	s_add_i32 s5, s5, s35
	s_add_i32 s6, s5, 0x0
	s_add_i32 s7, s5, 0x101004
	s_add_i32 s8, s5, 0x202008
	s_add_i32 s11, s5, 0x30300c
	s_add_i32 s15, s5, 0x404010
	s_mul_i32 s9, s4, 0x180c
	s_add_i32 s9, s9, s33
	buffer_load_dword v40, v28, s[16:19], s6 offen nt
	buffer_load_dword v41, v28, s[16:19], s7 offen nt
	buffer_load_dword v42, v28, s[16:19], s8 offen nt
	buffer_load_dword v43, v28, s[16:19], s11 offen nt
	buffer_load_dword v44, v28, s[16:19], s15 offen nt
	buffer_load_dwordx3 v[48:50], v27, s[24:27], s9 offen nt
	s_waitcnt vmcnt(12)
	v_mov_b32_dpp v60, v32 wave_shr:1 row_mask:0xf bank_mask:0xf bound_ctrl:1
	v_mov_b32_dpp v61, v33 wave_shr:1 row_mask:0xf bank_mask:0xf bound_ctrl:1
	v_mov_b32_dpp v62, v34 wave_shr:1 row_mask:0xf bank_mask:0xf bound_ctrl:1
	v_mov_b32_dpp v68, v32 wave_shl:1 row_mask:0xf bank_mask:0xf bound_ctrl:1
	v_mov_b32_dpp v69, v33 wave_shl:1 row_mask:0xf bank_mask:0xf bound_ctrl:1
	v_mov_b32_dpp v70, v34 wave_shl:1 row_mask:0xf bank_mask:0xf bound_ctrl:1
	v_mov_b32_dpp v98, v12 wave_shr:1 row_mask:0xf bank_mask:0xf bound_ctrl:1
	v_mov_b32_dpp v99, v13 wave_shr:1 row_mask:0xf bank_mask:0xf bound_ctrl:1
	v_mov_b32_dpp v52, v14 wave_shr:1 row_mask:0xf bank_mask:0xf bound_ctrl:1
	v_mov_b32_dpp v53, v15 wave_shr:1 row_mask:0xf bank_mask:0xf bound_ctrl:1
	v_mov_b32_dpp v102, v16 wave_shr:1 row_mask:0xf bank_mask:0xf bound_ctrl:1
	v_mov_b32_dpp v126, v12 wave_shl:1 row_mask:0xf bank_mask:0xf bound_ctrl:1
	v_mov_b32_dpp v127, v13 wave_shl:1 row_mask:0xf bank_mask:0xf bound_ctrl:1
	v_mov_b32_dpp v108, v14 wave_shl:1 row_mask:0xf bank_mask:0xf bound_ctrl:1
	v_mov_b32_dpp v109, v15 wave_shl:1 row_mask:0xf bank_mask:0xf bound_ctrl:1
	v_mov_b32_dpp v142, v16 wave_shl:1 row_mask:0xf bank_mask:0xf bound_ctrl:1
	v_pk_mul_f32 v[140:141], v[12:13], v[32:33] op_sel_hi:[1,0]
	v_pk_mul_f32 v[158:159], v[14:15], v[32:33] op_sel_hi:[1,0]
	v_mul_f32_e64 v144, v16, v32
	v_pk_mul_f32 v[192:193], v[12:13], v[32:33] op_sel:[0,1]
	v_pk_mul_f32 v[162:163], v[14:15], v[32:33] op_sel:[0,1]
	v_mul_f32_e64 v196, v16, v33
	v_pk_mul_f32 v[212:213], v[12:13], v[34:35] op_sel_hi:[1,0]
	v_pk_mul_f32 v[190:191], v[14:15], v[34:35] op_sel_hi:[1,0]
	v_mul_f32_e64 v216, v16, v34
	v_pk_add_f32 v[220:221], v[12:13], v[98:99]
	v_pk_add_f32 v[194:195], v[14:15], v[52:53]
	v_add_f32_e64 v224, v16, v102
	v_pk_fma_f32 v[140:141], v[98:99], v[60:61], v[140:141] op_sel_hi:[1,0,1]
	v_pk_fma_f32 v[158:159], v[52:53], v[60:61], v[158:159] op_sel_hi:[1,0,1]
	v_fma_f32 v144, v102, v60, v144
	v_pk_fma_f32 v[192:193], v[98:99], v[60:61], v[192:193] op_sel:[0,1,0]
	v_pk_fma_f32 v[162:163], v[52:53], v[60:61], v[162:163] op_sel:[0,1,0]
	v_fma_f32 v196, v102, v61, v196
	v_pk_fma_f32 v[212:213], v[98:99], v[62:63], v[212:213] op_sel_hi:[1,0,1]
	v_pk_fma_f32 v[190:191], v[52:53], v[62:63], v[190:191] op_sel_hi:[1,0,1]
	v_fma_f32 v216, v102, v62, v216
	v_pk_add_f32 v[220:221], v[220:221], v[126:127]
	v_pk_add_f32 v[194:195], v[194:195], v[108:109]
	v_add_f32_e64 v224, v224, v142
	v_pk_fma_f32 v[140:141], v[126:127], v[68:69], v[140:141] op_sel_hi:[1,0,1]
	v_pk_fma_f32 v[158:159], v[108:109], v[68:69], v[158:159] op_sel_hi:[1,0,1]
	v_fma_f32 v144, v142, v68, v144
	v_pk_fma_f32 v[192:193], v[126:127], v[68:69], v[192:193] op_sel:[0,1,0]
	v_pk_fma_f32 v[162:163], v[108:109], v[68:69], v[162:163] op_sel:[0,1,0]
	v_fma_f32 v196, v142, v69, v196
	v_pk_fma_f32 v[212:213], v[126:127], v[70:71], v[212:213] op_sel_hi:[1,0,1]
	v_pk_fma_f32 v[190:191], v[108:109], v[70:71], v[190:191] op_sel_hi:[1,0,1]
	v_fma_f32 v216, v142, v70, v216
	s_barrier
	ds_read_b128 v[228:231], v23 offset:3072
	ds_read_b128 v[232:235], v23 offset:4096
	ds_read_b128 v[236:239], v23 offset:5120
	v_pk_add_f32 v[52:53], v[58:59], v[220:221]
	v_pk_add_f32 v[58:59], v[88:89], v[194:195]
	v_add_f32_e64 v88, v134, v224
	v_pk_add_f32 v[98:99], v[198:199], v[140:141]
	v_pk_add_f32 v[108:109], v[84:85], v[158:159]
	v_add_f32_e64 v102, v90, v144
	v_pk_add_f32 v[90:91], v[106:107], v[192:193]
	v_pk_add_f32 v[84:85], v[100:101], v[162:163]
	v_add_f32_e64 v106, v110, v196
	v_pk_add_f32 v[110:111], v[174:175], v[212:213]
	v_pk_add_f32 v[100:101], v[132:133], v[190:191]
	v_add_f32_e64 v126, v114, v216
	s_waitcnt lgkmcnt(2)
	v_pk_fma_f32 v[98:99], v[228:229], v[52:53], v[98:99] op_sel_hi:[0,1,1] neg_lo:[1,0,0] neg_hi:[1,0,0]
	v_pk_fma_f32 v[108:109], v[228:229], v[58:59], v[108:109] op_sel_hi:[0,1,1] neg_lo:[1,0,0] neg_hi:[1,0,0]
	v_fma_f32 v102, -v228, v88, v102
	v_pk_fma_f32 v[90:91], v[228:229], v[52:53], v[90:91] op_sel:[1,0,0] neg_lo:[1,0,0] neg_hi:[1,0,0]
	v_pk_fma_f32 v[84:85], v[228:229], v[58:59], v[84:85] op_sel:[1,0,0] neg_lo:[1,0,0] neg_hi:[1,0,0]
	v_fma_f32 v106, -v229, v88, v106
	v_pk_fma_f32 v[110:111], v[230:231], v[52:53], v[110:111] op_sel_hi:[0,1,1] neg_lo:[1,0,0] neg_hi:[1,0,0]
	v_pk_fma_f32 v[100:101], v[230:231], v[58:59], v[100:101] op_sel_hi:[0,1,1] neg_lo:[1,0,0] neg_hi:[1,0,0]
	v_fma_f32 v126, -v230, v88, v126
	v_pk_mul_f32 v[132:133], v[230:231], v[98:99] op_sel:[1,0]
	v_pk_mul_f32 v[114:115], v[230:231], v[108:109] op_sel:[1,0]
	v_mul_f32_e64 v248, v231, v102
	s_waitcnt lgkmcnt(1)
	v_pk_mul_f32 v[240:241], v[232:233], v[98:99] op_sel_hi:[0,1]
	v_pk_mul_f32 v[134:135], v[232:233], v[108:109] op_sel_hi:[0,1]
	v_mul_f32_e64 v174, v232, v102
	v_pk_mul_f32 v[244:245], v[232:233], v[98:99] op_sel:[1,0]
	v_pk_mul_f32 v[142:143], v[232:233], v[108:109] op_sel:[1,0]
	v_mul_f32_e64 v198, v233, v102
	v_pk_fma_f32 v[132:133], v[232:233], v[90:91], v[132:133] op_sel_hi:[0,1,1]
	v_pk_fma_f32 v[114:115], v[232:233], v[84:85], v[114:115] op_sel_hi:[0,1,1]
	v_fma_f32 v248, v232, v106, v248
	v_pk_fma_f32 v[240:241], v[234:235], v[90:91], v[240:241] op_sel_hi:[0,1,1]
	v_pk_fma_f32 v[134:135], v[234:235], v[84:85], v[134:135] op_sel_hi:[0,1,1]
	v_fma_f32 v174, v234, v106, v174
	v_pk_fma_f32 v[244:245], v[234:235], v[90:91], v[244:245] op_sel:[1,0,0]
	v_pk_fma_f32 v[142:143], v[234:235], v[84:85], v[142:143] op_sel:[1,0,0]
	v_fma_f32 v198, v235, v106, v198
	v_pk_fma_f32 v[132:133], v[232:233], v[110:111], v[132:133] op_sel:[1,0,0]
	v_pk_fma_f32 v[114:115], v[232:233], v[100:101], v[114:115] op_sel:[1,0,0]
	v_fma_f32 v248, v233, v126, v248
	v_pk_fma_f32 v[240:241], v[234:235], v[110:111], v[240:241] op_sel:[1,0,0]
	v_pk_fma_f32 v[134:135], v[234:235], v[100:101], v[134:135] op_sel:[1,0,0]
	v_fma_f32 v174, v235, v126, v174
	s_waitcnt lgkmcnt(0)
	v_pk_fma_f32 v[244:245], v[236:237], v[110:111], v[244:245] op_sel_hi:[0,1,1]
	v_pk_fma_f32 v[142:143], v[236:237], v[100:101], v[142:143] op_sel_hi:[0,1,1]
	v_fma_f32 v198, v236, v126, v198
	v_pk_mul_f32 v[202:203], v[228:229], v[132:133] op_sel_hi:[0,1]
	v_pk_mul_f32 v[206:207], v[228:229], v[114:115] op_sel_hi:[0,1]
	v_mul_f32_e64 v210, v228, v248
	v_pk_fma_f32 v[202:203], v[228:229], v[240:241], v[202:203] op_sel:[1,0,0]
	v_pk_fma_f32 v[206:207], v[228:229], v[134:135], v[206:207] op_sel:[1,0,0]
	v_fma_f32 v210, v229, v174, v210
	v_pk_fma_f32 v[202:203], v[230:231], v[244:245], v[202:203] op_sel_hi:[0,1,1]
	v_pk_fma_f32 v[206:207], v[230:231], v[142:143], v[206:207] op_sel_hi:[0,1,1]
	v_fma_f32 v210, v230, v198, v210
	v_pk_fma_f32 v[202:203], v[236:237], v[52:53], v[202:203] op_sel:[1,0,0] neg_lo:[0,0,1] neg_hi:[0,0,1]
	v_pk_fma_f32 v[206:207], v[236:237], v[58:59], v[206:207] op_sel:[1,0,0] neg_lo:[0,0,1] neg_hi:[0,0,1]
	v_fma_f32 v210, v237, v88, -v210
	v_cmp_eq_u32_e64 s[10:11], 1, v239
	v_cmp_eq_u32_e64 s[14:15], 2, v239
	v_cmp_eq_u32_e64 s[20:21], 3, v239
	v_cmp_eq_u32_e64 s[22:23], 4, v239
	v_cmp_eq_u32_e64 s[30:31], 5, v239
	v_pk_add_f32 v[52:53], v[86:87], v[132:133]
	v_pk_add_f32 v[58:59], v[96:97], v[114:115]
	v_add_f32_e64 v84, v104, v248
	v_pk_add_f32 v[86:87], v[118:119], v[240:241]
	v_pk_add_f32 v[88:89], v[112:113], v[134:135]
	v_add_f32_e64 v90, v136, v174
	v_pk_add_f32 v[96:97], v[150:151], v[244:245]
	v_pk_add_f32 v[98:99], v[184:185], v[142:143]
	v_add_f32_e64 v100, v188, v198
	v_pk_add_f32 v[102:103], v[208:209], v[202:203]
	v_pk_add_f32 v[104:105], v[166:167], v[206:207]
	v_add_f32_e64 v106, v178, v210
	v_pk_fma_f32 v[110:111], v[64:65], v[52:53], v[102:103] op_sel_hi:[0,1,1]
	v_pk_fma_f32 v[108:109], v[64:65], v[58:59], v[104:105] op_sel_hi:[0,1,1]
	v_fma_f32 v118, v64, v84, v106
	v_pk_fma_f32 v[126:127], v[76:77], v[52:53], v[102:103] op_sel_hi:[0,1,1]
	v_pk_fma_f32 v[112:113], v[76:77], v[58:59], v[104:105] op_sel_hi:[0,1,1]
	v_fma_f32 v150, v76, v84, v106
	v_pk_fma_f32 v[110:111], v[64:65], v[86:87], v[110:111] op_sel:[1,0,0]
	v_pk_fma_f32 v[108:109], v[64:65], v[88:89], v[108:109] op_sel:[1,0,0]
	v_fma_f32 v118, v65, v90, v118
	v_pk_fma_f32 v[126:127], v[76:77], v[86:87], v[126:127] op_sel:[1,0,0]
	v_pk_fma_f32 v[112:113], v[76:77], v[88:89], v[112:113] op_sel:[1,0,0]
	v_fma_f32 v150, v77, v90, v150
	v_pk_fma_f32 v[110:111], v[66:67], v[96:97], v[110:111] op_sel_hi:[0,1,1]
	v_pk_fma_f32 v[108:109], v[66:67], v[98:99], v[108:109] op_sel_hi:[0,1,1]
	v_fma_f32 v118, v66, v100, v118
	v_pk_fma_f32 v[126:127], v[78:79], v[96:97], v[126:127] op_sel_hi:[0,1,1]
	v_pk_fma_f32 v[112:113], v[78:79], v[98:99], v[112:113] op_sel_hi:[0,1,1]
	v_fma_f32 v150, v78, v100, v150
	v_pk_fma_f32 v[102:103], v[80:81], v[52:53], v[102:103] op_sel_hi:[0,1,1]
	v_pk_fma_f32 v[104:105], v[80:81], v[58:59], v[104:105] op_sel_hi:[0,1,1]
	v_fma_f32 v106, v80, v84, v106
	v_pk_fma_f32 v[102:103], v[80:81], v[86:87], v[102:103] op_sel:[1,0,0]
	v_pk_fma_f32 v[104:105], v[80:81], v[88:89], v[104:105] op_sel:[1,0,0]
	v_fma_f32 v106, v81, v90, v106
	v_pk_fma_f32 v[102:103], v[82:83], v[96:97], v[102:103] op_sel_hi:[0,1,1]
	v_pk_fma_f32 v[104:105], v[82:83], v[98:99], v[104:105] op_sel_hi:[0,1,1]
	v_fma_f32 v106, v82, v100, v106
	v_cndmask_b32_e64 v136, 0, v1, s[10:11]
	v_cndmask_b32_e64 v137, 0, v1, s[14:15]
	v_cndmask_b32_e64 v166, 0, v1, s[20:21]
	v_cndmask_b32_e64 v167, 0, v1, s[22:23]
	v_cndmask_b32_e64 v184, 0, v1, s[30:31]
	v_add_f32_dpp v102, v110, v102 wave_shl:1 row_mask:0xf bank_mask:0xf bound_ctrl:1
	v_add_f32_dpp v103, v111, v103 wave_shl:1 row_mask:0xf bank_mask:0xf bound_ctrl:1
	v_add_f32_dpp v104, v108, v104 wave_shl:1 row_mask:0xf bank_mask:0xf bound_ctrl:1
	v_add_f32_dpp v105, v109, v105 wave_shl:1 row_mask:0xf bank_mask:0xf bound_ctrl:1
	v_add_f32_dpp v106, v118, v106 wave_shl:1 row_mask:0xf bank_mask:0xf bound_ctrl:1
	s_add_i32 s4, s34, 7
	s_cmpk_lt_i32 s4, 0x201
	s_cselect_b64 s[12:13], s[0:1], 0
	v_add_f32_dpp v102, v126, v102 wave_shr:1 row_mask:0xf bank_mask:0xf bound_ctrl:1
	v_add_f32_dpp v103, v127, v103 wave_shr:1 row_mask:0xf bank_mask:0xf bound_ctrl:1
	v_add_f32_dpp v104, v112, v104 wave_shr:1 row_mask:0xf bank_mask:0xf bound_ctrl:1
	v_add_f32_dpp v105, v113, v105 wave_shr:1 row_mask:0xf bank_mask:0xf bound_ctrl:1
	v_add_f32_dpp v106, v150, v106 wave_shr:1 row_mask:0xf bank_mask:0xf bound_ctrl:1
	v_pk_fma_f32 v[102:103], v[46:47], v[238:239], v[102:103] op_sel_hi:[1,0,1] neg_lo:[0,0,1] neg_hi:[0,0,1]
	v_pk_fma_f32 v[104:105], v[54:55], v[238:239], v[104:105] op_sel_hi:[1,0,1] neg_lo:[0,0,1] neg_hi:[0,0,1]
	v_fma_f32 v106, v56, v238, -v106
	v_pk_add_f32 v[102:103], v[102:103], v[136:137] neg_lo:[0,1] neg_hi:[0,1]
	v_pk_add_f32 v[104:105], v[104:105], v[166:167] neg_lo:[0,1] neg_hi:[0,1]
	v_add_f32_e64 v106, v106, -v184
	v_pk_mul_f32 v[178:179], v[102:103], v[102:103]
	v_pk_fma_f32 v[178:179], v[104:105], v[104:105], v[178:179]
	v_add_f32_e32 v178, v178, v179
	v_fma_f32 v178, v106, v106, v178
	v_cndmask_b32_e64 v179, 0, v178, s[12:13]
	v_add_f32_e32 v0, v0, v179
	s_waitcnt vmcnt(6)
	v_mov_b32_dpp v52, v36 wave_shr:1 row_mask:0xf bank_mask:0xf bound_ctrl:1
	v_mov_b32_dpp v53, v37 wave_shr:1 row_mask:0xf bank_mask:0xf bound_ctrl:1
	v_mov_b32_dpp v54, v38 wave_shr:1 row_mask:0xf bank_mask:0xf bound_ctrl:1
	v_mov_b32_dpp v56, v36 wave_shl:1 row_mask:0xf bank_mask:0xf bound_ctrl:1
	v_mov_b32_dpp v57, v37 wave_shl:1 row_mask:0xf bank_mask:0xf bound_ctrl:1
	v_mov_b32_dpp v58, v38 wave_shl:1 row_mask:0xf bank_mask:0xf bound_ctrl:1
	v_mov_b32_dpp v46, v20 wave_shr:1 row_mask:0xf bank_mask:0xf bound_ctrl:1
	v_mov_b32_dpp v47, v21 wave_shr:1 row_mask:0xf bank_mask:0xf bound_ctrl:1
	v_mov_b32_dpp v66, v24 wave_shr:1 row_mask:0xf bank_mask:0xf bound_ctrl:1
	v_mov_b32_dpp v67, v25 wave_shr:1 row_mask:0xf bank_mask:0xf bound_ctrl:1
	v_mov_b32_dpp v64, v30 wave_shr:1 row_mask:0xf bank_mask:0xf bound_ctrl:1
	v_mov_b32_dpp v78, v20 wave_shl:1 row_mask:0xf bank_mask:0xf bound_ctrl:1
	v_mov_b32_dpp v79, v21 wave_shl:1 row_mask:0xf bank_mask:0xf bound_ctrl:1
	v_mov_b32_dpp v82, v24 wave_shl:1 row_mask:0xf bank_mask:0xf bound_ctrl:1
	v_mov_b32_dpp v83, v25 wave_shl:1 row_mask:0xf bank_mask:0xf bound_ctrl:1
	v_mov_b32_dpp v76, v30 wave_shl:1 row_mask:0xf bank_mask:0xf bound_ctrl:1
	v_pk_mul_f32 v[80:81], v[20:21], v[36:37] op_sel_hi:[1,0]
	v_pk_mul_f32 v[84:85], v[24:25], v[36:37] op_sel_hi:[1,0]
	v_mul_f32_e64 v86, v30, v36
	v_pk_mul_f32 v[88:89], v[20:21], v[36:37] op_sel:[0,1]
	v_pk_mul_f32 v[96:97], v[24:25], v[36:37] op_sel:[0,1]
	v_mul_f32_e64 v90, v30, v37
	v_pk_mul_f32 v[100:101], v[20:21], v[38:39] op_sel_hi:[1,0]
	v_pk_mul_f32 v[104:105], v[24:25], v[38:39] op_sel_hi:[1,0]
	v_mul_f32_e64 v98, v30, v38
	v_pk_add_f32 v[108:109], v[20:21], v[46:47]
	v_pk_add_f32 v[112:113], v[24:25], v[66:67]
	v_add_f32_e64 v102, v30, v64
	v_pk_fma_f32 v[80:81], v[46:47], v[52:53], v[80:81] op_sel_hi:[1,0,1]
	v_pk_fma_f32 v[84:85], v[66:67], v[52:53], v[84:85] op_sel_hi:[1,0,1]
	v_fma_f32 v86, v64, v52, v86
	v_pk_fma_f32 v[88:89], v[46:47], v[52:53], v[88:89] op_sel:[0,1,0]
	v_pk_fma_f32 v[96:97], v[66:67], v[52:53], v[96:97] op_sel:[0,1,0]
	v_fma_f32 v90, v64, v53, v90
	v_pk_fma_f32 v[100:101], v[46:47], v[54:55], v[100:101] op_sel_hi:[1,0,1]
	v_pk_fma_f32 v[104:105], v[66:67], v[54:55], v[104:105] op_sel_hi:[1,0,1]
	v_fma_f32 v98, v64, v54, v98
	v_pk_add_f32 v[108:109], v[108:109], v[78:79]
	v_pk_add_f32 v[112:113], v[112:113], v[82:83]
	v_add_f32_e64 v102, v102, v76
	v_pk_fma_f32 v[80:81], v[78:79], v[56:57], v[80:81] op_sel_hi:[1,0,1]
	v_pk_fma_f32 v[84:85], v[82:83], v[56:57], v[84:85] op_sel_hi:[1,0,1]
	v_fma_f32 v86, v76, v56, v86
	v_pk_fma_f32 v[88:89], v[78:79], v[56:57], v[88:89] op_sel:[0,1,0]
	v_pk_fma_f32 v[96:97], v[82:83], v[56:57], v[96:97] op_sel:[0,1,0]
	v_fma_f32 v90, v76, v57, v90
	v_pk_fma_f32 v[100:101], v[78:79], v[58:59], v[100:101] op_sel_hi:[1,0,1]
	v_pk_fma_f32 v[104:105], v[82:83], v[58:59], v[104:105] op_sel_hi:[1,0,1]
	v_fma_f32 v98, v76, v58, v98
	s_barrier
	ds_read_b128 v[64:67], v23 offset:0
	ds_read_b128 v[76:79], v23 offset:1024
	ds_read_b128 v[228:231], v23 offset:2048
	v_pk_add_f32 v[136:137], v[220:221], v[108:109]
	v_pk_add_f32 v[46:47], v[182:183], v[136:137]
	v_pk_add_f32 v[82:83], v[194:195], v[112:113]
	v_pk_add_f32 v[106:107], v[128:129], v[82:83]
	v_add_f32_e64 v128, v224, v102
	v_add_f32_e64 v110, v214, v128
	v_pk_add_f32 v[184:185], v[140:141], v[80:81]
	v_pk_add_f32 v[188:189], v[122:123], v[184:185]
	v_pk_add_f32 v[118:119], v[158:159], v[84:85]
	v_pk_add_f32 v[140:141], v[116:117], v[118:119]
	v_add_f32_e64 v116, v144, v86
	v_add_f32_e64 v208, v130, v116
	v_pk_add_f32 v[144:145], v[192:193], v[88:89]
	v_pk_add_f32 v[220:221], v[138:139], v[144:145]
	v_pk_add_f32 v[122:123], v[162:163], v[96:97]
	v_pk_add_f32 v[192:193], v[120:121], v[122:123]
	v_add_f32_e64 v120, v196, v90
	v_add_f32_e64 v224, v146, v120
	v_pk_add_f32 v[196:197], v[212:213], v[100:101]
	v_pk_add_f32 v[232:233], v[154:155], v[196:197]
	v_pk_add_f32 v[126:127], v[190:191], v[104:105]
	v_pk_add_f32 v[212:213], v[124:125], v[126:127]
	v_add_f32_e64 v124, v216, v98
	v_add_f32_e64 v236, v170, v124
	s_waitcnt lgkmcnt(2)
	v_pk_fma_f32 v[188:189], v[64:65], v[46:47], v[188:189] op_sel_hi:[0,1,1] neg_lo:[1,0,0] neg_hi:[1,0,0]
	v_pk_fma_f32 v[140:141], v[64:65], v[106:107], v[140:141] op_sel_hi:[0,1,1] neg_lo:[1,0,0] neg_hi:[1,0,0]
	v_fma_f32 v208, -v64, v110, v208
	v_pk_fma_f32 v[220:221], v[64:65], v[46:47], v[220:221] op_sel:[1,0,0] neg_lo:[1,0,0] neg_hi:[1,0,0]
	v_pk_fma_f32 v[192:193], v[64:65], v[106:107], v[192:193] op_sel:[1,0,0] neg_lo:[1,0,0] neg_hi:[1,0,0]
	v_fma_f32 v224, -v65, v110, v224
	v_pk_fma_f32 v[232:233], v[66:67], v[46:47], v[232:233] op_sel_hi:[0,1,1] neg_lo:[1,0,0] neg_hi:[1,0,0]
	v_pk_fma_f32 v[212:213], v[66:67], v[106:107], v[212:213] op_sel_hi:[0,1,1] neg_lo:[1,0,0] neg_hi:[1,0,0]
	v_fma_f32 v236, -v66, v110, v236
	v_pk_mul_f32 v[130:131], v[66:67], v[188:189] op_sel:[1,0]
	v_pk_mul_f32 v[150:151], v[66:67], v[140:141] op_sel:[1,0]
	v_mul_f32_e64 v162, v67, v208
	s_waitcnt lgkmcnt(1)
	v_pk_mul_f32 v[138:139], v[76:77], v[188:189] op_sel_hi:[0,1]
	v_pk_mul_f32 v[154:155], v[76:77], v[140:141] op_sel_hi:[0,1]
	v_mul_f32_e64 v166, v76, v208
	v_pk_mul_f32 v[146:147], v[76:77], v[188:189] op_sel:[1,0]
	v_pk_mul_f32 v[158:159], v[76:77], v[140:141] op_sel:[1,0]
	v_mul_f32_e64 v170, v77, v208
	v_pk_fma_f32 v[130:131], v[76:77], v[220:221], v[130:131] op_sel_hi:[0,1,1]
	v_pk_fma_f32 v[150:151], v[76:77], v[192:193], v[150:151] op_sel_hi:[0,1,1]
	v_fma_f32 v162, v76, v224, v162
	v_pk_fma_f32 v[138:139], v[78:79], v[220:221], v[138:139] op_sel_hi:[0,1,1]
	v_pk_fma_f32 v[154:155], v[78:79], v[192:193], v[154:155] op_sel_hi:[0,1,1]
	v_fma_f32 v166, v78, v224, v166
	v_pk_fma_f32 v[146:147], v[78:79], v[220:221], v[146:147] op_sel:[1,0,0]
	v_pk_fma_f32 v[158:159], v[78:79], v[192:193], v[158:159] op_sel:[1,0,0]
	v_fma_f32 v170, v79, v224, v170
	v_pk_fma_f32 v[130:131], v[76:77], v[232:233], v[130:131] op_sel:[1,0,0]
	v_pk_fma_f32 v[150:151], v[76:77], v[212:213], v[150:151] op_sel:[1,0,0]
	v_fma_f32 v162, v77, v236, v162
	v_pk_fma_f32 v[138:139], v[78:79], v[232:233], v[138:139] op_sel:[1,0,0]
	v_pk_fma_f32 v[154:155], v[78:79], v[212:213], v[154:155] op_sel:[1,0,0]
	v_fma_f32 v166, v79, v236, v166
	s_waitcnt lgkmcnt(0)
	v_pk_fma_f32 v[146:147], v[228:229], v[232:233], v[146:147] op_sel_hi:[0,1,1]
	v_pk_fma_f32 v[158:159], v[228:229], v[212:213], v[158:159] op_sel_hi:[0,1,1]
	v_fma_f32 v170, v228, v236, v170
	v_pk_mul_f32 v[216:217], v[64:65], v[130:131] op_sel_hi:[0,1]
	v_pk_mul_f32 v[178:179], v[64:65], v[150:151] op_sel_hi:[0,1]
	v_mul_f32_e64 v182, v64, v162
	v_pk_fma_f32 v[216:217], v[64:65], v[138:139], v[216:217] op_sel:[1,0,0]
	v_pk_fma_f32 v[178:179], v[64:65], v[154:155], v[178:179] op_sel:[1,0,0]
	v_fma_f32 v182, v65, v166, v182
	v_pk_fma_f32 v[216:217], v[66:67], v[146:147], v[216:217] op_sel_hi:[0,1,1]
	v_pk_fma_f32 v[178:179], v[66:67], v[158:159], v[178:179] op_sel_hi:[0,1,1]
	v_fma_f32 v182, v66, v170, v182
	v_pk_fma_f32 v[216:217], v[228:229], v[46:47], v[216:217] op_sel:[1,0,0] neg_lo:[0,0,1] neg_hi:[0,0,1]
	v_pk_fma_f32 v[178:179], v[228:229], v[106:107], v[178:179] op_sel:[1,0,0] neg_lo:[0,0,1] neg_hi:[0,0,1]
	v_fma_f32 v182, v229, v110, -v182
	v_cmp_eq_u32_e64 s[10:11], 1, v231
	v_cmp_eq_u32_e64 s[14:15], 2, v231
	v_cmp_eq_u32_e64 s[20:21], 3, v231
	v_cmp_eq_u32_e64 s[22:23], 4, v231
	v_cmp_eq_u32_e64 s[30:31], 5, v231
	v_pk_add_f32 v[140:141], v[132:133], v[130:131]
	v_pk_add_f32 v[46:47], v[186:187], v[140:141]
	v_pk_add_f32 v[106:107], v[114:115], v[150:151]
	v_pk_add_f32 v[110:111], v[156:157], v[106:107]
	v_add_f32_e64 v114, v248, v162
	v_add_f32_e64 v132, v168, v114
	v_pk_add_f32 v[186:187], v[240:241], v[138:139]
	v_pk_add_f32 v[156:157], v[148:149], v[186:187]
	v_pk_add_f32 v[190:191], v[134:135], v[154:155]
	v_pk_add_f32 v[148:149], v[160:161], v[190:191]
	v_add_f32_e64 v134, v174, v166
	v_add_f32_e64 v160, v172, v134
	v_pk_add_f32 v[174:175], v[244:245], v[146:147]
	v_pk_add_f32 v[168:169], v[152:153], v[174:175]
	v_pk_add_f32 v[194:195], v[142:143], v[158:159]
	v_pk_add_f32 v[152:153], v[164:165], v[194:195]
	v_add_f32_e64 v142, v198, v170
	v_add_f32_e64 v164, v176, v142
	v_pk_add_f32 v[198:199], v[202:203], v[216:217]
	v_pk_add_f32 v[214:215], v[180:181], v[198:199]
	v_pk_add_f32 v[202:203], v[206:207], v[178:179]
	v_pk_add_f32 v[218:219], v[200:201], v[202:203]
	v_add_f32_e64 v206, v210, v182
	v_add_f32_e64 v222, v204, v206
	v_pk_fma_f32 v[210:211], v[72:73], v[46:47], v[214:215] op_sel_hi:[0,1,1]
	v_pk_fma_f32 v[226:227], v[72:73], v[110:111], v[218:219] op_sel_hi:[0,1,1]
	v_fma_f32 v234, v72, v132, v222
	v_pk_fma_f32 v[238:239], v[92:93], v[46:47], v[214:215] op_sel_hi:[0,1,1]
	v_pk_fma_f32 v[242:243], v[92:93], v[110:111], v[218:219] op_sel_hi:[0,1,1]
	v_fma_f32 v246, v92, v132, v222
	v_pk_fma_f32 v[210:211], v[72:73], v[156:157], v[210:211] op_sel:[1,0,0]
	v_pk_fma_f32 v[226:227], v[72:73], v[148:149], v[226:227] op_sel:[1,0,0]
	v_fma_f32 v234, v73, v160, v234
	v_pk_fma_f32 v[238:239], v[92:93], v[156:157], v[238:239] op_sel:[1,0,0]
	v_pk_fma_f32 v[242:243], v[92:93], v[148:149], v[242:243] op_sel:[1,0,0]
	v_fma_f32 v246, v93, v160, v246
	v_pk_fma_f32 v[210:211], v[74:75], v[168:169], v[210:211] op_sel_hi:[0,1,1]
	v_pk_fma_f32 v[226:227], v[74:75], v[152:153], v[226:227] op_sel_hi:[0,1,1]
	v_fma_f32 v234, v74, v164, v234
	v_pk_fma_f32 v[238:239], v[94:95], v[168:169], v[238:239] op_sel_hi:[0,1,1]
	v_pk_fma_f32 v[242:243], v[94:95], v[152:153], v[242:243] op_sel_hi:[0,1,1]
	v_fma_f32 v246, v94, v164, v246
	v_pk_fma_f32 v[214:215], v[8:9], v[46:47], v[214:215] op_sel_hi:[0,1,1]
	v_pk_fma_f32 v[218:219], v[8:9], v[110:111], v[218:219] op_sel_hi:[0,1,1]
	v_fma_f32 v222, v8, v132, v222
	v_pk_fma_f32 v[214:215], v[8:9], v[156:157], v[214:215] op_sel:[1,0,0]
	v_pk_fma_f32 v[218:219], v[8:9], v[148:149], v[218:219] op_sel:[1,0,0]
	v_fma_f32 v222, v9, v160, v222
	v_pk_fma_f32 v[214:215], v[10:11], v[168:169], v[214:215] op_sel_hi:[0,1,1]
	v_pk_fma_f32 v[218:219], v[10:11], v[152:153], v[218:219] op_sel_hi:[0,1,1]
	v_fma_f32 v222, v10, v164, v222
	v_cndmask_b32_e64 v172, 0, v1, s[10:11]
	v_cndmask_b32_e64 v173, 0, v1, s[14:15]
	v_cndmask_b32_e64 v176, 0, v1, s[20:21]
	v_cndmask_b32_e64 v177, 0, v1, s[22:23]
	v_cndmask_b32_e64 v180, 0, v1, s[30:31]
	v_add_f32_dpp v214, v210, v214 wave_shl:1 row_mask:0xf bank_mask:0xf bound_ctrl:1
	v_add_f32_dpp v215, v211, v215 wave_shl:1 row_mask:0xf bank_mask:0xf bound_ctrl:1
	v_add_f32_dpp v218, v226, v218 wave_shl:1 row_mask:0xf bank_mask:0xf bound_ctrl:1
	v_add_f32_dpp v219, v227, v219 wave_shl:1 row_mask:0xf bank_mask:0xf bound_ctrl:1
	v_add_f32_dpp v222, v234, v222 wave_shl:1 row_mask:0xf bank_mask:0xf bound_ctrl:1
	s_add_i32 s4, s34, 8
	s_cmpk_lt_i32 s4, 0x201
	s_cselect_b64 s[12:13], s[0:1], 0
	v_add_f32_dpp v214, v238, v214 wave_shr:1 row_mask:0xf bank_mask:0xf bound_ctrl:1
	v_add_f32_dpp v215, v239, v215 wave_shr:1 row_mask:0xf bank_mask:0xf bound_ctrl:1
	v_add_f32_dpp v218, v242, v218 wave_shr:1 row_mask:0xf bank_mask:0xf bound_ctrl:1
	v_add_f32_dpp v219, v243, v219 wave_shr:1 row_mask:0xf bank_mask:0xf bound_ctrl:1
	v_add_f32_dpp v222, v246, v222 wave_shr:1 row_mask:0xf bank_mask:0xf bound_ctrl:1
	v_pk_fma_f32 v[214:215], v[2:3], v[230:231], v[214:215] op_sel_hi:[1,0,1] neg_lo:[0,0,1] neg_hi:[0,0,1]
	v_pk_fma_f32 v[218:219], v[4:5], v[230:231], v[218:219] op_sel_hi:[1,0,1] neg_lo:[0,0,1] neg_hi:[0,0,1]
	v_fma_f32 v222, v6, v230, -v222
	v_pk_add_f32 v[214:215], v[214:215], v[172:173] neg_lo:[0,1] neg_hi:[0,1]
	v_pk_add_f32 v[218:219], v[218:219], v[176:177] neg_lo:[0,1] neg_hi:[0,1]
	v_add_f32_e64 v222, v222, -v180
	v_pk_mul_f32 v[188:189], v[214:215], v[214:215]
	v_pk_fma_f32 v[188:189], v[218:219], v[218:219], v[188:189]
	v_add_f32_e32 v188, v188, v189
	v_fma_f32 v188, v222, v222, v188
	v_cndmask_b32_e64 v189, 0, v188, s[12:13]
	v_add_f32_e32 v0, v0, v189
	s_waitcnt vmcnt(0)
	v_mov_b32_dpp v4, v48 wave_shr:1 row_mask:0xf bank_mask:0xf bound_ctrl:1
	v_mov_b32_dpp v5, v49 wave_shr:1 row_mask:0xf bank_mask:0xf bound_ctrl:1
	v_mov_b32_dpp v6, v50 wave_shr:1 row_mask:0xf bank_mask:0xf bound_ctrl:1
	v_mov_b32_dpp v8, v48 wave_shl:1 row_mask:0xf bank_mask:0xf bound_ctrl:1
	v_mov_b32_dpp v9, v49 wave_shl:1 row_mask:0xf bank_mask:0xf bound_ctrl:1
	v_mov_b32_dpp v10, v50 wave_shl:1 row_mask:0xf bank_mask:0xf bound_ctrl:1
	v_mov_b32_dpp v2, v40 wave_shr:1 row_mask:0xf bank_mask:0xf bound_ctrl:1
	v_mov_b32_dpp v3, v41 wave_shr:1 row_mask:0xf bank_mask:0xf bound_ctrl:1
	v_mov_b32_dpp v64, v42 wave_shr:1 row_mask:0xf bank_mask:0xf bound_ctrl:1
	v_mov_b32_dpp v65, v43 wave_shr:1 row_mask:0xf bank_mask:0xf bound_ctrl:1
	v_mov_b32_dpp v46, v44 wave_shr:1 row_mask:0xf bank_mask:0xf bound_ctrl:1
	v_mov_b32_dpp v66, v40 wave_shl:1 row_mask:0xf bank_mask:0xf bound_ctrl:1
	v_mov_b32_dpp v67, v41 wave_shl:1 row_mask:0xf bank_mask:0xf bound_ctrl:1
	v_mov_b32_dpp v72, v42 wave_shl:1 row_mask:0xf bank_mask:0xf bound_ctrl:1
	v_mov_b32_dpp v73, v43 wave_shl:1 row_mask:0xf bank_mask:0xf bound_ctrl:1
	v_mov_b32_dpp v74, v44 wave_shl:1 row_mask:0xf bank_mask:0xf bound_ctrl:1
	v_pk_mul_f32 v[76:77], v[40:41], v[48:49] op_sel_hi:[1,0]
	v_pk_mul_f32 v[78:79], v[42:43], v[48:49] op_sel_hi:[1,0]
	v_mul_f32_e64 v92, v44, v48
	v_pk_mul_f32 v[132:133], v[40:41], v[48:49] op_sel:[0,1]
	v_pk_mul_f32 v[94:95], v[42:43], v[48:49] op_sel:[0,1]
	v_mul_f32_e64 v148, v44, v49
	v_pk_mul_f32 v[152:153], v[40:41], v[50:51] op_sel_hi:[1,0]
	v_pk_mul_f32 v[110:111], v[42:43], v[50:51] op_sel_hi:[1,0]
	v_mul_f32_e64 v156, v44, v50
	v_pk_add_f32 v[160:161], v[40:41], v[2:3]
	v_pk_add_f32 v[210:211], v[42:43], v[64:65]
	v_add_f32_e64 v164, v44, v46
	v_pk_fma_f32 v[76:77], v[2:3], v[4:5], v[76:77] op_sel_hi:[1,0,1]
	v_pk_fma_f32 v[78:79], v[64:65], v[4:5], v[78:79] op_sel_hi:[1,0,1]
	v_fma_f32 v92, v46, v4, v92
	v_pk_fma_f32 v[132:133], v[2:3], v[4:5], v[132:133] op_sel:[0,1,0]
	v_pk_fma_f32 v[94:95], v[64:65], v[4:5], v[94:95] op_sel:[0,1,0]
	v_fma_f32 v148, v46, v5, v148
	v_pk_fma_f32 v[152:153], v[2:3], v[6:7], v[152:153] op_sel_hi:[1,0,1]
	v_pk_fma_f32 v[110:111], v[64:65], v[6:7], v[110:111] op_sel_hi:[1,0,1]
	v_fma_f32 v156, v46, v6, v156
	v_pk_add_f32 v[160:161], v[160:161], v[66:67]
	v_pk_add_f32 v[210:211], v[210:211], v[72:73]
	v_add_f32_e64 v164, v164, v74
	v_pk_fma_f32 v[76:77], v[66:67], v[8:9], v[76:77] op_sel_hi:[1,0,1]
	v_pk_fma_f32 v[78:79], v[72:73], v[8:9], v[78:79] op_sel_hi:[1,0,1]
	v_fma_f32 v92, v74, v8, v92
	v_pk_fma_f32 v[132:133], v[66:67], v[8:9], v[132:133] op_sel:[0,1,0]
	v_pk_fma_f32 v[94:95], v[72:73], v[8:9], v[94:95] op_sel:[0,1,0]
	v_fma_f32 v148, v74, v9, v148
	v_pk_fma_f32 v[152:153], v[66:67], v[10:11], v[152:153] op_sel_hi:[1,0,1]
	v_pk_fma_f32 v[110:111], v[72:73], v[10:11], v[110:111] op_sel_hi:[1,0,1]
	v_fma_f32 v156, v74, v10, v156
	s_barrier
	ds_read_b128 v[64:67], v23 offset:3072
	ds_read_b128 v[72:75], v23 offset:4096
	ds_read_b128 v[212:215], v23 offset:5120
	v_pk_add_f32 v[2:3], v[136:137], v[160:161]
	v_pk_add_f32 v[46:47], v[82:83], v[210:211]
	v_add_f32_e64 v82, v128, v164
	v_pk_add_f32 v[128:129], v[184:185], v[76:77]
	v_pk_add_f32 v[136:137], v[118:119], v[78:79]
	v_add_f32_e64 v168, v116, v92
	v_pk_add_f32 v[116:117], v[144:145], v[132:133]
	v_pk_add_f32 v[144:145], v[122:123], v[94:95]
	v_add_f32_e64 v172, v120, v148
	v_pk_add_f32 v[120:121], v[196:197], v[152:153]
	v_pk_add_f32 v[176:177], v[126:127], v[110:111]
	v_add_f32_e64 v180, v124, v156
	s_waitcnt lgkmcnt(2)
	v_pk_fma_f32 v[128:129], v[64:65], v[2:3], v[128:129] op_sel_hi:[0,1,1] neg_lo:[1,0,0] neg_hi:[1,0,0]
	v_pk_fma_f32 v[136:137], v[64:65], v[46:47], v[136:137] op_sel_hi:[0,1,1] neg_lo:[1,0,0] neg_hi:[1,0,0]
	v_fma_f32 v168, -v64, v82, v168
	v_pk_fma_f32 v[116:117], v[64:65], v[2:3], v[116:117] op_sel:[1,0,0] neg_lo:[1,0,0] neg_hi:[1,0,0]
	v_pk_fma_f32 v[144:145], v[64:65], v[46:47], v[144:145] op_sel:[1,0,0] neg_lo:[1,0,0] neg_hi:[1,0,0]
	v_fma_f32 v172, -v65, v82, v172
	v_pk_fma_f32 v[120:121], v[66:67], v[2:3], v[120:121] op_sel_hi:[0,1,1] neg_lo:[1,0,0] neg_hi:[1,0,0]
	v_pk_fma_f32 v[176:177], v[66:67], v[46:47], v[176:177] op_sel_hi:[0,1,1] neg_lo:[1,0,0] neg_hi:[1,0,0]
	v_fma_f32 v180, -v66, v82, v180
	v_pk_mul_f32 v[118:119], v[66:67], v[128:129] op_sel:[1,0]
	v_pk_mul_f32 v[218:219], v[66:67], v[136:137] op_sel:[1,0]
	v_mul_f32_e64 v230, v67, v168
	s_waitcnt lgkmcnt(1)
	v_pk_mul_f32 v[122:123], v[72:73], v[128:129] op_sel_hi:[0,1]
	v_pk_mul_f32 v[222:223], v[72:73], v[136:137] op_sel_hi:[0,1]
	v_mul_f32_e64 v234, v72, v168
	v_pk_mul_f32 v[126:127], v[72:73], v[128:129] op_sel:[1,0]
	v_pk_mul_f32 v[226:227], v[72:73], v[136:137] op_sel:[1,0]
	v_mul_f32_e64 v238, v73, v168
	v_pk_fma_f32 v[118:119], v[72:73], v[116:117], v[118:119] op_sel_hi:[0,1,1]
	v_pk_fma_f32 v[218:219], v[72:73], v[144:145], v[218:219] op_sel_hi:[0,1,1]
	v_fma_f32 v230, v72, v172, v230
	v_pk_fma_f32 v[122:123], v[74:75], v[116:117], v[122:123] op_sel_hi:[0,1,1]
	v_pk_fma_f32 v[222:223], v[74:75], v[144:145], v[222:223] op_sel_hi:[0,1,1]
	v_fma_f32 v234, v74, v172, v234
	v_pk_fma_f32 v[126:127], v[74:75], v[116:117], v[126:127] op_sel:[1,0,0]
	v_pk_fma_f32 v[226:227], v[74:75], v[144:145], v[226:227] op_sel:[1,0,0]
	v_fma_f32 v238, v75, v172, v238
	v_pk_fma_f32 v[118:119], v[72:73], v[120:121], v[118:119] op_sel:[1,0,0]
	v_pk_fma_f32 v[218:219], v[72:73], v[176:177], v[218:219] op_sel:[1,0,0]
	v_fma_f32 v230, v73, v180, v230
	v_pk_fma_f32 v[122:123], v[74:75], v[120:121], v[122:123] op_sel:[1,0,0]
	v_pk_fma_f32 v[222:223], v[74:75], v[176:177], v[222:223] op_sel:[1,0,0]
	v_fma_f32 v234, v75, v180, v234
	s_waitcnt lgkmcnt(0)
	v_pk_fma_f32 v[126:127], v[212:213], v[120:121], v[126:127] op_sel_hi:[0,1,1]
	v_pk_fma_f32 v[226:227], v[212:213], v[176:177], v[226:227] op_sel_hi:[0,1,1]
	v_fma_f32 v238, v212, v180, v238
	v_pk_mul_f32 v[124:125], v[64:65], v[118:119] op_sel_hi:[0,1]
	v_pk_mul_f32 v[184:185], v[64:65], v[218:219] op_sel_hi:[0,1]
	v_mul_f32_e64 v188, v64, v230
	v_pk_fma_f32 v[124:125], v[64:65], v[122:123], v[124:125] op_sel:[1,0,0]
	v_pk_fma_f32 v[184:185], v[64:65], v[222:223], v[184:185] op_sel:[1,0,0]
	v_fma_f32 v188, v65, v234, v188
	v_pk_fma_f32 v[124:125], v[66:67], v[126:127], v[124:125] op_sel_hi:[0,1,1]
	v_pk_fma_f32 v[184:185], v[66:67], v[226:227], v[184:185] op_sel_hi:[0,1,1]
	v_fma_f32 v188, v66, v238, v188
	v_pk_fma_f32 v[124:125], v[212:213], v[2:3], v[124:125] op_sel:[1,0,0] neg_lo:[0,0,1] neg_hi:[0,0,1]
	v_pk_fma_f32 v[184:185], v[212:213], v[46:47], v[184:185] op_sel:[1,0,0] neg_lo:[0,0,1] neg_hi:[0,0,1]
	v_fma_f32 v188, v213, v82, -v188
	v_cmp_eq_u32_e64 s[10:11], 1, v215
	v_cmp_eq_u32_e64 s[14:15], 2, v215
	v_cmp_eq_u32_e64 s[20:21], 3, v215
	v_cmp_eq_u32_e64 s[22:23], 4, v215
	v_cmp_eq_u32_e64 s[30:31], 5, v215
	v_pk_add_f32 v[2:3], v[140:141], v[118:119]
	v_pk_add_f32 v[46:47], v[106:107], v[218:219]
	v_add_f32_e64 v82, v114, v230
	v_pk_add_f32 v[106:107], v[186:187], v[122:123]
	v_pk_add_f32 v[114:115], v[190:191], v[222:223]
	v_add_f32_e64 v116, v134, v234
	v_pk_add_f32 v[120:121], v[174:175], v[126:127]
	v_pk_add_f32 v[128:129], v[194:195], v[226:227]
	v_add_f32_e64 v134, v142, v238
	v_pk_add_f32 v[136:137], v[198:199], v[124:125]
	v_pk_add_f32 v[140:141], v[202:203], v[184:185]
	v_add_f32_e64 v144, v206, v188
	v_pk_fma_f32 v[168:169], v[60:61], v[2:3], v[136:137] op_sel_hi:[0,1,1]
	v_pk_fma_f32 v[172:173], v[60:61], v[46:47], v[140:141] op_sel_hi:[0,1,1]
	v_fma_f32 v176, v60, v82, v144
	v_pk_fma_f32 v[180:181], v[68:69], v[2:3], v[136:137] op_sel_hi:[0,1,1]
	v_pk_fma_f32 v[192:193], v[68:69], v[46:47], v[140:141] op_sel_hi:[0,1,1]
	v_fma_f32 v196, v68, v82, v144
	v_pk_fma_f32 v[168:169], v[60:61], v[106:107], v[168:169] op_sel:[1,0,0]
	v_pk_fma_f32 v[172:173], v[60:61], v[114:115], v[172:173] op_sel:[1,0,0]
	v_fma_f32 v176, v61, v116, v176
	v_pk_fma_f32 v[180:181], v[68:69], v[106:107], v[180:181] op_sel:[1,0,0]
	v_pk_fma_f32 v[192:193], v[68:69], v[114:115], v[192:193] op_sel:[1,0,0]
	v_fma_f32 v196, v69, v116, v196
	v_pk_fma_f32 v[168:169], v[62:63], v[120:121], v[168:169] op_sel_hi:[0,1,1]
	v_pk_fma_f32 v[172:173], v[62:63], v[128:129], v[172:173] op_sel_hi:[0,1,1]
	v_fma_f32 v176, v62, v134, v176
	v_pk_fma_f32 v[180:181], v[70:71], v[120:121], v[180:181] op_sel_hi:[0,1,1]
	v_pk_fma_f32 v[192:193], v[70:71], v[128:129], v[192:193] op_sel_hi:[0,1,1]
	v_fma_f32 v196, v70, v134, v196
	v_pk_fma_f32 v[136:137], v[32:33], v[2:3], v[136:137] op_sel_hi:[0,1,1]
	v_pk_fma_f32 v[140:141], v[32:33], v[46:47], v[140:141] op_sel_hi:[0,1,1]
	v_fma_f32 v144, v32, v82, v144
	v_pk_fma_f32 v[136:137], v[32:33], v[106:107], v[136:137] op_sel:[1,0,0]
	v_pk_fma_f32 v[140:141], v[32:33], v[114:115], v[140:141] op_sel:[1,0,0]
	v_fma_f32 v144, v33, v116, v144
	v_pk_fma_f32 v[136:137], v[34:35], v[120:121], v[136:137] op_sel_hi:[0,1,1]
	v_pk_fma_f32 v[140:141], v[34:35], v[128:129], v[140:141] op_sel_hi:[0,1,1]
	v_fma_f32 v144, v34, v134, v144
	v_cndmask_b32_e64 v142, 0, v1, s[10:11]
	v_cndmask_b32_e64 v143, 0, v1, s[14:15]
	v_cndmask_b32_e64 v174, 0, v1, s[20:21]
	v_cndmask_b32_e64 v175, 0, v1, s[22:23]
	v_cndmask_b32_e64 v186, 0, v1, s[30:31]
	v_add_f32_dpp v136, v168, v136 wave_shl:1 row_mask:0xf bank_mask:0xf bound_ctrl:1
	v_add_f32_dpp v137, v169, v137 wave_shl:1 row_mask:0xf bank_mask:0xf bound_ctrl:1
	v_add_f32_dpp v140, v172, v140 wave_shl:1 row_mask:0xf bank_mask:0xf bound_ctrl:1
	v_add_f32_dpp v141, v173, v141 wave_shl:1 row_mask:0xf bank_mask:0xf bound_ctrl:1
	v_add_f32_dpp v144, v176, v144 wave_shl:1 row_mask:0xf bank_mask:0xf bound_ctrl:1
	s_add_i32 s4, s34, 9
	s_cmpk_lt_i32 s4, 0x201
	s_cselect_b64 s[12:13], s[0:1], 0
	v_add_f32_dpp v136, v180, v136 wave_shr:1 row_mask:0xf bank_mask:0xf bound_ctrl:1
	v_add_f32_dpp v137, v181, v137 wave_shr:1 row_mask:0xf bank_mask:0xf bound_ctrl:1
	v_add_f32_dpp v140, v192, v140 wave_shr:1 row_mask:0xf bank_mask:0xf bound_ctrl:1
	v_add_f32_dpp v141, v193, v141 wave_shr:1 row_mask:0xf bank_mask:0xf bound_ctrl:1
	v_add_f32_dpp v144, v196, v144 wave_shr:1 row_mask:0xf bank_mask:0xf bound_ctrl:1
	v_pk_fma_f32 v[136:137], v[12:13], v[214:215], v[136:137] op_sel_hi:[1,0,1] neg_lo:[0,0,1] neg_hi:[0,0,1]
	v_pk_fma_f32 v[140:141], v[14:15], v[214:215], v[140:141] op_sel_hi:[1,0,1] neg_lo:[0,0,1] neg_hi:[0,0,1]
	v_fma_f32 v144, v16, v214, -v144
	v_pk_add_f32 v[136:137], v[136:137], v[142:143] neg_lo:[0,1] neg_hi:[0,1]
	v_pk_add_f32 v[140:141], v[140:141], v[174:175] neg_lo:[0,1] neg_hi:[0,1]
	v_add_f32_e64 v144, v144, -v186
	v_pk_mul_f32 v[190:191], v[136:137], v[136:137]
	v_pk_fma_f32 v[190:191], v[140:141], v[140:141], v[190:191]
	v_add_f32_e32 v190, v190, v191
	v_fma_f32 v190, v144, v144, v190
	v_cndmask_b32_e64 v191, 0, v190, s[12:13]
	v_add_f32_e32 v0, v0, v191
